# v59 with the wide stores at system scope (sc0 sc1) instead of agent scope
# speedup vs baseline: 1.0257x; 1.0047x over previous
.LBB0_27:
	s_add_u32 s16, s15, s86
	s_addc_u32 s17, s34, s87
	s_add_u32 s36, s16, 0xd0000
	s_addc_u32 s37, s17, 0
	global_load_dwordx4 v[18:21], v1, s[36:37] offset:16
	global_load_dwordx4 v[62:65], v228, s[16:17]
	v_lshl_add_u64 v[38:39], v[26:27], 0, s[86:87]
	global_load_dwordx2 v[68:69], v[38:39], off offset:-1024
	global_load_dwordx2 v[70:71], v[38:39], off offset:-512
	global_load_dwordx2 v[72:73], v[38:39], off
	global_load_dwordx2 v[74:75], v[38:39], off offset:512
	v_lshl_add_u64 v[38:39], v[36:37], 0, s[86:87]
	global_load_dwordx2 v[60:61], v[38:39], off offset:-1024
	global_load_dwordx2 v[58:59], v[38:39], off offset:-512
	global_load_dwordx2 v[56:57], v[38:39], off
	global_load_dwordx2 v[54:55], v[38:39], off offset:512
	v_lshl_add_u64 v[38:39], v[32:33], 0, s[86:87]
	global_load_dwordx2 v[52:53], v[38:39], off offset:-1024
	global_load_dwordx2 v[50:51], v[38:39], off offset:-512
	global_load_dwordx2 v[48:49], v[38:39], off
	global_load_dwordx2 v[46:47], v[38:39], off offset:512
	s_add_i32 s16, s14, 3
	s_ashr_i32 s17, s16, 31
	s_lshl_b64 s[36:37], s[16:17], 11
	v_lshl_add_u64 v[38:39], v[22:23], 0, s[36:37]
	global_load_dwordx2 v[44:45], v[38:39], off
	global_load_dwordx2 v[42:43], v[38:39], off offset:512
	global_load_dwordx2 v[40:41], v[38:39], off offset:1024
	s_nop 0
	global_load_dwordx2 v[38:39], v[38:39], off offset:1536
	s_lshl_b64 s[16:17], s[16:17], 12
	s_add_i32 s14, s14, 4
	s_add_u32 s15, s15, 32
	s_addc_u32 s34, s34, 0
	v_lshl_add_u64 v[26:27], v[26:27], 0, s[38:39]
	v_lshl_add_u64 v[32:33], v[32:33], 0, s[38:39]
	v_lshl_add_u64 v[36:37], v[36:37], 0, s[38:39]
	s_cmp_ge_i32 s14, s31
	s_waitcnt vmcnt(15)
	v_lshlrev_b32_e32 v66, 16, v68
	v_ffbh_u32_e32 v0, v63
	v_min_u32_e32 v0, 32, v0
	v_lshlrev_b64 v[62:63], v0, v[62:63]
	v_min_u32_e32 v62, 1, v62
	v_or_b32_e32 v62, v63, v62
	v_cvt_f32_u32_e32 v62, v62
	v_sub_u32_e32 v0, 32, v0
	v_and_b32_e32 v67, 0xffff0000, v68
	v_lshlrev_b32_e32 v68, 16, v69
	v_ldexp_f32 v0, v62, v0
	v_fmamk_f32 v0, v0, 0x32800000, v196
	v_cmp_gt_f32_e32 vcc, s96, v0
	v_mul_f32_e32 v62, 0x4b800000, v0
	v_and_b32_e32 v69, 0xffff0000, v69
	v_cndmask_b32_e32 v0, v0, v62, vcc
	v_rsq_f32_e32 v0, v0
	s_nop 0
	v_mul_f32_e32 v62, 0x45800000, v0
	v_cndmask_b32_e32 v0, v0, v62, vcc
	v_pk_mul_f32 v[66:67], v[0:1], v[66:67] op_sel_hi:[0,1]
	v_pk_mul_f32 v[68:69], v[0:1], v[68:69] op_sel_hi:[0,1]
	v_lshl_add_u64 v[62:63], v[30:31], 0, s[0:1]
	v_pk_mul_f32 v[66:67], v[14:15], v[66:67]
	v_pk_mul_f32 v[68:69], v[16:17], v[68:69]
	global_store_dwordx4 v[62:63], v[66:69], off sc0 sc1
	v_lshl_add_u64 v[30:31], v[30:31], 0, s[40:41]
	s_waitcnt vmcnt(15)
	v_lshlrev_b32_e32 v66, 16, v70
	v_and_b32_e32 v67, 0xffff0000, v70
	v_lshlrev_b32_e32 v68, 16, v71
	v_and_b32_e32 v69, 0xffff0000, v71
	v_pk_mul_f32 v[66:67], v[0:1], v[66:67] op_sel_hi:[0,1]
	v_pk_mul_f32 v[68:69], v[0:1], v[68:69] op_sel_hi:[0,1]
	v_pk_mul_f32 v[66:67], v[10:11], v[66:67]
	v_pk_mul_f32 v[68:69], v[12:13], v[68:69]
	global_store_dwordx4 v[62:63], v[66:69], off offset:1024 sc0 sc1
	s_waitcnt vmcnt(15)
	s_nop 0
	v_lshlrev_b32_e32 v66, 16, v72
	v_and_b32_e32 v67, 0xffff0000, v72
	v_lshlrev_b32_e32 v68, 16, v73
	v_and_b32_e32 v69, 0xffff0000, v73
	v_pk_mul_f32 v[66:67], v[0:1], v[66:67] op_sel_hi:[0,1]
	v_pk_mul_f32 v[68:69], v[0:1], v[68:69] op_sel_hi:[0,1]
	v_pk_mul_f32 v[66:67], v[6:7], v[66:67]
	v_pk_mul_f32 v[68:69], v[8:9], v[68:69]
	global_store_dwordx4 v[62:63], v[66:69], off offset:2048 sc0 sc1
	s_waitcnt vmcnt(15)
	s_nop 0
	v_lshlrev_b32_e32 v66, 16, v74
	v_and_b32_e32 v67, 0xffff0000, v74
	v_lshlrev_b32_e32 v68, 16, v75
	v_and_b32_e32 v69, 0xffff0000, v75
	v_pk_mul_f32 v[66:67], v[0:1], v[66:67] op_sel_hi:[0,1]
	v_pk_mul_f32 v[68:69], v[0:1], v[68:69] op_sel_hi:[0,1]
	v_ffbh_u32_e32 v0, v65
	v_pk_mul_f32 v[66:67], v[2:3], v[66:67]
	v_pk_mul_f32 v[68:69], v[4:5], v[68:69]
	v_min_u32_e32 v0, 32, v0
	global_store_dwordx4 v[62:63], v[66:69], off offset:3072 sc0 sc1
	v_lshlrev_b64 v[62:63], v0, v[64:65]
	v_min_u32_e32 v62, 1, v62
	v_or_b32_e32 v62, v63, v62
	v_cvt_f32_u32_e32 v62, v62
	v_sub_u32_e32 v0, 32, v0
	s_waitcnt vmcnt(15)
	v_and_b32_e32 v63, 0xffff0000, v60
	v_lshl_add_u64 v[66:67], v[34:35], 0, s[0:1]
	v_ldexp_f32 v0, v62, v0
	v_fmamk_f32 v0, v0, 0x32800000, v196
	v_cmp_gt_f32_e32 vcc, s96, v0
	v_mul_f32_e32 v62, 0x4b800000, v0
	v_lshl_add_u64 v[34:35], v[34:35], 0, s[40:41]
	v_cndmask_b32_e32 v0, v0, v62, vcc
	v_rsq_f32_e32 v0, v0
	s_nop 0
	v_mul_f32_e32 v62, 0x45800000, v0
	v_cndmask_b32_e32 v0, v0, v62, vcc
	v_lshlrev_b32_e32 v62, 16, v60
	v_lshlrev_b32_e32 v60, 16, v61
	v_and_b32_e32 v61, 0xffff0000, v61
	v_pk_mul_f32 v[60:61], v[0:1], v[60:61] op_sel_hi:[0,1]
	v_pk_mul_f32 v[62:63], v[0:1], v[62:63] op_sel_hi:[0,1]
	v_pk_mul_f32 v[64:65], v[16:17], v[60:61]
	s_waitcnt vmcnt(14)
	v_lshlrev_b32_e32 v60, 16, v58
	v_and_b32_e32 v61, 0xffff0000, v58
	v_lshlrev_b32_e32 v58, 16, v59
	v_and_b32_e32 v59, 0xffff0000, v59
	v_pk_mul_f32 v[62:63], v[14:15], v[62:63]
	v_pk_mul_f32 v[58:59], v[0:1], v[58:59] op_sel_hi:[0,1]
	global_store_dwordx4 v[66:67], v[62:65], off sc0 sc1
	v_pk_mul_f32 v[60:61], v[0:1], v[60:61] op_sel_hi:[0,1]
	v_pk_mul_f32 v[60:61], v[10:11], v[60:61]
	v_pk_mul_f32 v[62:63], v[12:13], v[58:59]
	s_waitcnt vmcnt(14)
	v_lshlrev_b32_e32 v58, 16, v56
	v_and_b32_e32 v59, 0xffff0000, v56
	v_lshlrev_b32_e32 v56, 16, v57
	v_and_b32_e32 v57, 0xffff0000, v57
	v_pk_mul_f32 v[56:57], v[0:1], v[56:57] op_sel_hi:[0,1]
	global_store_dwordx4 v[66:67], v[60:63], off offset:1024 sc0 sc1
	v_pk_mul_f32 v[58:59], v[0:1], v[58:59] op_sel_hi:[0,1]
	v_pk_mul_f32 v[58:59], v[6:7], v[58:59]
	v_pk_mul_f32 v[60:61], v[8:9], v[56:57]
	s_waitcnt vmcnt(14)
	v_lshlrev_b32_e32 v56, 16, v54
	v_and_b32_e32 v57, 0xffff0000, v54
	v_lshlrev_b32_e32 v54, 16, v55
	v_and_b32_e32 v55, 0xffff0000, v55
	v_pk_mul_f32 v[56:57], v[0:1], v[56:57] op_sel_hi:[0,1]
	v_pk_mul_f32 v[54:55], v[0:1], v[54:55] op_sel_hi:[0,1]
	v_ffbh_u32_e32 v0, v19
	v_min_u32_e32 v0, 32, v0
	v_lshlrev_b64 v[18:19], v0, v[18:19]
	v_min_u32_e32 v18, 1, v18
	v_or_b32_e32 v18, v19, v18
	v_cvt_f32_u32_e32 v18, v18
	v_sub_u32_e32 v0, 32, v0
	global_store_dwordx4 v[66:67], v[58:61], off offset:2048 sc0 sc1
	v_pk_mul_f32 v[56:57], v[2:3], v[56:57]
	v_ldexp_f32 v0, v18, v0
	v_fmamk_f32 v0, v0, 0x32800000, v196
	v_cmp_gt_f32_e32 vcc, s96, v0
	v_mul_f32_e32 v18, 0x4b800000, v0
	v_pk_mul_f32 v[58:59], v[4:5], v[54:55]
	v_cndmask_b32_e32 v0, v0, v18, vcc
	v_rsq_f32_e32 v0, v0
	s_waitcnt vmcnt(14)
	v_lshlrev_b32_e32 v54, 16, v52
	v_and_b32_e32 v55, 0xffff0000, v52
	v_lshlrev_b32_e32 v52, 16, v53
	v_mul_f32_e32 v18, 0x45800000, v0
	v_cndmask_b32_e32 v0, v0, v18, vcc
	v_and_b32_e32 v53, 0xffff0000, v53
	v_pk_mul_f32 v[52:53], v[0:1], v[52:53] op_sel_hi:[0,1]
	global_store_dwordx4 v[66:67], v[56:59], off offset:3072 sc0 sc1
	v_pk_mul_f32 v[54:55], v[0:1], v[54:55] op_sel_hi:[0,1]
	v_lshl_add_u64 v[18:19], v[28:29], 0, s[0:1]
	v_pk_mul_f32 v[56:57], v[16:17], v[52:53]
	s_waitcnt vmcnt(14)
	v_lshlrev_b32_e32 v52, 16, v50
	v_and_b32_e32 v53, 0xffff0000, v50
	v_lshlrev_b32_e32 v50, 16, v51
	v_and_b32_e32 v51, 0xffff0000, v51
	v_pk_mul_f32 v[54:55], v[14:15], v[54:55]
	v_pk_mul_f32 v[50:51], v[0:1], v[50:51] op_sel_hi:[0,1]
	global_store_dwordx4 v[18:19], v[54:57], off sc0 sc1
	v_pk_mul_f32 v[52:53], v[0:1], v[52:53] op_sel_hi:[0,1]
	v_pk_mul_f32 v[52:53], v[10:11], v[52:53]
	v_pk_mul_f32 v[54:55], v[12:13], v[50:51]
	s_waitcnt vmcnt(14)
	v_lshlrev_b32_e32 v50, 16, v48
	v_and_b32_e32 v51, 0xffff0000, v48
	v_lshlrev_b32_e32 v48, 16, v49
	v_and_b32_e32 v49, 0xffff0000, v49
	v_pk_mul_f32 v[48:49], v[0:1], v[48:49] op_sel_hi:[0,1]
	global_store_dwordx4 v[18:19], v[52:55], off offset:1024 sc0 sc1
	v_pk_mul_f32 v[50:51], v[0:1], v[50:51] op_sel_hi:[0,1]
	v_pk_mul_f32 v[50:51], v[6:7], v[50:51]
	v_pk_mul_f32 v[52:53], v[8:9], v[48:49]
	s_waitcnt vmcnt(14)
	v_lshlrev_b32_e32 v48, 16, v46
	v_and_b32_e32 v49, 0xffff0000, v46
	v_lshlrev_b32_e32 v46, 16, v47
	v_and_b32_e32 v47, 0xffff0000, v47
	v_pk_mul_f32 v[48:49], v[0:1], v[48:49] op_sel_hi:[0,1]
	v_pk_mul_f32 v[46:47], v[0:1], v[46:47] op_sel_hi:[0,1]
	v_ffbh_u32_e32 v0, v21
	global_store_dwordx4 v[18:19], v[50:53], off offset:2048 sc0 sc1
	v_pk_mul_f32 v[48:49], v[2:3], v[48:49]
	v_min_u32_e32 v0, 32, v0
	v_pk_mul_f32 v[50:51], v[4:5], v[46:47]
	global_store_dwordx4 v[18:19], v[48:51], off offset:3072 sc0 sc1
	v_lshlrev_b64 v[18:19], v0, v[20:21]
	v_min_u32_e32 v18, 1, v18
	v_or_b32_e32 v18, v19, v18
	v_cvt_f32_u32_e32 v18, v18
	v_sub_u32_e32 v0, 32, v0
	s_waitcnt vmcnt(15)
	v_and_b32_e32 v19, 0xffff0000, v44
	v_lshlrev_b32_e32 v20, 16, v45
	v_ldexp_f32 v0, v18, v0
	v_fmamk_f32 v0, v0, 0x32800000, v196
	v_cmp_gt_f32_e32 vcc, s96, v0
	v_mul_f32_e32 v18, 0x4b800000, v0
	v_and_b32_e32 v21, 0xffff0000, v45
	v_cndmask_b32_e32 v0, v0, v18, vcc
	v_rsq_f32_e32 v0, v0
	v_lshl_add_u64 v[46:47], v[24:25], 0, s[16:17]
	v_lshl_add_u64 v[28:29], v[28:29], 0, s[40:41]
	v_mul_f32_e32 v18, 0x45800000, v0
	v_cndmask_b32_e32 v0, v0, v18, vcc
	v_lshlrev_b32_e32 v18, 16, v44
	v_pk_mul_f32 v[18:19], v[0:1], v[18:19] op_sel_hi:[0,1]
	v_pk_mul_f32 v[20:21], v[0:1], v[20:21] op_sel_hi:[0,1]
	v_pk_mul_f32 v[18:19], v[14:15], v[18:19]
	v_pk_mul_f32 v[20:21], v[16:17], v[20:21]
	global_store_dwordx4 v[46:47], v[18:21], off sc0 sc1
	s_waitcnt vmcnt(15)
	s_nop 0
	v_lshlrev_b32_e32 v18, 16, v42
	v_and_b32_e32 v19, 0xffff0000, v42
	v_lshlrev_b32_e32 v20, 16, v43
	v_and_b32_e32 v21, 0xffff0000, v43
	v_pk_mul_f32 v[18:19], v[0:1], v[18:19] op_sel_hi:[0,1]
	v_pk_mul_f32 v[20:21], v[0:1], v[20:21] op_sel_hi:[0,1]
	v_pk_mul_f32 v[18:19], v[10:11], v[18:19]
	v_pk_mul_f32 v[20:21], v[12:13], v[20:21]
	global_store_dwordx4 v[46:47], v[18:21], off offset:1024 sc0 sc1
	s_waitcnt vmcnt(15)
	s_nop 0
	v_lshlrev_b32_e32 v18, 16, v40
	v_and_b32_e32 v19, 0xffff0000, v40
	v_lshlrev_b32_e32 v20, 16, v41
	v_and_b32_e32 v21, 0xffff0000, v41
	v_pk_mul_f32 v[18:19], v[0:1], v[18:19] op_sel_hi:[0,1]
	v_pk_mul_f32 v[20:21], v[0:1], v[20:21] op_sel_hi:[0,1]
	v_pk_mul_f32 v[18:19], v[6:7], v[18:19]
	v_pk_mul_f32 v[20:21], v[8:9], v[20:21]
	global_store_dwordx4 v[46:47], v[18:21], off offset:2048 sc0 sc1
	s_waitcnt vmcnt(15)
	s_nop 0
	v_lshlrev_b32_e32 v18, 16, v38
	v_and_b32_e32 v19, 0xffff0000, v38
	v_lshlrev_b32_e32 v20, 16, v39
	v_and_b32_e32 v21, 0xffff0000, v39
	v_pk_mul_f32 v[18:19], v[0:1], v[18:19] op_sel_hi:[0,1]
	v_pk_mul_f32 v[20:21], v[0:1], v[20:21] op_sel_hi:[0,1]
	v_pk_mul_f32 v[18:19], v[2:3], v[18:19]
	v_pk_mul_f32 v[20:21], v[4:5], v[20:21]
	global_store_dwordx4 v[46:47], v[18:21], off offset:3072 sc0 sc1
	s_cbranch_scc0 .LBB0_27

.LBB0_77:
	s_or_b64 exec, exec, s[64:65]
	v_lshlrev_b64 v[70:71], 2, v[74:75]
	v_lshl_add_u64 v[2:3], s[56:57], 0, v[70:71]
	v_lshl_or_b32 v0, v66, 6, v67
	global_load_dwordx4 v[66:69], v[2:3], off offset:16
	global_load_dwordx4 v[86:89], v[2:3], off
	v_lshl_add_u64 v[2:3], s[60:61], 0, v[70:71]
	v_lshl_add_u64 v[72:73], s[62:63], 0, v[70:71]
	v_lshl_add_u64 v[76:77], s[58:59], 0, v[70:71]
	global_load_dwordx4 v[62:65], v[2:3], off offset:16
	global_load_dwordx4 v[90:93], v[2:3], off
	s_nop 0
	global_load_dwordx4 v[2:5], v[72:73], off offset:16
	global_load_dwordx4 v[94:97], v[72:73], off
	s_nop 0
	global_load_dwordx4 v[70:73], v[76:77], off offset:16
	global_load_dwordx4 v[98:101], v[76:77], off
	v_lshlrev_b32_e32 v76, 16, v58
	v_and_b32_e32 v77, 0xffff0000, v58
	v_lshlrev_b32_e32 v58, 16, v59
	v_and_b32_e32 v59, 0xffff0000, v59
	s_waitcnt vmcnt(0)
	v_pk_fma_f32 v[76:77], v[86:87], v[76:77], v[98:99]
	v_lshlrev_b32_e32 v86, 16, v14
	v_and_b32_e32 v87, 0xffff0000, v14
	v_pk_fma_f32 v[76:77], v[90:91], v[86:87], v[76:77]
	v_lshlrev_b32_e32 v86, 16, v54
	v_and_b32_e32 v87, 0xffff0000, v54
	v_pk_fma_f32 v[76:77], v[94:95], v[86:87], v[76:77]
	v_pk_fma_f32 v[58:59], v[88:89], v[58:59], v[100:101]
	v_mul_f32_e32 v14, 0x3d372713, v76
	v_mul_f32_e32 v14, v76, v14
	v_fma_f32 v14, v76, v14, v76
	v_mul_f32_e32 v14, 0xc0135761, v14
	v_exp_f32_e32 v14, v14
	v_lshlrev_b32_e32 v54, 16, v55
	v_and_b32_e32 v55, 0xffff0000, v55
	v_add_f32_e32 v14, 1.0, v14
	v_rcp_f32_e32 v86, v14
	v_mul_f32_e32 v14, 0x3d372713, v77
	v_mul_f32_e32 v14, v77, v14
	v_fma_f32 v14, v77, v14, v77
	v_mul_f32_e32 v14, 0xc0135761, v14
	v_exp_f32_e32 v14, v14
	s_nop 0
	v_add_f32_e32 v14, 1.0, v14
	v_rcp_f32_e32 v87, v14
	v_lshlrev_b32_e32 v14, 16, v15
	v_and_b32_e32 v15, 0xffff0000, v15
	v_pk_fma_f32 v[14:15], v[92:93], v[14:15], v[58:59]
	v_pk_mul_f32 v[76:77], v[76:77], v[86:87]
	v_pk_fma_f32 v[14:15], v[96:97], v[54:55], v[14:15]
	v_lshlrev_b32_e32 v86, 16, v50
	v_and_b32_e32 v87, 0xffff0000, v50
	v_mul_f32_e32 v50, 0x3d372713, v14
	v_mul_f32_e32 v50, v14, v50
	v_fma_f32 v50, v14, v50, v14
	v_mul_f32_e32 v50, 0xc0135761, v50
	v_exp_f32_e32 v50, v50
	v_pk_mul_f32 v[76:77], v[76:77], v[86:87]
	v_add_f32_e32 v50, 1.0, v50
	v_rcp_f32_e32 v54, v50
	v_mul_f32_e32 v50, 0x3d372713, v15
	v_mul_f32_e32 v50, v15, v50
	v_fma_f32 v50, v15, v50, v15
	v_mul_f32_e32 v50, 0xc0135761, v50
	v_exp_f32_e32 v50, v50
	s_nop 0
	v_add_f32_e32 v50, 1.0, v50
	v_rcp_f32_e32 v55, v50
	v_lshlrev_b32_e32 v50, 16, v51
	v_and_b32_e32 v51, 0xffff0000, v51
	v_pk_mul_f32 v[14:15], v[14:15], v[54:55]
	s_nop 0
	v_pk_mul_f32 v[14:15], v[14:15], v[50:51]
	v_lshlrev_b32_e32 v50, 16, v60
	v_and_b32_e32 v51, 0xffff0000, v60
	v_pk_fma_f32 v[50:51], v[66:67], v[50:51], v[70:71]
	v_lshlrev_b32_e32 v54, 16, v16
	v_and_b32_e32 v55, 0xffff0000, v16
	v_pk_fma_f32 v[50:51], v[62:63], v[54:55], v[50:51]
	v_lshlrev_b32_e32 v54, 16, v56
	v_and_b32_e32 v55, 0xffff0000, v56
	v_pk_fma_f32 v[2:3], v[2:3], v[54:55], v[50:51]
	s_nop 0
	v_mul_f32_e32 v16, 0x3d372713, v2
	v_mul_f32_e32 v16, v2, v16
	v_fma_f32 v16, v2, v16, v2
	v_mul_f32_e32 v16, 0xc0135761, v16
	v_exp_f32_e32 v16, v16
	s_nop 0
	v_add_f32_e32 v16, 1.0, v16
	v_rcp_f32_e32 v50, v16
	v_mul_f32_e32 v16, 0x3d372713, v3
	v_mul_f32_e32 v16, v3, v16
	v_fma_f32 v16, v3, v16, v3
	v_mul_f32_e32 v16, 0xc0135761, v16
	v_exp_f32_e32 v16, v16
	s_nop 0
	v_add_f32_e32 v16, 1.0, v16
	v_rcp_f32_e32 v51, v16
	v_lshlrev_b32_e32 v16, 16, v17
	v_and_b32_e32 v17, 0xffff0000, v17
	v_pk_mul_f32 v[2:3], v[2:3], v[50:51]
	v_lshlrev_b32_e32 v50, 16, v52
	v_and_b32_e32 v51, 0xffff0000, v52
	v_pk_mul_f32 v[2:3], v[2:3], v[50:51]
	v_lshlrev_b32_e32 v50, 16, v61
	v_and_b32_e32 v51, 0xffff0000, v61
	v_pk_fma_f32 v[50:51], v[68:69], v[50:51], v[72:73]
	v_cvt_pk_bf16_f32 v52, v2, v3
	v_pk_fma_f32 v[16:17], v[64:65], v[16:17], v[50:51]
	v_lshlrev_b32_e32 v50, 16, v57
	v_and_b32_e32 v51, 0xffff0000, v57
	v_pk_fma_f32 v[4:5], v[4:5], v[50:51], v[16:17]
	v_mov_b64_e32 v[2:3], s[0:1]
	v_mul_f32_e32 v16, 0x3d372713, v4
	v_mul_f32_e32 v17, 0x3d372713, v5
	v_mul_f32_e32 v16, v4, v16
	v_mul_f32_e32 v17, v5, v17
	v_fma_f32 v16, v4, v16, v4
	v_fma_f32 v17, v5, v17, v5
	v_mul_f32_e32 v16, 0xc0135761, v16
	v_mul_f32_e32 v17, 0xc0135761, v17
	v_exp_f32_e32 v16, v16
	v_exp_f32_e32 v17, v17
	v_mad_i64_i32 v[2:3], s[42:43], v0, s2, v[2:3]
	v_add_f32_e32 v16, 1.0, v16
	v_add_f32_e32 v17, 1.0, v17
	v_rcp_f32_e32 v16, v16
	v_rcp_f32_e32 v17, v17
	v_cvt_pk_bf16_f32 v50, v76, v77
	v_cvt_pk_bf16_f32 v51, v14, v15
	v_lshl_add_u64 v[2:3], v[74:75], 1, v[2:3]
	v_pk_mul_f32 v[4:5], v[4:5], v[16:17]
	v_lshlrev_b32_e32 v16, 16, v53
	v_and_b32_e32 v17, 0xffff0000, v53
	v_pk_mul_f32 v[4:5], v[4:5], v[16:17]
	s_nop 0
	v_cvt_pk_bf16_f32 v53, v4, v5
	global_store_dwordx4 v[2:3], v[50:53], off sc0 sc1
	s_and_saveexec_b64 s[42:43], s[40:41]
	s_cbranch_execz .LBB0_79
	v_add_u32_e32 v0, v84, v83
	v_mad_i32_i24 v2, v0, s90, v80
	v_lshl_add_u32 v58, v2, 3, v234
	v_lshrrev_b32_e32 v2, 1, v0
	v_ashrrev_i32_e32 v59, 31, v58
	v_add_u32_e32 v2, s34, v2
	v_and_b32_e32 v0, 1, v0
	v_lshlrev_b64 v[54:55], 2, v[58:59]
	v_lshl_or_b32 v0, v2, 6, v0
	v_lshl_add_u64 v[2:3], s[56:57], 0, v[54:55]
	global_load_dwordx4 v[50:53], v[2:3], off offset:16
	global_load_dwordx4 v[60:63], v[2:3], off
	v_lshl_add_u64 v[2:3], s[60:61], 0, v[54:55]
	v_lshl_add_u64 v[56:57], s[62:63], 0, v[54:55]
	v_lshl_add_u64 v[72:73], s[58:59], 0, v[54:55]
	global_load_dwordx4 v[14:17], v[2:3], off offset:16
	global_load_dwordx4 v[64:67], v[2:3], off
	s_nop 0
	global_load_dwordx4 v[2:5], v[56:57], off offset:16
	global_load_dwordx4 v[68:71], v[56:57], off
	s_nop 0
	global_load_dwordx4 v[54:57], v[72:73], off offset:16
	s_nop 0
	global_load_dwordx4 v[72:75], v[72:73], off
	v_lshlrev_b32_e32 v76, 16, v38
	v_and_b32_e32 v77, 0xffff0000, v38
	s_waitcnt vmcnt(0)
	v_pk_fma_f32 v[60:61], v[60:61], v[76:77], v[72:73]
	v_lshlrev_b32_e32 v72, 16, v18
	v_and_b32_e32 v73, 0xffff0000, v18
	v_pk_fma_f32 v[60:61], v[64:65], v[72:73], v[60:61]
	v_lshlrev_b32_e32 v64, 16, v26
	v_and_b32_e32 v65, 0xffff0000, v26
	v_pk_fma_f32 v[60:61], v[68:69], v[64:65], v[60:61]
	s_nop 0
	v_mul_f32_e32 v18, 0x3d372713, v60
	v_mul_f32_e32 v18, v60, v18
	v_fma_f32 v18, v60, v18, v60
	v_mul_f32_e32 v18, 0xc0135761, v18
	v_exp_f32_e32 v18, v18
	s_nop 0
	v_add_f32_e32 v18, 1.0, v18
	v_rcp_f32_e32 v64, v18
	v_mul_f32_e32 v18, 0x3d372713, v61
	v_mul_f32_e32 v18, v61, v18
	v_fma_f32 v18, v61, v18, v61
	v_mul_f32_e32 v18, 0xc0135761, v18
	v_exp_f32_e32 v18, v18
	s_nop 0
	v_add_f32_e32 v18, 1.0, v18
	v_rcp_f32_e32 v65, v18
	v_lshlrev_b32_e32 v18, 16, v19
	v_and_b32_e32 v19, 0xffff0000, v19
	v_pk_mul_f32 v[60:61], v[60:61], v[64:65]
	v_lshlrev_b32_e32 v64, 16, v46
	v_and_b32_e32 v65, 0xffff0000, v46
	v_pk_mul_f32 v[60:61], v[60:61], v[64:65]
	v_lshlrev_b32_e32 v64, 16, v39
	v_and_b32_e32 v65, 0xffff0000, v39
	v_pk_fma_f32 v[62:63], v[62:63], v[64:65], v[74:75]
	s_nop 0
	v_pk_fma_f32 v[18:19], v[66:67], v[18:19], v[62:63]
	v_lshlrev_b32_e32 v62, 16, v27
	v_and_b32_e32 v63, 0xffff0000, v27
	v_pk_fma_f32 v[18:19], v[70:71], v[62:63], v[18:19]
	s_nop 0
	v_mul_f32_e32 v62, 0x3d372713, v18
	v_mul_f32_e32 v63, 0x3d372713, v19
	v_mul_f32_e32 v62, v18, v62
	v_mul_f32_e32 v63, v19, v63
	v_fma_f32 v62, v18, v62, v18
	v_fma_f32 v63, v19, v63, v19
	v_mul_f32_e32 v62, 0xc0135761, v62
	v_mul_f32_e32 v63, 0xc0135761, v63
	v_exp_f32_e32 v62, v62
	v_exp_f32_e32 v63, v63
	v_add_f32_e32 v62, 1.0, v62
	v_add_f32_e32 v63, 1.0, v63
	v_rcp_f32_e32 v62, v62
	v_rcp_f32_e32 v63, v63
	s_nop 0
	v_pk_mul_f32 v[18:19], v[18:19], v[62:63]
	v_lshlrev_b32_e32 v62, 16, v47
	v_and_b32_e32 v63, 0xffff0000, v47
	v_pk_mul_f32 v[18:19], v[18:19], v[62:63]
	v_lshlrev_b32_e32 v62, 16, v40
	v_and_b32_e32 v63, 0xffff0000, v40
	v_pk_fma_f32 v[50:51], v[50:51], v[62:63], v[54:55]
	v_lshlrev_b32_e32 v54, 16, v20
	v_and_b32_e32 v55, 0xffff0000, v20
	v_pk_fma_f32 v[14:15], v[14:15], v[54:55], v[50:51]
	v_lshlrev_b32_e32 v50, 16, v28
	v_and_b32_e32 v51, 0xffff0000, v28
	v_pk_fma_f32 v[2:3], v[2:3], v[50:51], v[14:15]
	v_lshlrev_b32_e32 v20, 16, v21
	v_mul_f32_e32 v14, 0x3d372713, v2
	v_mul_f32_e32 v15, 0x3d372713, v3
	v_mul_f32_e32 v14, v2, v14
	v_mul_f32_e32 v15, v3, v15
	v_fma_f32 v14, v2, v14, v2
	v_fma_f32 v15, v3, v15, v3
	v_mul_f32_e32 v14, 0xc0135761, v14
	v_mul_f32_e32 v15, 0xc0135761, v15
	v_exp_f32_e32 v14, v14
	v_exp_f32_e32 v15, v15
	v_and_b32_e32 v21, 0xffff0000, v21
	v_add_f32_e32 v14, 1.0, v14
	v_add_f32_e32 v15, 1.0, v15
	v_rcp_f32_e32 v14, v14
	v_rcp_f32_e32 v15, v15
	s_nop 0
	v_pk_mul_f32 v[2:3], v[2:3], v[14:15]
	v_lshlrev_b32_e32 v14, 16, v48
	v_and_b32_e32 v15, 0xffff0000, v48
	v_pk_mul_f32 v[2:3], v[2:3], v[14:15]
	v_lshlrev_b32_e32 v14, 16, v41
	v_and_b32_e32 v15, 0xffff0000, v41
	v_pk_fma_f32 v[14:15], v[52:53], v[14:15], v[56:57]
	s_nop 0
	v_pk_fma_f32 v[14:15], v[16:17], v[20:21], v[14:15]
	v_lshlrev_b32_e32 v16, 16, v29
	v_and_b32_e32 v17, 0xffff0000, v29
	v_pk_fma_f32 v[4:5], v[4:5], v[16:17], v[14:15]
	v_cvt_pk_bf16_f32 v16, v2, v3
	v_mul_f32_e32 v14, 0x3d372713, v4
	v_mul_f32_e32 v15, 0x3d372713, v5
	v_mul_f32_e32 v14, v4, v14
	v_mul_f32_e32 v15, v5, v15
	v_fma_f32 v14, v4, v14, v4
	v_fma_f32 v15, v5, v15, v5
	v_mul_f32_e32 v14, 0xc0135761, v14
	v_mul_f32_e32 v15, 0xc0135761, v15
	v_exp_f32_e32 v14, v14
	v_exp_f32_e32 v15, v15
	v_mov_b64_e32 v[2:3], s[0:1]
	v_mad_i64_i32 v[2:3], s[40:41], v0, s2, v[2:3]
	v_add_f32_e32 v14, 1.0, v14
	v_add_f32_e32 v15, 1.0, v15
	v_rcp_f32_e32 v14, v14
	v_rcp_f32_e32 v15, v15
	v_lshl_add_u64 v[2:3], v[58:59], 1, v[2:3]
	v_pk_mul_f32 v[4:5], v[4:5], v[14:15]
	v_lshlrev_b32_e32 v14, 16, v49
	v_and_b32_e32 v15, 0xffff0000, v49
	v_pk_mul_f32 v[4:5], v[4:5], v[14:15]
	v_cvt_pk_bf16_f32 v14, v60, v61
	v_cvt_pk_bf16_f32 v15, v18, v19
	v_cvt_pk_bf16_f32 v17, v4, v5
	global_store_dwordx4 v[2:3], v[14:17], off sc0 sc1
.LBB0_79:
	s_or_b64 exec, exec, s[42:43]
	s_and_saveexec_b64 s[40:41], s[38:39]
	s_cbranch_execz .LBB0_42
	v_add_u32_e32 v0, v82, v81
	v_mad_i32_i24 v2, v0, s90, v80
	v_lshl_add_u32 v54, v2, 3, v230
	v_lshrrev_b32_e32 v2, 1, v0
	v_ashrrev_i32_e32 v55, 31, v54
	v_add_u32_e32 v2, s34, v2
	v_and_b32_e32 v0, 1, v0
	v_lshlrev_b64 v[50:51], 2, v[54:55]
	v_lshl_or_b32 v0, v2, 6, v0
	v_lshl_add_u64 v[2:3], s[56:57], 0, v[50:51]
	global_load_dwordx4 v[18:21], v[2:3], off offset:16
	global_load_dwordx4 v[56:59], v[2:3], off
	v_lshl_add_u64 v[2:3], s[60:61], 0, v[50:51]
	v_lshl_add_u64 v[52:53], s[62:63], 0, v[50:51]
	v_lshl_add_u64 v[68:69], s[58:59], 0, v[50:51]
	global_load_dwordx4 v[14:17], v[2:3], off offset:16
	global_load_dwordx4 v[60:63], v[2:3], off
	s_nop 0
	global_load_dwordx4 v[2:5], v[52:53], off offset:16
	global_load_dwordx4 v[64:67], v[52:53], off
	s_nop 0
	global_load_dwordx4 v[50:53], v[68:69], off offset:16
	s_nop 0
	global_load_dwordx4 v[68:71], v[68:69], off
	v_lshlrev_b32_e32 v72, 16, v34
	v_and_b32_e32 v73, 0xffff0000, v34
	s_waitcnt vmcnt(0)
	v_pk_fma_f32 v[56:57], v[56:57], v[72:73], v[68:69]
	v_lshlrev_b32_e32 v68, 16, v22
	v_and_b32_e32 v69, 0xffff0000, v22
	v_pk_fma_f32 v[56:57], v[60:61], v[68:69], v[56:57]
	v_lshlrev_b32_e32 v60, 16, v30
	v_and_b32_e32 v61, 0xffff0000, v30
	v_pk_fma_f32 v[56:57], v[64:65], v[60:61], v[56:57]
	s_nop 0
	v_mul_f32_e32 v22, 0x3d372713, v56
	v_mul_f32_e32 v22, v56, v22
	v_fma_f32 v22, v56, v22, v56
	v_mul_f32_e32 v22, 0xc0135761, v22
	v_exp_f32_e32 v22, v22
	s_nop 0
	v_add_f32_e32 v22, 1.0, v22
	v_rcp_f32_e32 v60, v22
	v_mul_f32_e32 v22, 0x3d372713, v57
	v_mul_f32_e32 v22, v57, v22
	v_fma_f32 v22, v57, v22, v57
	v_mul_f32_e32 v22, 0xc0135761, v22
	v_exp_f32_e32 v22, v22
	s_nop 0
	v_add_f32_e32 v22, 1.0, v22
	v_rcp_f32_e32 v61, v22
	v_lshlrev_b32_e32 v22, 16, v23
	v_and_b32_e32 v23, 0xffff0000, v23
	v_pk_mul_f32 v[56:57], v[56:57], v[60:61]
	v_lshlrev_b32_e32 v60, 16, v42
	v_and_b32_e32 v61, 0xffff0000, v42
	v_pk_mul_f32 v[56:57], v[56:57], v[60:61]
	v_lshlrev_b32_e32 v60, 16, v35
	v_and_b32_e32 v61, 0xffff0000, v35
	v_pk_fma_f32 v[58:59], v[58:59], v[60:61], v[70:71]
	s_nop 0
	v_pk_fma_f32 v[22:23], v[62:63], v[22:23], v[58:59]
	v_lshlrev_b32_e32 v58, 16, v31
	v_and_b32_e32 v59, 0xffff0000, v31
	v_pk_fma_f32 v[22:23], v[66:67], v[58:59], v[22:23]
	s_nop 0
	v_mul_f32_e32 v58, 0x3d372713, v22
	v_mul_f32_e32 v59, 0x3d372713, v23
	v_mul_f32_e32 v58, v22, v58
	v_mul_f32_e32 v59, v23, v59
	v_fma_f32 v58, v22, v58, v22
	v_fma_f32 v59, v23, v59, v23
	v_mul_f32_e32 v58, 0xc0135761, v58
	v_mul_f32_e32 v59, 0xc0135761, v59
	v_exp_f32_e32 v58, v58
	v_exp_f32_e32 v59, v59
	v_add_f32_e32 v58, 1.0, v58
	v_add_f32_e32 v59, 1.0, v59
	v_rcp_f32_e32 v58, v58
	v_rcp_f32_e32 v59, v59
	s_nop 0
	v_pk_mul_f32 v[22:23], v[22:23], v[58:59]
	v_lshlrev_b32_e32 v58, 16, v43
	v_and_b32_e32 v59, 0xffff0000, v43
	v_pk_mul_f32 v[22:23], v[22:23], v[58:59]
	v_lshlrev_b32_e32 v58, 16, v36
	v_and_b32_e32 v59, 0xffff0000, v36
	v_pk_fma_f32 v[18:19], v[18:19], v[58:59], v[50:51]
	v_lshlrev_b32_e32 v50, 16, v24
	v_and_b32_e32 v51, 0xffff0000, v24
	v_pk_fma_f32 v[14:15], v[14:15], v[50:51], v[18:19]
	v_lshlrev_b32_e32 v18, 16, v32
	v_and_b32_e32 v19, 0xffff0000, v32
	v_pk_fma_f32 v[2:3], v[2:3], v[18:19], v[14:15]
	v_lshlrev_b32_e32 v18, 16, v25
	v_mul_f32_e32 v14, 0x3d372713, v2
	v_mul_f32_e32 v15, 0x3d372713, v3
	v_mul_f32_e32 v14, v2, v14
	v_mul_f32_e32 v15, v3, v15
	v_fma_f32 v14, v2, v14, v2
	v_fma_f32 v15, v3, v15, v3
	v_mul_f32_e32 v14, 0xc0135761, v14
	v_mul_f32_e32 v15, 0xc0135761, v15
	v_exp_f32_e32 v14, v14
	v_exp_f32_e32 v15, v15
	v_and_b32_e32 v19, 0xffff0000, v25
	v_add_f32_e32 v14, 1.0, v14
	v_add_f32_e32 v15, 1.0, v15
	v_rcp_f32_e32 v14, v14
	v_rcp_f32_e32 v15, v15
	s_nop 0
	v_pk_mul_f32 v[2:3], v[2:3], v[14:15]
	v_lshlrev_b32_e32 v14, 16, v44
	v_and_b32_e32 v15, 0xffff0000, v44
	v_pk_mul_f32 v[2:3], v[2:3], v[14:15]
	v_lshlrev_b32_e32 v14, 16, v37
	v_and_b32_e32 v15, 0xffff0000, v37
	v_pk_fma_f32 v[14:15], v[20:21], v[14:15], v[52:53]
	s_nop 0
	v_pk_fma_f32 v[14:15], v[16:17], v[18:19], v[14:15]
	v_lshlrev_b32_e32 v16, 16, v33
	v_and_b32_e32 v17, 0xffff0000, v33
	v_pk_fma_f32 v[4:5], v[4:5], v[16:17], v[14:15]
	v_cvt_pk_bf16_f32 v16, v2, v3
	v_mul_f32_e32 v14, 0x3d372713, v4
	v_mul_f32_e32 v15, 0x3d372713, v5
	v_mul_f32_e32 v14, v4, v14
	v_mul_f32_e32 v15, v5, v15
	v_fma_f32 v14, v4, v14, v4
	v_fma_f32 v15, v5, v15, v5
	v_mul_f32_e32 v14, 0xc0135761, v14
	v_mul_f32_e32 v15, 0xc0135761, v15
	v_exp_f32_e32 v14, v14
	v_exp_f32_e32 v15, v15
	v_mov_b64_e32 v[2:3], s[0:1]
	v_mad_i64_i32 v[2:3], s[38:39], v0, s2, v[2:3]
	v_add_f32_e32 v14, 1.0, v14
	v_add_f32_e32 v15, 1.0, v15
	v_rcp_f32_e32 v14, v14
	v_rcp_f32_e32 v15, v15
	v_lshl_add_u64 v[2:3], v[54:55], 1, v[2:3]
	v_pk_mul_f32 v[4:5], v[4:5], v[14:15]
	v_lshlrev_b32_e32 v14, 16, v45
	v_and_b32_e32 v15, 0xffff0000, v45
	v_pk_mul_f32 v[4:5], v[4:5], v[14:15]
	v_cvt_pk_bf16_f32 v14, v56, v57
	v_cvt_pk_bf16_f32 v15, v22, v23
	v_cvt_pk_bf16_f32 v17, v4, v5
	global_store_dwordx4 v[2:3], v[14:17], off sc0 sc1
	s_branch .LBB0_42

.LBB0_105:
	s_add_u32 s16, s74, 0x2200000
	v_readlane_b32 s0, v253, 39
	s_addc_u32 s17, s75, 0
	v_readlane_b32 s1, v253, 40
	s_and_b64 s[0:1], s[0:1], exec
	v_readlane_b32 s0, v253, 34
	s_cselect_b32 s14, s0, s16
	s_mov_b32 s0, -1
	v_readlane_b32 s1, v253, 35
	s_waitcnt vmcnt(0)
	s_barrier
	s_cselect_b32 s15, s1, s17
	v_mbcnt_lo_u32_b32 v0, s0, 0
	v_mbcnt_hi_u32_b32 v170, s0, v0
	s_ashr_i32 s39, s38, 31
	s_lshl_b32 s1, s62, 5
	s_lshl_b64 s[34:35], s[38:39], 8
	v_lshrrev_b32_e32 v0, 1, v170
	s_lshl_b32 s0, s91, 8
	s_or_b32 s34, s34, s1
	v_and_b32_e32 v0, 56, v0
	v_and_b32_e32 v131, 64, v231
	v_and_b32_e32 v130, 15, v170
	s_add_i32 s29, s0, s63
	v_lshl_add_u64 v[158:159], s[34:35], 0, v[0:1]
	v_xor_b32_e32 v0, 16, v231
	v_add_u32_e32 v131, 64, v131
	v_or_b32_e32 v160, s29, v130
	v_cmp_lt_i32_e32 vcc, v0, v131
	v_lshlrev_b64 v[176:177], 1, v[158:159]
	v_ashrrev_i32_e32 v161, 31, v160
	v_cndmask_b32_e32 v0, v231, v0, vcc
	v_lshlrev_b32_e32 v171, 2, v0
	v_xor_b32_e32 v0, 32, v231
	v_lshl_add_u64 v[162:163], s[16:17], 0, v[176:177]
	v_lshlrev_b64 v[178:179], 11, v[160:161]
	v_cmp_lt_i32_e32 vcc, v0, v131
	v_or_b32_e32 v182, s63, v130
	v_lshl_add_u64 v[130:131], v[162:163], 0, v[178:179]
	global_load_dwordx4 v[172:175], v[130:131], off
	global_load_dwordx4 v[154:157], v[130:131], off offset:256
	v_or_b32_e32 v130, 16, v160
	v_ashrrev_i32_e32 v131, 31, v130
	v_lshlrev_b64 v[168:169], 11, v[130:131]
	v_lshl_add_u64 v[130:131], v[162:163], 0, v[168:169]
	global_load_dwordx4 v[150:153], v[130:131], off
	global_load_dwordx4 v[146:149], v[130:131], off offset:256
	v_or_b32_e32 v130, 32, v160
	v_ashrrev_i32_e32 v131, 31, v130
	v_lshlrev_b64 v[166:167], 11, v[130:131]
	v_lshl_add_u64 v[130:131], v[162:163], 0, v[166:167]
	global_load_dwordx4 v[142:145], v[130:131], off
	global_load_dwordx4 v[138:141], v[130:131], off offset:256
	v_or_b32_e32 v130, 48, v160
	v_ashrrev_i32_e32 v131, 31, v130
	v_lshlrev_b64 v[164:165], 11, v[130:131]
	v_lshl_add_u64 v[130:131], v[162:163], 0, v[164:165]
	global_load_dwordx4 v[134:137], v[130:131], off
	s_nop 0
	global_load_dwordx4 v[130:133], v[130:131], off offset:256
	v_lshl_add_u64 v[178:179], s[14:15], 0, v[178:179]
	v_lshl_add_u64 v[176:177], v[178:179], 0, v[176:177]
	v_cndmask_b32_e32 v0, v231, v0, vcc
	v_lshlrev_b32_e32 v0, 2, v0
	s_lshl_b32 s1, s62, 2
	v_cmp_gt_u32_e32 vcc, 16, v170
	s_waitcnt vmcnt(0)
	v_lshlrev_b32_e32 v180, 16, v172
	v_and_b32_e32 v181, 0xffff0000, v172
	v_lshlrev_b32_e32 v172, 16, v173
	v_and_b32_e32 v173, 0xffff0000, v173
	v_pk_add_f32 v[128:129], v[128:129], v[172:173]
	v_lshlrev_b32_e32 v172, 16, v174
	v_and_b32_e32 v173, 0xffff0000, v174
	v_pk_add_f32 v[172:173], v[122:123], v[172:173]
	v_lshlrev_b32_e32 v122, 16, v175
	v_and_b32_e32 v123, 0xffff0000, v175
	v_pk_add_f32 v[126:127], v[126:127], v[180:181]
	v_pk_add_f32 v[174:175], v[124:125], v[122:123]
	v_cvt_pk_bf16_f32 v122, v126, v127
	v_cvt_pk_bf16_f32 v123, v128, v129
	v_cvt_pk_bf16_f32 v124, v172, v173
	v_cvt_pk_bf16_f32 v125, v174, v175
	global_store_dwordx4 v[176:177], v[122:125], off sc0 sc1
	s_nop 1
	v_pk_mul_f32 v[122:123], v[126:127], v[126:127]
	v_pk_mul_f32 v[126:127], v[172:173], v[172:173]
	v_lshlrev_b32_e32 v172, 16, v154
	v_and_b32_e32 v173, 0xffff0000, v154
	v_lshlrev_b32_e32 v154, 16, v155
	v_and_b32_e32 v155, 0xffff0000, v155
	v_pk_add_f32 v[120:121], v[120:121], v[154:155]
	v_lshlrev_b32_e32 v154, 16, v156
	v_and_b32_e32 v155, 0xffff0000, v156
	v_pk_add_f32 v[154:155], v[114:115], v[154:155]
	v_lshlrev_b32_e32 v114, 16, v157
	v_and_b32_e32 v115, 0xffff0000, v157
	v_pk_add_f32 v[118:119], v[118:119], v[172:173]
	v_pk_add_f32 v[156:157], v[116:117], v[114:115]
	v_cvt_pk_bf16_f32 v114, v118, v119
	v_cvt_pk_bf16_f32 v115, v120, v121
	v_cvt_pk_bf16_f32 v116, v154, v155
	v_cvt_pk_bf16_f32 v117, v156, v157
	global_store_dwordx4 v[176:177], v[114:117], off offset:256 sc0 sc1
	v_pk_mul_f32 v[124:125], v[128:129], v[128:129]
	v_pk_mul_f32 v[128:129], v[174:175], v[174:175]
	v_pk_mul_f32 v[114:115], v[118:119], v[118:119]
	v_pk_mul_f32 v[116:117], v[120:121], v[120:121]
	v_add_f32_e32 v114, v114, v115
	v_add_f32_e32 v116, v116, v117
	v_pk_mul_f32 v[118:119], v[154:155], v[154:155]
	v_pk_mul_f32 v[120:121], v[156:157], v[156:157]
	v_add_f32_e32 v114, v114, v116
	v_add_f32_e32 v115, v128, v129
	v_add_f32_e32 v116, v126, v127
	v_add_f32_e32 v120, v120, v121
	v_add_f32_e32 v118, v118, v119
	v_add_f32_e32 v115, v116, v115
	v_add_f32_e32 v116, v124, v125
	v_add_f32_e32 v117, v122, v123
	v_add_f32_e32 v118, v118, v120
	v_add_f32_e32 v116, v117, v116
	v_add_f32_e32 v114, v114, v118
	v_add_f32_e32 v115, v116, v115
	v_add_f32_e32 v114, v115, v114
	ds_bpermute_b32 v115, v171, v114
	s_waitcnt lgkmcnt(0)
	v_add_f32_e32 v115, v114, v115
	ds_bpermute_b32 v116, v0, v115
	v_lshl_or_b32 v114, v182, 4, s1
	s_and_saveexec_b64 s[16:17], vcc
	s_cbranch_execz .LBB0_107
	s_waitcnt lgkmcnt(0)
	v_add_f32_e32 v115, v115, v116
	ds_write_b32 v114, v115
.LBB0_107:
	s_or_b64 exec, exec, s[16:17]
	s_waitcnt lgkmcnt(0)
	v_lshlrev_b32_e32 v116, 16, v150
	v_and_b32_e32 v117, 0xffff0000, v150
	v_pk_add_f32 v[110:111], v[110:111], v[116:117]
	v_lshlrev_b32_e32 v116, 16, v151
	v_and_b32_e32 v117, 0xffff0000, v151
	v_pk_add_f32 v[112:113], v[112:113], v[116:117]
	v_lshlrev_b32_e32 v116, 16, v152
	v_and_b32_e32 v117, 0xffff0000, v152
	v_pk_add_f32 v[116:117], v[106:107], v[116:117]
	v_lshlrev_b32_e32 v106, 16, v153
	v_and_b32_e32 v107, 0xffff0000, v153
	v_pk_add_f32 v[118:119], v[108:109], v[106:107]
	v_lshl_add_u64 v[120:121], s[14:15], 0, v[168:169]
	v_cvt_pk_bf16_f32 v106, v110, v111
	v_cvt_pk_bf16_f32 v107, v112, v113
	v_cvt_pk_bf16_f32 v108, v116, v117
	v_cvt_pk_bf16_f32 v109, v118, v119
	v_lshl_add_u64 v[120:121], v[158:159], 1, v[120:121]
	global_store_dwordx4 v[120:121], v[106:109], off sc0 sc1
	s_nop 1
	v_pk_mul_f32 v[106:107], v[110:111], v[110:111]
	v_pk_mul_f32 v[110:111], v[116:117], v[116:117]
	v_lshlrev_b32_e32 v116, 16, v146
	v_and_b32_e32 v117, 0xffff0000, v146
	v_pk_add_f32 v[102:103], v[102:103], v[116:117]
	v_lshlrev_b32_e32 v116, 16, v147
	v_and_b32_e32 v117, 0xffff0000, v147
	v_pk_add_f32 v[104:105], v[104:105], v[116:117]
	v_lshlrev_b32_e32 v116, 16, v148
	v_and_b32_e32 v117, 0xffff0000, v148
	v_pk_add_f32 v[116:117], v[98:99], v[116:117]
	v_lshlrev_b32_e32 v98, 16, v149
	v_and_b32_e32 v99, 0xffff0000, v149
	v_pk_mul_f32 v[108:109], v[112:113], v[112:113]
	v_pk_mul_f32 v[112:113], v[118:119], v[118:119]
	v_pk_add_f32 v[118:119], v[100:101], v[98:99]
	v_cvt_pk_bf16_f32 v98, v102, v103
	v_cvt_pk_bf16_f32 v99, v104, v105
	v_cvt_pk_bf16_f32 v100, v116, v117
	v_cvt_pk_bf16_f32 v101, v118, v119
	global_store_dwordx4 v[120:121], v[98:101], off offset:256 sc0 sc1
	s_nop 1
	v_pk_mul_f32 v[98:99], v[102:103], v[102:103]
	v_pk_mul_f32 v[100:101], v[104:105], v[104:105]
	v_add_f32_e32 v98, v98, v99
	v_add_f32_e32 v100, v100, v101
	v_pk_mul_f32 v[102:103], v[116:117], v[116:117]
	v_pk_mul_f32 v[104:105], v[118:119], v[118:119]
	v_add_f32_e32 v98, v98, v100
	v_add_f32_e32 v99, v112, v113
	v_add_f32_e32 v100, v110, v111
	v_add_f32_e32 v104, v104, v105
	v_add_f32_e32 v102, v102, v103
	v_add_f32_e32 v99, v100, v99
	v_add_f32_e32 v100, v108, v109
	v_add_f32_e32 v101, v106, v107
	v_add_f32_e32 v102, v102, v104
	v_add_f32_e32 v100, v101, v100
	v_add_f32_e32 v98, v98, v102
	v_add_f32_e32 v99, v100, v99
	v_add_f32_e32 v98, v99, v98
	ds_bpermute_b32 v99, v171, v98
	s_waitcnt lgkmcnt(0)
	v_add_f32_e32 v98, v98, v99
	ds_bpermute_b32 v99, v0, v98
	s_and_saveexec_b64 s[16:17], vcc
	v_readlane_b32 s91, v253, 27
	v_readlane_b32 s92, v253, 28
	s_mov_b32 s89, 0x2e8ba2e9
	s_movk_i32 s90, 0xfea0
	s_movk_i32 s94, 0x2000
	v_readlane_b32 s93, v253, 29
	s_cbranch_execz .LBB0_109
	s_waitcnt lgkmcnt(0)
	v_add_f32_e32 v98, v98, v99
	ds_write_b32 v114, v98 offset:256
.LBB0_109:
	s_or_b64 exec, exec, s[16:17]
	v_lshlrev_b32_e32 v98, 16, v142
	s_waitcnt lgkmcnt(0)
	v_and_b32_e32 v99, 0xffff0000, v142
	v_pk_add_f32 v[94:95], v[94:95], v[98:99]
	v_lshlrev_b32_e32 v98, 16, v143
	v_and_b32_e32 v99, 0xffff0000, v143
	v_pk_add_f32 v[96:97], v[96:97], v[98:99]
	v_lshlrev_b32_e32 v98, 16, v144
	v_and_b32_e32 v99, 0xffff0000, v144
	v_pk_add_f32 v[98:99], v[90:91], v[98:99]
	v_lshlrev_b32_e32 v90, 16, v145
	v_and_b32_e32 v91, 0xffff0000, v145
	v_pk_add_f32 v[100:101], v[92:93], v[90:91]
	v_lshl_add_u64 v[102:103], s[14:15], 0, v[166:167]
	v_cvt_pk_bf16_f32 v90, v94, v95
	v_cvt_pk_bf16_f32 v91, v96, v97
	v_cvt_pk_bf16_f32 v92, v98, v99
	v_cvt_pk_bf16_f32 v93, v100, v101
	v_lshl_add_u64 v[102:103], v[158:159], 1, v[102:103]
	global_store_dwordx4 v[102:103], v[90:93], off sc0 sc1
	s_nop 1
	v_pk_mul_f32 v[90:91], v[94:95], v[94:95]
	v_pk_mul_f32 v[94:95], v[98:99], v[98:99]
	v_lshlrev_b32_e32 v98, 16, v138
	v_and_b32_e32 v99, 0xffff0000, v138
	v_pk_add_f32 v[86:87], v[86:87], v[98:99]
	v_lshlrev_b32_e32 v98, 16, v139
	v_and_b32_e32 v99, 0xffff0000, v139
	v_pk_add_f32 v[88:89], v[88:89], v[98:99]
	v_lshlrev_b32_e32 v98, 16, v140
	v_and_b32_e32 v99, 0xffff0000, v140
	v_pk_add_f32 v[98:99], v[82:83], v[98:99]
	v_lshlrev_b32_e32 v82, 16, v141
	v_and_b32_e32 v83, 0xffff0000, v141
	v_pk_mul_f32 v[92:93], v[96:97], v[96:97]
	v_pk_mul_f32 v[96:97], v[100:101], v[100:101]
	v_pk_add_f32 v[100:101], v[84:85], v[82:83]
	v_cvt_pk_bf16_f32 v82, v86, v87
	v_cvt_pk_bf16_f32 v83, v88, v89
	v_cvt_pk_bf16_f32 v84, v98, v99
	v_cvt_pk_bf16_f32 v85, v100, v101
	global_store_dwordx4 v[102:103], v[82:85], off offset:256 sc0 sc1
	s_nop 1
	v_pk_mul_f32 v[82:83], v[86:87], v[86:87]
	v_pk_mul_f32 v[84:85], v[88:89], v[88:89]
	v_add_f32_e32 v82, v82, v83
	v_add_f32_e32 v84, v84, v85
	v_pk_mul_f32 v[86:87], v[98:99], v[98:99]
	v_pk_mul_f32 v[88:89], v[100:101], v[100:101]
	v_add_f32_e32 v82, v82, v84
	v_add_f32_e32 v83, v96, v97
	v_add_f32_e32 v84, v94, v95
	v_add_f32_e32 v88, v88, v89
	v_add_f32_e32 v86, v86, v87
	v_add_f32_e32 v83, v84, v83
	v_add_f32_e32 v84, v92, v93
	v_add_f32_e32 v85, v90, v91
	v_add_f32_e32 v86, v86, v88
	v_add_f32_e32 v84, v85, v84
	v_add_f32_e32 v82, v82, v86
	v_add_f32_e32 v83, v84, v83
	v_add_f32_e32 v82, v83, v82
	ds_bpermute_b32 v83, v171, v82
	s_waitcnt lgkmcnt(0)
	v_add_f32_e32 v82, v82, v83
	ds_bpermute_b32 v83, v0, v82
	s_and_saveexec_b64 s[16:17], vcc
	s_cbranch_execz .LBB0_111
	s_waitcnt lgkmcnt(0)
	v_add_f32_e32 v82, v82, v83
	ds_write_b32 v114, v82 offset:512
.LBB0_111:
	s_or_b64 exec, exec, s[16:17]
	v_lshlrev_b32_e32 v82, 16, v134
	s_waitcnt lgkmcnt(0)
	v_and_b32_e32 v83, 0xffff0000, v134
	v_pk_add_f32 v[78:79], v[78:79], v[82:83]
	v_lshlrev_b32_e32 v82, 16, v135
	v_and_b32_e32 v83, 0xffff0000, v135
	v_pk_add_f32 v[80:81], v[80:81], v[82:83]
	v_lshlrev_b32_e32 v82, 16, v136
	v_and_b32_e32 v83, 0xffff0000, v136
	v_pk_add_f32 v[82:83], v[74:75], v[82:83]
	v_lshlrev_b32_e32 v74, 16, v137
	v_and_b32_e32 v75, 0xffff0000, v137
	v_pk_add_f32 v[84:85], v[76:77], v[74:75]
	v_lshl_add_u64 v[86:87], s[14:15], 0, v[164:165]
	v_cvt_pk_bf16_f32 v74, v78, v79
	v_cvt_pk_bf16_f32 v75, v80, v81
	v_cvt_pk_bf16_f32 v76, v82, v83
	v_cvt_pk_bf16_f32 v77, v84, v85
	v_lshl_add_u64 v[86:87], v[158:159], 1, v[86:87]
	global_store_dwordx4 v[86:87], v[74:77], off sc0 sc1
	s_nop 1
	v_pk_mul_f32 v[74:75], v[78:79], v[78:79]
	v_pk_mul_f32 v[78:79], v[82:83], v[82:83]
	v_lshlrev_b32_e32 v82, 16, v130
	v_and_b32_e32 v83, 0xffff0000, v130
	v_pk_add_f32 v[70:71], v[70:71], v[82:83]
	v_lshlrev_b32_e32 v82, 16, v131
	v_and_b32_e32 v83, 0xffff0000, v131
	v_pk_add_f32 v[72:73], v[72:73], v[82:83]
	v_lshlrev_b32_e32 v82, 16, v132
	v_and_b32_e32 v83, 0xffff0000, v132
	v_pk_add_f32 v[82:83], v[66:67], v[82:83]
	v_lshlrev_b32_e32 v66, 16, v133
	v_and_b32_e32 v67, 0xffff0000, v133
	v_pk_mul_f32 v[76:77], v[80:81], v[80:81]
	v_pk_mul_f32 v[80:81], v[84:85], v[84:85]
	v_pk_add_f32 v[84:85], v[68:69], v[66:67]
	v_cvt_pk_bf16_f32 v66, v70, v71
	v_cvt_pk_bf16_f32 v67, v72, v73
	v_cvt_pk_bf16_f32 v68, v82, v83
	v_cvt_pk_bf16_f32 v69, v84, v85
	global_store_dwordx4 v[86:87], v[66:69], off offset:256 sc0 sc1
	s_nop 1
	v_pk_mul_f32 v[66:67], v[70:71], v[70:71]
	v_pk_mul_f32 v[68:69], v[72:73], v[72:73]
	v_add_f32_e32 v66, v66, v67
	v_add_f32_e32 v68, v68, v69
	v_pk_mul_f32 v[70:71], v[82:83], v[82:83]
	v_pk_mul_f32 v[72:73], v[84:85], v[84:85]
	v_add_f32_e32 v66, v66, v68
	v_add_f32_e32 v67, v80, v81
	v_add_f32_e32 v68, v78, v79
	v_add_f32_e32 v72, v72, v73
	v_add_f32_e32 v70, v70, v71
	v_add_f32_e32 v67, v68, v67
	v_add_f32_e32 v68, v76, v77
	v_add_f32_e32 v69, v74, v75
	v_add_f32_e32 v70, v70, v72
	v_add_f32_e32 v68, v69, v68
	v_add_f32_e32 v66, v66, v70
	v_add_f32_e32 v67, v68, v67
	v_add_f32_e32 v66, v67, v66
	ds_bpermute_b32 v67, v171, v66
	s_waitcnt lgkmcnt(0)
	v_add_f32_e32 v66, v66, v67
	ds_bpermute_b32 v67, v0, v66
	s_and_saveexec_b64 s[16:17], vcc
	s_cbranch_execz .LBB0_113
	s_waitcnt lgkmcnt(0)
	v_add_f32_e32 v66, v66, v67
	ds_write_b32 v114, v66 offset:768
.LBB0_113:
	s_or_b64 exec, exec, s[16:17]
	s_waitcnt lgkmcnt(0)
	v_lshlrev_b64 v[66:67], 11, v[160:161]
	v_lshl_add_u64 v[104:105], v[66:67], 0, s[20:21]
	v_lshl_add_u64 v[68:69], v[162:163], 0, v[104:105]
	global_load_dwordx4 v[96:99], v[68:69], off
	global_load_dwordx4 v[100:103], v[68:69], off offset:256
	s_mov_b64 s[16:17], 0x48000
	v_lshl_add_u64 v[94:95], v[66:67], 0, s[16:17]
	s_mov_b64 s[16:17], 0x58000
	v_lshl_add_u64 v[68:69], v[162:163], 0, v[94:95]
	v_lshl_add_u64 v[92:93], v[66:67], 0, s[22:23]
	v_lshl_add_u64 v[90:91], v[66:67], 0, s[16:17]
	global_load_dwordx4 v[86:89], v[68:69], off
	global_load_dwordx4 v[82:85], v[68:69], off offset:256
	v_lshl_add_u64 v[68:69], v[162:163], 0, v[92:93]
	v_lshl_add_u64 v[66:67], v[162:163], 0, v[90:91]
	global_load_dwordx4 v[78:81], v[68:69], off
	global_load_dwordx4 v[74:77], v[68:69], off offset:256
	global_load_dwordx4 v[70:73], v[66:67], off
	s_nop 0
	global_load_dwordx4 v[66:69], v[66:67], off offset:256
	v_lshl_add_u64 v[104:105], s[14:15], 0, v[104:105]
	v_lshl_add_u64 v[104:105], v[158:159], 1, v[104:105]
	s_waitcnt vmcnt(7)
	v_lshlrev_b32_e32 v106, 16, v96
	v_and_b32_e32 v107, 0xffff0000, v96
	v_lshlrev_b32_e32 v96, 16, v97
	v_and_b32_e32 v97, 0xffff0000, v97
	v_pk_add_f32 v[64:65], v[64:65], v[96:97]
	v_lshlrev_b32_e32 v96, 16, v98
	v_and_b32_e32 v97, 0xffff0000, v98
	v_pk_add_f32 v[96:97], v[58:59], v[96:97]
	v_lshlrev_b32_e32 v58, 16, v99
	v_and_b32_e32 v59, 0xffff0000, v99
	v_pk_add_f32 v[62:63], v[62:63], v[106:107]
	v_pk_add_f32 v[98:99], v[60:61], v[58:59]
	v_cvt_pk_bf16_f32 v58, v62, v63
	v_cvt_pk_bf16_f32 v59, v64, v65
	v_cvt_pk_bf16_f32 v60, v96, v97
	v_cvt_pk_bf16_f32 v61, v98, v99
	global_store_dwordx4 v[104:105], v[58:61], off sc0 sc1
	s_nop 1
	v_pk_mul_f32 v[58:59], v[62:63], v[62:63]
	v_pk_mul_f32 v[62:63], v[96:97], v[96:97]
	s_waitcnt vmcnt(7)
	v_lshlrev_b32_e32 v96, 16, v100
	v_and_b32_e32 v97, 0xffff0000, v100
	v_pk_add_f32 v[54:55], v[54:55], v[96:97]
	v_lshlrev_b32_e32 v96, 16, v101
	v_and_b32_e32 v97, 0xffff0000, v101
	v_pk_add_f32 v[56:57], v[56:57], v[96:97]
	v_lshlrev_b32_e32 v96, 16, v102
	v_and_b32_e32 v97, 0xffff0000, v102
	v_pk_add_f32 v[96:97], v[50:51], v[96:97]
	v_lshlrev_b32_e32 v50, 16, v103
	v_and_b32_e32 v51, 0xffff0000, v103
	v_pk_mul_f32 v[60:61], v[64:65], v[64:65]
	v_pk_mul_f32 v[64:65], v[98:99], v[98:99]
	v_pk_add_f32 v[98:99], v[52:53], v[50:51]
	v_cvt_pk_bf16_f32 v50, v54, v55
	v_cvt_pk_bf16_f32 v51, v56, v57
	v_cvt_pk_bf16_f32 v52, v96, v97
	v_cvt_pk_bf16_f32 v53, v98, v99
	global_store_dwordx4 v[104:105], v[50:53], off offset:256 sc0 sc1
	s_nop 1
	v_pk_mul_f32 v[50:51], v[54:55], v[54:55]
	v_pk_mul_f32 v[52:53], v[56:57], v[56:57]
	v_add_f32_e32 v50, v50, v51
	v_add_f32_e32 v52, v52, v53
	v_pk_mul_f32 v[54:55], v[96:97], v[96:97]
	v_pk_mul_f32 v[56:57], v[98:99], v[98:99]
	v_add_f32_e32 v50, v50, v52
	v_add_f32_e32 v51, v64, v65
	v_add_f32_e32 v52, v62, v63
	v_add_f32_e32 v56, v56, v57
	v_add_f32_e32 v54, v54, v55
	v_add_f32_e32 v51, v52, v51
	v_add_f32_e32 v52, v60, v61
	v_add_f32_e32 v53, v58, v59
	v_add_f32_e32 v54, v54, v56
	v_add_f32_e32 v52, v53, v52
	v_add_f32_e32 v50, v50, v54
	v_add_f32_e32 v51, v52, v51
	v_add_f32_e32 v50, v51, v50
	ds_bpermute_b32 v51, v171, v50
	s_waitcnt lgkmcnt(0)
	v_add_f32_e32 v50, v50, v51
	ds_bpermute_b32 v51, v0, v50
	s_and_saveexec_b64 s[16:17], vcc
	s_cbranch_execz .LBB0_115
	s_waitcnt lgkmcnt(0)
	v_add_f32_e32 v50, v50, v51
	ds_write_b32 v114, v50 offset:2048
.LBB0_115:
	s_or_b64 exec, exec, s[16:17]
	s_waitcnt vmcnt(7)
	v_lshlrev_b32_e32 v50, 16, v86
	s_waitcnt lgkmcnt(0)
	v_and_b32_e32 v51, 0xffff0000, v86
	v_pk_add_f32 v[46:47], v[46:47], v[50:51]
	v_lshlrev_b32_e32 v50, 16, v87
	v_and_b32_e32 v51, 0xffff0000, v87
	v_pk_add_f32 v[48:49], v[48:49], v[50:51]
	v_lshlrev_b32_e32 v50, 16, v88
	v_and_b32_e32 v51, 0xffff0000, v88
	v_pk_add_f32 v[50:51], v[42:43], v[50:51]
	v_lshlrev_b32_e32 v42, 16, v89
	v_and_b32_e32 v43, 0xffff0000, v89
	v_pk_add_f32 v[52:53], v[44:45], v[42:43]
	v_lshl_add_u64 v[54:55], s[14:15], 0, v[94:95]
	v_cvt_pk_bf16_f32 v42, v46, v47
	v_cvt_pk_bf16_f32 v43, v48, v49
	v_cvt_pk_bf16_f32 v44, v50, v51
	v_cvt_pk_bf16_f32 v45, v52, v53
	v_lshl_add_u64 v[54:55], v[158:159], 1, v[54:55]
	global_store_dwordx4 v[54:55], v[42:45], off sc0 sc1
	s_nop 1
	v_pk_mul_f32 v[42:43], v[46:47], v[46:47]
	v_pk_mul_f32 v[46:47], v[50:51], v[50:51]
	s_waitcnt vmcnt(7)
	v_lshlrev_b32_e32 v50, 16, v82
	v_and_b32_e32 v51, 0xffff0000, v82
	v_pk_add_f32 v[38:39], v[38:39], v[50:51]
	v_lshlrev_b32_e32 v50, 16, v83
	v_and_b32_e32 v51, 0xffff0000, v83
	v_pk_add_f32 v[40:41], v[40:41], v[50:51]
	v_lshlrev_b32_e32 v50, 16, v84
	v_and_b32_e32 v51, 0xffff0000, v84
	v_pk_add_f32 v[50:51], v[34:35], v[50:51]
	v_lshlrev_b32_e32 v34, 16, v85
	v_and_b32_e32 v35, 0xffff0000, v85
	v_pk_mul_f32 v[44:45], v[48:49], v[48:49]
	v_pk_mul_f32 v[48:49], v[52:53], v[52:53]
	v_pk_add_f32 v[52:53], v[36:37], v[34:35]
	v_cvt_pk_bf16_f32 v34, v38, v39
	v_cvt_pk_bf16_f32 v35, v40, v41
	v_cvt_pk_bf16_f32 v36, v50, v51
	v_cvt_pk_bf16_f32 v37, v52, v53
	global_store_dwordx4 v[54:55], v[34:37], off offset:256 sc0 sc1
	s_nop 1
	v_pk_mul_f32 v[34:35], v[38:39], v[38:39]
	v_pk_mul_f32 v[36:37], v[40:41], v[40:41]
	v_add_f32_e32 v34, v34, v35
	v_add_f32_e32 v36, v36, v37
	v_pk_mul_f32 v[38:39], v[50:51], v[50:51]
	v_pk_mul_f32 v[40:41], v[52:53], v[52:53]
	v_add_f32_e32 v34, v34, v36
	v_add_f32_e32 v35, v48, v49
	v_add_f32_e32 v36, v46, v47
	v_add_f32_e32 v40, v40, v41
	v_add_f32_e32 v38, v38, v39
	v_add_f32_e32 v35, v36, v35
	v_add_f32_e32 v36, v44, v45
	v_add_f32_e32 v37, v42, v43
	v_add_f32_e32 v38, v38, v40
	v_add_f32_e32 v36, v37, v36
	v_add_f32_e32 v34, v34, v38
	v_add_f32_e32 v35, v36, v35
	v_add_f32_e32 v34, v35, v34
	ds_bpermute_b32 v35, v171, v34
	s_waitcnt lgkmcnt(0)
	v_add_f32_e32 v34, v34, v35
	ds_bpermute_b32 v35, v0, v34
	s_and_saveexec_b64 s[16:17], vcc
	s_cbranch_execz .LBB0_117
	s_waitcnt lgkmcnt(0)
	v_add_f32_e32 v34, v34, v35
	ds_write_b32 v114, v34 offset:2304
.LBB0_117:
	s_or_b64 exec, exec, s[16:17]
	s_waitcnt vmcnt(7)
	v_lshlrev_b32_e32 v34, 16, v78
	s_waitcnt lgkmcnt(0)
	v_and_b32_e32 v35, 0xffff0000, v78
	v_pk_add_f32 v[30:31], v[30:31], v[34:35]
	v_lshlrev_b32_e32 v34, 16, v79
	v_and_b32_e32 v35, 0xffff0000, v79
	v_pk_add_f32 v[32:33], v[32:33], v[34:35]
	v_lshlrev_b32_e32 v34, 16, v80
	v_and_b32_e32 v35, 0xffff0000, v80
	v_pk_add_f32 v[34:35], v[26:27], v[34:35]
	v_lshlrev_b32_e32 v26, 16, v81
	v_and_b32_e32 v27, 0xffff0000, v81
	v_pk_add_f32 v[36:37], v[28:29], v[26:27]
	v_lshl_add_u64 v[38:39], s[14:15], 0, v[92:93]
	v_cvt_pk_bf16_f32 v26, v30, v31
	v_cvt_pk_bf16_f32 v27, v32, v33
	v_cvt_pk_bf16_f32 v28, v34, v35
	v_cvt_pk_bf16_f32 v29, v36, v37
	v_lshl_add_u64 v[38:39], v[158:159], 1, v[38:39]
	global_store_dwordx4 v[38:39], v[26:29], off sc0 sc1
	s_nop 1
	v_pk_mul_f32 v[26:27], v[30:31], v[30:31]
	v_pk_mul_f32 v[30:31], v[34:35], v[34:35]
	s_waitcnt vmcnt(7)
	v_lshlrev_b32_e32 v34, 16, v74
	v_and_b32_e32 v35, 0xffff0000, v74
	v_pk_add_f32 v[22:23], v[22:23], v[34:35]
	v_lshlrev_b32_e32 v34, 16, v75
	v_and_b32_e32 v35, 0xffff0000, v75
	v_pk_add_f32 v[24:25], v[24:25], v[34:35]
	v_lshlrev_b32_e32 v34, 16, v76
	v_and_b32_e32 v35, 0xffff0000, v76
	v_pk_add_f32 v[34:35], v[18:19], v[34:35]
	v_lshlrev_b32_e32 v18, 16, v77
	v_and_b32_e32 v19, 0xffff0000, v77
	v_pk_mul_f32 v[28:29], v[32:33], v[32:33]
	v_pk_mul_f32 v[32:33], v[36:37], v[36:37]
	v_pk_add_f32 v[36:37], v[20:21], v[18:19]
	v_cvt_pk_bf16_f32 v18, v22, v23
	v_cvt_pk_bf16_f32 v19, v24, v25
	v_cvt_pk_bf16_f32 v20, v34, v35
	v_cvt_pk_bf16_f32 v21, v36, v37
	global_store_dwordx4 v[38:39], v[18:21], off offset:256 sc0 sc1
	s_nop 1
	v_pk_mul_f32 v[18:19], v[22:23], v[22:23]
	v_pk_mul_f32 v[20:21], v[24:25], v[24:25]
	v_add_f32_e32 v18, v18, v19
	v_add_f32_e32 v20, v20, v21
	v_pk_mul_f32 v[22:23], v[34:35], v[34:35]
	v_pk_mul_f32 v[24:25], v[36:37], v[36:37]
	v_add_f32_e32 v18, v18, v20
	v_add_f32_e32 v19, v32, v33
	v_add_f32_e32 v20, v30, v31
	v_add_f32_e32 v24, v24, v25
	v_add_f32_e32 v22, v22, v23
	v_add_f32_e32 v19, v20, v19
	v_add_f32_e32 v20, v28, v29
	v_add_f32_e32 v21, v26, v27
	v_add_f32_e32 v22, v22, v24
	v_add_f32_e32 v20, v21, v20
	v_add_f32_e32 v18, v18, v22
	v_add_f32_e32 v19, v20, v19
	v_add_f32_e32 v18, v19, v18
	ds_bpermute_b32 v19, v171, v18
	s_waitcnt lgkmcnt(0)
	v_add_f32_e32 v18, v18, v19
	ds_bpermute_b32 v19, v0, v18
	s_and_saveexec_b64 s[16:17], vcc
	s_cbranch_execz .LBB0_119
	s_waitcnt lgkmcnt(0)
	v_add_f32_e32 v18, v18, v19
	ds_write_b32 v114, v18 offset:2560
.LBB0_119:
	s_or_b64 exec, exec, s[16:17]
	s_waitcnt vmcnt(7)
	v_lshlrev_b32_e32 v18, 16, v70
	s_waitcnt lgkmcnt(0)
	v_and_b32_e32 v19, 0xffff0000, v70
	v_pk_add_f32 v[14:15], v[14:15], v[18:19]
	v_lshlrev_b32_e32 v18, 16, v71
	v_and_b32_e32 v19, 0xffff0000, v71
	v_pk_add_f32 v[16:17], v[16:17], v[18:19]
	v_lshlrev_b32_e32 v18, 16, v72
	v_and_b32_e32 v19, 0xffff0000, v72
	v_pk_add_f32 v[18:19], v[10:11], v[18:19]
	v_lshlrev_b32_e32 v10, 16, v73
	v_and_b32_e32 v11, 0xffff0000, v73
	v_pk_add_f32 v[20:21], v[12:13], v[10:11]
	v_lshl_add_u64 v[22:23], s[14:15], 0, v[90:91]
	v_cvt_pk_bf16_f32 v10, v14, v15
	v_cvt_pk_bf16_f32 v11, v16, v17
	v_cvt_pk_bf16_f32 v12, v18, v19
	v_cvt_pk_bf16_f32 v13, v20, v21
	v_lshl_add_u64 v[22:23], v[158:159], 1, v[22:23]
	global_store_dwordx4 v[22:23], v[10:13], off sc0 sc1
	s_nop 1
	v_pk_mul_f32 v[10:11], v[14:15], v[14:15]
	v_pk_mul_f32 v[14:15], v[18:19], v[18:19]
	s_waitcnt vmcnt(7)
	v_lshlrev_b32_e32 v18, 16, v66
	v_and_b32_e32 v19, 0xffff0000, v66
	v_pk_add_f32 v[6:7], v[6:7], v[18:19]
	v_lshlrev_b32_e32 v18, 16, v67
	v_and_b32_e32 v19, 0xffff0000, v67
	v_pk_add_f32 v[8:9], v[8:9], v[18:19]
	v_lshlrev_b32_e32 v18, 16, v68
	v_and_b32_e32 v19, 0xffff0000, v68
	v_pk_add_f32 v[18:19], v[2:3], v[18:19]
	v_lshlrev_b32_e32 v2, 16, v69
	v_and_b32_e32 v3, 0xffff0000, v69
	v_pk_mul_f32 v[12:13], v[16:17], v[16:17]
	v_pk_mul_f32 v[16:17], v[20:21], v[20:21]
	v_pk_add_f32 v[20:21], v[4:5], v[2:3]
	v_cvt_pk_bf16_f32 v2, v6, v7
	v_cvt_pk_bf16_f32 v3, v8, v9
	v_cvt_pk_bf16_f32 v4, v18, v19
	v_cvt_pk_bf16_f32 v5, v20, v21
	global_store_dwordx4 v[22:23], v[2:5], off offset:256 sc0 sc1
	s_nop 1
	v_pk_mul_f32 v[2:3], v[6:7], v[6:7]
	v_pk_mul_f32 v[4:5], v[8:9], v[8:9]
	v_add_f32_e32 v2, v2, v3
	v_add_f32_e32 v4, v4, v5
	v_pk_mul_f32 v[6:7], v[18:19], v[18:19]
	v_pk_mul_f32 v[8:9], v[20:21], v[20:21]
	v_add_f32_e32 v2, v2, v4
	v_add_f32_e32 v3, v16, v17
	v_add_f32_e32 v4, v14, v15
	v_add_f32_e32 v8, v8, v9
	v_add_f32_e32 v6, v6, v7
	v_add_f32_e32 v3, v4, v3
	v_add_f32_e32 v4, v12, v13
	v_add_f32_e32 v5, v10, v11
	v_add_f32_e32 v6, v6, v8
	v_add_f32_e32 v4, v5, v4
	v_add_f32_e32 v2, v2, v6
	v_add_f32_e32 v3, v4, v3
	v_add_f32_e32 v2, v3, v2
	ds_bpermute_b32 v3, v171, v2
	s_waitcnt lgkmcnt(0)
	v_add_f32_e32 v2, v2, v3
	ds_bpermute_b32 v0, v0, v2
	s_and_saveexec_b64 s[14:15], vcc
	s_cbranch_execz .LBB0_121
	s_waitcnt lgkmcnt(0)
	v_add_f32_e32 v0, v2, v0
	ds_write_b32 v114, v0 offset:2816

.LBB0_155:
	v_readlane_b32 s38, v253, 32
	s_andn2_b64 vcc, exec, s[48:49]
	s_lshl_b32 s52, s38, 14
	v_readlane_b32 s39, v253, 33
	s_cbranch_vccnz .LBB0_159
	s_and_b64 vcc, exec, s[36:37]
	s_cbranch_vccnz .LBB0_158
	v_lshrrev_b32_e32 v0, 3, v198
	v_and_b32_e32 v67, 7, v235
	v_lshlrev_b32_e32 v98, 4, v67
	v_mul_u32_u24_e32 v69, 0x84, v0
	v_add3_u32 v69, s52, v98, v69
	s_waitcnt vmcnt(7)
	v_pk_mul_f32 v[30:31], v[30:31], v[66:67] op_sel_hi:[1,0]
	ds_write2_b32 v69, v30, v31 offset1:1
	v_pk_mul_f32 v[30:31], v[32:33], v[66:67] op_sel_hi:[1,0]
	ds_write2_b32 v69, v30, v31 offset0:2 offset1:3
	v_add_u32_e32 v32, 0x420, v69
	s_waitcnt vmcnt(6)
	v_pk_mul_f32 v[30:31], v[38:39], v[68:69] op_sel_hi:[1,0]
	ds_write2_b32 v32, v30, v31 offset1:1
	v_add_u32_e32 v32, 0x428, v69
	v_pk_mul_f32 v[30:31], v[40:41], v[68:69] op_sel_hi:[1,0]
	ds_write2_b32 v32, v30, v31 offset1:1
	v_add_u32_e32 v32, 0x840, v69
	s_waitcnt vmcnt(5)
	v_pk_mul_f32 v[30:31], v[34:35], v[74:75] op_sel_hi:[1,0]
	ds_write2_b32 v32, v30, v31 offset1:1
	v_add_u32_e32 v32, 0x848, v69
	v_pk_mul_f32 v[30:31], v[36:37], v[74:75] op_sel_hi:[1,0]
	ds_write2_b32 v32, v30, v31 offset1:1
	v_add_u32_e32 v32, 0xc60, v69
	s_waitcnt vmcnt(4)
	v_pk_mul_f32 v[30:31], v[46:47], v[76:77] op_sel_hi:[1,0]
	ds_write2_b32 v32, v30, v31 offset1:1
	v_add_u32_e32 v32, 0xc68, v69
	v_pk_mul_f32 v[30:31], v[48:49], v[76:77] op_sel_hi:[1,0]
	ds_write2_b32 v32, v30, v31 offset1:1
	v_add_u32_e32 v32, 0x1080, v69
	s_waitcnt vmcnt(3)
	v_pk_mul_f32 v[30:31], v[42:43], v[82:83] op_sel_hi:[1,0]
	ds_write2_b32 v32, v30, v31 offset1:1
	v_add_u32_e32 v32, 0x1088, v69
	v_pk_mul_f32 v[30:31], v[44:45], v[82:83] op_sel_hi:[1,0]
	ds_write2_b32 v32, v30, v31 offset1:1
	v_add_u32_e32 v32, 0x14a0, v69
	s_waitcnt vmcnt(2)
	v_pk_mul_f32 v[30:31], v[54:55], v[84:85] op_sel_hi:[1,0]
	ds_write2_b32 v32, v30, v31 offset1:1
	v_add_u32_e32 v32, 0x14a8, v69
	v_pk_mul_f32 v[30:31], v[56:57], v[84:85] op_sel_hi:[1,0]
	ds_write2_b32 v32, v30, v31 offset1:1
	v_add_u32_e32 v32, 0x18c0, v69
	s_waitcnt vmcnt(1)
	v_pk_mul_f32 v[30:31], v[50:51], v[90:91] op_sel_hi:[1,0]
	ds_write2_b32 v32, v30, v31 offset1:1
	v_add_u32_e32 v32, 0x18c8, v69
	v_pk_mul_f32 v[30:31], v[52:53], v[90:91] op_sel_hi:[1,0]
	ds_write2_b32 v32, v30, v31 offset1:1
	v_add_u32_e32 v32, 0x1ce0, v69
	s_waitcnt vmcnt(0)
	v_pk_mul_f32 v[30:31], v[58:59], v[92:93] op_sel_hi:[1,0]
	ds_write2_b32 v32, v30, v31 offset1:1
	v_add_u32_e32 v32, 0x1ce8, v69
	v_pk_mul_f32 v[30:31], v[60:61], v[92:93] op_sel_hi:[1,0]
	ds_write2_b32 v32, v30, v31 offset1:1
	s_waitcnt lgkmcnt(0)
	v_mul_u32_u24_e32 v30, 0x420, v67
	v_lshlrev_b32_e32 v31, 2, v0
	v_add3_u32 v52, s52, v30, v31
	ds_read2_b32 v[34:35], v52 offset0:33 offset1:41
	ds_read2_b32 v[36:37], v52 offset1:8
	ds_read2_b32 v[38:39], v52 offset0:66 offset1:74
	ds_read2_b32 v[40:41], v52 offset0:99 offset1:107
	ds_read2_b32 v[42:43], v52 offset0:132 offset1:140
	ds_read2_b32 v[44:45], v52 offset0:165 offset1:173
	ds_read2_b32 v[46:47], v52 offset0:198 offset1:206
	ds_read2_b32 v[48:49], v52 offset0:231 offset1:239
	v_lshlrev_b32_e32 v0, 11, v0
	v_lshl_add_u64 v[50:51], s[16:17], 0, v[0:1]
	v_mov_b32_e32 v99, v1
	s_waitcnt lgkmcnt(6)
	v_cvt_pk_bf16_f32 v30, v36, v34
	s_waitcnt lgkmcnt(4)
	v_cvt_pk_bf16_f32 v31, v38, v40
	s_waitcnt lgkmcnt(2)
	v_cvt_pk_bf16_f32 v32, v42, v44
	s_waitcnt lgkmcnt(0)
	v_cvt_pk_bf16_f32 v33, v46, v48
	v_lshl_add_u64 v[50:51], v[50:51], 0, v[98:99]
	global_store_dwordx4 v[50:51], v[30:33], off sc0 sc1
	v_or_b32_e32 v34, 0x4000, v0
	s_nop 0
	v_cvt_pk_bf16_f32 v30, v37, v35
	v_cvt_pk_bf16_f32 v31, v39, v41
	v_cvt_pk_bf16_f32 v32, v43, v45
	v_cvt_pk_bf16_f32 v33, v47, v49
	v_mov_b32_e32 v35, v1
	ds_read2_b32 v[36:37], v52 offset0:49 offset1:57
	ds_read2_b32 v[38:39], v52 offset0:16 offset1:24
	ds_read2_b32 v[40:41], v52 offset0:82 offset1:90
	ds_read2_b32 v[42:43], v52 offset0:115 offset1:123
	ds_read2_b32 v[44:45], v52 offset0:148 offset1:156
	ds_read2_b32 v[46:47], v52 offset0:181 offset1:189
	ds_read2_b32 v[48:49], v52 offset0:214 offset1:222
	ds_read2_b32 v[50:51], v52 offset0:247 offset1:255
	v_lshl_add_u64 v[34:35], s[16:17], 0, v[34:35]
	v_lshl_add_u64 v[34:35], v[34:35], 0, v[98:99]
	global_store_dwordx4 v[34:35], v[30:33], off sc0 sc1
	v_or_b32_e32 v34, 0x8000, v0
	v_mov_b32_e32 v35, v1
	v_lshl_add_u64 v[34:35], s[16:17], 0, v[34:35]
	s_waitcnt lgkmcnt(6)
	v_cvt_pk_bf16_f32 v30, v38, v36
	s_waitcnt lgkmcnt(4)
	v_cvt_pk_bf16_f32 v31, v40, v42
	s_waitcnt lgkmcnt(2)
	v_cvt_pk_bf16_f32 v32, v44, v46
	s_waitcnt lgkmcnt(0)
	v_cvt_pk_bf16_f32 v33, v48, v50
	v_lshl_add_u64 v[34:35], v[34:35], 0, v[98:99]
	v_or_b32_e32 v0, 0xc000, v0
	global_store_dwordx4 v[34:35], v[30:33], off sc0 sc1
	v_lshl_add_u64 v[34:35], s[16:17], 0, v[0:1]
	v_lshl_add_u64 v[34:35], v[34:35], 0, v[98:99]
	v_cvt_pk_bf16_f32 v30, v39, v37
	v_cvt_pk_bf16_f32 v31, v41, v43
	v_cvt_pk_bf16_f32 v32, v45, v47
	v_cvt_pk_bf16_f32 v33, v49, v51
	global_store_dwordx4 v[34:35], v[30:33], off sc0 sc1
	s_waitcnt lgkmcnt(0)

.LBB0_174:
	s_andn2_b64 vcc, exec, s[38:39]
	s_cbranch_vccnz .LBB0_178
	s_cmp_eq_u32 s31, 0
	s_cbranch_scc1 .LBB0_177
	v_lshrrev_b32_e32 v0, 3, v198
	s_waitcnt vmcnt(7)
	v_and_b32_e32 v31, 7, v235
	v_lshlrev_b32_e32 v30, 4, v31
	v_mul_u32_u24_e32 v32, 0x84, v0
	v_add3_u32 v32, s52, v30, v32
	v_pk_mul_f32 v[2:3], v[2:3], v[70:71] op_sel_hi:[1,0]
	ds_write2_b32 v32, v2, v3 offset1:1
	v_pk_mul_f32 v[2:3], v[4:5], v[70:71] op_sel_hi:[1,0]
	ds_write2_b32 v32, v2, v3 offset0:2 offset1:3
	v_add_u32_e32 v4, 0x420, v32
	s_waitcnt vmcnt(6)
	v_pk_mul_f32 v[2:3], v[10:11], v[72:73] op_sel_hi:[1,0]
	ds_write2_b32 v4, v2, v3 offset1:1
	v_add_u32_e32 v4, 0x428, v32
	v_pk_mul_f32 v[2:3], v[12:13], v[72:73] op_sel_hi:[1,0]
	ds_write2_b32 v4, v2, v3 offset1:1
	v_add_u32_e32 v4, 0x840, v32
	s_waitcnt vmcnt(5)
	v_pk_mul_f32 v[2:3], v[6:7], v[78:79] op_sel_hi:[1,0]
	ds_write2_b32 v4, v2, v3 offset1:1
	v_add_u32_e32 v4, 0x848, v32
	v_pk_mul_f32 v[2:3], v[8:9], v[78:79] op_sel_hi:[1,0]
	ds_write2_b32 v4, v2, v3 offset1:1
	v_add_u32_e32 v4, 0xc60, v32
	s_waitcnt vmcnt(4)
	v_pk_mul_f32 v[2:3], v[18:19], v[80:81] op_sel_hi:[1,0]
	ds_write2_b32 v4, v2, v3 offset1:1
	v_add_u32_e32 v4, 0xc68, v32
	v_pk_mul_f32 v[2:3], v[20:21], v[80:81] op_sel_hi:[1,0]
	ds_write2_b32 v4, v2, v3 offset1:1
	v_add_u32_e32 v4, 0x1080, v32
	s_waitcnt vmcnt(3)
	v_pk_mul_f32 v[2:3], v[14:15], v[86:87] op_sel_hi:[1,0]
	ds_write2_b32 v4, v2, v3 offset1:1
	v_add_u32_e32 v4, 0x1088, v32
	v_pk_mul_f32 v[2:3], v[16:17], v[86:87] op_sel_hi:[1,0]
	ds_write2_b32 v4, v2, v3 offset1:1
	v_add_u32_e32 v4, 0x14a0, v32
	s_waitcnt vmcnt(2)
	v_pk_mul_f32 v[2:3], v[26:27], v[88:89] op_sel_hi:[1,0]
	ds_write2_b32 v4, v2, v3 offset1:1
	v_add_u32_e32 v4, 0x14a8, v32
	v_pk_mul_f32 v[2:3], v[28:29], v[88:89] op_sel_hi:[1,0]
	ds_write2_b32 v4, v2, v3 offset1:1
	v_add_u32_e32 v4, 0x18c0, v32
	s_waitcnt vmcnt(1)
	v_pk_mul_f32 v[2:3], v[22:23], v[94:95] op_sel_hi:[1,0]
	ds_write2_b32 v4, v2, v3 offset1:1
	v_add_u32_e32 v4, 0x18c8, v32
	v_pk_mul_f32 v[2:3], v[24:25], v[94:95] op_sel_hi:[1,0]
	ds_write2_b32 v4, v2, v3 offset1:1
	v_add_u32_e32 v4, 0x1ce0, v32
	s_waitcnt vmcnt(0)
	v_pk_mul_f32 v[2:3], v[62:63], v[96:97] op_sel_hi:[1,0]
	ds_write2_b32 v4, v2, v3 offset1:1
	v_add_u32_e32 v4, 0x1ce8, v32
	v_pk_mul_f32 v[2:3], v[64:65], v[96:97] op_sel_hi:[1,0]
	ds_write2_b32 v4, v2, v3 offset1:1
	s_waitcnt lgkmcnt(0)
	v_mul_u32_u24_e32 v2, 0x420, v31
	v_lshlrev_b32_e32 v3, 2, v0
	v_add3_u32 v24, s52, v2, v3
	ds_read2_b32 v[6:7], v24 offset0:33 offset1:41
	ds_read2_b32 v[8:9], v24 offset1:8
	ds_read2_b32 v[10:11], v24 offset0:66 offset1:74
	ds_read2_b32 v[12:13], v24 offset0:99 offset1:107
	ds_read2_b32 v[14:15], v24 offset0:132 offset1:140
	ds_read2_b32 v[16:17], v24 offset0:165 offset1:173
	ds_read2_b32 v[18:19], v24 offset0:198 offset1:206
	ds_read2_b32 v[20:21], v24 offset0:231 offset1:239
	v_lshlrev_b32_e32 v0, 11, v0
	v_lshl_add_u64 v[22:23], s[14:15], 0, v[0:1]
	v_mov_b32_e32 v31, v1
	s_waitcnt lgkmcnt(6)
	v_cvt_pk_bf16_f32 v2, v8, v6
	s_waitcnt lgkmcnt(4)
	v_cvt_pk_bf16_f32 v3, v10, v12
	s_waitcnt lgkmcnt(2)
	v_cvt_pk_bf16_f32 v4, v14, v16
	s_waitcnt lgkmcnt(0)
	v_cvt_pk_bf16_f32 v5, v18, v20
	v_lshl_add_u64 v[22:23], v[22:23], 0, v[30:31]
	global_store_dwordx4 v[22:23], v[2:5], off sc0 sc1
	v_or_b32_e32 v6, 0x4000, v0
	s_nop 0
	v_cvt_pk_bf16_f32 v2, v9, v7
	v_cvt_pk_bf16_f32 v3, v11, v13
	v_cvt_pk_bf16_f32 v4, v15, v17
	v_cvt_pk_bf16_f32 v5, v19, v21
	v_mov_b32_e32 v7, v1
	ds_read2_b32 v[8:9], v24 offset0:49 offset1:57
	ds_read2_b32 v[10:11], v24 offset0:16 offset1:24
	ds_read2_b32 v[12:13], v24 offset0:82 offset1:90
	ds_read2_b32 v[14:15], v24 offset0:115 offset1:123
	ds_read2_b32 v[16:17], v24 offset0:148 offset1:156
	ds_read2_b32 v[18:19], v24 offset0:181 offset1:189
	ds_read2_b32 v[20:21], v24 offset0:214 offset1:222
	ds_read2_b32 v[22:23], v24 offset0:247 offset1:255
	v_lshl_add_u64 v[6:7], s[14:15], 0, v[6:7]
	v_lshl_add_u64 v[6:7], v[6:7], 0, v[30:31]
	global_store_dwordx4 v[6:7], v[2:5], off sc0 sc1
	v_or_b32_e32 v6, 0x8000, v0
	v_mov_b32_e32 v7, v1
	v_lshl_add_u64 v[6:7], s[14:15], 0, v[6:7]
	s_waitcnt lgkmcnt(6)
	v_cvt_pk_bf16_f32 v2, v10, v8
	s_waitcnt lgkmcnt(4)
	v_cvt_pk_bf16_f32 v3, v12, v14
	s_waitcnt lgkmcnt(2)
	v_cvt_pk_bf16_f32 v4, v16, v18
	s_waitcnt lgkmcnt(0)
	v_cvt_pk_bf16_f32 v5, v20, v22
	v_lshl_add_u64 v[6:7], v[6:7], 0, v[30:31]
	v_or_b32_e32 v0, 0xc000, v0
	global_store_dwordx4 v[6:7], v[2:5], off sc0 sc1
	v_lshl_add_u64 v[6:7], s[14:15], 0, v[0:1]
	v_lshl_add_u64 v[6:7], v[6:7], 0, v[30:31]
	v_cvt_pk_bf16_f32 v2, v11, v9
	v_cvt_pk_bf16_f32 v3, v13, v15
	v_cvt_pk_bf16_f32 v4, v17, v19
	v_cvt_pk_bf16_f32 v5, v21, v23
	global_store_dwordx4 v[6:7], v[2:5], off sc0 sc1
	s_waitcnt lgkmcnt(0)

.LBB0_193:
	s_andn2_b64 vcc, exec, s[38:39]
	s_cbranch_vccnz .LBB0_197
	s_cmp_eq_u32 s31, 0
	s_cbranch_scc1 .LBB0_196
	v_lshrrev_b32_e32 v0, 3, v198
	s_waitcnt vmcnt(0)
	v_and_b32_e32 v63, 7, v235
	v_lshlrev_b32_e32 v62, 4, v63
	v_mul_u32_u24_e32 v64, 0x84, v0
	v_add3_u32 v64, s52, v62, v64
	v_pk_mul_f32 v[34:35], v[34:35], v[74:75] op_sel_hi:[1,0]
	ds_write2_b32 v64, v34, v35 offset1:1
	v_pk_mul_f32 v[34:35], v[36:37], v[74:75] op_sel_hi:[1,0]
	ds_write2_b32 v64, v34, v35 offset0:2 offset1:3
	v_add_u32_e32 v36, 0x420, v64
	v_pk_mul_f32 v[34:35], v[42:43], v[76:77] op_sel_hi:[1,0]
	ds_write2_b32 v36, v34, v35 offset1:1
	v_add_u32_e32 v36, 0x428, v64
	v_pk_mul_f32 v[34:35], v[44:45], v[76:77] op_sel_hi:[1,0]
	ds_write2_b32 v36, v34, v35 offset1:1
	v_add_u32_e32 v36, 0x840, v64
	v_pk_mul_f32 v[34:35], v[38:39], v[82:83] op_sel_hi:[1,0]
	ds_write2_b32 v36, v34, v35 offset1:1
	v_add_u32_e32 v36, 0x848, v64
	v_pk_mul_f32 v[34:35], v[40:41], v[82:83] op_sel_hi:[1,0]
	ds_write2_b32 v36, v34, v35 offset1:1
	v_add_u32_e32 v36, 0xc60, v64
	v_pk_mul_f32 v[34:35], v[50:51], v[84:85] op_sel_hi:[1,0]
	ds_write2_b32 v36, v34, v35 offset1:1
	v_add_u32_e32 v36, 0xc68, v64
	v_pk_mul_f32 v[34:35], v[52:53], v[84:85] op_sel_hi:[1,0]
	ds_write2_b32 v36, v34, v35 offset1:1
	v_add_u32_e32 v36, 0x1080, v64
	v_pk_mul_f32 v[34:35], v[46:47], v[90:91] op_sel_hi:[1,0]
	ds_write2_b32 v36, v34, v35 offset1:1
	v_add_u32_e32 v36, 0x1088, v64
	v_pk_mul_f32 v[34:35], v[48:49], v[90:91] op_sel_hi:[1,0]
	ds_write2_b32 v36, v34, v35 offset1:1
	v_add_u32_e32 v36, 0x14a0, v64
	v_pk_mul_f32 v[34:35], v[58:59], v[92:93] op_sel_hi:[1,0]
	ds_write2_b32 v36, v34, v35 offset1:1
	v_add_u32_e32 v36, 0x14a8, v64
	v_pk_mul_f32 v[34:35], v[60:61], v[92:93] op_sel_hi:[1,0]
	ds_write2_b32 v36, v34, v35 offset1:1
	v_add_u32_e32 v36, 0x18c0, v64
	v_pk_mul_f32 v[34:35], v[54:55], v[98:99] op_sel_hi:[1,0]
	ds_write2_b32 v36, v34, v35 offset1:1
	v_add_u32_e32 v36, 0x18c8, v64
	v_pk_mul_f32 v[34:35], v[56:57], v[98:99] op_sel_hi:[1,0]
	ds_write2_b32 v36, v34, v35 offset1:1
	v_add_u32_e32 v36, 0x1ce0, v64
	v_pk_mul_f32 v[34:35], v[66:67], v[100:101] op_sel_hi:[1,0]
	ds_write2_b32 v36, v34, v35 offset1:1
	v_add_u32_e32 v36, 0x1ce8, v64
	v_pk_mul_f32 v[34:35], v[68:69], v[100:101] op_sel_hi:[1,0]
	ds_write2_b32 v36, v34, v35 offset1:1
	s_waitcnt lgkmcnt(0)
	v_mul_u32_u24_e32 v34, 0x420, v63
	v_lshlrev_b32_e32 v35, 2, v0
	v_add3_u32 v56, s52, v34, v35
	ds_read2_b32 v[38:39], v56 offset0:33 offset1:41
	ds_read2_b32 v[40:41], v56 offset1:8
	ds_read2_b32 v[42:43], v56 offset0:66 offset1:74
	ds_read2_b32 v[44:45], v56 offset0:99 offset1:107
	ds_read2_b32 v[46:47], v56 offset0:132 offset1:140
	ds_read2_b32 v[48:49], v56 offset0:165 offset1:173
	ds_read2_b32 v[50:51], v56 offset0:198 offset1:206
	ds_read2_b32 v[52:53], v56 offset0:231 offset1:239
	v_lshlrev_b32_e32 v0, 11, v0
	v_lshl_add_u64 v[54:55], s[16:17], 0, v[0:1]
	v_mov_b32_e32 v63, v1
	s_waitcnt lgkmcnt(6)
	v_cvt_pk_bf16_f32 v34, v40, v38
	s_waitcnt lgkmcnt(4)
	v_cvt_pk_bf16_f32 v35, v42, v44
	s_waitcnt lgkmcnt(2)
	v_cvt_pk_bf16_f32 v36, v46, v48
	s_waitcnt lgkmcnt(0)
	v_cvt_pk_bf16_f32 v37, v50, v52
	v_lshl_add_u64 v[54:55], v[54:55], 0, v[62:63]
	global_store_dwordx4 v[54:55], v[34:37], off sc0 sc1
	v_or_b32_e32 v38, 0x4000, v0
	s_nop 0
	v_cvt_pk_bf16_f32 v34, v41, v39
	v_cvt_pk_bf16_f32 v35, v43, v45
	v_cvt_pk_bf16_f32 v36, v47, v49
	v_cvt_pk_bf16_f32 v37, v51, v53
	v_mov_b32_e32 v39, v1
	ds_read2_b32 v[40:41], v56 offset0:49 offset1:57
	ds_read2_b32 v[42:43], v56 offset0:16 offset1:24
	ds_read2_b32 v[44:45], v56 offset0:82 offset1:90
	ds_read2_b32 v[46:47], v56 offset0:115 offset1:123
	ds_read2_b32 v[48:49], v56 offset0:148 offset1:156
	ds_read2_b32 v[50:51], v56 offset0:181 offset1:189
	ds_read2_b32 v[52:53], v56 offset0:214 offset1:222
	ds_read2_b32 v[54:55], v56 offset0:247 offset1:255
	v_lshl_add_u64 v[38:39], s[16:17], 0, v[38:39]
	v_lshl_add_u64 v[38:39], v[38:39], 0, v[62:63]
	global_store_dwordx4 v[38:39], v[34:37], off sc0 sc1
	v_or_b32_e32 v38, 0x8000, v0
	v_mov_b32_e32 v39, v1
	v_lshl_add_u64 v[38:39], s[16:17], 0, v[38:39]
	s_waitcnt lgkmcnt(6)
	v_cvt_pk_bf16_f32 v34, v42, v40
	s_waitcnt lgkmcnt(4)
	v_cvt_pk_bf16_f32 v35, v44, v46
	s_waitcnt lgkmcnt(2)
	v_cvt_pk_bf16_f32 v36, v48, v50
	s_waitcnt lgkmcnt(0)
	v_cvt_pk_bf16_f32 v37, v52, v54
	v_lshl_add_u64 v[38:39], v[38:39], 0, v[62:63]
	v_or_b32_e32 v0, 0xc000, v0
	global_store_dwordx4 v[38:39], v[34:37], off sc0 sc1
	v_lshl_add_u64 v[38:39], s[16:17], 0, v[0:1]
	v_lshl_add_u64 v[38:39], v[38:39], 0, v[62:63]
	v_cvt_pk_bf16_f32 v34, v43, v41
	v_cvt_pk_bf16_f32 v35, v45, v47
	v_cvt_pk_bf16_f32 v36, v49, v51
	v_cvt_pk_bf16_f32 v37, v53, v55
	global_store_dwordx4 v[38:39], v[34:37], off sc0 sc1
	s_waitcnt lgkmcnt(0)

.LBB0_215:
	s_andn2_b64 vcc, exec, s[50:51]
	s_cbranch_vccnz .LBB0_219
	s_cmp_eq_u32 s31, 0
	s_cbranch_scc1 .LBB0_218
	s_waitcnt vmcnt(6)
	v_pk_mul_f32 v[2:3], v[120:121], v[2:3] op_sel_hi:[0,1]
	ds_write2_b32 v101, v2, v3 offset1:1
	v_pk_mul_f32 v[2:3], v[120:121], v[4:5] op_sel_hi:[0,1]
	ds_write2_b32 v101, v2, v3 offset0:2 offset1:3
	s_waitcnt vmcnt(7)
	v_pk_mul_f32 v[2:3], v[118:119], v[10:11] op_sel_hi:[0,1]
	v_add_u32_e32 v0, 0x420, v101
	ds_write2_b32 v0, v2, v3 offset1:1
	v_pk_mul_f32 v[2:3], v[118:119], v[12:13] op_sel_hi:[0,1]
	v_add_u32_e32 v0, 0x428, v101
	ds_write2_b32 v0, v2, v3 offset1:1
	s_waitcnt vmcnt(6)
	v_pk_mul_f32 v[2:3], v[124:125], v[6:7] op_sel_hi:[0,1]
	v_add_u32_e32 v0, 0x840, v101
	ds_write2_b32 v0, v2, v3 offset1:1
	v_pk_mul_f32 v[2:3], v[124:125], v[8:9] op_sel_hi:[0,1]
	v_add_u32_e32 v0, 0x848, v101
	ds_write2_b32 v0, v2, v3 offset1:1
	s_waitcnt vmcnt(5)
	v_pk_mul_f32 v[2:3], v[122:123], v[22:23] op_sel_hi:[0,1]
	v_add_u32_e32 v0, 0xc60, v101
	ds_write2_b32 v0, v2, v3 offset1:1
	v_pk_mul_f32 v[2:3], v[122:123], v[24:25] op_sel_hi:[0,1]
	v_add_u32_e32 v0, 0xc68, v101
	ds_write2_b32 v0, v2, v3 offset1:1
	s_waitcnt vmcnt(4)
	v_pk_mul_f32 v[2:3], v[128:129], v[14:15] op_sel_hi:[0,1]
	v_add_u32_e32 v0, 0x1080, v101
	ds_write2_b32 v0, v2, v3 offset1:1
	v_pk_mul_f32 v[2:3], v[128:129], v[16:17] op_sel_hi:[0,1]
	v_add_u32_e32 v0, 0x1088, v101
	ds_write2_b32 v0, v2, v3 offset1:1
	s_waitcnt vmcnt(5)
	v_pk_mul_f32 v[2:3], v[126:127], v[26:27] op_sel_hi:[0,1]
	v_add_u32_e32 v0, 0x14a0, v101
	ds_write2_b32 v0, v2, v3 offset1:1
	v_pk_mul_f32 v[2:3], v[126:127], v[28:29] op_sel_hi:[0,1]
	v_add_u32_e32 v0, 0x14a8, v101
	ds_write2_b32 v0, v2, v3 offset1:1
	s_waitcnt vmcnt(4)
	v_pk_mul_f32 v[2:3], v[132:133], v[18:19] op_sel_hi:[0,1]
	v_add_u32_e32 v0, 0x18c0, v101
	ds_write2_b32 v0, v2, v3 offset1:1
	v_pk_mul_f32 v[2:3], v[132:133], v[20:21] op_sel_hi:[0,1]
	v_add_u32_e32 v0, 0x18c8, v101
	ds_write2_b32 v0, v2, v3 offset1:1
	s_waitcnt vmcnt(0)
	v_pk_mul_f32 v[2:3], v[130:131], v[30:31] op_sel_hi:[0,1]
	v_add_u32_e32 v0, 0x1ce0, v101
	ds_write2_b32 v0, v2, v3 offset1:1
	v_pk_mul_f32 v[2:3], v[130:131], v[32:33] op_sel_hi:[0,1]
	v_add_u32_e32 v0, 0x1ce8, v101
	ds_write2_b32 v0, v2, v3 offset1:1
	s_waitcnt lgkmcnt(0)
	ds_read2_b32 v[6:7], v99 offset0:33 offset1:41
	ds_read2_b32 v[8:9], v99 offset1:8
	ds_read2_b32 v[10:11], v99 offset0:66 offset1:74
	ds_read2_b32 v[12:13], v99 offset0:99 offset1:107
	ds_read2_b32 v[14:15], v99 offset0:132 offset1:140
	ds_read2_b32 v[16:17], v99 offset0:165 offset1:173
	ds_read2_b32 v[18:19], v99 offset0:198 offset1:206
	ds_read2_b32 v[20:21], v99 offset0:231 offset1:239
	v_lshl_add_u64 v[22:23], s[14:15], 0, v[116:117]
	v_lshlrev_b32_e32 v0, 1, v106
	s_waitcnt lgkmcnt(6)
	v_cvt_pk_bf16_f32 v2, v8, v6
	s_waitcnt lgkmcnt(4)
	v_cvt_pk_bf16_f32 v3, v10, v12
	s_waitcnt lgkmcnt(2)
	v_cvt_pk_bf16_f32 v4, v14, v16
	s_waitcnt lgkmcnt(0)
	v_cvt_pk_bf16_f32 v5, v18, v20
	v_lshl_add_u64 v[22:23], v[22:23], 0, v[0:1]
	global_store_dwordx4 v[22:23], v[2:5], off sc0 sc1
	s_nop 1
	v_cvt_pk_bf16_f32 v2, v9, v7
	v_cvt_pk_bf16_f32 v3, v11, v13
	v_cvt_pk_bf16_f32 v4, v15, v17
	v_cvt_pk_bf16_f32 v5, v19, v21
	ds_read2_b32 v[8:9], v99 offset0:49 offset1:57
	ds_read2_b32 v[10:11], v99 offset0:16 offset1:24
	ds_read2_b32 v[12:13], v99 offset0:82 offset1:90
	ds_read2_b32 v[14:15], v99 offset0:115 offset1:123
	ds_read2_b32 v[16:17], v99 offset0:148 offset1:156
	ds_read2_b32 v[18:19], v99 offset0:181 offset1:189
	ds_read2_b32 v[20:21], v99 offset0:214 offset1:222
	ds_read2_b32 v[22:23], v99 offset0:247 offset1:255
	v_lshl_add_u64 v[6:7], s[14:15], 0, v[114:115]
	v_lshl_add_u64 v[6:7], v[6:7], 0, v[0:1]
	global_store_dwordx4 v[6:7], v[2:5], off sc0 sc1
	v_lshl_add_u64 v[6:7], s[14:15], 0, v[112:113]
	v_lshl_add_u64 v[6:7], v[6:7], 0, v[0:1]
	s_waitcnt lgkmcnt(6)
	v_cvt_pk_bf16_f32 v2, v10, v8
	s_waitcnt lgkmcnt(4)
	v_cvt_pk_bf16_f32 v3, v12, v14
	s_waitcnt lgkmcnt(2)
	v_cvt_pk_bf16_f32 v4, v16, v18
	s_waitcnt lgkmcnt(0)
	v_cvt_pk_bf16_f32 v5, v20, v22
	global_store_dwordx4 v[6:7], v[2:5], off sc0 sc1
	v_lshl_add_u64 v[6:7], s[14:15], 0, v[110:111]
	v_lshl_add_u64 v[6:7], v[6:7], 0, v[0:1]
	v_cvt_pk_bf16_f32 v2, v11, v9
	v_cvt_pk_bf16_f32 v3, v13, v15
	v_cvt_pk_bf16_f32 v4, v17, v19
	v_cvt_pk_bf16_f32 v5, v21, v23
	global_store_dwordx4 v[6:7], v[2:5], off sc0 sc1
	s_waitcnt lgkmcnt(0)

.LBB0_233:
	s_andn2_b64 vcc, exec, s[50:51]
	s_cbranch_vccnz .LBB0_200
	s_cmp_eq_u32 s31, 0
	s_cbranch_scc1 .LBB0_199
	s_waitcnt vmcnt(6)
	v_pk_mul_f32 v[2:3], v[2:3], v[120:121] op_sel_hi:[1,0]
	ds_write2_b32 v101, v2, v3 offset1:1
	v_pk_mul_f32 v[2:3], v[4:5], v[120:121] op_sel_hi:[1,0]
	ds_write2_b32 v101, v2, v3 offset0:2 offset1:3
	v_pk_mul_f32 v[2:3], v[10:11], v[118:119] op_sel_hi:[1,0]
	v_add_u32_e32 v0, 0x420, v101
	ds_write2_b32 v0, v2, v3 offset1:1
	v_pk_mul_f32 v[2:3], v[12:13], v[118:119] op_sel_hi:[1,0]
	v_add_u32_e32 v0, 0x428, v101
	ds_write2_b32 v0, v2, v3 offset1:1
	v_pk_mul_f32 v[2:3], v[6:7], v[124:125] op_sel_hi:[1,0]
	v_add_u32_e32 v0, 0x840, v101
	ds_write2_b32 v0, v2, v3 offset1:1
	v_pk_mul_f32 v[2:3], v[8:9], v[124:125] op_sel_hi:[1,0]
	v_add_u32_e32 v0, 0x848, v101
	ds_write2_b32 v0, v2, v3 offset1:1
	s_waitcnt vmcnt(5)
	v_pk_mul_f32 v[2:3], v[22:23], v[122:123] op_sel_hi:[1,0]
	v_add_u32_e32 v0, 0xc60, v101
	ds_write2_b32 v0, v2, v3 offset1:1
	v_pk_mul_f32 v[2:3], v[24:25], v[122:123] op_sel_hi:[1,0]
	v_add_u32_e32 v0, 0xc68, v101
	ds_write2_b32 v0, v2, v3 offset1:1
	s_waitcnt vmcnt(4)
	v_pk_mul_f32 v[2:3], v[14:15], v[128:129] op_sel_hi:[1,0]
	v_add_u32_e32 v0, 0x1080, v101
	ds_write2_b32 v0, v2, v3 offset1:1
	v_pk_mul_f32 v[2:3], v[16:17], v[128:129] op_sel_hi:[1,0]
	v_add_u32_e32 v0, 0x1088, v101
	ds_write2_b32 v0, v2, v3 offset1:1
	v_pk_mul_f32 v[2:3], v[26:27], v[126:127] op_sel_hi:[1,0]
	v_add_u32_e32 v0, 0x14a0, v101
	ds_write2_b32 v0, v2, v3 offset1:1
	v_pk_mul_f32 v[2:3], v[28:29], v[126:127] op_sel_hi:[1,0]
	v_add_u32_e32 v0, 0x14a8, v101
	ds_write2_b32 v0, v2, v3 offset1:1
	v_pk_mul_f32 v[2:3], v[18:19], v[132:133] op_sel_hi:[1,0]
	v_add_u32_e32 v0, 0x18c0, v101
	ds_write2_b32 v0, v2, v3 offset1:1
	v_pk_mul_f32 v[2:3], v[20:21], v[132:133] op_sel_hi:[1,0]
	v_add_u32_e32 v0, 0x18c8, v101
	ds_write2_b32 v0, v2, v3 offset1:1
	s_waitcnt vmcnt(0)
	v_pk_mul_f32 v[2:3], v[30:31], v[130:131] op_sel_hi:[1,0]
	v_add_u32_e32 v0, 0x1ce0, v101
	ds_write2_b32 v0, v2, v3 offset1:1
	v_pk_mul_f32 v[2:3], v[32:33], v[130:131] op_sel_hi:[1,0]
	v_add_u32_e32 v0, 0x1ce8, v101
	ds_write2_b32 v0, v2, v3 offset1:1
	s_waitcnt lgkmcnt(0)
	ds_read2_b32 v[6:7], v99 offset0:33 offset1:41
	ds_read2_b32 v[8:9], v99 offset1:8
	ds_read2_b32 v[10:11], v99 offset0:66 offset1:74
	ds_read2_b32 v[12:13], v99 offset0:99 offset1:107
	ds_read2_b32 v[14:15], v99 offset0:132 offset1:140
	ds_read2_b32 v[16:17], v99 offset0:165 offset1:173
	ds_read2_b32 v[18:19], v99 offset0:198 offset1:206
	ds_read2_b32 v[20:21], v99 offset0:231 offset1:239
	v_lshl_add_u64 v[22:23], s[14:15], 0, v[116:117]
	v_lshlrev_b32_e32 v0, 1, v106
	s_waitcnt lgkmcnt(6)
	v_cvt_pk_bf16_f32 v2, v8, v6
	s_waitcnt lgkmcnt(4)
	v_cvt_pk_bf16_f32 v3, v10, v12
	s_waitcnt lgkmcnt(2)
	v_cvt_pk_bf16_f32 v4, v14, v16
	s_waitcnt lgkmcnt(0)
	v_cvt_pk_bf16_f32 v5, v18, v20
	v_lshl_add_u64 v[22:23], v[22:23], 0, v[0:1]
	global_store_dwordx4 v[22:23], v[2:5], off sc0 sc1
	s_nop 1
	v_cvt_pk_bf16_f32 v2, v9, v7
	v_cvt_pk_bf16_f32 v3, v11, v13
	v_cvt_pk_bf16_f32 v4, v15, v17
	v_cvt_pk_bf16_f32 v5, v19, v21
	ds_read2_b32 v[8:9], v99 offset0:49 offset1:57
	ds_read2_b32 v[10:11], v99 offset0:16 offset1:24
	ds_read2_b32 v[12:13], v99 offset0:82 offset1:90
	ds_read2_b32 v[14:15], v99 offset0:115 offset1:123
	ds_read2_b32 v[16:17], v99 offset0:148 offset1:156
	ds_read2_b32 v[18:19], v99 offset0:181 offset1:189
	ds_read2_b32 v[20:21], v99 offset0:214 offset1:222
	ds_read2_b32 v[22:23], v99 offset0:247 offset1:255
	v_lshl_add_u64 v[6:7], s[14:15], 0, v[114:115]
	v_lshl_add_u64 v[6:7], v[6:7], 0, v[0:1]
	global_store_dwordx4 v[6:7], v[2:5], off sc0 sc1
	v_lshl_add_u64 v[6:7], s[14:15], 0, v[112:113]
	v_lshl_add_u64 v[6:7], v[6:7], 0, v[0:1]
	s_waitcnt lgkmcnt(6)
	v_cvt_pk_bf16_f32 v2, v10, v8
	s_waitcnt lgkmcnt(4)
	v_cvt_pk_bf16_f32 v3, v12, v14
	s_waitcnt lgkmcnt(2)
	v_cvt_pk_bf16_f32 v4, v16, v18
	s_waitcnt lgkmcnt(0)
	v_cvt_pk_bf16_f32 v5, v20, v22
	global_store_dwordx4 v[6:7], v[2:5], off sc0 sc1
	v_lshl_add_u64 v[6:7], s[14:15], 0, v[110:111]
	v_lshl_add_u64 v[6:7], v[6:7], 0, v[0:1]
	v_cvt_pk_bf16_f32 v2, v11, v9
	v_cvt_pk_bf16_f32 v3, v13, v15
	v_cvt_pk_bf16_f32 v4, v17, v19
	v_cvt_pk_bf16_f32 v5, v21, v23
	global_store_dwordx4 v[6:7], v[2:5], off sc0 sc1
	s_waitcnt lgkmcnt(0)
	s_branch .LBB0_199

.LBB0_258:
	s_and_b64 vcc, exec, s[38:39]
	s_cbranch_vccz .LBB0_262
	s_cmp_eq_u32 s31, 0
	s_cbranch_scc1 .LBB0_261
	s_waitcnt vmcnt(6)
	v_pk_mul_f32 v[2:3], v[2:3], v[120:121] op_sel_hi:[1,0]
	ds_write2_b32 v101, v2, v3 offset1:1
	v_pk_mul_f32 v[2:3], v[4:5], v[120:121] op_sel_hi:[1,0]
	ds_write2_b32 v101, v2, v3 offset0:2 offset1:3
	v_pk_mul_f32 v[2:3], v[10:11], v[118:119] op_sel_hi:[1,0]
	v_add_u32_e32 v4, 0x420, v101
	ds_write2_b32 v4, v2, v3 offset1:1
	v_pk_mul_f32 v[2:3], v[12:13], v[118:119] op_sel_hi:[1,0]
	v_add_u32_e32 v4, 0x428, v101
	ds_write2_b32 v4, v2, v3 offset1:1
	v_pk_mul_f32 v[2:3], v[6:7], v[124:125] op_sel_hi:[1,0]
	v_add_u32_e32 v4, 0x840, v101
	ds_write2_b32 v4, v2, v3 offset1:1
	v_pk_mul_f32 v[2:3], v[8:9], v[124:125] op_sel_hi:[1,0]
	v_add_u32_e32 v4, 0x848, v101
	ds_write2_b32 v4, v2, v3 offset1:1
	s_waitcnt vmcnt(5)
	v_pk_mul_f32 v[2:3], v[22:23], v[122:123] op_sel_hi:[1,0]
	v_add_u32_e32 v4, 0xc60, v101
	ds_write2_b32 v4, v2, v3 offset1:1
	v_pk_mul_f32 v[2:3], v[24:25], v[122:123] op_sel_hi:[1,0]
	v_add_u32_e32 v4, 0xc68, v101
	ds_write2_b32 v4, v2, v3 offset1:1
	s_waitcnt vmcnt(4)
	v_pk_mul_f32 v[2:3], v[14:15], v[128:129] op_sel_hi:[1,0]
	v_add_u32_e32 v4, 0x1080, v101
	ds_write2_b32 v4, v2, v3 offset1:1
	v_pk_mul_f32 v[2:3], v[16:17], v[128:129] op_sel_hi:[1,0]
	v_add_u32_e32 v4, 0x1088, v101
	ds_write2_b32 v4, v2, v3 offset1:1
	v_pk_mul_f32 v[2:3], v[26:27], v[126:127] op_sel_hi:[1,0]
	v_add_u32_e32 v4, 0x14a0, v101
	ds_write2_b32 v4, v2, v3 offset1:1
	v_pk_mul_f32 v[2:3], v[28:29], v[126:127] op_sel_hi:[1,0]
	v_add_u32_e32 v4, 0x14a8, v101
	ds_write2_b32 v4, v2, v3 offset1:1
	v_pk_mul_f32 v[2:3], v[18:19], v[132:133] op_sel_hi:[1,0]
	v_add_u32_e32 v4, 0x18c0, v101
	ds_write2_b32 v4, v2, v3 offset1:1
	v_pk_mul_f32 v[2:3], v[20:21], v[132:133] op_sel_hi:[1,0]
	v_add_u32_e32 v4, 0x18c8, v101
	ds_write2_b32 v4, v2, v3 offset1:1
	s_waitcnt vmcnt(0)
	v_pk_mul_f32 v[2:3], v[30:31], v[130:131] op_sel_hi:[1,0]
	v_add_u32_e32 v4, 0x1ce0, v101
	ds_write2_b32 v4, v2, v3 offset1:1
	v_pk_mul_f32 v[2:3], v[32:33], v[130:131] op_sel_hi:[1,0]
	v_add_u32_e32 v4, 0x1ce8, v101
	ds_write2_b32 v4, v2, v3 offset1:1
	s_waitcnt lgkmcnt(0)
	ds_read2_b32 v[6:7], v99 offset0:33 offset1:41
	ds_read2_b32 v[8:9], v99 offset1:8
	ds_read2_b32 v[10:11], v99 offset0:66 offset1:74
	ds_read2_b32 v[12:13], v99 offset0:99 offset1:107
	ds_read2_b32 v[14:15], v99 offset0:132 offset1:140
	ds_read2_b32 v[16:17], v99 offset0:165 offset1:173
	ds_read2_b32 v[18:19], v99 offset0:198 offset1:206
	ds_read2_b32 v[20:21], v99 offset0:231 offset1:239
	v_lshl_add_u64 v[22:23], s[14:15], 0, v[116:117]
	v_lshlrev_b32_e32 v24, 1, v106
	v_mov_b32_e32 v25, v1
	s_waitcnt lgkmcnt(6)
	v_cvt_pk_bf16_f32 v2, v8, v6
	s_waitcnt lgkmcnt(4)
	v_cvt_pk_bf16_f32 v3, v10, v12
	s_waitcnt lgkmcnt(2)
	v_cvt_pk_bf16_f32 v4, v14, v16
	s_waitcnt lgkmcnt(0)
	v_cvt_pk_bf16_f32 v5, v18, v20
	v_lshl_add_u64 v[22:23], v[22:23], 0, v[24:25]
	global_store_dwordx4 v[22:23], v[2:5], off sc0 sc1
	s_nop 1
	v_cvt_pk_bf16_f32 v2, v9, v7
	v_cvt_pk_bf16_f32 v3, v11, v13
	v_cvt_pk_bf16_f32 v4, v15, v17
	v_cvt_pk_bf16_f32 v5, v19, v21
	ds_read2_b32 v[8:9], v99 offset0:49 offset1:57
	ds_read2_b32 v[10:11], v99 offset0:16 offset1:24
	ds_read2_b32 v[12:13], v99 offset0:82 offset1:90
	ds_read2_b32 v[14:15], v99 offset0:115 offset1:123
	ds_read2_b32 v[16:17], v99 offset0:148 offset1:156
	ds_read2_b32 v[18:19], v99 offset0:181 offset1:189
	ds_read2_b32 v[20:21], v99 offset0:214 offset1:222
	ds_read2_b32 v[22:23], v99 offset0:247 offset1:255
	v_lshl_add_u64 v[6:7], s[14:15], 0, v[114:115]
	v_lshl_add_u64 v[6:7], v[6:7], 0, v[24:25]
	global_store_dwordx4 v[6:7], v[2:5], off sc0 sc1
	v_lshl_add_u64 v[6:7], s[14:15], 0, v[112:113]
	v_lshl_add_u64 v[6:7], v[6:7], 0, v[24:25]
	s_waitcnt lgkmcnt(6)
	v_cvt_pk_bf16_f32 v2, v10, v8
	s_waitcnt lgkmcnt(4)
	v_cvt_pk_bf16_f32 v3, v12, v14
	s_waitcnt lgkmcnt(2)
	v_cvt_pk_bf16_f32 v4, v16, v18
	s_waitcnt lgkmcnt(0)
	v_cvt_pk_bf16_f32 v5, v20, v22
	global_store_dwordx4 v[6:7], v[2:5], off sc0 sc1
	v_lshl_add_u64 v[6:7], s[14:15], 0, v[110:111]
	v_lshl_add_u64 v[6:7], v[6:7], 0, v[24:25]
	v_cvt_pk_bf16_f32 v2, v11, v9
	v_cvt_pk_bf16_f32 v3, v13, v15
	v_cvt_pk_bf16_f32 v4, v17, v19
	v_cvt_pk_bf16_f32 v5, v21, v23
	global_store_dwordx4 v[6:7], v[2:5], off sc0 sc1
	s_waitcnt lgkmcnt(0)

.LBB0_277:
	s_andn2_b64 vcc, exec, s[38:39]
	s_cbranch_vccnz .LBB0_281
	s_cmp_eq_u32 s31, 0
	s_cbranch_scc1 .LBB0_280
	s_waitcnt vmcnt(0)
	v_pk_mul_f32 v[2:3], v[58:59], v[134:135] op_sel_hi:[1,0]
	ds_write2_b32 v101, v2, v3 offset1:1
	v_pk_mul_f32 v[2:3], v[60:61], v[134:135] op_sel_hi:[1,0]
	ds_write2_b32 v101, v2, v3 offset0:2 offset1:3
	v_pk_mul_f32 v[2:3], v[74:75], v[136:137] op_sel_hi:[1,0]
	v_add_u32_e32 v4, 0x420, v101
	ds_write2_b32 v4, v2, v3 offset1:1
	v_pk_mul_f32 v[2:3], v[76:77], v[136:137] op_sel_hi:[1,0]
	v_add_u32_e32 v4, 0x428, v101
	ds_write2_b32 v4, v2, v3 offset1:1
	v_pk_mul_f32 v[2:3], v[70:71], v[138:139] op_sel_hi:[1,0]
	v_add_u32_e32 v4, 0x840, v101
	ds_write2_b32 v4, v2, v3 offset1:1
	v_pk_mul_f32 v[2:3], v[72:73], v[138:139] op_sel_hi:[1,0]
	v_add_u32_e32 v4, 0x848, v101
	ds_write2_b32 v4, v2, v3 offset1:1
	v_pk_mul_f32 v[2:3], v[82:83], v[140:141] op_sel_hi:[1,0]
	v_add_u32_e32 v4, 0xc60, v101
	ds_write2_b32 v4, v2, v3 offset1:1
	v_pk_mul_f32 v[2:3], v[84:85], v[140:141] op_sel_hi:[1,0]
	v_add_u32_e32 v4, 0xc68, v101
	ds_write2_b32 v4, v2, v3 offset1:1
	v_pk_mul_f32 v[2:3], v[78:79], v[142:143] op_sel_hi:[1,0]
	v_add_u32_e32 v4, 0x1080, v101
	ds_write2_b32 v4, v2, v3 offset1:1
	v_pk_mul_f32 v[2:3], v[80:81], v[142:143] op_sel_hi:[1,0]
	v_add_u32_e32 v4, 0x1088, v101
	ds_write2_b32 v4, v2, v3 offset1:1
	v_pk_mul_f32 v[2:3], v[90:91], v[144:145] op_sel_hi:[1,0]
	v_add_u32_e32 v4, 0x14a0, v101
	ds_write2_b32 v4, v2, v3 offset1:1
	v_pk_mul_f32 v[2:3], v[92:93], v[144:145] op_sel_hi:[1,0]
	v_add_u32_e32 v4, 0x14a8, v101
	ds_write2_b32 v4, v2, v3 offset1:1
	v_pk_mul_f32 v[2:3], v[86:87], v[146:147] op_sel_hi:[1,0]
	v_add_u32_e32 v4, 0x18c0, v101
	ds_write2_b32 v4, v2, v3 offset1:1
	v_pk_mul_f32 v[2:3], v[88:89], v[146:147] op_sel_hi:[1,0]
	v_add_u32_e32 v4, 0x18c8, v101
	ds_write2_b32 v4, v2, v3 offset1:1
	v_pk_mul_f32 v[2:3], v[94:95], v[148:149] op_sel_hi:[1,0]
	v_add_u32_e32 v4, 0x1ce0, v101
	ds_write2_b32 v4, v2, v3 offset1:1
	v_pk_mul_f32 v[2:3], v[96:97], v[148:149] op_sel_hi:[1,0]
	v_add_u32_e32 v4, 0x1ce8, v101
	ds_write2_b32 v4, v2, v3 offset1:1
	s_waitcnt lgkmcnt(0)
	ds_read2_b32 v[6:7], v99 offset0:33 offset1:41
	ds_read2_b32 v[8:9], v99 offset1:8
	ds_read2_b32 v[10:11], v99 offset0:66 offset1:74
	ds_read2_b32 v[12:13], v99 offset0:99 offset1:107
	ds_read2_b32 v[14:15], v99 offset0:132 offset1:140
	ds_read2_b32 v[16:17], v99 offset0:165 offset1:173
	ds_read2_b32 v[18:19], v99 offset0:198 offset1:206
	ds_read2_b32 v[20:21], v99 offset0:231 offset1:239
	v_lshl_add_u64 v[22:23], s[16:17], 0, v[116:117]
	v_lshlrev_b32_e32 v24, 1, v106
	v_mov_b32_e32 v25, v1
	s_waitcnt lgkmcnt(6)
	v_cvt_pk_bf16_f32 v2, v8, v6
	s_waitcnt lgkmcnt(4)
	v_cvt_pk_bf16_f32 v3, v10, v12
	s_waitcnt lgkmcnt(2)
	v_cvt_pk_bf16_f32 v4, v14, v16
	s_waitcnt lgkmcnt(0)
	v_cvt_pk_bf16_f32 v5, v18, v20
	v_lshl_add_u64 v[22:23], v[22:23], 0, v[24:25]
	global_store_dwordx4 v[22:23], v[2:5], off sc0 sc1
	s_nop 1
	v_cvt_pk_bf16_f32 v2, v9, v7
	v_cvt_pk_bf16_f32 v3, v11, v13
	v_cvt_pk_bf16_f32 v4, v15, v17
	v_cvt_pk_bf16_f32 v5, v19, v21
	ds_read2_b32 v[8:9], v99 offset0:49 offset1:57
	ds_read2_b32 v[10:11], v99 offset0:16 offset1:24
	ds_read2_b32 v[12:13], v99 offset0:82 offset1:90
	ds_read2_b32 v[14:15], v99 offset0:115 offset1:123
	ds_read2_b32 v[16:17], v99 offset0:148 offset1:156
	ds_read2_b32 v[18:19], v99 offset0:181 offset1:189
	ds_read2_b32 v[20:21], v99 offset0:214 offset1:222
	ds_read2_b32 v[22:23], v99 offset0:247 offset1:255
	v_lshl_add_u64 v[6:7], s[16:17], 0, v[114:115]
	v_lshl_add_u64 v[6:7], v[6:7], 0, v[24:25]
	global_store_dwordx4 v[6:7], v[2:5], off sc0 sc1
	v_lshl_add_u64 v[6:7], s[16:17], 0, v[112:113]
	v_lshl_add_u64 v[6:7], v[6:7], 0, v[24:25]
	s_waitcnt lgkmcnt(6)
	v_cvt_pk_bf16_f32 v2, v10, v8
	s_waitcnt lgkmcnt(4)
	v_cvt_pk_bf16_f32 v3, v12, v14
	s_waitcnt lgkmcnt(2)
	v_cvt_pk_bf16_f32 v4, v16, v18
	s_waitcnt lgkmcnt(0)
	v_cvt_pk_bf16_f32 v5, v20, v22
	global_store_dwordx4 v[6:7], v[2:5], off sc0 sc1
	v_lshl_add_u64 v[6:7], s[16:17], 0, v[110:111]
	v_lshl_add_u64 v[6:7], v[6:7], 0, v[24:25]
	v_cvt_pk_bf16_f32 v2, v11, v9
	v_cvt_pk_bf16_f32 v3, v13, v15
	v_cvt_pk_bf16_f32 v4, v17, v19
	v_cvt_pk_bf16_f32 v5, v21, v23
	global_store_dwordx4 v[6:7], v[2:5], off sc0 sc1
	s_waitcnt lgkmcnt(0)

.LBB0_287:
	s_andn2_b64 vcc, exec, s[36:37]
	s_cbranch_vccnz .LBB0_284
	s_cmp_eq_u32 s31, 0
	s_cbranch_scc1 .LBB0_283
	s_waitcnt vmcnt(6)
	v_pk_mul_f32 v[34:35], v[124:125], v[34:35] op_sel_hi:[0,1]
	ds_write2_b32 v101, v34, v35 offset1:1
	v_pk_mul_f32 v[34:35], v[124:125], v[36:37] op_sel_hi:[0,1]
	ds_write2_b32 v101, v34, v35 offset0:2 offset1:3
	s_waitcnt vmcnt(5)
	v_pk_mul_f32 v[34:35], v[126:127], v[42:43] op_sel_hi:[0,1]
	v_add_u32_e32 v36, 0x420, v101
	ds_write2_b32 v36, v34, v35 offset1:1
	v_pk_mul_f32 v[34:35], v[126:127], v[44:45] op_sel_hi:[0,1]
	v_add_u32_e32 v36, 0x428, v101
	ds_write2_b32 v36, v34, v35 offset1:1
	s_waitcnt vmcnt(4)
	v_pk_mul_f32 v[34:35], v[132:133], v[38:39] op_sel_hi:[0,1]
	v_add_u32_e32 v36, 0x840, v101
	ds_write2_b32 v36, v34, v35 offset1:1
	v_pk_mul_f32 v[34:35], v[132:133], v[40:41] op_sel_hi:[0,1]
	v_add_u32_e32 v36, 0x848, v101
	ds_write2_b32 v36, v34, v35 offset1:1
	v_pk_mul_f32 v[34:35], v[122:123], v[50:51] op_sel_hi:[0,1]
	v_add_u32_e32 v36, 0xc60, v101
	ds_write2_b32 v36, v34, v35 offset1:1
	v_pk_mul_f32 v[34:35], v[122:123], v[52:53] op_sel_hi:[0,1]
	v_add_u32_e32 v36, 0xc68, v101
	ds_write2_b32 v36, v34, v35 offset1:1
	s_waitcnt vmcnt(3)
	v_pk_mul_f32 v[34:35], v[130:131], v[46:47] op_sel_hi:[0,1]
	v_add_u32_e32 v36, 0x1080, v101
	ds_write2_b32 v36, v34, v35 offset1:1
	v_pk_mul_f32 v[34:35], v[130:131], v[48:49] op_sel_hi:[0,1]
	v_add_u32_e32 v36, 0x1088, v101
	ds_write2_b32 v36, v34, v35 offset1:1
	s_waitcnt vmcnt(0)
	v_pk_mul_f32 v[34:35], v[120:121], v[62:63] op_sel_hi:[0,1]
	v_add_u32_e32 v36, 0x14a0, v101
	ds_write2_b32 v36, v34, v35 offset1:1
	v_pk_mul_f32 v[34:35], v[120:121], v[64:65] op_sel_hi:[0,1]
	v_add_u32_e32 v36, 0x14a8, v101
	ds_write2_b32 v36, v34, v35 offset1:1
	v_pk_mul_f32 v[34:35], v[128:129], v[54:55] op_sel_hi:[0,1]
	v_add_u32_e32 v36, 0x18c0, v101
	ds_write2_b32 v36, v34, v35 offset1:1
	v_pk_mul_f32 v[34:35], v[128:129], v[56:57] op_sel_hi:[0,1]
	v_add_u32_e32 v36, 0x18c8, v101
	ds_write2_b32 v36, v34, v35 offset1:1
	v_pk_mul_f32 v[34:35], v[118:119], v[66:67] op_sel_hi:[0,1]
	v_add_u32_e32 v36, 0x1ce0, v101
	ds_write2_b32 v36, v34, v35 offset1:1
	v_pk_mul_f32 v[34:35], v[118:119], v[68:69] op_sel_hi:[0,1]
	v_add_u32_e32 v36, 0x1ce8, v101
	ds_write2_b32 v36, v34, v35 offset1:1
	s_waitcnt lgkmcnt(0)
	ds_read2_b32 v[38:39], v99 offset0:33 offset1:41
	ds_read2_b32 v[40:41], v99 offset1:8
	ds_read2_b32 v[42:43], v99 offset0:66 offset1:74
	ds_read2_b32 v[44:45], v99 offset0:99 offset1:107
	ds_read2_b32 v[46:47], v99 offset0:132 offset1:140
	ds_read2_b32 v[48:49], v99 offset0:165 offset1:173
	ds_read2_b32 v[50:51], v99 offset0:198 offset1:206
	ds_read2_b32 v[52:53], v99 offset0:231 offset1:239
	v_mad_u64_u32 v[54:55], s[36:37], s34, v104, 0
	v_lshl_add_u64 v[54:55], v[54:55], 1, s[14:15]
	v_lshlrev_b32_e32 v56, 1, v106
	v_mov_b32_e32 v57, v1
	s_waitcnt lgkmcnt(6)
	v_cvt_pk_bf16_f32 v34, v40, v38
	s_waitcnt lgkmcnt(4)
	v_cvt_pk_bf16_f32 v35, v42, v44
	s_waitcnt lgkmcnt(2)
	v_cvt_pk_bf16_f32 v36, v46, v48
	s_waitcnt lgkmcnt(0)
	v_cvt_pk_bf16_f32 v37, v50, v52
	v_lshl_add_u64 v[54:55], v[54:55], 0, v[56:57]
	global_store_dwordx4 v[54:55], v[34:37], off sc0 sc1
	s_nop 1
	v_cvt_pk_bf16_f32 v34, v41, v39
	v_cvt_pk_bf16_f32 v35, v43, v45
	v_cvt_pk_bf16_f32 v36, v47, v49
	v_cvt_pk_bf16_f32 v37, v51, v53
	v_mad_u64_u32 v[38:39], s[36:37], s34, v102, 0
	ds_read2_b32 v[40:41], v99 offset0:16 offset1:24
	ds_read2_b32 v[42:43], v99 offset0:49 offset1:57
	ds_read2_b32 v[44:45], v99 offset0:82 offset1:90
	ds_read2_b32 v[46:47], v99 offset0:115 offset1:123
	ds_read2_b32 v[48:49], v99 offset0:148 offset1:156
	ds_read2_b32 v[50:51], v99 offset0:181 offset1:189
	ds_read2_b32 v[52:53], v99 offset0:214 offset1:222
	ds_read2_b32 v[54:55], v99 offset0:247 offset1:255
	v_lshl_add_u64 v[38:39], v[38:39], 1, s[14:15]
	v_lshl_add_u64 v[38:39], v[38:39], 0, v[56:57]
	global_store_dwordx4 v[38:39], v[34:37], off sc0 sc1
	v_mad_u64_u32 v[38:39], s[36:37], s34, v100, 0
	v_lshl_add_u64 v[38:39], v[38:39], 1, s[14:15]
	s_waitcnt lgkmcnt(6)
	v_cvt_pk_bf16_f32 v34, v40, v42
	s_waitcnt lgkmcnt(4)
	v_cvt_pk_bf16_f32 v35, v44, v46
	s_waitcnt lgkmcnt(2)
	v_cvt_pk_bf16_f32 v36, v48, v50
	s_waitcnt lgkmcnt(0)
	v_cvt_pk_bf16_f32 v37, v52, v54
	v_lshl_add_u64 v[38:39], v[38:39], 0, v[56:57]
	global_store_dwordx4 v[38:39], v[34:37], off sc0 sc1
	v_mad_u64_u32 v[38:39], s[36:37], s34, v98, 0
	v_lshl_add_u64 v[38:39], v[38:39], 1, s[14:15]
	v_cvt_pk_bf16_f32 v34, v41, v43
	v_cvt_pk_bf16_f32 v35, v45, v47
	v_cvt_pk_bf16_f32 v36, v49, v51
	v_cvt_pk_bf16_f32 v37, v53, v55
	v_lshl_add_u64 v[38:39], v[38:39], 0, v[56:57]
	global_store_dwordx4 v[38:39], v[34:37], off sc0 sc1
	s_waitcnt lgkmcnt(0)
	s_branch .LBB0_283

.LBB0_292:
	s_and_b64 vcc, exec, s[16:17]
	s_cbranch_vccz .LBB0_296
	s_cmp_eq_u32 s31, 0
	s_cbranch_scc1 .LBB0_295
	s_waitcnt vmcnt(6)
	v_pk_mul_f32 v[34:35], v[34:35], v[124:125] op_sel_hi:[1,0]
	ds_write2_b32 v101, v34, v35 offset1:1
	v_pk_mul_f32 v[34:35], v[36:37], v[124:125] op_sel_hi:[1,0]
	ds_write2_b32 v101, v34, v35 offset0:2 offset1:3
	s_waitcnt vmcnt(5)
	v_pk_mul_f32 v[34:35], v[42:43], v[126:127] op_sel_hi:[1,0]
	v_add_u32_e32 v0, 0x420, v101
	ds_write2_b32 v0, v34, v35 offset1:1
	v_pk_mul_f32 v[34:35], v[44:45], v[126:127] op_sel_hi:[1,0]
	v_add_u32_e32 v0, 0x428, v101
	ds_write2_b32 v0, v34, v35 offset1:1
	s_waitcnt vmcnt(4)
	v_pk_mul_f32 v[34:35], v[38:39], v[132:133] op_sel_hi:[1,0]
	v_add_u32_e32 v0, 0x840, v101
	ds_write2_b32 v0, v34, v35 offset1:1
	v_pk_mul_f32 v[34:35], v[40:41], v[132:133] op_sel_hi:[1,0]
	v_add_u32_e32 v0, 0x848, v101
	ds_write2_b32 v0, v34, v35 offset1:1
	v_pk_mul_f32 v[34:35], v[50:51], v[122:123] op_sel_hi:[1,0]
	v_add_u32_e32 v0, 0xc60, v101
	ds_write2_b32 v0, v34, v35 offset1:1
	v_pk_mul_f32 v[34:35], v[52:53], v[122:123] op_sel_hi:[1,0]
	v_add_u32_e32 v0, 0xc68, v101
	ds_write2_b32 v0, v34, v35 offset1:1
	s_waitcnt vmcnt(3)
	v_pk_mul_f32 v[34:35], v[46:47], v[130:131] op_sel_hi:[1,0]
	v_add_u32_e32 v0, 0x1080, v101
	ds_write2_b32 v0, v34, v35 offset1:1
	v_pk_mul_f32 v[34:35], v[48:49], v[130:131] op_sel_hi:[1,0]
	v_add_u32_e32 v0, 0x1088, v101
	ds_write2_b32 v0, v34, v35 offset1:1
	s_waitcnt vmcnt(0)
	v_pk_mul_f32 v[34:35], v[62:63], v[120:121] op_sel_hi:[1,0]
	v_add_u32_e32 v0, 0x14a0, v101
	ds_write2_b32 v0, v34, v35 offset1:1
	v_pk_mul_f32 v[34:35], v[64:65], v[120:121] op_sel_hi:[1,0]
	v_add_u32_e32 v0, 0x14a8, v101
	ds_write2_b32 v0, v34, v35 offset1:1
	v_pk_mul_f32 v[34:35], v[54:55], v[128:129] op_sel_hi:[1,0]
	v_add_u32_e32 v0, 0x18c0, v101
	ds_write2_b32 v0, v34, v35 offset1:1
	v_pk_mul_f32 v[34:35], v[56:57], v[128:129] op_sel_hi:[1,0]
	v_add_u32_e32 v0, 0x18c8, v101
	ds_write2_b32 v0, v34, v35 offset1:1
	v_pk_mul_f32 v[34:35], v[66:67], v[118:119] op_sel_hi:[1,0]
	v_add_u32_e32 v0, 0x1ce0, v101
	ds_write2_b32 v0, v34, v35 offset1:1
	v_pk_mul_f32 v[34:35], v[68:69], v[118:119] op_sel_hi:[1,0]
	v_add_u32_e32 v0, 0x1ce8, v101
	ds_write2_b32 v0, v34, v35 offset1:1
	s_waitcnt lgkmcnt(0)
	ds_read2_b32 v[38:39], v99 offset0:33 offset1:41
	ds_read2_b32 v[40:41], v99 offset1:8
	ds_read2_b32 v[42:43], v99 offset0:66 offset1:74
	ds_read2_b32 v[44:45], v99 offset0:99 offset1:107
	ds_read2_b32 v[46:47], v99 offset0:132 offset1:140
	ds_read2_b32 v[48:49], v99 offset0:165 offset1:173
	ds_read2_b32 v[50:51], v99 offset0:198 offset1:206
	ds_read2_b32 v[52:53], v99 offset0:231 offset1:239
	v_mul_u32_u24_e32 v0, s34, v104
	v_lshlrev_b32_e32 v0, 1, v0
	v_lshl_add_u64 v[54:55], s[14:15], 0, v[0:1]
	v_lshlrev_b32_e32 v0, 1, v106
	s_lshl_b32 s14, s34, 3
	s_waitcnt lgkmcnt(6)
	v_cvt_pk_bf16_f32 v34, v40, v38
	s_waitcnt lgkmcnt(4)
	v_cvt_pk_bf16_f32 v35, v42, v44
	s_waitcnt lgkmcnt(2)
	v_cvt_pk_bf16_f32 v36, v46, v48
	s_waitcnt lgkmcnt(0)
	v_cvt_pk_bf16_f32 v37, v50, v52
	v_lshl_add_u64 v[56:57], v[54:55], 0, v[0:1]
	s_ashr_i32 s15, s14, 31
	global_store_dwordx4 v[56:57], v[34:37], off sc0 sc1
	s_lshl_b64 s[14:15], s[14:15], 1
	s_nop 0
	v_cvt_pk_bf16_f32 v34, v41, v39
	v_cvt_pk_bf16_f32 v35, v43, v45
	v_cvt_pk_bf16_f32 v36, v47, v49
	v_cvt_pk_bf16_f32 v37, v51, v53
	v_lshl_add_u64 v[38:39], v[54:55], 0, s[14:15]
	ds_read2_b32 v[42:43], v99 offset0:16 offset1:24
	ds_read2_b32 v[44:45], v99 offset0:49 offset1:57
	ds_read2_b32 v[46:47], v99 offset0:82 offset1:90
	ds_read2_b32 v[48:49], v99 offset0:115 offset1:123
	ds_read2_b32 v[50:51], v99 offset0:148 offset1:156
	ds_read2_b32 v[52:53], v99 offset0:181 offset1:189
	ds_read2_b32 v[54:55], v99 offset0:214 offset1:222
	ds_read2_b32 v[56:57], v99 offset0:247 offset1:255
	v_lshl_add_u64 v[40:41], v[38:39], 0, v[0:1]
	v_lshl_add_u64 v[38:39], v[38:39], 0, s[14:15]
	global_store_dwordx4 v[40:41], v[34:37], off sc0 sc1
	v_lshl_add_u64 v[40:41], v[38:39], 0, v[0:1]
	v_lshl_add_u64 v[38:39], v[38:39], 0, s[14:15]
	s_waitcnt lgkmcnt(6)
	v_cvt_pk_bf16_f32 v34, v42, v44
	s_waitcnt lgkmcnt(4)
	v_cvt_pk_bf16_f32 v35, v46, v48
	s_waitcnt lgkmcnt(2)
	v_cvt_pk_bf16_f32 v36, v50, v52
	s_waitcnt lgkmcnt(0)
	v_cvt_pk_bf16_f32 v37, v54, v56
	global_store_dwordx4 v[40:41], v[34:37], off sc0 sc1
	v_lshl_add_u64 v[38:39], v[38:39], 0, v[0:1]
	s_nop 0
	v_cvt_pk_bf16_f32 v34, v43, v45
	v_cvt_pk_bf16_f32 v35, v47, v49
	v_cvt_pk_bf16_f32 v36, v51, v53
	v_cvt_pk_bf16_f32 v37, v55, v57
	global_store_dwordx4 v[38:39], v[34:37], off sc0 sc1
	s_waitcnt lgkmcnt(0)

.LBB0_314:
	s_andn2_b64 vcc, exec, s[44:45]
	s_cbranch_vccnz .LBB0_318
	s_cmp_eq_u32 s31, 0
	s_cbranch_scc1 .LBB0_317
	s_waitcnt vmcnt(1)
	v_pk_mul_f32 v[26:27], v[126:127], v[26:27] op_sel_hi:[0,1]
	v_add_u32_e32 v0, 0x420, v101
	ds_write2_b32 v0, v26, v27 offset1:1
	v_pk_mul_f32 v[26:27], v[126:127], v[28:29] op_sel_hi:[0,1]
	v_add_u32_e32 v0, 0x428, v101
	ds_write2_b32 v0, v26, v27 offset1:1
	v_pk_mul_f32 v[22:23], v[132:133], v[22:23] op_sel_hi:[0,1]
	v_add_u32_e32 v0, 0x840, v101
	ds_write2_b32 v0, v22, v23 offset1:1
	v_pk_mul_f32 v[22:23], v[132:133], v[24:25] op_sel_hi:[0,1]
	v_add_u32_e32 v0, 0x848, v101
	ds_write2_b32 v0, v22, v23 offset1:1
	v_pk_mul_f32 v[18:19], v[122:123], v[18:19] op_sel_hi:[0,1]
	v_add_u32_e32 v0, 0xc60, v101
	ds_write2_b32 v0, v18, v19 offset1:1
	v_pk_mul_f32 v[18:19], v[122:123], v[20:21] op_sel_hi:[0,1]
	v_add_u32_e32 v0, 0xc68, v101
	ds_write2_b32 v0, v18, v19 offset1:1
	v_pk_mul_f32 v[14:15], v[130:131], v[14:15] op_sel_hi:[0,1]
	v_add_u32_e32 v0, 0x1080, v101
	ds_write2_b32 v0, v14, v15 offset1:1
	v_pk_mul_f32 v[14:15], v[130:131], v[16:17] op_sel_hi:[0,1]
	v_add_u32_e32 v0, 0x1088, v101
	ds_write2_b32 v0, v14, v15 offset1:1
	v_pk_mul_f32 v[10:11], v[120:121], v[10:11] op_sel_hi:[0,1]
	v_add_u32_e32 v0, 0x14a0, v101
	ds_write2_b32 v0, v10, v11 offset1:1
	v_pk_mul_f32 v[10:11], v[120:121], v[12:13] op_sel_hi:[0,1]
	v_add_u32_e32 v0, 0x14a8, v101
	ds_write2_b32 v0, v10, v11 offset1:1
	v_pk_mul_f32 v[6:7], v[128:129], v[6:7] op_sel_hi:[0,1]
	v_add_u32_e32 v0, 0x18c0, v101
	ds_write2_b32 v0, v6, v7 offset1:1
	v_pk_mul_f32 v[6:7], v[128:129], v[8:9] op_sel_hi:[0,1]
	v_add_u32_e32 v0, 0x18c8, v101
	s_waitcnt vmcnt(0)
	v_pk_mul_f32 v[30:31], v[124:125], v[30:31] op_sel_hi:[0,1]
	ds_write2_b32 v0, v6, v7 offset1:1
	v_pk_mul_f32 v[2:3], v[118:119], v[2:3] op_sel_hi:[0,1]
	v_add_u32_e32 v0, 0x1ce0, v101
	ds_write2_b32 v101, v30, v31 offset1:1
	v_pk_mul_f32 v[30:31], v[124:125], v[32:33] op_sel_hi:[0,1]
	ds_write2_b32 v0, v2, v3 offset1:1
	v_pk_mul_f32 v[2:3], v[118:119], v[4:5] op_sel_hi:[0,1]
	v_add_u32_e32 v0, 0x1ce8, v101
	ds_write2_b32 v101, v30, v31 offset0:2 offset1:3
	ds_write2_b32 v0, v2, v3 offset1:1
	s_waitcnt lgkmcnt(0)
	ds_read2_b32 v[6:7], v99 offset0:33 offset1:41
	ds_read2_b32 v[8:9], v99 offset1:8
	ds_read2_b32 v[10:11], v99 offset0:66 offset1:74
	ds_read2_b32 v[12:13], v99 offset0:99 offset1:107
	ds_read2_b32 v[14:15], v99 offset0:132 offset1:140
	ds_read2_b32 v[16:17], v99 offset0:165 offset1:173
	ds_read2_b32 v[18:19], v99 offset0:198 offset1:206
	ds_read2_b32 v[20:21], v99 offset0:231 offset1:239
	v_mad_u64_u32 v[22:23], s[44:45], s34, v104, 0
	v_lshl_add_u64 v[22:23], v[22:23], 1, s[0:1]
	v_lshlrev_b32_e32 v0, 1, v106
	s_waitcnt lgkmcnt(6)
	v_cvt_pk_bf16_f32 v2, v8, v6
	s_waitcnt lgkmcnt(4)
	v_cvt_pk_bf16_f32 v3, v10, v12
	s_waitcnt lgkmcnt(2)
	v_cvt_pk_bf16_f32 v4, v14, v16
	s_waitcnt lgkmcnt(0)
	v_cvt_pk_bf16_f32 v5, v18, v20
	v_lshl_add_u64 v[22:23], v[22:23], 0, v[0:1]
	global_store_dwordx4 v[22:23], v[2:5], off sc0 sc1
	s_nop 1
	v_cvt_pk_bf16_f32 v2, v9, v7
	v_cvt_pk_bf16_f32 v3, v11, v13
	v_cvt_pk_bf16_f32 v4, v15, v17
	v_cvt_pk_bf16_f32 v5, v19, v21
	v_mad_u64_u32 v[6:7], s[44:45], s34, v102, 0
	ds_read2_b32 v[8:9], v99 offset0:16 offset1:24
	ds_read2_b32 v[10:11], v99 offset0:49 offset1:57
	ds_read2_b32 v[12:13], v99 offset0:82 offset1:90
	ds_read2_b32 v[14:15], v99 offset0:115 offset1:123
	ds_read2_b32 v[16:17], v99 offset0:148 offset1:156
	ds_read2_b32 v[18:19], v99 offset0:181 offset1:189
	ds_read2_b32 v[20:21], v99 offset0:214 offset1:222
	ds_read2_b32 v[22:23], v99 offset0:247 offset1:255
	v_lshl_add_u64 v[6:7], v[6:7], 1, s[0:1]
	v_lshl_add_u64 v[6:7], v[6:7], 0, v[0:1]
	global_store_dwordx4 v[6:7], v[2:5], off sc0 sc1
	v_mad_u64_u32 v[6:7], s[44:45], s34, v100, 0
	v_lshl_add_u64 v[6:7], v[6:7], 1, s[0:1]
	s_waitcnt lgkmcnt(6)
	v_cvt_pk_bf16_f32 v2, v8, v10
	s_waitcnt lgkmcnt(4)
	v_cvt_pk_bf16_f32 v3, v12, v14
	s_waitcnt lgkmcnt(2)
	v_cvt_pk_bf16_f32 v4, v16, v18
	s_waitcnt lgkmcnt(0)
	v_cvt_pk_bf16_f32 v5, v20, v22
	v_lshl_add_u64 v[6:7], v[6:7], 0, v[0:1]
	global_store_dwordx4 v[6:7], v[2:5], off sc0 sc1
	v_mad_u64_u32 v[6:7], s[44:45], s34, v98, 0
	v_lshl_add_u64 v[6:7], v[6:7], 1, s[0:1]
	v_cvt_pk_bf16_f32 v2, v9, v11
	v_cvt_pk_bf16_f32 v3, v13, v15
	v_cvt_pk_bf16_f32 v4, v17, v19
	v_cvt_pk_bf16_f32 v5, v21, v23
	v_lshl_add_u64 v[6:7], v[6:7], 0, v[0:1]
	global_store_dwordx4 v[6:7], v[2:5], off sc0 sc1
	s_waitcnt lgkmcnt(0)

.LBB0_332:
	s_andn2_b64 vcc, exec, s[44:45]
	s_cbranch_vccnz .LBB0_299
	s_cmp_eq_u32 s31, 0
	s_cbranch_scc1 .LBB0_298
	s_waitcnt vmcnt(1)
	v_pk_mul_f32 v[26:27], v[26:27], v[126:127] op_sel_hi:[1,0]
	v_add_u32_e32 v0, 0x420, v101
	ds_write2_b32 v0, v26, v27 offset1:1
	v_pk_mul_f32 v[26:27], v[28:29], v[126:127] op_sel_hi:[1,0]
	v_add_u32_e32 v0, 0x428, v101
	ds_write2_b32 v0, v26, v27 offset1:1
	v_pk_mul_f32 v[22:23], v[22:23], v[132:133] op_sel_hi:[1,0]
	v_add_u32_e32 v0, 0x840, v101
	ds_write2_b32 v0, v22, v23 offset1:1
	v_pk_mul_f32 v[22:23], v[24:25], v[132:133] op_sel_hi:[1,0]
	v_add_u32_e32 v0, 0x848, v101
	ds_write2_b32 v0, v22, v23 offset1:1
	v_pk_mul_f32 v[18:19], v[18:19], v[122:123] op_sel_hi:[1,0]
	v_add_u32_e32 v0, 0xc60, v101
	ds_write2_b32 v0, v18, v19 offset1:1
	v_pk_mul_f32 v[18:19], v[20:21], v[122:123] op_sel_hi:[1,0]
	v_add_u32_e32 v0, 0xc68, v101
	ds_write2_b32 v0, v18, v19 offset1:1
	v_pk_mul_f32 v[14:15], v[14:15], v[130:131] op_sel_hi:[1,0]
	v_add_u32_e32 v0, 0x1080, v101
	ds_write2_b32 v0, v14, v15 offset1:1
	v_pk_mul_f32 v[14:15], v[16:17], v[130:131] op_sel_hi:[1,0]
	v_add_u32_e32 v0, 0x1088, v101
	ds_write2_b32 v0, v14, v15 offset1:1
	v_pk_mul_f32 v[10:11], v[10:11], v[120:121] op_sel_hi:[1,0]
	v_add_u32_e32 v0, 0x14a0, v101
	ds_write2_b32 v0, v10, v11 offset1:1
	v_pk_mul_f32 v[10:11], v[12:13], v[120:121] op_sel_hi:[1,0]
	v_add_u32_e32 v0, 0x14a8, v101
	ds_write2_b32 v0, v10, v11 offset1:1
	v_pk_mul_f32 v[6:7], v[6:7], v[128:129] op_sel_hi:[1,0]
	v_add_u32_e32 v0, 0x18c0, v101
	ds_write2_b32 v0, v6, v7 offset1:1
	v_pk_mul_f32 v[6:7], v[8:9], v[128:129] op_sel_hi:[1,0]
	v_add_u32_e32 v0, 0x18c8, v101
	s_waitcnt vmcnt(0)
	v_pk_mul_f32 v[30:31], v[30:31], v[124:125] op_sel_hi:[1,0]
	ds_write2_b32 v0, v6, v7 offset1:1
	v_pk_mul_f32 v[2:3], v[2:3], v[118:119] op_sel_hi:[1,0]
	v_add_u32_e32 v0, 0x1ce0, v101
	ds_write2_b32 v101, v30, v31 offset1:1
	v_pk_mul_f32 v[30:31], v[32:33], v[124:125] op_sel_hi:[1,0]
	ds_write2_b32 v0, v2, v3 offset1:1
	v_pk_mul_f32 v[2:3], v[4:5], v[118:119] op_sel_hi:[1,0]
	v_add_u32_e32 v0, 0x1ce8, v101
	ds_write2_b32 v101, v30, v31 offset0:2 offset1:3
	ds_write2_b32 v0, v2, v3 offset1:1
	s_waitcnt lgkmcnt(0)
	ds_read2_b32 v[6:7], v99 offset0:33 offset1:41
	ds_read2_b32 v[8:9], v99 offset1:8
	ds_read2_b32 v[10:11], v99 offset0:66 offset1:74
	ds_read2_b32 v[12:13], v99 offset0:99 offset1:107
	ds_read2_b32 v[14:15], v99 offset0:132 offset1:140
	ds_read2_b32 v[16:17], v99 offset0:165 offset1:173
	ds_read2_b32 v[18:19], v99 offset0:198 offset1:206
	ds_read2_b32 v[20:21], v99 offset0:231 offset1:239
	v_mad_u64_u32 v[22:23], s[36:37], s34, v104, 0
	v_lshl_add_u64 v[22:23], v[22:23], 1, s[0:1]
	v_lshlrev_b32_e32 v0, 1, v106
	s_waitcnt lgkmcnt(6)
	v_cvt_pk_bf16_f32 v2, v8, v6
	s_waitcnt lgkmcnt(4)
	v_cvt_pk_bf16_f32 v3, v10, v12
	s_waitcnt lgkmcnt(2)
	v_cvt_pk_bf16_f32 v4, v14, v16
	s_waitcnt lgkmcnt(0)
	v_cvt_pk_bf16_f32 v5, v18, v20
	v_lshl_add_u64 v[22:23], v[22:23], 0, v[0:1]
	global_store_dwordx4 v[22:23], v[2:5], off sc0 sc1
	s_nop 1
	v_cvt_pk_bf16_f32 v2, v9, v7
	v_cvt_pk_bf16_f32 v3, v11, v13
	v_cvt_pk_bf16_f32 v4, v15, v17
	v_cvt_pk_bf16_f32 v5, v19, v21
	v_mad_u64_u32 v[6:7], s[36:37], s34, v102, 0
	ds_read2_b32 v[8:9], v99 offset0:16 offset1:24
	ds_read2_b32 v[10:11], v99 offset0:49 offset1:57
	ds_read2_b32 v[12:13], v99 offset0:82 offset1:90
	ds_read2_b32 v[14:15], v99 offset0:115 offset1:123
	ds_read2_b32 v[16:17], v99 offset0:148 offset1:156
	ds_read2_b32 v[18:19], v99 offset0:181 offset1:189
	ds_read2_b32 v[20:21], v99 offset0:214 offset1:222
	ds_read2_b32 v[22:23], v99 offset0:247 offset1:255
	v_lshl_add_u64 v[6:7], v[6:7], 1, s[0:1]
	v_lshl_add_u64 v[6:7], v[6:7], 0, v[0:1]
	global_store_dwordx4 v[6:7], v[2:5], off sc0 sc1
	v_mad_u64_u32 v[6:7], s[36:37], s34, v100, 0
	v_lshl_add_u64 v[6:7], v[6:7], 1, s[0:1]
	s_waitcnt lgkmcnt(6)
	v_cvt_pk_bf16_f32 v2, v8, v10
	s_waitcnt lgkmcnt(4)
	v_cvt_pk_bf16_f32 v3, v12, v14
	s_waitcnt lgkmcnt(2)
	v_cvt_pk_bf16_f32 v4, v16, v18
	s_waitcnt lgkmcnt(0)
	v_cvt_pk_bf16_f32 v5, v20, v22
	v_lshl_add_u64 v[6:7], v[6:7], 0, v[0:1]
	global_store_dwordx4 v[6:7], v[2:5], off sc0 sc1
	v_mad_u64_u32 v[6:7], s[36:37], s34, v98, 0
	v_lshl_add_u64 v[6:7], v[6:7], 1, s[0:1]
	v_cvt_pk_bf16_f32 v2, v9, v11
	v_cvt_pk_bf16_f32 v3, v13, v15
	v_cvt_pk_bf16_f32 v4, v17, v19
	v_cvt_pk_bf16_f32 v5, v21, v23
	v_lshl_add_u64 v[6:7], v[6:7], 0, v[0:1]
	global_store_dwordx4 v[6:7], v[2:5], off sc0 sc1
	s_waitcnt lgkmcnt(0)
	s_branch .LBB0_298

.LBB0_343:
	s_cmp_eq_u32 s31, 0
	s_cbranch_scc1 .LBB0_345
	s_waitcnt vmcnt(1)
	v_pk_mul_f32 v[26:27], v[26:27], v[126:127] op_sel_hi:[1,0]
	v_add_u32_e32 v0, 0x420, v101
	ds_write2_b32 v0, v26, v27 offset1:1
	v_pk_mul_f32 v[26:27], v[28:29], v[126:127] op_sel_hi:[1,0]
	v_add_u32_e32 v0, 0x428, v101
	ds_write2_b32 v0, v26, v27 offset1:1
	v_pk_mul_f32 v[22:23], v[22:23], v[132:133] op_sel_hi:[1,0]
	v_add_u32_e32 v0, 0x840, v101
	ds_write2_b32 v0, v22, v23 offset1:1
	v_pk_mul_f32 v[22:23], v[24:25], v[132:133] op_sel_hi:[1,0]
	v_add_u32_e32 v0, 0x848, v101
	ds_write2_b32 v0, v22, v23 offset1:1
	v_pk_mul_f32 v[18:19], v[18:19], v[122:123] op_sel_hi:[1,0]
	v_add_u32_e32 v0, 0xc60, v101
	ds_write2_b32 v0, v18, v19 offset1:1
	v_pk_mul_f32 v[18:19], v[20:21], v[122:123] op_sel_hi:[1,0]
	v_add_u32_e32 v0, 0xc68, v101
	ds_write2_b32 v0, v18, v19 offset1:1
	v_pk_mul_f32 v[14:15], v[14:15], v[130:131] op_sel_hi:[1,0]
	v_add_u32_e32 v0, 0x1080, v101
	ds_write2_b32 v0, v14, v15 offset1:1
	v_pk_mul_f32 v[14:15], v[16:17], v[130:131] op_sel_hi:[1,0]
	v_add_u32_e32 v0, 0x1088, v101
	ds_write2_b32 v0, v14, v15 offset1:1
	v_pk_mul_f32 v[10:11], v[10:11], v[120:121] op_sel_hi:[1,0]
	v_add_u32_e32 v0, 0x14a0, v101
	ds_write2_b32 v0, v10, v11 offset1:1
	v_pk_mul_f32 v[10:11], v[12:13], v[120:121] op_sel_hi:[1,0]
	v_add_u32_e32 v0, 0x14a8, v101
	ds_write2_b32 v0, v10, v11 offset1:1
	v_pk_mul_f32 v[6:7], v[6:7], v[128:129] op_sel_hi:[1,0]
	v_add_u32_e32 v0, 0x18c0, v101
	ds_write2_b32 v0, v6, v7 offset1:1
	v_pk_mul_f32 v[6:7], v[8:9], v[128:129] op_sel_hi:[1,0]
	v_add_u32_e32 v0, 0x18c8, v101
	s_waitcnt vmcnt(0)
	v_pk_mul_f32 v[30:31], v[30:31], v[124:125] op_sel_hi:[1,0]
	ds_write2_b32 v0, v6, v7 offset1:1
	v_pk_mul_f32 v[2:3], v[2:3], v[118:119] op_sel_hi:[1,0]
	v_add_u32_e32 v0, 0x1ce0, v101
	ds_write2_b32 v101, v30, v31 offset1:1
	v_pk_mul_f32 v[30:31], v[32:33], v[124:125] op_sel_hi:[1,0]
	ds_write2_b32 v0, v2, v3 offset1:1
	v_pk_mul_f32 v[2:3], v[4:5], v[118:119] op_sel_hi:[1,0]
	v_add_u32_e32 v0, 0x1ce8, v101
	ds_write2_b32 v101, v30, v31 offset0:2 offset1:3
	ds_write2_b32 v0, v2, v3 offset1:1
	s_waitcnt lgkmcnt(0)
	ds_read2_b32 v[6:7], v99 offset0:33 offset1:41
	ds_read2_b32 v[8:9], v99 offset1:8
	ds_read2_b32 v[10:11], v99 offset0:66 offset1:74
	ds_read2_b32 v[12:13], v99 offset0:99 offset1:107
	ds_read2_b32 v[14:15], v99 offset0:132 offset1:140
	ds_read2_b32 v[16:17], v99 offset0:165 offset1:173
	ds_read2_b32 v[18:19], v99 offset0:198 offset1:206
	ds_read2_b32 v[20:21], v99 offset0:231 offset1:239
	v_mad_u64_u32 v[22:23], s[14:15], s34, v104, 0
	v_lshl_add_u64 v[22:23], v[22:23], 1, s[0:1]
	v_lshlrev_b32_e32 v0, 1, v106
	s_waitcnt lgkmcnt(6)
	v_cvt_pk_bf16_f32 v2, v8, v6
	s_waitcnt lgkmcnt(4)
	v_cvt_pk_bf16_f32 v3, v10, v12
	s_waitcnt lgkmcnt(2)
	v_cvt_pk_bf16_f32 v4, v14, v16
	s_waitcnt lgkmcnt(0)
	v_cvt_pk_bf16_f32 v5, v18, v20
	v_lshl_add_u64 v[22:23], v[22:23], 0, v[0:1]
	global_store_dwordx4 v[22:23], v[2:5], off sc0 sc1
	s_nop 1
	v_cvt_pk_bf16_f32 v2, v9, v7
	v_cvt_pk_bf16_f32 v3, v11, v13
	v_cvt_pk_bf16_f32 v4, v15, v17
	v_cvt_pk_bf16_f32 v5, v19, v21
	v_mad_u64_u32 v[6:7], s[14:15], s34, v102, 0
	ds_read2_b32 v[8:9], v99 offset0:16 offset1:24
	ds_read2_b32 v[10:11], v99 offset0:49 offset1:57
	ds_read2_b32 v[12:13], v99 offset0:82 offset1:90
	ds_read2_b32 v[14:15], v99 offset0:115 offset1:123
	ds_read2_b32 v[16:17], v99 offset0:148 offset1:156
	ds_read2_b32 v[18:19], v99 offset0:181 offset1:189
	ds_read2_b32 v[20:21], v99 offset0:214 offset1:222
	ds_read2_b32 v[22:23], v99 offset0:247 offset1:255
	v_lshl_add_u64 v[6:7], v[6:7], 1, s[0:1]
	v_lshl_add_u64 v[6:7], v[6:7], 0, v[0:1]
	global_store_dwordx4 v[6:7], v[2:5], off sc0 sc1
	v_mad_u64_u32 v[6:7], s[14:15], s34, v100, 0
	v_lshl_add_u64 v[6:7], v[6:7], 1, s[0:1]
	s_waitcnt lgkmcnt(6)
	v_cvt_pk_bf16_f32 v2, v8, v10
	s_waitcnt lgkmcnt(4)
	v_cvt_pk_bf16_f32 v3, v12, v14
	s_waitcnt lgkmcnt(2)
	v_cvt_pk_bf16_f32 v4, v16, v18
	s_waitcnt lgkmcnt(0)
	v_cvt_pk_bf16_f32 v5, v20, v22
	v_lshl_add_u64 v[6:7], v[6:7], 0, v[0:1]
	global_store_dwordx4 v[6:7], v[2:5], off sc0 sc1
	v_mad_u64_u32 v[6:7], s[14:15], s34, v98, 0
	v_lshl_add_u64 v[6:7], v[6:7], 1, s[0:1]
	v_cvt_pk_bf16_f32 v2, v9, v11
	v_cvt_pk_bf16_f32 v3, v13, v15
	v_cvt_pk_bf16_f32 v4, v17, v19
	v_cvt_pk_bf16_f32 v5, v21, v23
	v_lshl_add_u64 v[6:7], v[6:7], 0, v[0:1]
	global_store_dwordx4 v[6:7], v[2:5], off sc0 sc1
	s_waitcnt lgkmcnt(0)

.LBB0_362:
	s_or_saveexec_b64 s[38:39], s[38:39]
	s_lshl_b64 s[40:41], s[66:67], 2
	s_xor_b64 exec, exec, s[38:39]
	s_cbranch_execz .LBB0_364
	v_or_b32_e32 v203, s40, v0
	v_mov_b64_e32 v[200:201], s[42:43]
	v_mad_u64_u32 v[200:201], s[82:83], v203, s2, v[200:201]
	v_mov_b32_e32 v195, v194
	v_mad_i32_i24 v201, s41, v232, v201
	s_lshl_b64 s[50:51], s[66:67], 1
	v_cvt_pk_bf16_f32 v154, v190, v191
	v_cvt_pk_bf16_f32 v155, v188, v189
	v_cvt_pk_bf16_f32 v156, v160, v161
	v_cvt_pk_bf16_f32 v157, v158, v159
	v_lshl_add_u64 v[200:201], v[182:183], 1, v[200:201]
	v_pk_mul_f32 v[146:147], v[194:195], v[146:147]
	v_or_b32_e32 v202, s50, v0
	global_store_dwordx4 v[200:201], v[154:157], off sc0 sc1
	v_pk_mul_f32 v[150:151], v[194:195], v[150:151]
	s_nop 0
	v_mov_b32_e32 v154, v194
	v_mov_b32_e32 v155, v194
	v_cvt_pk_bf16_f32 v156, v146, v147
	v_mov_b64_e32 v[146:147], s[44:45]
	v_pk_mul_f32 v[152:153], v[154:155], v[152:153]
	v_pk_mul_f32 v[148:149], v[154:155], v[148:149]
	v_mad_u64_u32 v[200:201], s[82:83], v202, s2, v[146:147]
	v_cvt_pk_bf16_f32 v154, v150, v151
	v_cvt_pk_bf16_f32 v155, v152, v153
	v_cvt_pk_bf16_f32 v157, v148, v149
	v_mad_i32_i24 v201, s51, v232, v201
.LBB0_364:
	s_or_b64 exec, exec, s[38:39]
	v_mul_f32_e32 v146, 0x4b800000, v192
	v_cndmask_b32_e32 v146, v192, v146, vcc
	v_rsq_f32_e32 v146, v146
	s_mov_b32 s38, 0x32800000
	v_mul_f32_e32 v147, 0x45800000, v146
	v_cndmask_b32_e32 v192, v146, v147, vcc
	v_ffbh_u32_e32 v146, v187
	v_min_u32_e32 v148, 32, v146
	v_lshlrev_b64 v[146:147], v148, v[186:187]
	v_min_u32_e32 v146, 1, v146
	v_or_b32_e32 v146, v147, v146
	v_cvt_f32_u32_e32 v146, v146
	v_sub_u32_e32 v147, 32, v148
	v_pk_mul_f32 v[142:143], v[192:193], v[142:143] op_sel_hi:[0,1]
	v_pk_mul_f32 v[134:135], v[192:193], v[134:135] op_sel_hi:[0,1]
	v_ldexp_f32 v147, v146, v147
	v_ffbh_u32_e32 v146, v185
	v_min_u32_e32 v146, 32, v146
	v_lshlrev_b64 v[148:149], v146, v[184:185]
	v_min_u32_e32 v148, 1, v148
	v_or_b32_e32 v148, v149, v148
	v_cvt_f32_u32_e32 v148, v148
	v_sub_u32_e32 v146, 32, v146
	v_pk_mul_f32 v[144:145], v[192:193], v[144:145] op_sel_hi:[0,1]
	v_pk_mul_f32 v[136:137], v[192:193], v[136:137] op_sel_hi:[0,1]
	v_ldexp_f32 v146, v148, v146
	v_pk_fma_f32 v[146:147], v[146:147], s[38:39], v[196:197] op_sel_hi:[1,0,0]
	v_pk_mul_f32 v[130:131], v[192:193], v[130:131] op_sel_hi:[0,1]
	v_mul_f32_e32 v148, 0x4b800000, v147
	v_cmp_gt_f32_e64 s[38:39], s96, v147
	v_pk_mul_f32 v[132:133], v[192:193], v[132:133] op_sel_hi:[0,1]
	v_cmp_gt_f32_e32 vcc, s96, v146
	v_cndmask_b32_e64 v147, v147, v148, s[38:39]
	v_rsq_f32_e32 v147, v147
	s_nop 0
	v_mul_f32_e32 v148, 0x45800000, v147
	v_cndmask_b32_e64 v152, v147, v148, s[38:39]
	v_lshlrev_b64 v[148:149], 1, v[182:183]
	v_lshl_add_u64 v[184:185], v[200:201], 0, v[148:149]
	global_store_dwordx4 v[184:185], v[154:157], off sc0 sc1
	v_pk_mul_f32 v[126:127], v[152:153], v[126:127] op_sel_hi:[0,1]
	v_pk_mul_f32 v[118:119], v[152:153], v[118:119] op_sel_hi:[0,1]
	v_mov_b32_e32 v156, v1
	v_mov_b32_e32 v157, v1
	v_mov_b32_e32 v154, v1
	v_mov_b32_dpp v156, v190 row_ror:2 row_mask:0xf bank_mask:0xf
	v_mov_b32_e32 v155, v1
	v_mov_b32_dpp v157, v191 row_ror:2 row_mask:0xf bank_mask:0xf
	v_mov_b32_dpp v154, v190 row_ror:1 row_mask:0xf bank_mask:0xf
	v_mov_b32_dpp v156, v142 row_shr:2 row_mask:0xf bank_mask:0xf
	v_mov_b32_dpp v155, v191 row_ror:1 row_mask:0xf bank_mask:0xf
	v_mov_b32_dpp v157, v143 row_shr:2 row_mask:0xf bank_mask:0xf
	v_mov_b32_dpp v154, v142 row_shr:1 row_mask:0xf bank_mask:0xf
	v_mov_b32_dpp v155, v143 row_shr:1 row_mask:0xf bank_mask:0xf
	v_pk_fma_f32 v[156:157], v[74:75], v[156:157], v[86:87]
	v_pk_mul_f32 v[128:129], v[152:153], v[128:129] op_sel_hi:[0,1]
	v_pk_fma_f32 v[154:155], v[78:79], v[154:155], v[156:157]
	v_pk_mul_f32 v[120:121], v[152:153], v[120:121] op_sel_hi:[0,1]
	v_pk_fma_f32 v[154:155], v[142:143], v[82:83], v[154:155]
	v_pk_mul_f32 v[114:115], v[152:153], v[114:115] op_sel_hi:[0,1]
	v_mul_f32_e32 v151, 0x3d372713, v154
	v_mul_f32_e32 v151, v154, v151
	v_fma_f32 v151, v154, v151, v154
	v_mul_f32_e32 v151, 0xc0135761, v151
	v_exp_f32_e32 v151, v151
	v_mul_f32_e32 v147, 0x4b800000, v146
	v_cndmask_b32_e32 v146, v146, v147, vcc
	v_rsq_f32_e32 v146, v146
	v_add_f32_e32 v151, 1.0, v151
	v_rcp_f32_e32 v156, v151
	v_mul_f32_e32 v151, 0x3d372713, v155
	v_mul_f32_e32 v151, v155, v151
	v_fma_f32 v151, v155, v151, v155
	v_mul_f32_e32 v151, 0xc0135761, v151
	v_exp_f32_e32 v151, v151
	v_pk_mul_f32 v[116:117], v[152:153], v[116:117] op_sel_hi:[0,1]
	v_mul_f32_e32 v147, 0x45800000, v146
	v_cndmask_b32_e32 v150, v146, v147, vcc
	v_add_f32_e32 v151, 1.0, v151
	v_rcp_f32_e32 v157, v151
	v_cmp_lt_u32_e32 vcc, 13, v0
	v_lshl_add_u64 v[146:147], v[0:1], 0, -12
	v_pk_mul_f32 v[154:155], v[154:155], v[156:157]
	v_mov_b32_e32 v156, v1
	v_mov_b32_e32 v157, v1
	v_pk_mul_f32 v[154:155], v[134:135], v[154:155]
	v_mov_b32_e32 v134, v1
	v_mov_b32_dpp v156, v188 row_ror:2 row_mask:0xf bank_mask:0xf
	v_mov_b32_e32 v135, v1
	v_mov_b32_dpp v157, v189 row_ror:2 row_mask:0xf bank_mask:0xf
	v_mov_b32_dpp v134, v188 row_ror:1 row_mask:0xf bank_mask:0xf
	v_mov_b32_dpp v156, v144 row_shr:2 row_mask:0xf bank_mask:0xf
	v_mov_b32_dpp v135, v189 row_ror:1 row_mask:0xf bank_mask:0xf
	v_mov_b32_dpp v157, v145 row_shr:2 row_mask:0xf bank_mask:0xf
	v_mov_b32_dpp v134, v144 row_shr:1 row_mask:0xf bank_mask:0xf
	v_mov_b32_dpp v135, v145 row_shr:1 row_mask:0xf bank_mask:0xf
	v_pk_fma_f32 v[156:157], v[76:77], v[156:157], v[88:89]
	s_nop 0
	v_pk_fma_f32 v[134:135], v[80:81], v[134:135], v[156:157]
	s_nop 0
	v_pk_fma_f32 v[134:135], v[144:145], v[84:85], v[134:135]
	s_nop 0
	v_mul_f32_e32 v151, 0x3d372713, v134
	v_mul_f32_e32 v151, v134, v151
	v_fma_f32 v151, v134, v151, v134
	v_mul_f32_e32 v151, 0xc0135761, v151
	v_exp_f32_e32 v151, v151
	s_nop 0
	v_add_f32_e32 v151, 1.0, v151
	v_rcp_f32_e32 v156, v151
	v_mul_f32_e32 v151, 0x3d372713, v135
	v_mul_f32_e32 v151, v135, v151
	v_fma_f32 v151, v135, v151, v135
	v_mul_f32_e32 v151, 0xc0135761, v151
	v_exp_f32_e32 v151, v151
	s_nop 0
	v_add_f32_e32 v151, 1.0, v151
	v_rcp_f32_e32 v157, v151
	v_pk_mul_f32 v[110:111], v[150:151], v[110:111] op_sel_hi:[0,1]
	v_pk_mul_f32 v[102:103], v[150:151], v[102:103] op_sel_hi:[0,1]
	v_pk_mul_f32 v[112:113], v[150:151], v[112:113] op_sel_hi:[0,1]
	v_pk_mul_f32 v[134:135], v[134:135], v[156:157]
	v_pk_mul_f32 v[104:105], v[150:151], v[104:105] op_sel_hi:[0,1]
	v_pk_mul_f32 v[156:157], v[136:137], v[134:135]
	v_pk_mul_f32 v[134:135], v[192:193], v[140:141] op_sel_hi:[0,1]
	v_mov_b32_e32 v140, v1
	v_mov_b32_e32 v141, v1
	v_pk_mul_f32 v[136:137], v[192:193], v[138:139] op_sel_hi:[0,1]
	v_mov_b32_e32 v138, v1
	v_mov_b32_dpp v140, v160 row_ror:2 row_mask:0xf bank_mask:0xf
	v_mov_b32_e32 v139, v1
	v_mov_b32_dpp v141, v161 row_ror:2 row_mask:0xf bank_mask:0xf
	v_mov_b32_dpp v138, v160 row_ror:1 row_mask:0xf bank_mask:0xf
	v_mov_b32_dpp v140, v136 row_shr:2 row_mask:0xf bank_mask:0xf
	v_mov_b32_dpp v139, v161 row_ror:1 row_mask:0xf bank_mask:0xf
	v_mov_b32_dpp v141, v137 row_shr:2 row_mask:0xf bank_mask:0xf
	v_mov_b32_dpp v138, v136 row_shr:1 row_mask:0xf bank_mask:0xf
	v_mov_b32_dpp v139, v137 row_shr:1 row_mask:0xf bank_mask:0xf
	v_pk_fma_f32 v[140:141], v[46:47], v[140:141], v[62:63]
	v_pk_mul_f32 v[98:99], v[150:151], v[98:99] op_sel_hi:[0,1]
	v_pk_fma_f32 v[138:139], v[50:51], v[138:139], v[140:141]
	v_pk_mul_f32 v[100:101], v[150:151], v[100:101] op_sel_hi:[0,1]
	v_pk_fma_f32 v[138:139], v[136:137], v[58:59], v[138:139]
	s_nop 0
	v_mul_f32_e32 v140, 0x3d372713, v138
	v_mul_f32_e32 v141, 0x3d372713, v139
	v_mul_f32_e32 v140, v138, v140
	v_mul_f32_e32 v141, v139, v141
	v_fma_f32 v140, v138, v140, v138
	v_fma_f32 v141, v139, v141, v139
	v_mul_f32_e32 v140, 0xc0135761, v140
	v_mul_f32_e32 v141, 0xc0135761, v141
	v_exp_f32_e32 v140, v140
	v_exp_f32_e32 v141, v141
	v_add_f32_e32 v140, 1.0, v140
	v_add_f32_e32 v141, 1.0, v141
	v_rcp_f32_e32 v140, v140
	v_rcp_f32_e32 v141, v141
	s_nop 0
	v_pk_mul_f32 v[138:139], v[138:139], v[140:141]
	v_mov_b32_e32 v140, v1
	v_mov_b32_e32 v141, v1
	v_pk_mul_f32 v[130:131], v[130:131], v[138:139]
	v_mov_b32_e32 v138, v1
	v_mov_b32_dpp v140, v158 row_ror:2 row_mask:0xf bank_mask:0xf
	v_mov_b32_e32 v139, v1
	v_mov_b32_dpp v141, v159 row_ror:2 row_mask:0xf bank_mask:0xf
	v_mov_b32_dpp v138, v158 row_ror:1 row_mask:0xf bank_mask:0xf
	v_mov_b32_dpp v140, v134 row_shr:2 row_mask:0xf bank_mask:0xf
	v_mov_b32_dpp v139, v159 row_ror:1 row_mask:0xf bank_mask:0xf
	v_mov_b32_dpp v141, v135 row_shr:2 row_mask:0xf bank_mask:0xf
	v_mov_b32_dpp v138, v134 row_shr:1 row_mask:0xf bank_mask:0xf
	v_mov_b32_dpp v139, v135 row_shr:1 row_mask:0xf bank_mask:0xf
	v_pk_fma_f32 v[140:141], v[48:49], v[140:141], v[64:65]
	s_nop 0
	v_pk_fma_f32 v[138:139], v[52:53], v[138:139], v[140:141]
	s_nop 0
	v_pk_fma_f32 v[138:139], v[134:135], v[60:61], v[138:139]
	s_nop 0
	v_mul_f32_e32 v140, 0x3d372713, v138
	v_mul_f32_e32 v141, 0x3d372713, v139
	v_mul_f32_e32 v140, v138, v140
	v_mul_f32_e32 v141, v139, v141
	v_fma_f32 v140, v138, v140, v138
	v_fma_f32 v141, v139, v141, v139
	v_mul_f32_e32 v140, 0xc0135761, v140
	v_mul_f32_e32 v141, 0xc0135761, v141
	v_exp_f32_e32 v140, v140
	v_exp_f32_e32 v141, v141
	v_add_f32_e32 v140, 1.0, v140
	v_add_f32_e32 v141, 1.0, v141
	v_rcp_f32_e32 v140, v140
	v_rcp_f32_e32 v141, v141
	s_nop 0
	v_pk_mul_f32 v[138:139], v[138:139], v[140:141]
	s_nop 0
	v_pk_mul_f32 v[132:133], v[132:133], v[138:139]
	v_cvt_pk_bf16_f32 v140, v130, v131
	v_cvt_pk_bf16_f32 v141, v132, v133
	v_or_b32_e32 v132, 16, v193
	v_mov_b64_e32 v[130:131], s[16:17]
	v_mad_i64_i32 v[132:133], s[38:39], v132, s2, v[130:131]
	v_cvt_pk_bf16_f32 v138, v154, v155
	v_cvt_pk_bf16_f32 v139, v156, v157
	v_lshl_add_u64 v[132:133], v[132:133], 0, v[148:149]
	global_store_dwordx4 v[132:133], v[138:141], off sc0 sc1
	v_mov_b32_e32 v132, v1
	v_mov_b32_e32 v133, v1
	v_mov_b32_e32 v138, v1
	v_mov_b32_e32 v139, v1
	v_mov_b32_dpp v132, v142 row_ror:1 row_mask:0xf bank_mask:0xf
	v_mov_b32_dpp v138, v142 row_ror:2 row_mask:0xf bank_mask:0xf
	v_mov_b32_dpp v139, v143 row_ror:2 row_mask:0xf bank_mask:0xf
	v_mov_b32_dpp v133, v143 row_ror:1 row_mask:0xf bank_mask:0xf
	v_mov_b32_dpp v138, v126 row_shr:2 row_mask:0xf bank_mask:0xf
	v_mov_b32_dpp v139, v127 row_shr:2 row_mask:0xf bank_mask:0xf
	v_mov_b32_dpp v132, v126 row_shr:1 row_mask:0xf bank_mask:0xf
	v_mov_b32_dpp v133, v127 row_shr:1 row_mask:0xf bank_mask:0xf
	v_pk_fma_f32 v[138:139], v[74:75], v[138:139], v[86:87]
	s_nop 0
	v_pk_fma_f32 v[132:133], v[78:79], v[132:133], v[138:139]
	s_nop 0
	v_pk_fma_f32 v[132:133], v[126:127], v[82:83], v[132:133]
	s_nop 0
	v_mul_f32_e32 v138, 0x3d372713, v132
	v_mul_f32_e32 v139, 0x3d372713, v133
	v_mul_f32_e32 v138, v132, v138
	v_mul_f32_e32 v139, v133, v139
	v_fma_f32 v138, v132, v138, v132
	v_fma_f32 v139, v133, v139, v133
	v_mul_f32_e32 v138, 0xc0135761, v138
	v_mul_f32_e32 v139, 0xc0135761, v139
	v_exp_f32_e32 v138, v138
	v_exp_f32_e32 v139, v139
	v_add_f32_e32 v138, 1.0, v138
	v_add_f32_e32 v139, 1.0, v139
	v_rcp_f32_e32 v138, v138
	v_rcp_f32_e32 v139, v139
	s_nop 0
	v_pk_mul_f32 v[132:133], v[132:133], v[138:139]
	v_mov_b32_e32 v138, v1
	v_mov_b32_e32 v139, v1
	v_pk_mul_f32 v[132:133], v[118:119], v[132:133]
	v_mov_b32_e32 v118, v1
	v_mov_b32_dpp v138, v144 row_ror:2 row_mask:0xf bank_mask:0xf
	v_mov_b32_e32 v119, v1
	v_mov_b32_dpp v139, v145 row_ror:2 row_mask:0xf bank_mask:0xf
	v_mov_b32_dpp v118, v144 row_ror:1 row_mask:0xf bank_mask:0xf
	v_mov_b32_dpp v138, v128 row_shr:2 row_mask:0xf bank_mask:0xf
	v_mov_b32_dpp v119, v145 row_ror:1 row_mask:0xf bank_mask:0xf
	v_mov_b32_dpp v139, v129 row_shr:2 row_mask:0xf bank_mask:0xf
	v_mov_b32_dpp v118, v128 row_shr:1 row_mask:0xf bank_mask:0xf
	v_mov_b32_dpp v119, v129 row_shr:1 row_mask:0xf bank_mask:0xf
	v_pk_fma_f32 v[138:139], v[76:77], v[138:139], v[88:89]
	s_nop 0
	v_pk_fma_f32 v[118:119], v[80:81], v[118:119], v[138:139]
	s_nop 0
	v_pk_fma_f32 v[118:119], v[128:129], v[84:85], v[118:119]
	s_nop 0
	v_mul_f32_e32 v138, 0x3d372713, v118
	v_mul_f32_e32 v139, 0x3d372713, v119
	v_mul_f32_e32 v138, v118, v138
	v_mul_f32_e32 v139, v119, v139
	v_fma_f32 v138, v118, v138, v118
	v_fma_f32 v139, v119, v139, v119
	v_mul_f32_e32 v138, 0xc0135761, v138
	v_mul_f32_e32 v139, 0xc0135761, v139
	v_exp_f32_e32 v138, v138
	v_exp_f32_e32 v139, v139
	v_add_f32_e32 v138, 1.0, v138
	v_add_f32_e32 v139, 1.0, v139
	v_rcp_f32_e32 v138, v138
	v_rcp_f32_e32 v139, v139
	s_nop 0
	v_pk_mul_f32 v[118:119], v[118:119], v[138:139]
	s_nop 0
	v_pk_mul_f32 v[138:139], v[120:121], v[118:119]
	v_pk_mul_f32 v[118:119], v[152:153], v[124:125] op_sel_hi:[0,1]
	v_mov_b32_e32 v124, v1
	v_mov_b32_e32 v125, v1
	v_pk_mul_f32 v[120:121], v[152:153], v[122:123] op_sel_hi:[0,1]
	v_mov_b32_e32 v122, v1
	v_mov_b32_dpp v124, v136 row_ror:2 row_mask:0xf bank_mask:0xf
	v_mov_b32_e32 v123, v1
	v_mov_b32_dpp v125, v137 row_ror:2 row_mask:0xf bank_mask:0xf
	v_mov_b32_dpp v122, v136 row_ror:1 row_mask:0xf bank_mask:0xf
	v_mov_b32_dpp v124, v120 row_shr:2 row_mask:0xf bank_mask:0xf
	v_mov_b32_dpp v123, v137 row_ror:1 row_mask:0xf bank_mask:0xf
	v_mov_b32_dpp v125, v121 row_shr:2 row_mask:0xf bank_mask:0xf
	v_mov_b32_dpp v122, v120 row_shr:1 row_mask:0xf bank_mask:0xf
	v_mov_b32_dpp v123, v121 row_shr:1 row_mask:0xf bank_mask:0xf
	v_pk_fma_f32 v[124:125], v[46:47], v[124:125], v[62:63]
	s_nop 0
	v_pk_fma_f32 v[122:123], v[50:51], v[122:123], v[124:125]
	s_nop 0
	v_pk_fma_f32 v[122:123], v[120:121], v[58:59], v[122:123]
	s_nop 0
	v_mul_f32_e32 v124, 0x3d372713, v122
	v_mul_f32_e32 v125, 0x3d372713, v123
	v_mul_f32_e32 v124, v122, v124
	v_mul_f32_e32 v125, v123, v125
	v_fma_f32 v124, v122, v124, v122
	v_fma_f32 v125, v123, v125, v123
	v_mul_f32_e32 v124, 0xc0135761, v124
	v_mul_f32_e32 v125, 0xc0135761, v125
	v_exp_f32_e32 v124, v124
	v_exp_f32_e32 v125, v125
	v_add_f32_e32 v124, 1.0, v124
	v_add_f32_e32 v125, 1.0, v125
	v_rcp_f32_e32 v124, v124
	v_rcp_f32_e32 v125, v125
	s_nop 0
	v_pk_mul_f32 v[122:123], v[122:123], v[124:125]
	v_mov_b32_e32 v124, v1
	v_mov_b32_e32 v125, v1
	v_pk_mul_f32 v[122:123], v[114:115], v[122:123]
	v_mov_b32_e32 v114, v1
	v_mov_b32_dpp v124, v134 row_ror:2 row_mask:0xf bank_mask:0xf
	v_mov_b32_e32 v115, v1
	v_mov_b32_dpp v125, v135 row_ror:2 row_mask:0xf bank_mask:0xf
	v_mov_b32_dpp v114, v134 row_ror:1 row_mask:0xf bank_mask:0xf
	v_mov_b32_dpp v124, v118 row_shr:2 row_mask:0xf bank_mask:0xf
	v_mov_b32_dpp v115, v135 row_ror:1 row_mask:0xf bank_mask:0xf
	v_mov_b32_dpp v125, v119 row_shr:2 row_mask:0xf bank_mask:0xf
	v_mov_b32_dpp v114, v118 row_shr:1 row_mask:0xf bank_mask:0xf
	v_mov_b32_dpp v115, v119 row_shr:1 row_mask:0xf bank_mask:0xf
	v_pk_fma_f32 v[124:125], v[48:49], v[124:125], v[64:65]
	s_nop 0
	v_pk_fma_f32 v[114:115], v[52:53], v[114:115], v[124:125]
	s_nop 0
	v_pk_fma_f32 v[114:115], v[118:119], v[60:61], v[114:115]
	s_nop 0
	v_mul_f32_e32 v124, 0x3d372713, v114
	v_mul_f32_e32 v125, 0x3d372713, v115
	v_mul_f32_e32 v124, v114, v124
	v_mul_f32_e32 v125, v115, v125
	v_fma_f32 v124, v114, v124, v114
	v_fma_f32 v125, v115, v125, v115
	v_mul_f32_e32 v124, 0xc0135761, v124
	v_mul_f32_e32 v125, 0xc0135761, v125
	v_exp_f32_e32 v124, v124
	v_exp_f32_e32 v125, v125
	v_add_f32_e32 v124, 1.0, v124
	v_add_f32_e32 v125, 1.0, v125
	v_rcp_f32_e32 v124, v124
	v_rcp_f32_e32 v125, v125
	s_nop 0
	v_pk_mul_f32 v[114:115], v[114:115], v[124:125]
	s_nop 0
	v_pk_mul_f32 v[124:125], v[116:117], v[114:115]
	v_cvt_pk_bf16_f32 v116, v122, v123
	v_or_b32_e32 v122, 32, v193
	v_mad_i64_i32 v[122:123], s[38:39], v122, s2, v[130:131]
	v_cvt_pk_bf16_f32 v114, v132, v133
	v_cvt_pk_bf16_f32 v115, v138, v139
	v_cvt_pk_bf16_f32 v117, v124, v125
	v_lshl_add_u64 v[122:123], v[122:123], 0, v[148:149]
	global_store_dwordx4 v[122:123], v[114:117], off sc0 sc1
	s_nop 1
	v_mov_b32_e32 v116, v1
	v_mov_b32_e32 v117, v1
	v_mov_b32_e32 v114, v1
	v_mov_b32_dpp v116, v126 row_ror:2 row_mask:0xf bank_mask:0xf
	v_mov_b32_e32 v115, v1
	v_mov_b32_dpp v117, v127 row_ror:2 row_mask:0xf bank_mask:0xf
	v_mov_b32_dpp v114, v126 row_ror:1 row_mask:0xf bank_mask:0xf
	v_mov_b32_dpp v116, v110 row_shr:2 row_mask:0xf bank_mask:0xf
	v_mov_b32_dpp v115, v127 row_ror:1 row_mask:0xf bank_mask:0xf
	v_mov_b32_dpp v117, v111 row_shr:2 row_mask:0xf bank_mask:0xf
	v_mov_b32_dpp v114, v110 row_shr:1 row_mask:0xf bank_mask:0xf
	v_mov_b32_dpp v115, v111 row_shr:1 row_mask:0xf bank_mask:0xf
	v_pk_fma_f32 v[116:117], v[74:75], v[116:117], v[86:87]
	s_nop 0
	v_pk_fma_f32 v[114:115], v[78:79], v[114:115], v[116:117]
	s_nop 0
	v_pk_fma_f32 v[114:115], v[110:111], v[82:83], v[114:115]
	s_nop 0
	v_mul_f32_e32 v116, 0x3d372713, v114
	v_mul_f32_e32 v117, 0x3d372713, v115
	v_mul_f32_e32 v116, v114, v116
	v_mul_f32_e32 v117, v115, v117
	v_fma_f32 v116, v114, v116, v114
	v_fma_f32 v117, v115, v117, v115
	v_mul_f32_e32 v116, 0xc0135761, v116
	v_mul_f32_e32 v117, 0xc0135761, v117
	v_exp_f32_e32 v116, v116
	v_exp_f32_e32 v117, v117
	v_add_f32_e32 v116, 1.0, v116
	v_add_f32_e32 v117, 1.0, v117
	v_rcp_f32_e32 v116, v116
	v_rcp_f32_e32 v117, v117
	s_nop 0
	v_pk_mul_f32 v[114:115], v[114:115], v[116:117]
	v_mov_b32_e32 v116, v1
	v_mov_b32_e32 v117, v1
	v_pk_mul_f32 v[114:115], v[102:103], v[114:115]
	v_mov_b32_e32 v102, v1
	v_mov_b32_dpp v116, v128 row_ror:2 row_mask:0xf bank_mask:0xf
	v_mov_b32_e32 v103, v1
	v_mov_b32_dpp v117, v129 row_ror:2 row_mask:0xf bank_mask:0xf
	v_mov_b32_dpp v102, v128 row_ror:1 row_mask:0xf bank_mask:0xf
	v_mov_b32_dpp v116, v112 row_shr:2 row_mask:0xf bank_mask:0xf
	v_mov_b32_dpp v103, v129 row_ror:1 row_mask:0xf bank_mask:0xf
	v_mov_b32_dpp v117, v113 row_shr:2 row_mask:0xf bank_mask:0xf
	v_mov_b32_dpp v102, v112 row_shr:1 row_mask:0xf bank_mask:0xf
	v_mov_b32_dpp v103, v113 row_shr:1 row_mask:0xf bank_mask:0xf
	v_pk_fma_f32 v[116:117], v[76:77], v[116:117], v[88:89]
	s_nop 0
	v_pk_fma_f32 v[102:103], v[80:81], v[102:103], v[116:117]
	s_nop 0
	v_pk_fma_f32 v[102:103], v[112:113], v[84:85], v[102:103]
	s_nop 0
	v_mul_f32_e32 v116, 0x3d372713, v102
	v_mul_f32_e32 v117, 0x3d372713, v103
	v_mul_f32_e32 v116, v102, v116
	v_mul_f32_e32 v117, v103, v117
	v_fma_f32 v116, v102, v116, v102
	v_fma_f32 v117, v103, v117, v103
	v_mul_f32_e32 v116, 0xc0135761, v116
	v_mul_f32_e32 v117, 0xc0135761, v117
	v_exp_f32_e32 v116, v116
	v_exp_f32_e32 v117, v117
	v_add_f32_e32 v116, 1.0, v116
	v_add_f32_e32 v117, 1.0, v117
	v_rcp_f32_e32 v116, v116
	v_rcp_f32_e32 v117, v117
	s_nop 0
	v_pk_mul_f32 v[102:103], v[102:103], v[116:117]
	s_nop 0
	v_pk_mul_f32 v[116:117], v[104:105], v[102:103]
	v_pk_mul_f32 v[102:103], v[150:151], v[108:109] op_sel_hi:[0,1]
	v_mov_b32_e32 v108, v1
	v_mov_b32_e32 v109, v1
	v_pk_mul_f32 v[104:105], v[150:151], v[106:107] op_sel_hi:[0,1]
	v_mov_b32_e32 v106, v1
	v_mov_b32_dpp v108, v120 row_ror:2 row_mask:0xf bank_mask:0xf
	v_mov_b32_e32 v107, v1
	v_mov_b32_dpp v109, v121 row_ror:2 row_mask:0xf bank_mask:0xf
	v_mov_b32_dpp v106, v120 row_ror:1 row_mask:0xf bank_mask:0xf
	v_mov_b32_dpp v108, v104 row_shr:2 row_mask:0xf bank_mask:0xf
	v_mov_b32_dpp v107, v121 row_ror:1 row_mask:0xf bank_mask:0xf
	v_mov_b32_dpp v109, v105 row_shr:2 row_mask:0xf bank_mask:0xf
	v_mov_b32_dpp v106, v104 row_shr:1 row_mask:0xf bank_mask:0xf
	v_mov_b32_dpp v107, v105 row_shr:1 row_mask:0xf bank_mask:0xf
	v_pk_fma_f32 v[108:109], v[46:47], v[108:109], v[62:63]
	s_nop 0
	v_pk_fma_f32 v[106:107], v[50:51], v[106:107], v[108:109]
	s_nop 0
	v_pk_fma_f32 v[106:107], v[104:105], v[58:59], v[106:107]
	s_nop 0
	v_mul_f32_e32 v108, 0x3d372713, v106
	v_mul_f32_e32 v109, 0x3d372713, v107
	v_mul_f32_e32 v108, v106, v108
	v_mul_f32_e32 v109, v107, v109
	v_fma_f32 v108, v106, v108, v106
	v_fma_f32 v109, v107, v109, v107
	v_mul_f32_e32 v108, 0xc0135761, v108
	v_mul_f32_e32 v109, 0xc0135761, v109
	v_exp_f32_e32 v108, v108
	v_exp_f32_e32 v109, v109
	v_add_f32_e32 v108, 1.0, v108
	v_add_f32_e32 v109, 1.0, v109
	v_rcp_f32_e32 v108, v108
	v_rcp_f32_e32 v109, v109
	s_nop 0
	v_pk_mul_f32 v[106:107], v[106:107], v[108:109]
	v_mov_b32_e32 v108, v1
	v_mov_b32_e32 v109, v1
	v_pk_mul_f32 v[106:107], v[98:99], v[106:107]
	v_mov_b32_e32 v98, v1
	v_mov_b32_dpp v108, v118 row_ror:2 row_mask:0xf bank_mask:0xf
	v_mov_b32_e32 v99, v1
	v_mov_b32_dpp v109, v119 row_ror:2 row_mask:0xf bank_mask:0xf
	v_mov_b32_dpp v98, v118 row_ror:1 row_mask:0xf bank_mask:0xf
	v_mov_b32_dpp v108, v102 row_shr:2 row_mask:0xf bank_mask:0xf
	v_mov_b32_dpp v99, v119 row_ror:1 row_mask:0xf bank_mask:0xf
	v_mov_b32_dpp v109, v103 row_shr:2 row_mask:0xf bank_mask:0xf
	v_mov_b32_dpp v98, v102 row_shr:1 row_mask:0xf bank_mask:0xf
	v_mov_b32_dpp v99, v103 row_shr:1 row_mask:0xf bank_mask:0xf
	v_pk_fma_f32 v[108:109], v[48:49], v[108:109], v[64:65]
	s_nop 0
	v_pk_fma_f32 v[98:99], v[52:53], v[98:99], v[108:109]
	s_nop 0
	v_pk_fma_f32 v[98:99], v[102:103], v[60:61], v[98:99]
	s_nop 0
	v_mul_f32_e32 v108, 0x3d372713, v98
	v_mul_f32_e32 v109, 0x3d372713, v99
	v_mul_f32_e32 v108, v98, v108
	v_mul_f32_e32 v109, v99, v109
	v_fma_f32 v108, v98, v108, v98
	v_fma_f32 v109, v99, v109, v99
	v_mul_f32_e32 v108, 0xc0135761, v108
	v_mul_f32_e32 v109, 0xc0135761, v109
	v_exp_f32_e32 v108, v108
	v_exp_f32_e32 v109, v109
	v_add_f32_e32 v108, 1.0, v108
	v_add_f32_e32 v109, 1.0, v109
	v_rcp_f32_e32 v108, v108
	v_rcp_f32_e32 v109, v109
	s_nop 0
	v_pk_mul_f32 v[98:99], v[98:99], v[108:109]
	s_nop 0
	v_pk_mul_f32 v[108:109], v[100:101], v[98:99]
	v_cvt_pk_bf16_f32 v100, v106, v107
	v_or_b32_e32 v106, 48, v193
	v_mad_i64_i32 v[106:107], s[38:39], v106, s2, v[130:131]
	v_cvt_pk_bf16_f32 v98, v114, v115
	v_cvt_pk_bf16_f32 v99, v116, v117
	v_cvt_pk_bf16_f32 v101, v108, v109
	v_lshl_add_u64 v[106:107], v[106:107], 0, v[148:149]
	global_store_dwordx4 v[106:107], v[98:101], off sc0 sc1
	s_mov_b64 s[38:39], exec
	s_and_b64 s[50:51], s[38:39], vcc
	v_mov_b32_e32 v228, v221
	s_mov_b64 exec, s[50:51]
	s_cbranch_execz .LBB0_366
	v_lshl_add_u64 v[106:107], v[146:147], 0, s[40:41]
	v_cvt_pk_bf16_f32 v101, v102, v103
	v_mov_b64_e32 v[102:103], s[42:43]
	v_mad_u64_u32 v[102:103], s[40:41], v106, s2, v[102:103]
	v_mad_i32_i24 v103, v107, s2, v103
	v_cvt_pk_bf16_f32 v98, v110, v111
	v_cvt_pk_bf16_f32 v99, v112, v113
	v_cvt_pk_bf16_f32 v100, v104, v105
	v_lshl_add_u64 v[102:103], v[182:183], 1, v[102:103]
	global_store_dwordx4 v[102:103], v[98:101], off sc0 sc1

.LBB0_368:
	s_or_saveexec_b64 s[36:37], s[36:37]
	s_lshl_b64 s[40:41], s[66:67], 2
	s_xor_b64 exec, exec, s[36:37]
	s_cbranch_execz .LBB0_370
	s_lshl_b64 s[50:51], s[66:67], 1
	v_or_b32_e32 v103, s50, v0
	v_or_b32_e32 v0, s40, v0
	v_mov_b64_e32 v[106:107], s[42:43]
	v_mad_u64_u32 v[106:107], s[66:67], v0, s2, v[106:107]
	v_mov_b32_e32 v105, v104
	v_mad_i32_i24 v107, s41, v232, v107
	v_cvt_pk_bf16_f32 v90, v100, v101
	v_cvt_pk_bf16_f32 v91, v98, v99
	v_cvt_pk_bf16_f32 v92, v96, v97
	v_cvt_pk_bf16_f32 v93, v94, v95
	v_lshl_add_u64 v[106:107], v[182:183], 1, v[106:107]
	v_pk_mul_f32 v[66:67], v[104:105], v[66:67]
	global_store_dwordx4 v[106:107], v[90:93], off sc0 sc1
	v_pk_mul_f32 v[70:71], v[104:105], v[70:71]
	s_nop 0
	v_mov_b32_e32 v90, v104
	v_mov_b32_e32 v91, v104
	v_cvt_pk_bf16_f32 v92, v66, v67
	v_mov_b64_e32 v[66:67], s[44:45]
	v_pk_mul_f32 v[72:73], v[90:91], v[72:73]
	v_pk_mul_f32 v[68:69], v[90:91], v[68:69]
	v_mad_u64_u32 v[110:111], s[66:67], v103, s2, v[66:67]
	v_cvt_pk_bf16_f32 v90, v70, v71
	v_cvt_pk_bf16_f32 v91, v72, v73
	v_cvt_pk_bf16_f32 v93, v68, v69
	v_mad_i32_i24 v111, s51, v232, v111
.LBB0_370:
	s_or_b64 exec, exec, s[36:37]
	v_mul_f32_e32 v0, 0x4b800000, v102
	v_cndmask_b32_e64 v0, v102, v0, s[38:39]
	v_rsq_f32_e32 v0, v0
	s_mov_b32 s36, 0x32800000
	v_mov_b32_e32 v72, v1
	v_mov_b32_e32 v73, v1
	v_mul_f32_e32 v66, 0x45800000, v0
	v_cndmask_b32_e64 v68, v0, v66, s[38:39]
	v_ffbh_u32_e32 v0, v177
	v_min_u32_e32 v0, 32, v0
	v_lshlrev_b64 v[66:67], v0, v[176:177]
	v_min_u32_e32 v66, 1, v66
	v_or_b32_e32 v66, v67, v66
	v_cvt_f32_u32_e32 v66, v66
	v_sub_u32_e32 v0, 32, v0
	v_pk_mul_f32 v[54:55], v[68:69], v[54:55] op_sel_hi:[0,1]
	v_mov_b32_dpp v72, v100 row_ror:2 row_mask:0xf bank_mask:0xf
	v_ldexp_f32 v67, v66, v0
	v_ffbh_u32_e32 v0, v175
	v_min_u32_e32 v0, 32, v0
	v_lshlrev_b64 v[70:71], v0, v[174:175]
	v_min_u32_e32 v66, 1, v70
	v_or_b32_e32 v66, v71, v66
	v_cvt_f32_u32_e32 v66, v66
	v_sub_u32_e32 v0, 32, v0
	v_mov_b32_dpp v73, v101 row_ror:2 row_mask:0xf bank_mask:0xf
	v_mov_b32_dpp v72, v54 row_shr:2 row_mask:0xf bank_mask:0xf
	v_ldexp_f32 v66, v66, v0
	v_pk_fma_f32 v[70:71], v[66:67], s[36:37], v[196:197] op_sel_hi:[1,0,0]
	v_mov_b32_dpp v73, v55 row_shr:2 row_mask:0xf bank_mask:0xf
	v_mul_f32_e32 v0, 0x4b800000, v71
	v_cmp_gt_f32_e64 s[38:39], s96, v71
	v_cmp_gt_f32_e64 s[36:37], s96, v70
	v_pk_fma_f32 v[72:73], v[74:75], v[72:73], v[86:87]
	v_cndmask_b32_e64 v0, v71, v0, s[38:39]
	v_rsq_f32_e32 v0, v0
	v_pk_mul_f32 v[38:39], v[68:69], v[38:39] op_sel_hi:[0,1]
	v_pk_mul_f32 v[56:57], v[68:69], v[56:57] op_sel_hi:[0,1]
	v_pk_mul_f32 v[40:41], v[68:69], v[40:41] op_sel_hi:[0,1]
	v_mul_f32_e32 v66, 0x45800000, v0
	v_cndmask_b32_e64 v66, v0, v66, s[38:39]
	v_mul_f32_e32 v0, 0x4b800000, v70
	v_cndmask_b32_e64 v0, v70, v0, s[36:37]
	v_lshl_add_u64 v[70:71], v[110:111], 0, v[148:149]
	v_rsq_f32_e32 v0, v0
	global_store_dwordx4 v[70:71], v[90:93], off sc0 sc1
	v_mov_b32_e32 v70, v1
	v_mov_b32_e32 v71, v1
	v_mul_f32_e32 v67, 0x45800000, v0
	v_mov_b32_dpp v70, v100 row_ror:1 row_mask:0xf bank_mask:0xf
	v_mov_b32_dpp v71, v101 row_ror:1 row_mask:0xf bank_mask:0xf
	v_cndmask_b32_e64 v0, v0, v67, s[36:37]
	v_mov_b32_dpp v70, v54 row_shr:1 row_mask:0xf bank_mask:0xf
	v_mov_b32_dpp v71, v55 row_shr:1 row_mask:0xf bank_mask:0xf
	v_pk_fma_f32 v[70:71], v[78:79], v[70:71], v[72:73]
	v_pk_mul_f32 v[34:35], v[68:69], v[34:35] op_sel_hi:[0,1]
	v_pk_fma_f32 v[70:71], v[54:55], v[82:83], v[70:71]
	v_pk_mul_f32 v[36:37], v[68:69], v[36:37] op_sel_hi:[0,1]
	v_mul_f32_e32 v67, 0x3d372713, v70
	v_mul_f32_e32 v67, v70, v67
	v_fma_f32 v67, v70, v67, v70
	v_mul_f32_e32 v67, 0xc0135761, v67
	v_exp_f32_e32 v67, v67
	v_pk_mul_f32 v[14:15], v[0:1], v[14:15] op_sel_hi:[0,1]
	v_pk_mul_f32 v[6:7], v[0:1], v[6:7] op_sel_hi:[0,1]
	v_pk_mul_f32 v[16:17], v[0:1], v[16:17] op_sel_hi:[0,1]
	v_add_f32_e32 v67, 1.0, v67
	v_rcp_f32_e32 v72, v67
	v_mul_f32_e32 v67, 0x3d372713, v71
	v_mul_f32_e32 v67, v71, v67
	v_fma_f32 v67, v71, v67, v71
	v_mul_f32_e32 v67, 0xc0135761, v67
	v_exp_f32_e32 v67, v67
	v_pk_mul_f32 v[8:9], v[0:1], v[8:9] op_sel_hi:[0,1]
	v_pk_mul_f32 v[2:3], v[0:1], v[2:3] op_sel_hi:[0,1]
	v_pk_mul_f32 v[4:5], v[0:1], v[4:5] op_sel_hi:[0,1]
	v_add_f32_e32 v67, 1.0, v67
	v_rcp_f32_e32 v73, v67
	s_nop 0
	v_pk_mul_f32 v[70:71], v[70:71], v[72:73]
	v_mov_b32_e32 v72, v1
	v_mov_b32_e32 v73, v1
	v_pk_mul_f32 v[70:71], v[38:39], v[70:71]
	v_mov_b32_e32 v38, v1
	v_mov_b32_dpp v72, v98 row_ror:2 row_mask:0xf bank_mask:0xf
	v_mov_b32_e32 v39, v1
	v_mov_b32_dpp v73, v99 row_ror:2 row_mask:0xf bank_mask:0xf
	v_mov_b32_dpp v38, v98 row_ror:1 row_mask:0xf bank_mask:0xf
	v_mov_b32_dpp v72, v56 row_shr:2 row_mask:0xf bank_mask:0xf
	v_mov_b32_dpp v39, v99 row_ror:1 row_mask:0xf bank_mask:0xf
	v_mov_b32_dpp v73, v57 row_shr:2 row_mask:0xf bank_mask:0xf
	v_mov_b32_dpp v38, v56 row_shr:1 row_mask:0xf bank_mask:0xf
	v_mov_b32_dpp v39, v57 row_shr:1 row_mask:0xf bank_mask:0xf
	v_pk_fma_f32 v[72:73], v[76:77], v[72:73], v[88:89]
	s_nop 0
	v_pk_fma_f32 v[38:39], v[80:81], v[38:39], v[72:73]
	s_nop 0
	v_pk_fma_f32 v[38:39], v[56:57], v[84:85], v[38:39]
	s_nop 0
	v_mul_f32_e32 v67, 0x3d372713, v38
	v_mul_f32_e32 v67, v38, v67
	v_fma_f32 v67, v38, v67, v38
	v_mul_f32_e32 v67, 0xc0135761, v67
	v_exp_f32_e32 v67, v67
	s_nop 0
	v_add_f32_e32 v67, 1.0, v67
	v_rcp_f32_e32 v72, v67
	v_mul_f32_e32 v67, 0x3d372713, v39
	v_mul_f32_e32 v67, v39, v67
	v_fma_f32 v67, v39, v67, v39
	v_mul_f32_e32 v67, 0xc0135761, v67
	v_exp_f32_e32 v67, v67
	s_nop 0
	v_add_f32_e32 v67, 1.0, v67
	v_rcp_f32_e32 v73, v67
	v_pk_mul_f32 v[30:31], v[66:67], v[30:31] op_sel_hi:[0,1]
	v_pk_mul_f32 v[22:23], v[66:67], v[22:23] op_sel_hi:[0,1]
	v_pk_mul_f32 v[32:33], v[66:67], v[32:33] op_sel_hi:[0,1]
	v_pk_mul_f32 v[38:39], v[38:39], v[72:73]
	v_pk_mul_f32 v[24:25], v[66:67], v[24:25] op_sel_hi:[0,1]
	v_pk_mul_f32 v[72:73], v[40:41], v[38:39]
	v_pk_mul_f32 v[38:39], v[68:69], v[44:45] op_sel_hi:[0,1]
	v_mov_b32_e32 v44, v1
	v_mov_b32_e32 v45, v1
	v_pk_mul_f32 v[40:41], v[68:69], v[42:43] op_sel_hi:[0,1]
	v_mov_b32_e32 v42, v1
	v_mov_b32_dpp v44, v96 row_ror:2 row_mask:0xf bank_mask:0xf
	v_mov_b32_e32 v43, v1
	v_mov_b32_dpp v45, v97 row_ror:2 row_mask:0xf bank_mask:0xf
	v_mov_b32_dpp v42, v96 row_ror:1 row_mask:0xf bank_mask:0xf
	v_mov_b32_dpp v44, v40 row_shr:2 row_mask:0xf bank_mask:0xf
	v_mov_b32_dpp v43, v97 row_ror:1 row_mask:0xf bank_mask:0xf
	v_mov_b32_dpp v45, v41 row_shr:2 row_mask:0xf bank_mask:0xf
	v_mov_b32_dpp v42, v40 row_shr:1 row_mask:0xf bank_mask:0xf
	v_mov_b32_dpp v43, v41 row_shr:1 row_mask:0xf bank_mask:0xf
	v_pk_fma_f32 v[44:45], v[46:47], v[44:45], v[62:63]
	v_pk_mul_f32 v[18:19], v[66:67], v[18:19] op_sel_hi:[0,1]
	v_pk_fma_f32 v[42:43], v[50:51], v[42:43], v[44:45]
	v_pk_mul_f32 v[20:21], v[66:67], v[20:21] op_sel_hi:[0,1]
	v_pk_fma_f32 v[42:43], v[40:41], v[58:59], v[42:43]
	s_nop 0
	v_mul_f32_e32 v44, 0x3d372713, v42
	v_mul_f32_e32 v45, 0x3d372713, v43
	v_mul_f32_e32 v44, v42, v44
	v_mul_f32_e32 v45, v43, v45
	v_fma_f32 v44, v42, v44, v42
	v_fma_f32 v45, v43, v45, v43
	v_mul_f32_e32 v44, 0xc0135761, v44
	v_mul_f32_e32 v45, 0xc0135761, v45
	v_exp_f32_e32 v44, v44
	v_exp_f32_e32 v45, v45
	v_add_f32_e32 v44, 1.0, v44
	v_add_f32_e32 v45, 1.0, v45
	v_rcp_f32_e32 v44, v44
	v_rcp_f32_e32 v45, v45
	s_nop 0
	v_pk_mul_f32 v[42:43], v[42:43], v[44:45]
	v_mov_b32_e32 v44, v1
	v_mov_b32_e32 v45, v1
	v_pk_mul_f32 v[34:35], v[34:35], v[42:43]
	v_mov_b32_e32 v42, v1
	v_mov_b32_dpp v44, v94 row_ror:2 row_mask:0xf bank_mask:0xf
	v_mov_b32_e32 v43, v1
	v_mov_b32_dpp v45, v95 row_ror:2 row_mask:0xf bank_mask:0xf
	v_mov_b32_dpp v42, v94 row_ror:1 row_mask:0xf bank_mask:0xf
	v_mov_b32_dpp v44, v38 row_shr:2 row_mask:0xf bank_mask:0xf
	v_mov_b32_dpp v43, v95 row_ror:1 row_mask:0xf bank_mask:0xf
	v_mov_b32_dpp v45, v39 row_shr:2 row_mask:0xf bank_mask:0xf
	v_mov_b32_dpp v42, v38 row_shr:1 row_mask:0xf bank_mask:0xf
	v_mov_b32_dpp v43, v39 row_shr:1 row_mask:0xf bank_mask:0xf
	v_pk_fma_f32 v[44:45], v[48:49], v[44:45], v[64:65]
	s_nop 0
	v_pk_fma_f32 v[42:43], v[52:53], v[42:43], v[44:45]
	s_nop 0
	v_pk_fma_f32 v[42:43], v[38:39], v[60:61], v[42:43]
	s_nop 0
	v_mul_f32_e32 v44, 0x3d372713, v42
	v_mul_f32_e32 v45, 0x3d372713, v43
	v_mul_f32_e32 v44, v42, v44
	v_mul_f32_e32 v45, v43, v45
	v_fma_f32 v44, v42, v44, v42
	v_fma_f32 v45, v43, v45, v43
	v_mul_f32_e32 v44, 0xc0135761, v44
	v_mul_f32_e32 v45, 0xc0135761, v45
	v_exp_f32_e32 v44, v44
	v_exp_f32_e32 v45, v45
	v_add_f32_e32 v44, 1.0, v44
	v_add_f32_e32 v45, 1.0, v45
	v_rcp_f32_e32 v44, v44
	v_rcp_f32_e32 v45, v45
	s_nop 0
	v_pk_mul_f32 v[42:43], v[42:43], v[44:45]
	s_nop 0
	v_pk_mul_f32 v[36:37], v[36:37], v[42:43]
	v_cvt_pk_bf16_f32 v44, v34, v35
	v_cvt_pk_bf16_f32 v45, v36, v37
	v_add_u32_e32 v36, 0x90, v193
	v_mov_b64_e32 v[34:35], s[16:17]
	v_mad_i64_i32 v[36:37], s[36:37], v36, s2, v[34:35]
	v_cvt_pk_bf16_f32 v42, v70, v71
	v_cvt_pk_bf16_f32 v43, v72, v73
	v_lshl_add_u64 v[36:37], v[36:37], 0, v[148:149]
	global_store_dwordx4 v[36:37], v[42:45], off sc0 sc1
	v_mov_b32_e32 v36, v1
	v_mov_b32_e32 v37, v1
	v_mov_b32_e32 v42, v1
	v_mov_b32_e32 v43, v1
	v_mov_b32_dpp v36, v54 row_ror:1 row_mask:0xf bank_mask:0xf
	v_mov_b32_dpp v42, v54 row_ror:2 row_mask:0xf bank_mask:0xf
	v_mov_b32_dpp v43, v55 row_ror:2 row_mask:0xf bank_mask:0xf
	v_mov_b32_dpp v37, v55 row_ror:1 row_mask:0xf bank_mask:0xf
	v_mov_b32_dpp v42, v30 row_shr:2 row_mask:0xf bank_mask:0xf
	v_mov_b32_dpp v43, v31 row_shr:2 row_mask:0xf bank_mask:0xf
	v_mov_b32_dpp v36, v30 row_shr:1 row_mask:0xf bank_mask:0xf
	v_mov_b32_dpp v37, v31 row_shr:1 row_mask:0xf bank_mask:0xf
	v_pk_fma_f32 v[42:43], v[74:75], v[42:43], v[86:87]
	s_nop 0
	v_pk_fma_f32 v[36:37], v[78:79], v[36:37], v[42:43]
	s_nop 0
	v_pk_fma_f32 v[36:37], v[30:31], v[82:83], v[36:37]
	s_nop 0
	v_mul_f32_e32 v42, 0x3d372713, v36
	v_mul_f32_e32 v43, 0x3d372713, v37
	v_mul_f32_e32 v42, v36, v42
	v_mul_f32_e32 v43, v37, v43
	v_fma_f32 v42, v36, v42, v36
	v_fma_f32 v43, v37, v43, v37
	v_mul_f32_e32 v42, 0xc0135761, v42
	v_mul_f32_e32 v43, 0xc0135761, v43
	v_exp_f32_e32 v42, v42
	v_exp_f32_e32 v43, v43
	v_add_f32_e32 v42, 1.0, v42
	v_add_f32_e32 v43, 1.0, v43
	v_rcp_f32_e32 v42, v42
	v_rcp_f32_e32 v43, v43
	s_nop 0
	v_pk_mul_f32 v[36:37], v[36:37], v[42:43]
	v_mov_b32_e32 v42, v1
	v_mov_b32_e32 v43, v1
	v_pk_mul_f32 v[36:37], v[22:23], v[36:37]
	v_mov_b32_e32 v22, v1
	v_mov_b32_dpp v42, v56 row_ror:2 row_mask:0xf bank_mask:0xf
	v_mov_b32_e32 v23, v1
	v_mov_b32_dpp v43, v57 row_ror:2 row_mask:0xf bank_mask:0xf
	v_mov_b32_dpp v22, v56 row_ror:1 row_mask:0xf bank_mask:0xf
	v_mov_b32_dpp v42, v32 row_shr:2 row_mask:0xf bank_mask:0xf
	v_mov_b32_dpp v23, v57 row_ror:1 row_mask:0xf bank_mask:0xf
	v_mov_b32_dpp v43, v33 row_shr:2 row_mask:0xf bank_mask:0xf
	v_mov_b32_dpp v22, v32 row_shr:1 row_mask:0xf bank_mask:0xf
	v_mov_b32_dpp v23, v33 row_shr:1 row_mask:0xf bank_mask:0xf
	v_pk_fma_f32 v[42:43], v[76:77], v[42:43], v[88:89]
	s_nop 0
	v_pk_fma_f32 v[22:23], v[80:81], v[22:23], v[42:43]
	s_nop 0
	v_pk_fma_f32 v[22:23], v[32:33], v[84:85], v[22:23]
	s_nop 0
	v_mul_f32_e32 v42, 0x3d372713, v22
	v_mul_f32_e32 v43, 0x3d372713, v23
	v_mul_f32_e32 v42, v22, v42
	v_mul_f32_e32 v43, v23, v43
	v_fma_f32 v42, v22, v42, v22
	v_fma_f32 v43, v23, v43, v23
	v_mul_f32_e32 v42, 0xc0135761, v42
	v_mul_f32_e32 v43, 0xc0135761, v43
	v_exp_f32_e32 v42, v42
	v_exp_f32_e32 v43, v43
	v_add_f32_e32 v42, 1.0, v42
	v_add_f32_e32 v43, 1.0, v43
	v_rcp_f32_e32 v42, v42
	v_rcp_f32_e32 v43, v43
	s_nop 0
	v_pk_mul_f32 v[22:23], v[22:23], v[42:43]
	s_nop 0
	v_pk_mul_f32 v[42:43], v[24:25], v[22:23]
	v_pk_mul_f32 v[22:23], v[66:67], v[28:29] op_sel_hi:[0,1]
	v_mov_b32_e32 v28, v1
	v_mov_b32_e32 v29, v1
	v_pk_mul_f32 v[24:25], v[66:67], v[26:27] op_sel_hi:[0,1]
	v_mov_b32_e32 v26, v1
	v_mov_b32_dpp v28, v40 row_ror:2 row_mask:0xf bank_mask:0xf
	v_mov_b32_e32 v27, v1
	v_mov_b32_dpp v29, v41 row_ror:2 row_mask:0xf bank_mask:0xf
	v_mov_b32_dpp v26, v40 row_ror:1 row_mask:0xf bank_mask:0xf
	v_mov_b32_dpp v28, v24 row_shr:2 row_mask:0xf bank_mask:0xf
	v_mov_b32_dpp v27, v41 row_ror:1 row_mask:0xf bank_mask:0xf
	v_mov_b32_dpp v29, v25 row_shr:2 row_mask:0xf bank_mask:0xf
	v_mov_b32_dpp v26, v24 row_shr:1 row_mask:0xf bank_mask:0xf
	v_mov_b32_dpp v27, v25 row_shr:1 row_mask:0xf bank_mask:0xf
	v_pk_fma_f32 v[28:29], v[46:47], v[28:29], v[62:63]
	s_nop 0
	v_pk_fma_f32 v[26:27], v[50:51], v[26:27], v[28:29]
	s_nop 0
	v_pk_fma_f32 v[26:27], v[24:25], v[58:59], v[26:27]
	s_nop 0
	v_mul_f32_e32 v28, 0x3d372713, v26
	v_mul_f32_e32 v29, 0x3d372713, v27
	v_mul_f32_e32 v28, v26, v28
	v_mul_f32_e32 v29, v27, v29
	v_fma_f32 v28, v26, v28, v26
	v_fma_f32 v29, v27, v29, v27
	v_mul_f32_e32 v28, 0xc0135761, v28
	v_mul_f32_e32 v29, 0xc0135761, v29
	v_exp_f32_e32 v28, v28
	v_exp_f32_e32 v29, v29
	v_add_f32_e32 v28, 1.0, v28
	v_add_f32_e32 v29, 1.0, v29
	v_rcp_f32_e32 v28, v28
	v_rcp_f32_e32 v29, v29
	s_nop 0
	v_pk_mul_f32 v[26:27], v[26:27], v[28:29]
	v_mov_b32_e32 v28, v1
	v_mov_b32_e32 v29, v1
	v_pk_mul_f32 v[26:27], v[18:19], v[26:27]
	v_mov_b32_e32 v18, v1
	v_mov_b32_dpp v28, v38 row_ror:2 row_mask:0xf bank_mask:0xf
	v_mov_b32_e32 v19, v1
	v_mov_b32_dpp v29, v39 row_ror:2 row_mask:0xf bank_mask:0xf
	v_mov_b32_dpp v18, v38 row_ror:1 row_mask:0xf bank_mask:0xf
	v_mov_b32_dpp v28, v22 row_shr:2 row_mask:0xf bank_mask:0xf
	v_mov_b32_dpp v19, v39 row_ror:1 row_mask:0xf bank_mask:0xf
	v_mov_b32_dpp v29, v23 row_shr:2 row_mask:0xf bank_mask:0xf
	v_mov_b32_dpp v18, v22 row_shr:1 row_mask:0xf bank_mask:0xf
	v_mov_b32_dpp v19, v23 row_shr:1 row_mask:0xf bank_mask:0xf
	v_pk_fma_f32 v[28:29], v[48:49], v[28:29], v[64:65]
	s_nop 0
	v_pk_fma_f32 v[18:19], v[52:53], v[18:19], v[28:29]
	s_nop 0
	v_pk_fma_f32 v[18:19], v[22:23], v[60:61], v[18:19]
	s_nop 0
	v_mul_f32_e32 v28, 0x3d372713, v18
	v_mul_f32_e32 v29, 0x3d372713, v19
	v_mul_f32_e32 v28, v18, v28
	v_mul_f32_e32 v29, v19, v29
	v_fma_f32 v28, v18, v28, v18
	v_fma_f32 v29, v19, v29, v19
	v_mul_f32_e32 v28, 0xc0135761, v28
	v_mul_f32_e32 v29, 0xc0135761, v29
	v_exp_f32_e32 v28, v28
	v_exp_f32_e32 v29, v29
	v_add_f32_e32 v28, 1.0, v28
	v_add_f32_e32 v29, 1.0, v29
	v_rcp_f32_e32 v28, v28
	v_rcp_f32_e32 v29, v29
	s_nop 0
	v_pk_mul_f32 v[18:19], v[18:19], v[28:29]
	s_nop 0
	v_pk_mul_f32 v[28:29], v[20:21], v[18:19]
	v_cvt_pk_bf16_f32 v20, v26, v27
	v_add_u32_e32 v26, 0xa0, v193
	v_mad_i64_i32 v[26:27], s[36:37], v26, s2, v[34:35]
	v_cvt_pk_bf16_f32 v18, v36, v37
	v_cvt_pk_bf16_f32 v19, v42, v43
	v_cvt_pk_bf16_f32 v21, v28, v29
	v_lshl_add_u64 v[26:27], v[26:27], 0, v[148:149]
	global_store_dwordx4 v[26:27], v[18:21], off sc0 sc1
	s_nop 1
	v_mov_b32_e32 v20, v1
	v_mov_b32_e32 v21, v1
	v_mov_b32_e32 v18, v1
	v_mov_b32_dpp v20, v30 row_ror:2 row_mask:0xf bank_mask:0xf
	v_mov_b32_e32 v19, v1
	v_mov_b32_dpp v21, v31 row_ror:2 row_mask:0xf bank_mask:0xf
	v_mov_b32_dpp v18, v30 row_ror:1 row_mask:0xf bank_mask:0xf
	v_mov_b32_dpp v20, v14 row_shr:2 row_mask:0xf bank_mask:0xf
	v_mov_b32_dpp v19, v31 row_ror:1 row_mask:0xf bank_mask:0xf
	v_mov_b32_dpp v21, v15 row_shr:2 row_mask:0xf bank_mask:0xf
	v_mov_b32_dpp v18, v14 row_shr:1 row_mask:0xf bank_mask:0xf
	v_mov_b32_dpp v19, v15 row_shr:1 row_mask:0xf bank_mask:0xf
	v_pk_fma_f32 v[20:21], v[74:75], v[20:21], v[86:87]
	s_nop 0
	v_pk_fma_f32 v[18:19], v[78:79], v[18:19], v[20:21]
	s_nop 0
	v_pk_fma_f32 v[18:19], v[14:15], v[82:83], v[18:19]
	s_nop 0
	v_mul_f32_e32 v20, 0x3d372713, v18
	v_mul_f32_e32 v21, 0x3d372713, v19
	v_mul_f32_e32 v20, v18, v20
	v_mul_f32_e32 v21, v19, v21
	v_fma_f32 v20, v18, v20, v18
	v_fma_f32 v21, v19, v21, v19
	v_mul_f32_e32 v20, 0xc0135761, v20
	v_mul_f32_e32 v21, 0xc0135761, v21
	v_exp_f32_e32 v20, v20
	v_exp_f32_e32 v21, v21
	v_add_f32_e32 v20, 1.0, v20
	v_add_f32_e32 v21, 1.0, v21
	v_rcp_f32_e32 v20, v20
	v_rcp_f32_e32 v21, v21
	s_nop 0
	v_pk_mul_f32 v[18:19], v[18:19], v[20:21]
	v_mov_b32_e32 v20, v1
	v_mov_b32_e32 v21, v1
	v_pk_mul_f32 v[18:19], v[6:7], v[18:19]
	v_mov_b32_e32 v6, v1
	v_mov_b32_dpp v20, v32 row_ror:2 row_mask:0xf bank_mask:0xf
	v_mov_b32_e32 v7, v1
	v_mov_b32_dpp v21, v33 row_ror:2 row_mask:0xf bank_mask:0xf
	v_mov_b32_dpp v6, v32 row_ror:1 row_mask:0xf bank_mask:0xf
	v_mov_b32_dpp v20, v16 row_shr:2 row_mask:0xf bank_mask:0xf
	v_mov_b32_dpp v7, v33 row_ror:1 row_mask:0xf bank_mask:0xf
	v_mov_b32_dpp v21, v17 row_shr:2 row_mask:0xf bank_mask:0xf
	v_mov_b32_dpp v6, v16 row_shr:1 row_mask:0xf bank_mask:0xf
	v_mov_b32_dpp v7, v17 row_shr:1 row_mask:0xf bank_mask:0xf
	v_pk_fma_f32 v[20:21], v[76:77], v[20:21], v[88:89]
	s_nop 0
	v_pk_fma_f32 v[6:7], v[80:81], v[6:7], v[20:21]
	s_nop 0
	v_pk_fma_f32 v[6:7], v[16:17], v[84:85], v[6:7]
	s_nop 0
	v_mul_f32_e32 v20, 0x3d372713, v6
	v_mul_f32_e32 v21, 0x3d372713, v7
	v_mul_f32_e32 v20, v6, v20
	v_mul_f32_e32 v21, v7, v21
	v_fma_f32 v20, v6, v20, v6
	v_fma_f32 v21, v7, v21, v7
	v_mul_f32_e32 v20, 0xc0135761, v20
	v_mul_f32_e32 v21, 0xc0135761, v21
	v_exp_f32_e32 v20, v20
	v_exp_f32_e32 v21, v21
	v_add_f32_e32 v20, 1.0, v20
	v_add_f32_e32 v21, 1.0, v21
	v_rcp_f32_e32 v20, v20
	v_rcp_f32_e32 v21, v21
	s_nop 0
	v_pk_mul_f32 v[6:7], v[6:7], v[20:21]
	s_nop 0
	v_pk_mul_f32 v[20:21], v[8:9], v[6:7]
	v_pk_mul_f32 v[6:7], v[0:1], v[12:13] op_sel_hi:[0,1]
	v_mov_b32_e32 v12, v1
	v_mov_b32_e32 v13, v1
	v_pk_mul_f32 v[8:9], v[0:1], v[10:11] op_sel_hi:[0,1]
	v_mov_b32_e32 v10, v1
	v_mov_b32_dpp v12, v24 row_ror:2 row_mask:0xf bank_mask:0xf
	v_mov_b32_e32 v11, v1
	v_mov_b32_dpp v13, v25 row_ror:2 row_mask:0xf bank_mask:0xf
	v_mov_b32_dpp v10, v24 row_ror:1 row_mask:0xf bank_mask:0xf
	v_mov_b32_dpp v12, v8 row_shr:2 row_mask:0xf bank_mask:0xf
	v_mov_b32_dpp v11, v25 row_ror:1 row_mask:0xf bank_mask:0xf
	v_mov_b32_dpp v13, v9 row_shr:2 row_mask:0xf bank_mask:0xf
	v_mov_b32_dpp v10, v8 row_shr:1 row_mask:0xf bank_mask:0xf
	v_mov_b32_dpp v11, v9 row_shr:1 row_mask:0xf bank_mask:0xf
	v_pk_fma_f32 v[12:13], v[46:47], v[12:13], v[62:63]
	s_nop 0
	v_pk_fma_f32 v[10:11], v[50:51], v[10:11], v[12:13]
	s_nop 0
	v_pk_fma_f32 v[10:11], v[8:9], v[58:59], v[10:11]
	s_nop 0
	v_mul_f32_e32 v12, 0x3d372713, v10
	v_mul_f32_e32 v13, 0x3d372713, v11
	v_mul_f32_e32 v12, v10, v12
	v_mul_f32_e32 v13, v11, v13
	v_fma_f32 v12, v10, v12, v10
	v_fma_f32 v13, v11, v13, v11
	v_mul_f32_e32 v12, 0xc0135761, v12
	v_mul_f32_e32 v13, 0xc0135761, v13
	v_exp_f32_e32 v12, v12
	v_exp_f32_e32 v13, v13
	v_add_f32_e32 v12, 1.0, v12
	v_add_f32_e32 v13, 1.0, v13
	v_rcp_f32_e32 v12, v12
	v_rcp_f32_e32 v13, v13
	s_nop 0
	v_pk_mul_f32 v[10:11], v[10:11], v[12:13]
	v_mov_b32_e32 v12, v1
	v_mov_b32_e32 v13, v1
	v_pk_mul_f32 v[10:11], v[2:3], v[10:11]
	v_mov_b32_e32 v2, v1
	v_mov_b32_dpp v12, v22 row_ror:2 row_mask:0xf bank_mask:0xf
	v_mov_b32_e32 v3, v1
	v_mov_b32_dpp v13, v23 row_ror:2 row_mask:0xf bank_mask:0xf
	v_mov_b32_dpp v2, v22 row_ror:1 row_mask:0xf bank_mask:0xf
	v_mov_b32_dpp v12, v6 row_shr:2 row_mask:0xf bank_mask:0xf
	v_mov_b32_dpp v3, v23 row_ror:1 row_mask:0xf bank_mask:0xf
	v_mov_b32_dpp v13, v7 row_shr:2 row_mask:0xf bank_mask:0xf
	v_mov_b32_dpp v2, v6 row_shr:1 row_mask:0xf bank_mask:0xf
	v_mov_b32_dpp v3, v7 row_shr:1 row_mask:0xf bank_mask:0xf
	v_pk_fma_f32 v[12:13], v[48:49], v[12:13], v[64:65]
	s_nop 0
	v_pk_fma_f32 v[2:3], v[52:53], v[2:3], v[12:13]
	s_nop 0
	v_pk_fma_f32 v[2:3], v[6:7], v[60:61], v[2:3]
	s_nop 0
	v_mul_f32_e32 v12, 0x3d372713, v2
	v_mul_f32_e32 v0, 0x3d372713, v3
	v_mul_f32_e32 v12, v2, v12
	v_mul_f32_e32 v0, v3, v0
	v_fma_f32 v12, v2, v12, v2
	v_fma_f32 v0, v3, v0, v3
	v_mul_f32_e32 v12, 0xc0135761, v12
	v_mul_f32_e32 v0, 0xc0135761, v0
	v_exp_f32_e32 v12, v12
	v_exp_f32_e32 v0, v0
	v_add_f32_e32 v12, 1.0, v12
	v_add_f32_e32 v0, 1.0, v0
	v_rcp_f32_e32 v12, v12
	v_rcp_f32_e32 v13, v0
	v_add_u32_e32 v0, 0xb0, v193
	v_pk_mul_f32 v[2:3], v[2:3], v[12:13]
	s_nop 0
	v_pk_mul_f32 v[12:13], v[4:5], v[2:3]
	v_cvt_pk_bf16_f32 v4, v10, v11
	v_mad_i64_i32 v[10:11], s[36:37], v0, s2, v[34:35]
	v_cvt_pk_bf16_f32 v2, v18, v19
	v_cvt_pk_bf16_f32 v3, v20, v21
	v_cvt_pk_bf16_f32 v5, v12, v13
	v_lshl_add_u64 v[10:11], v[10:11], 0, v[148:149]
	global_store_dwordx4 v[10:11], v[2:5], off sc0 sc1
	s_and_saveexec_b64 s[36:37], vcc
	s_cbranch_execz .LBB0_372
	v_lshl_add_u64 v[10:11], v[146:147], 0, s[40:41]
	v_cvt_pk_bf16_f32 v5, v6, v7
	v_mov_b64_e32 v[6:7], s[42:43]
	v_mad_u64_u32 v[6:7], s[38:39], v10, s2, v[6:7]
	v_mad_i32_i24 v7, v11, s2, v7
	v_cvt_pk_bf16_f32 v2, v14, v15
	v_cvt_pk_bf16_f32 v3, v16, v17
	v_cvt_pk_bf16_f32 v4, v8, v9
	v_lshl_add_u64 v[6:7], v[182:183], 1, v[6:7]
	global_store_dwordx4 v[6:7], v[2:5], off sc0 sc1

.LBB0_404:
	s_mov_b32 s0, -1
	s_add_u32 s14, s74, 0x2200000
	s_waitcnt vmcnt(0)
	s_barrier
	s_addc_u32 s15, s75, 0
	v_mbcnt_lo_u32_b32 v0, s0, 0
	v_mbcnt_hi_u32_b32 v166, s0, v0
	s_lshl_b32 s0, s88, 8
	v_and_b32_e32 v130, 15, v166
	s_add_i32 s17, s0, s63
	v_or_b32_e32 v156, s17, v130
	s_ashr_i32 s17, s16, 31
	s_lshl_b32 s1, s62, 5
	s_lshl_b64 s[16:17], s[16:17], 8
	v_lshrrev_b32_e32 v0, 1, v166
	s_or_b32 s16, s16, s1
	v_and_b32_e32 v0, 56, v0
	v_and_b32_e32 v131, 64, v231
	v_lshl_add_u64 v[154:155], s[16:17], 0, v[0:1]
	v_xor_b32_e32 v0, 16, v231
	v_add_u32_e32 v131, 64, v131
	v_cmp_lt_i32_e32 vcc, v0, v131
	v_lshlrev_b64 v[178:179], 1, v[154:155]
	s_mov_b64 s[16:17], 0x8800000
	v_cndmask_b32_e32 v0, v231, v0, vcc
	v_lshlrev_b32_e32 v168, 2, v0
	v_xor_b32_e32 v0, 32, v231
	v_cmp_lt_i32_e32 vcc, v0, v131
	v_ashrrev_i32_e32 v157, 31, v156
	v_lshlrev_b64 v[180:181], 11, v[156:157]
	v_cndmask_b32_e32 v0, v231, v0, vcc
	v_lshlrev_b32_e32 v167, 2, v0
	v_or_b32_e32 v0, s63, v130
	v_lshl_add_u64 v[130:131], s[74:75], 0, v[178:179]
	v_lshl_add_u64 v[158:159], v[130:131], 0, s[16:17]
	v_lshl_add_u64 v[130:131], v[158:159], 0, v[180:181]
	global_load_dwordx4 v[170:173], v[130:131], off
	global_load_dwordx4 v[174:177], v[130:131], off offset:256
	v_or_b32_e32 v130, 16, v156
	v_ashrrev_i32_e32 v131, 31, v130
	v_lshlrev_b64 v[164:165], 11, v[130:131]
	v_lshl_add_u64 v[130:131], v[158:159], 0, v[164:165]
	global_load_dwordx4 v[150:153], v[130:131], off
	global_load_dwordx4 v[146:149], v[130:131], off offset:256
	v_or_b32_e32 v130, 32, v156
	v_ashrrev_i32_e32 v131, 31, v130
	v_lshlrev_b64 v[162:163], 11, v[130:131]
	v_lshl_add_u64 v[130:131], v[158:159], 0, v[162:163]
	global_load_dwordx4 v[142:145], v[130:131], off
	global_load_dwordx4 v[138:141], v[130:131], off offset:256
	v_or_b32_e32 v130, 48, v156
	v_ashrrev_i32_e32 v131, 31, v130
	v_lshlrev_b64 v[160:161], 11, v[130:131]
	v_lshl_add_u64 v[130:131], v[158:159], 0, v[160:161]
	global_load_dwordx4 v[134:137], v[130:131], off
	s_nop 0
	global_load_dwordx4 v[130:133], v[130:131], off offset:256
	v_lshl_add_u64 v[180:181], s[14:15], 0, v[180:181]
	v_lshl_add_u64 v[178:179], v[180:181], 0, v[178:179]
	v_cmp_gt_u32_e32 vcc, 16, v166
	s_lshl_b32 s1, s62, 2
	s_waitcnt vmcnt(0)
	v_lshlrev_b32_e32 v182, 16, v170
	v_and_b32_e32 v183, 0xffff0000, v170
	v_lshlrev_b32_e32 v170, 16, v171
	v_and_b32_e32 v171, 0xffff0000, v171
	v_pk_add_f32 v[128:129], v[128:129], v[170:171]
	v_lshlrev_b32_e32 v170, 16, v172
	v_and_b32_e32 v171, 0xffff0000, v172
	v_pk_add_f32 v[170:171], v[122:123], v[170:171]
	v_lshlrev_b32_e32 v122, 16, v173
	v_and_b32_e32 v123, 0xffff0000, v173
	v_pk_add_f32 v[126:127], v[126:127], v[182:183]
	v_pk_add_f32 v[172:173], v[124:125], v[122:123]
	v_cvt_pk_bf16_f32 v122, v126, v127
	v_cvt_pk_bf16_f32 v123, v128, v129
	v_cvt_pk_bf16_f32 v124, v170, v171
	v_cvt_pk_bf16_f32 v125, v172, v173
	global_store_dwordx4 v[178:179], v[122:125], off sc0 sc1
	s_nop 1
	v_pk_mul_f32 v[122:123], v[126:127], v[126:127]
	v_pk_mul_f32 v[126:127], v[170:171], v[170:171]
	v_lshlrev_b32_e32 v170, 16, v174
	v_and_b32_e32 v171, 0xffff0000, v174
	v_pk_add_f32 v[118:119], v[118:119], v[170:171]
	v_lshlrev_b32_e32 v170, 16, v175
	v_and_b32_e32 v171, 0xffff0000, v175
	v_pk_add_f32 v[120:121], v[120:121], v[170:171]
	v_lshlrev_b32_e32 v170, 16, v176
	v_and_b32_e32 v171, 0xffff0000, v176
	v_pk_add_f32 v[170:171], v[114:115], v[170:171]
	v_lshlrev_b32_e32 v114, 16, v177
	v_and_b32_e32 v115, 0xffff0000, v177
	v_pk_mul_f32 v[124:125], v[128:129], v[128:129]
	v_pk_mul_f32 v[128:129], v[172:173], v[172:173]
	v_pk_add_f32 v[172:173], v[116:117], v[114:115]
	v_cvt_pk_bf16_f32 v114, v118, v119
	v_cvt_pk_bf16_f32 v115, v120, v121
	v_cvt_pk_bf16_f32 v116, v170, v171
	v_cvt_pk_bf16_f32 v117, v172, v173
	global_store_dwordx4 v[178:179], v[114:117], off offset:256 sc0 sc1
	s_nop 1
	v_pk_mul_f32 v[114:115], v[118:119], v[118:119]
	v_pk_mul_f32 v[116:117], v[120:121], v[120:121]
	v_add_f32_e32 v114, v114, v115
	v_add_f32_e32 v116, v116, v117
	v_pk_mul_f32 v[118:119], v[170:171], v[170:171]
	v_pk_mul_f32 v[120:121], v[172:173], v[172:173]
	v_add_f32_e32 v114, v114, v116
	v_add_f32_e32 v115, v128, v129
	v_add_f32_e32 v116, v126, v127
	v_add_f32_e32 v120, v120, v121
	v_add_f32_e32 v118, v118, v119
	v_add_f32_e32 v115, v116, v115
	v_add_f32_e32 v116, v124, v125
	v_add_f32_e32 v117, v122, v123
	v_add_f32_e32 v118, v118, v120
	v_add_f32_e32 v116, v117, v116
	v_add_f32_e32 v114, v114, v118
	v_add_f32_e32 v115, v116, v115
	v_add_f32_e32 v114, v115, v114
	ds_bpermute_b32 v115, v168, v114
	s_waitcnt lgkmcnt(0)
	v_add_f32_e32 v114, v114, v115
	ds_bpermute_b32 v115, v167, v114
	s_and_saveexec_b64 s[16:17], vcc
	s_cbranch_execz .LBB0_406
	v_lshl_or_b32 v116, v0, 4, s1
	s_waitcnt lgkmcnt(0)
	v_add_f32_e32 v114, v114, v115
	ds_write_b32 v116, v114
.LBB0_406:
	s_or_b64 exec, exec, s[16:17]
	v_lshlrev_b32_e32 v114, 16, v150
	s_waitcnt lgkmcnt(0)
	v_and_b32_e32 v115, 0xffff0000, v150
	v_pk_add_f32 v[110:111], v[110:111], v[114:115]
	v_lshlrev_b32_e32 v114, 16, v151
	v_and_b32_e32 v115, 0xffff0000, v151
	v_pk_add_f32 v[112:113], v[112:113], v[114:115]
	v_lshlrev_b32_e32 v114, 16, v152
	v_and_b32_e32 v115, 0xffff0000, v152
	v_pk_add_f32 v[114:115], v[106:107], v[114:115]
	v_lshlrev_b32_e32 v106, 16, v153
	v_and_b32_e32 v107, 0xffff0000, v153
	v_pk_add_f32 v[116:117], v[108:109], v[106:107]
	v_lshl_add_u64 v[118:119], s[14:15], 0, v[164:165]
	v_cvt_pk_bf16_f32 v106, v110, v111
	v_cvt_pk_bf16_f32 v107, v112, v113
	v_cvt_pk_bf16_f32 v108, v114, v115
	v_cvt_pk_bf16_f32 v109, v116, v117
	v_lshl_add_u64 v[118:119], v[154:155], 1, v[118:119]
	global_store_dwordx4 v[118:119], v[106:109], off sc0 sc1
	s_nop 1
	v_pk_mul_f32 v[106:107], v[110:111], v[110:111]
	v_pk_mul_f32 v[110:111], v[114:115], v[114:115]
	v_lshlrev_b32_e32 v114, 16, v146
	v_and_b32_e32 v115, 0xffff0000, v146
	v_pk_add_f32 v[102:103], v[102:103], v[114:115]
	v_lshlrev_b32_e32 v114, 16, v147
	v_and_b32_e32 v115, 0xffff0000, v147
	v_pk_add_f32 v[104:105], v[104:105], v[114:115]
	v_lshlrev_b32_e32 v114, 16, v148
	v_and_b32_e32 v115, 0xffff0000, v148
	v_pk_add_f32 v[114:115], v[98:99], v[114:115]
	v_lshlrev_b32_e32 v98, 16, v149
	v_and_b32_e32 v99, 0xffff0000, v149
	v_pk_mul_f32 v[108:109], v[112:113], v[112:113]
	v_pk_mul_f32 v[112:113], v[116:117], v[116:117]
	v_pk_add_f32 v[116:117], v[100:101], v[98:99]
	v_cvt_pk_bf16_f32 v98, v102, v103
	v_cvt_pk_bf16_f32 v99, v104, v105
	v_cvt_pk_bf16_f32 v100, v114, v115
	v_cvt_pk_bf16_f32 v101, v116, v117
	global_store_dwordx4 v[118:119], v[98:101], off offset:256 sc0 sc1
	s_nop 1
	v_pk_mul_f32 v[98:99], v[102:103], v[102:103]
	v_pk_mul_f32 v[100:101], v[104:105], v[104:105]
	v_add_f32_e32 v98, v98, v99
	v_add_f32_e32 v100, v100, v101
	v_pk_mul_f32 v[102:103], v[114:115], v[114:115]
	v_pk_mul_f32 v[104:105], v[116:117], v[116:117]
	v_add_f32_e32 v98, v98, v100
	v_add_f32_e32 v99, v112, v113
	v_add_f32_e32 v100, v110, v111
	v_add_f32_e32 v104, v104, v105
	v_add_f32_e32 v102, v102, v103
	v_add_f32_e32 v99, v100, v99
	v_add_f32_e32 v100, v108, v109
	v_add_f32_e32 v101, v106, v107
	v_add_f32_e32 v102, v102, v104
	v_add_f32_e32 v100, v101, v100
	v_add_f32_e32 v98, v98, v102
	v_add_f32_e32 v99, v100, v99
	v_add_f32_e32 v98, v99, v98
	ds_bpermute_b32 v99, v168, v98
	s_waitcnt lgkmcnt(0)
	v_add_f32_e32 v98, v98, v99
	ds_bpermute_b32 v99, v167, v98
	s_and_saveexec_b64 s[16:17], vcc
	s_mov_b32 s89, 0x2e8ba2e9
	s_mov_b32 s29, 0x47800000
	s_cbranch_execz .LBB0_408
	v_lshl_or_b32 v100, v0, 4, s1
	s_waitcnt lgkmcnt(0)
	v_add_f32_e32 v98, v98, v99
	ds_write_b32 v100, v98 offset:256
.LBB0_408:
	s_or_b64 exec, exec, s[16:17]
	v_lshlrev_b32_e32 v98, 16, v142
	s_waitcnt lgkmcnt(0)
	v_and_b32_e32 v99, 0xffff0000, v142
	v_pk_add_f32 v[94:95], v[94:95], v[98:99]
	v_lshlrev_b32_e32 v98, 16, v143
	v_and_b32_e32 v99, 0xffff0000, v143
	v_pk_add_f32 v[96:97], v[96:97], v[98:99]
	v_lshlrev_b32_e32 v98, 16, v144
	v_and_b32_e32 v99, 0xffff0000, v144
	v_pk_add_f32 v[98:99], v[90:91], v[98:99]
	v_lshlrev_b32_e32 v90, 16, v145
	v_and_b32_e32 v91, 0xffff0000, v145
	v_pk_add_f32 v[100:101], v[92:93], v[90:91]
	v_lshl_add_u64 v[102:103], s[14:15], 0, v[162:163]
	v_cvt_pk_bf16_f32 v90, v94, v95
	v_cvt_pk_bf16_f32 v91, v96, v97
	v_cvt_pk_bf16_f32 v92, v98, v99
	v_cvt_pk_bf16_f32 v93, v100, v101
	v_lshl_add_u64 v[102:103], v[154:155], 1, v[102:103]
	global_store_dwordx4 v[102:103], v[90:93], off sc0 sc1
	s_nop 1
	v_pk_mul_f32 v[90:91], v[94:95], v[94:95]
	v_pk_mul_f32 v[94:95], v[98:99], v[98:99]
	v_lshlrev_b32_e32 v98, 16, v138
	v_and_b32_e32 v99, 0xffff0000, v138
	v_pk_add_f32 v[86:87], v[86:87], v[98:99]
	v_lshlrev_b32_e32 v98, 16, v139
	v_and_b32_e32 v99, 0xffff0000, v139
	v_pk_add_f32 v[88:89], v[88:89], v[98:99]
	v_lshlrev_b32_e32 v98, 16, v140
	v_and_b32_e32 v99, 0xffff0000, v140
	v_pk_add_f32 v[98:99], v[82:83], v[98:99]
	v_lshlrev_b32_e32 v82, 16, v141
	v_and_b32_e32 v83, 0xffff0000, v141
	v_pk_mul_f32 v[92:93], v[96:97], v[96:97]
	v_pk_mul_f32 v[96:97], v[100:101], v[100:101]
	v_pk_add_f32 v[100:101], v[84:85], v[82:83]
	v_cvt_pk_bf16_f32 v82, v86, v87
	v_cvt_pk_bf16_f32 v83, v88, v89
	v_cvt_pk_bf16_f32 v84, v98, v99
	v_cvt_pk_bf16_f32 v85, v100, v101
	global_store_dwordx4 v[102:103], v[82:85], off offset:256 sc0 sc1
	s_nop 1
	v_pk_mul_f32 v[82:83], v[86:87], v[86:87]
	v_pk_mul_f32 v[84:85], v[88:89], v[88:89]
	v_add_f32_e32 v82, v82, v83
	v_add_f32_e32 v84, v84, v85
	v_pk_mul_f32 v[86:87], v[98:99], v[98:99]
	v_pk_mul_f32 v[88:89], v[100:101], v[100:101]
	v_add_f32_e32 v82, v82, v84
	v_add_f32_e32 v83, v96, v97
	v_add_f32_e32 v84, v94, v95
	v_add_f32_e32 v88, v88, v89
	v_add_f32_e32 v86, v86, v87
	v_add_f32_e32 v83, v84, v83
	v_add_f32_e32 v84, v92, v93
	v_add_f32_e32 v85, v90, v91
	v_add_f32_e32 v86, v86, v88
	v_add_f32_e32 v84, v85, v84
	v_add_f32_e32 v82, v82, v86
	v_add_f32_e32 v83, v84, v83
	v_add_f32_e32 v82, v83, v82
	ds_bpermute_b32 v83, v168, v82
	s_waitcnt lgkmcnt(0)
	v_add_f32_e32 v82, v82, v83
	ds_bpermute_b32 v83, v167, v82
	s_and_saveexec_b64 s[16:17], vcc
	s_cbranch_execz .LBB0_410
	v_lshl_or_b32 v84, v0, 4, s1
	s_waitcnt lgkmcnt(0)
	v_add_f32_e32 v82, v82, v83
	ds_write_b32 v84, v82 offset:512
.LBB0_410:
	s_or_b64 exec, exec, s[16:17]
	v_lshlrev_b32_e32 v82, 16, v134
	s_waitcnt lgkmcnt(0)
	v_and_b32_e32 v83, 0xffff0000, v134
	v_pk_add_f32 v[78:79], v[78:79], v[82:83]
	v_lshlrev_b32_e32 v82, 16, v135
	v_and_b32_e32 v83, 0xffff0000, v135
	v_pk_add_f32 v[80:81], v[80:81], v[82:83]
	v_lshlrev_b32_e32 v82, 16, v136
	v_and_b32_e32 v83, 0xffff0000, v136
	v_pk_add_f32 v[82:83], v[74:75], v[82:83]
	v_lshlrev_b32_e32 v74, 16, v137
	v_and_b32_e32 v75, 0xffff0000, v137
	v_pk_add_f32 v[84:85], v[76:77], v[74:75]
	v_lshl_add_u64 v[86:87], s[14:15], 0, v[160:161]
	v_cvt_pk_bf16_f32 v74, v78, v79
	v_cvt_pk_bf16_f32 v75, v80, v81
	v_cvt_pk_bf16_f32 v76, v82, v83
	v_cvt_pk_bf16_f32 v77, v84, v85
	v_lshl_add_u64 v[86:87], v[154:155], 1, v[86:87]
	global_store_dwordx4 v[86:87], v[74:77], off sc0 sc1
	s_nop 1
	v_pk_mul_f32 v[74:75], v[78:79], v[78:79]
	v_pk_mul_f32 v[78:79], v[82:83], v[82:83]
	v_lshlrev_b32_e32 v82, 16, v130
	v_and_b32_e32 v83, 0xffff0000, v130
	v_pk_add_f32 v[70:71], v[70:71], v[82:83]
	v_lshlrev_b32_e32 v82, 16, v131
	v_and_b32_e32 v83, 0xffff0000, v131
	v_pk_add_f32 v[72:73], v[72:73], v[82:83]
	v_lshlrev_b32_e32 v82, 16, v132
	v_and_b32_e32 v83, 0xffff0000, v132
	v_pk_add_f32 v[82:83], v[66:67], v[82:83]
	v_lshlrev_b32_e32 v66, 16, v133
	v_and_b32_e32 v67, 0xffff0000, v133
	v_pk_mul_f32 v[76:77], v[80:81], v[80:81]
	v_pk_mul_f32 v[80:81], v[84:85], v[84:85]
	v_pk_add_f32 v[84:85], v[68:69], v[66:67]
	v_cvt_pk_bf16_f32 v66, v70, v71
	v_cvt_pk_bf16_f32 v67, v72, v73
	v_cvt_pk_bf16_f32 v68, v82, v83
	v_cvt_pk_bf16_f32 v69, v84, v85
	global_store_dwordx4 v[86:87], v[66:69], off offset:256 sc0 sc1
	s_nop 1
	v_pk_mul_f32 v[66:67], v[70:71], v[70:71]
	v_pk_mul_f32 v[68:69], v[72:73], v[72:73]
	v_add_f32_e32 v66, v66, v67
	v_add_f32_e32 v68, v68, v69
	v_pk_mul_f32 v[70:71], v[82:83], v[82:83]
	v_pk_mul_f32 v[72:73], v[84:85], v[84:85]
	v_add_f32_e32 v66, v66, v68
	v_add_f32_e32 v67, v80, v81
	v_add_f32_e32 v68, v78, v79
	v_add_f32_e32 v72, v72, v73
	v_add_f32_e32 v70, v70, v71
	v_add_f32_e32 v67, v68, v67
	v_add_f32_e32 v68, v76, v77
	v_add_f32_e32 v69, v74, v75
	v_add_f32_e32 v70, v70, v72
	v_add_f32_e32 v68, v69, v68
	v_add_f32_e32 v66, v66, v70
	v_add_f32_e32 v67, v68, v67
	v_add_f32_e32 v66, v67, v66
	ds_bpermute_b32 v67, v168, v66
	s_waitcnt lgkmcnt(0)
	v_add_f32_e32 v66, v66, v67
	ds_bpermute_b32 v67, v167, v66
	s_and_saveexec_b64 s[16:17], vcc
	s_cbranch_execz .LBB0_412
	v_lshl_or_b32 v68, v0, 4, s1
	s_waitcnt lgkmcnt(0)
	v_add_f32_e32 v66, v66, v67
	ds_write_b32 v68, v66 offset:768
.LBB0_412:
	s_or_b64 exec, exec, s[16:17]
	s_waitcnt lgkmcnt(0)
	v_lshlrev_b64 v[66:67], 11, v[156:157]
	v_lshl_add_u64 v[104:105], v[66:67], 0, s[20:21]
	v_lshl_add_u64 v[68:69], v[158:159], 0, v[104:105]
	global_load_dwordx4 v[96:99], v[68:69], off
	global_load_dwordx4 v[100:103], v[68:69], off offset:256
	s_mov_b64 s[16:17], 0x48000
	v_lshl_add_u64 v[94:95], v[66:67], 0, s[16:17]
	s_mov_b64 s[16:17], 0x58000
	v_lshl_add_u64 v[68:69], v[158:159], 0, v[94:95]
	v_lshl_add_u64 v[92:93], v[66:67], 0, s[22:23]
	v_lshl_add_u64 v[90:91], v[66:67], 0, s[16:17]
	global_load_dwordx4 v[86:89], v[68:69], off
	global_load_dwordx4 v[82:85], v[68:69], off offset:256
	v_lshl_add_u64 v[68:69], v[158:159], 0, v[92:93]
	v_lshl_add_u64 v[66:67], v[158:159], 0, v[90:91]
	global_load_dwordx4 v[78:81], v[68:69], off
	global_load_dwordx4 v[74:77], v[68:69], off offset:256
	global_load_dwordx4 v[70:73], v[66:67], off
	s_nop 0
	global_load_dwordx4 v[66:69], v[66:67], off offset:256
	v_lshl_add_u64 v[104:105], s[14:15], 0, v[104:105]
	v_lshl_add_u64 v[104:105], v[154:155], 1, v[104:105]
	s_waitcnt vmcnt(7)
	v_lshlrev_b32_e32 v106, 16, v96
	v_and_b32_e32 v107, 0xffff0000, v96
	v_lshlrev_b32_e32 v96, 16, v97
	v_and_b32_e32 v97, 0xffff0000, v97
	v_pk_add_f32 v[64:65], v[64:65], v[96:97]
	v_lshlrev_b32_e32 v96, 16, v98
	v_and_b32_e32 v97, 0xffff0000, v98
	v_pk_add_f32 v[96:97], v[58:59], v[96:97]
	v_lshlrev_b32_e32 v58, 16, v99
	v_and_b32_e32 v59, 0xffff0000, v99
	v_pk_add_f32 v[62:63], v[62:63], v[106:107]
	v_pk_add_f32 v[98:99], v[60:61], v[58:59]
	v_cvt_pk_bf16_f32 v58, v62, v63
	v_cvt_pk_bf16_f32 v59, v64, v65
	v_cvt_pk_bf16_f32 v60, v96, v97
	v_cvt_pk_bf16_f32 v61, v98, v99
	global_store_dwordx4 v[104:105], v[58:61], off sc0 sc1
	s_nop 1
	v_pk_mul_f32 v[58:59], v[62:63], v[62:63]
	v_pk_mul_f32 v[62:63], v[96:97], v[96:97]
	s_waitcnt vmcnt(7)
	v_lshlrev_b32_e32 v96, 16, v100
	v_and_b32_e32 v97, 0xffff0000, v100
	v_pk_add_f32 v[54:55], v[54:55], v[96:97]
	v_lshlrev_b32_e32 v96, 16, v101
	v_and_b32_e32 v97, 0xffff0000, v101
	v_pk_add_f32 v[56:57], v[56:57], v[96:97]
	v_lshlrev_b32_e32 v96, 16, v102
	v_and_b32_e32 v97, 0xffff0000, v102
	v_pk_add_f32 v[96:97], v[50:51], v[96:97]
	v_lshlrev_b32_e32 v50, 16, v103
	v_and_b32_e32 v51, 0xffff0000, v103
	v_pk_mul_f32 v[60:61], v[64:65], v[64:65]
	v_pk_mul_f32 v[64:65], v[98:99], v[98:99]
	v_pk_add_f32 v[98:99], v[52:53], v[50:51]
	v_cvt_pk_bf16_f32 v50, v54, v55
	v_cvt_pk_bf16_f32 v51, v56, v57
	v_cvt_pk_bf16_f32 v52, v96, v97
	v_cvt_pk_bf16_f32 v53, v98, v99
	global_store_dwordx4 v[104:105], v[50:53], off offset:256 sc0 sc1
	s_nop 1
	v_pk_mul_f32 v[50:51], v[54:55], v[54:55]
	v_pk_mul_f32 v[52:53], v[56:57], v[56:57]
	v_add_f32_e32 v50, v50, v51
	v_add_f32_e32 v52, v52, v53
	v_pk_mul_f32 v[54:55], v[96:97], v[96:97]
	v_pk_mul_f32 v[56:57], v[98:99], v[98:99]
	v_add_f32_e32 v50, v50, v52
	v_add_f32_e32 v51, v64, v65
	v_add_f32_e32 v52, v62, v63
	v_add_f32_e32 v56, v56, v57
	v_add_f32_e32 v54, v54, v55
	v_add_f32_e32 v51, v52, v51
	v_add_f32_e32 v52, v60, v61
	v_add_f32_e32 v53, v58, v59
	v_add_f32_e32 v54, v54, v56
	v_add_f32_e32 v52, v53, v52
	v_add_f32_e32 v50, v50, v54
	v_add_f32_e32 v51, v52, v51
	v_add_f32_e32 v50, v51, v50
	ds_bpermute_b32 v51, v168, v50
	s_waitcnt lgkmcnt(0)
	v_add_f32_e32 v50, v50, v51
	ds_bpermute_b32 v51, v167, v50
	s_and_saveexec_b64 s[16:17], vcc
	s_cbranch_execz .LBB0_414
	v_lshl_or_b32 v52, v0, 4, s1
	s_waitcnt lgkmcnt(0)
	v_add_f32_e32 v50, v50, v51
	ds_write_b32 v52, v50 offset:2048
.LBB0_414:
	s_or_b64 exec, exec, s[16:17]
	s_waitcnt vmcnt(7)
	v_lshlrev_b32_e32 v50, 16, v86
	s_waitcnt lgkmcnt(0)
	v_and_b32_e32 v51, 0xffff0000, v86
	v_pk_add_f32 v[46:47], v[46:47], v[50:51]
	v_lshlrev_b32_e32 v50, 16, v87
	v_and_b32_e32 v51, 0xffff0000, v87
	v_pk_add_f32 v[48:49], v[48:49], v[50:51]
	v_lshlrev_b32_e32 v50, 16, v88
	v_and_b32_e32 v51, 0xffff0000, v88
	v_pk_add_f32 v[50:51], v[42:43], v[50:51]
	v_lshlrev_b32_e32 v42, 16, v89
	v_and_b32_e32 v43, 0xffff0000, v89
	v_pk_add_f32 v[52:53], v[44:45], v[42:43]
	v_lshl_add_u64 v[54:55], s[14:15], 0, v[94:95]
	v_cvt_pk_bf16_f32 v42, v46, v47
	v_cvt_pk_bf16_f32 v43, v48, v49
	v_cvt_pk_bf16_f32 v44, v50, v51
	v_cvt_pk_bf16_f32 v45, v52, v53
	v_lshl_add_u64 v[54:55], v[154:155], 1, v[54:55]
	global_store_dwordx4 v[54:55], v[42:45], off sc0 sc1
	s_nop 1
	v_pk_mul_f32 v[42:43], v[46:47], v[46:47]
	v_pk_mul_f32 v[46:47], v[50:51], v[50:51]
	s_waitcnt vmcnt(7)
	v_lshlrev_b32_e32 v50, 16, v82
	v_and_b32_e32 v51, 0xffff0000, v82
	v_pk_add_f32 v[38:39], v[38:39], v[50:51]
	v_lshlrev_b32_e32 v50, 16, v83
	v_and_b32_e32 v51, 0xffff0000, v83
	v_pk_add_f32 v[40:41], v[40:41], v[50:51]
	v_lshlrev_b32_e32 v50, 16, v84
	v_and_b32_e32 v51, 0xffff0000, v84
	v_pk_add_f32 v[50:51], v[34:35], v[50:51]
	v_lshlrev_b32_e32 v34, 16, v85
	v_and_b32_e32 v35, 0xffff0000, v85
	v_pk_mul_f32 v[44:45], v[48:49], v[48:49]
	v_pk_mul_f32 v[48:49], v[52:53], v[52:53]
	v_pk_add_f32 v[52:53], v[36:37], v[34:35]
	v_cvt_pk_bf16_f32 v34, v38, v39
	v_cvt_pk_bf16_f32 v35, v40, v41
	v_cvt_pk_bf16_f32 v36, v50, v51
	v_cvt_pk_bf16_f32 v37, v52, v53
	global_store_dwordx4 v[54:55], v[34:37], off offset:256 sc0 sc1
	s_nop 1
	v_pk_mul_f32 v[34:35], v[38:39], v[38:39]
	v_pk_mul_f32 v[36:37], v[40:41], v[40:41]
	v_add_f32_e32 v34, v34, v35
	v_add_f32_e32 v36, v36, v37
	v_pk_mul_f32 v[38:39], v[50:51], v[50:51]
	v_pk_mul_f32 v[40:41], v[52:53], v[52:53]
	v_add_f32_e32 v34, v34, v36
	v_add_f32_e32 v35, v48, v49
	v_add_f32_e32 v36, v46, v47
	v_add_f32_e32 v40, v40, v41
	v_add_f32_e32 v38, v38, v39
	v_add_f32_e32 v35, v36, v35
	v_add_f32_e32 v36, v44, v45
	v_add_f32_e32 v37, v42, v43
	v_add_f32_e32 v38, v38, v40
	v_add_f32_e32 v36, v37, v36
	v_add_f32_e32 v34, v34, v38
	v_add_f32_e32 v35, v36, v35
	v_add_f32_e32 v34, v35, v34
	ds_bpermute_b32 v35, v168, v34
	s_waitcnt lgkmcnt(0)
	v_add_f32_e32 v34, v34, v35
	ds_bpermute_b32 v35, v167, v34
	s_and_saveexec_b64 s[16:17], vcc
	s_cbranch_execz .LBB0_416
	v_lshl_or_b32 v36, v0, 4, s1
	s_waitcnt lgkmcnt(0)
	v_add_f32_e32 v34, v34, v35
	ds_write_b32 v36, v34 offset:2304
.LBB0_416:
	s_or_b64 exec, exec, s[16:17]
	s_waitcnt vmcnt(7)
	v_lshlrev_b32_e32 v34, 16, v78
	s_waitcnt lgkmcnt(0)
	v_and_b32_e32 v35, 0xffff0000, v78
	v_pk_add_f32 v[30:31], v[30:31], v[34:35]
	v_lshlrev_b32_e32 v34, 16, v79
	v_and_b32_e32 v35, 0xffff0000, v79
	v_pk_add_f32 v[32:33], v[32:33], v[34:35]
	v_lshlrev_b32_e32 v34, 16, v80
	v_and_b32_e32 v35, 0xffff0000, v80
	v_pk_add_f32 v[34:35], v[26:27], v[34:35]
	v_lshlrev_b32_e32 v26, 16, v81
	v_and_b32_e32 v27, 0xffff0000, v81
	v_pk_add_f32 v[36:37], v[28:29], v[26:27]
	v_lshl_add_u64 v[38:39], s[14:15], 0, v[92:93]
	v_cvt_pk_bf16_f32 v26, v30, v31
	v_cvt_pk_bf16_f32 v27, v32, v33
	v_cvt_pk_bf16_f32 v28, v34, v35
	v_cvt_pk_bf16_f32 v29, v36, v37
	v_lshl_add_u64 v[38:39], v[154:155], 1, v[38:39]
	global_store_dwordx4 v[38:39], v[26:29], off sc0 sc1
	s_nop 1
	v_pk_mul_f32 v[26:27], v[30:31], v[30:31]
	v_pk_mul_f32 v[30:31], v[34:35], v[34:35]
	s_waitcnt vmcnt(7)
	v_lshlrev_b32_e32 v34, 16, v74
	v_and_b32_e32 v35, 0xffff0000, v74
	v_pk_add_f32 v[22:23], v[22:23], v[34:35]
	v_lshlrev_b32_e32 v34, 16, v75
	v_and_b32_e32 v35, 0xffff0000, v75
	v_pk_add_f32 v[24:25], v[24:25], v[34:35]
	v_lshlrev_b32_e32 v34, 16, v76
	v_and_b32_e32 v35, 0xffff0000, v76
	v_pk_add_f32 v[34:35], v[18:19], v[34:35]
	v_lshlrev_b32_e32 v18, 16, v77
	v_and_b32_e32 v19, 0xffff0000, v77
	v_pk_mul_f32 v[28:29], v[32:33], v[32:33]
	v_pk_mul_f32 v[32:33], v[36:37], v[36:37]
	v_pk_add_f32 v[36:37], v[20:21], v[18:19]
	v_cvt_pk_bf16_f32 v18, v22, v23
	v_cvt_pk_bf16_f32 v19, v24, v25
	v_cvt_pk_bf16_f32 v20, v34, v35
	v_cvt_pk_bf16_f32 v21, v36, v37
	global_store_dwordx4 v[38:39], v[18:21], off offset:256 sc0 sc1
	s_nop 1
	v_pk_mul_f32 v[18:19], v[22:23], v[22:23]
	v_pk_mul_f32 v[20:21], v[24:25], v[24:25]
	v_add_f32_e32 v18, v18, v19
	v_add_f32_e32 v20, v20, v21
	v_pk_mul_f32 v[22:23], v[34:35], v[34:35]
	v_pk_mul_f32 v[24:25], v[36:37], v[36:37]
	v_add_f32_e32 v18, v18, v20
	v_add_f32_e32 v19, v32, v33
	v_add_f32_e32 v20, v30, v31
	v_add_f32_e32 v24, v24, v25
	v_add_f32_e32 v22, v22, v23
	v_add_f32_e32 v19, v20, v19
	v_add_f32_e32 v20, v28, v29
	v_add_f32_e32 v21, v26, v27
	v_add_f32_e32 v22, v22, v24
	v_add_f32_e32 v20, v21, v20
	v_add_f32_e32 v18, v18, v22
	v_add_f32_e32 v19, v20, v19
	v_add_f32_e32 v18, v19, v18
	ds_bpermute_b32 v19, v168, v18
	s_waitcnt lgkmcnt(0)
	v_add_f32_e32 v18, v18, v19
	ds_bpermute_b32 v19, v167, v18
	s_and_saveexec_b64 s[16:17], vcc
	s_cbranch_execz .LBB0_418
	v_lshl_or_b32 v20, v0, 4, s1
	s_waitcnt lgkmcnt(0)
	v_add_f32_e32 v18, v18, v19
	ds_write_b32 v20, v18 offset:2560
.LBB0_418:
	s_or_b64 exec, exec, s[16:17]
	s_waitcnt vmcnt(7)
	v_lshlrev_b32_e32 v18, 16, v70
	s_waitcnt lgkmcnt(0)
	v_and_b32_e32 v19, 0xffff0000, v70
	v_pk_add_f32 v[14:15], v[14:15], v[18:19]
	v_lshlrev_b32_e32 v18, 16, v71
	v_and_b32_e32 v19, 0xffff0000, v71
	v_pk_add_f32 v[16:17], v[16:17], v[18:19]
	v_lshlrev_b32_e32 v18, 16, v72
	v_and_b32_e32 v19, 0xffff0000, v72
	v_pk_add_f32 v[18:19], v[10:11], v[18:19]
	v_lshlrev_b32_e32 v10, 16, v73
	v_and_b32_e32 v11, 0xffff0000, v73
	v_pk_add_f32 v[20:21], v[12:13], v[10:11]
	v_lshl_add_u64 v[22:23], s[14:15], 0, v[90:91]
	v_cvt_pk_bf16_f32 v10, v14, v15
	v_cvt_pk_bf16_f32 v11, v16, v17
	v_cvt_pk_bf16_f32 v12, v18, v19
	v_cvt_pk_bf16_f32 v13, v20, v21
	v_lshl_add_u64 v[22:23], v[154:155], 1, v[22:23]
	global_store_dwordx4 v[22:23], v[10:13], off sc0 sc1
	s_nop 1
	v_pk_mul_f32 v[10:11], v[14:15], v[14:15]
	v_pk_mul_f32 v[14:15], v[18:19], v[18:19]
	s_waitcnt vmcnt(7)
	v_lshlrev_b32_e32 v18, 16, v66
	v_and_b32_e32 v19, 0xffff0000, v66
	v_pk_add_f32 v[6:7], v[6:7], v[18:19]
	v_lshlrev_b32_e32 v18, 16, v67
	v_and_b32_e32 v19, 0xffff0000, v67
	v_pk_add_f32 v[8:9], v[8:9], v[18:19]
	v_lshlrev_b32_e32 v18, 16, v68
	v_and_b32_e32 v19, 0xffff0000, v68
	v_pk_add_f32 v[18:19], v[2:3], v[18:19]
	v_lshlrev_b32_e32 v2, 16, v69
	v_and_b32_e32 v3, 0xffff0000, v69
	v_pk_mul_f32 v[12:13], v[16:17], v[16:17]
	v_pk_mul_f32 v[16:17], v[20:21], v[20:21]
	v_pk_add_f32 v[20:21], v[4:5], v[2:3]
	v_cvt_pk_bf16_f32 v2, v6, v7
	v_cvt_pk_bf16_f32 v3, v8, v9
	v_cvt_pk_bf16_f32 v4, v18, v19
	v_cvt_pk_bf16_f32 v5, v20, v21
	global_store_dwordx4 v[22:23], v[2:5], off offset:256 sc0 sc1
	s_nop 1
	v_pk_mul_f32 v[2:3], v[6:7], v[6:7]
	v_pk_mul_f32 v[4:5], v[8:9], v[8:9]
	v_add_f32_e32 v2, v2, v3
	v_add_f32_e32 v4, v4, v5
	v_pk_mul_f32 v[6:7], v[18:19], v[18:19]
	v_pk_mul_f32 v[8:9], v[20:21], v[20:21]
	v_add_f32_e32 v2, v2, v4
	v_add_f32_e32 v3, v16, v17
	v_add_f32_e32 v4, v14, v15
	v_add_f32_e32 v8, v8, v9
	v_add_f32_e32 v6, v6, v7
	v_add_f32_e32 v3, v4, v3
	v_add_f32_e32 v4, v12, v13
	v_add_f32_e32 v5, v10, v11
	v_add_f32_e32 v6, v6, v8
	v_add_f32_e32 v4, v5, v4
	v_add_f32_e32 v2, v2, v6
	v_add_f32_e32 v3, v4, v3
	v_add_f32_e32 v2, v3, v2
	ds_bpermute_b32 v3, v168, v2
	s_waitcnt lgkmcnt(0)
	v_add_f32_e32 v2, v2, v3
	ds_bpermute_b32 v3, v167, v2
	s_and_saveexec_b64 s[14:15], vcc
	s_cbranch_execz .LBB0_420
	v_lshl_or_b32 v0, v0, 4, s1
	s_waitcnt lgkmcnt(0)
	v_add_f32_e32 v2, v2, v3
	ds_write_b32 v0, v2 offset:2816

.LBB0_478:
	s_or_b64 exec, exec, s[14:15]
	s_lshl_b32 s14, s34, 8
	s_add_i32 s14, s14, s1
	s_ashr_i32 s1, s0, 31
	s_waitcnt lgkmcnt(0)
	s_barrier
	s_lshl_b64 s[0:1], s[0:1], 9
	s_add_u32 s0, s74, s0
	ds_read_b128 v[136:139], v192 offset:4096
	v_or_b32_e32 v130, s14, v193
	s_addc_u32 s1, s75, s1
	s_lshl_b32 s14, s31, 6
	s_add_u32 s0, s0, s14
	s_addc_u32 s1, s1, 0
	v_and_b32_e32 v0, 0x70, v0
	s_waitcnt lgkmcnt(1)
	v_lshl_add_u64 v[18:19], s[0:1], 0, v[0:1]
	s_mov_b64 s[0:1], 0xa800000
	v_lshl_add_u64 v[134:135], v[18:19], 0, s[0:1]
	s_waitcnt lgkmcnt(0)
	v_mov_b32_e32 v18, v137
	v_mov_b32_e32 v19, v138
	v_mov_b32_e32 v137, v139
	v_pk_add_f32 v[18:19], v[18:19], v[136:137]
	s_nop 0
	v_add_f32_e32 v0, v18, v19
	v_div_scale_f32 v18, s[0:1], v0, v0, 1.0
	v_rcp_f32_e32 v19, v18
	s_nop 0
	v_fma_f32 v131, -v18, v19, 1.0
	v_fmac_f32_e32 v19, v131, v19
	v_div_scale_f32 v131, vcc, 1.0, v0, 1.0
	v_mul_f32_e32 v136, v131, v19
	v_fma_f32 v137, -v18, v136, v131
	v_fmac_f32_e32 v136, v137, v19
	v_fma_f32 v18, -v18, v136, v131
	v_div_fmas_f32 v18, v18, v19, v136
	v_div_fixup_f32 v0, v18, v0, 1.0
	v_ashrrev_i32_e32 v131, 31, v130
	v_lshlrev_b64 v[18:19], 11, v[130:131]
	v_pk_mul_f32 v[118:119], v[118:119], v[0:1] op_sel_hi:[1,0]
	v_pk_mul_f32 v[116:117], v[116:117], v[0:1] op_sel_hi:[1,0]
	v_pk_mul_f32 v[122:123], v[122:123], v[0:1] op_sel_hi:[1,0]
	v_pk_mul_f32 v[120:121], v[120:121], v[0:1] op_sel_hi:[1,0]
	v_lshl_add_u64 v[18:19], v[134:135], 0, v[18:19]
	v_cvt_pk_bf16_f32 v116, v116, v117
	v_cvt_pk_bf16_f32 v117, v118, v119
	v_cvt_pk_bf16_f32 v118, v120, v121
	v_cvt_pk_bf16_f32 v119, v122, v123
	global_store_dwordx4 v[18:19], v[116:119], off sc0 sc1
	v_pk_mul_f32 v[120:121], v[132:133], v[0:1] op_sel_hi:[1,0]
	v_pk_mul_f32 v[122:123], v[128:129], v[0:1] op_sel_hi:[1,0]
	v_pk_mul_f32 v[118:119], v[126:127], v[0:1] op_sel_hi:[1,0]
	v_pk_mul_f32 v[116:117], v[124:125], v[0:1] op_sel_hi:[1,0]
	s_nop 0
	v_cvt_pk_bf16_f32 v116, v116, v117
	v_cvt_pk_bf16_f32 v117, v118, v119
	v_cvt_pk_bf16_f32 v118, v122, v123
	v_cvt_pk_bf16_f32 v119, v120, v121
	global_store_dwordx4 v[18:19], v[116:119], off offset:256 sc0 sc1
	ds_read_b128 v[116:119], v192 offset:4352
	s_waitcnt lgkmcnt(0)
	v_mov_b32_e32 v120, v117
	v_mov_b32_e32 v121, v118
	v_mov_b32_e32 v117, v119
	v_pk_add_f32 v[116:117], v[120:121], v[116:117]
	s_nop 0
	v_add_f32_e32 v0, v116, v117
	v_div_scale_f32 v116, s[0:1], v0, v0, 1.0
	v_rcp_f32_e32 v117, v116
	s_nop 0
	v_fma_f32 v118, -v116, v117, 1.0
	v_fmac_f32_e32 v117, v118, v117
	v_div_scale_f32 v118, vcc, 1.0, v0, 1.0
	v_mul_f32_e32 v119, v118, v117
	v_fma_f32 v120, -v116, v119, v118
	v_fmac_f32_e32 v119, v120, v117
	v_fma_f32 v116, -v116, v119, v118
	v_div_fmas_f32 v116, v116, v117, v119
	v_div_fixup_f32 v0, v116, v0, 1.0
	v_or_b32_e32 v116, 16, v130
	v_ashrrev_i32_e32 v117, 31, v116
	v_lshlrev_b64 v[116:117], 11, v[116:117]
	v_pk_mul_f32 v[94:95], v[94:95], v[0:1] op_sel_hi:[1,0]
	v_pk_mul_f32 v[84:85], v[84:85], v[0:1] op_sel_hi:[1,0]
	v_pk_mul_f32 v[90:91], v[90:91], v[0:1] op_sel_hi:[1,0]
	v_lshl_add_u64 v[120:121], v[134:135], 0, v[116:117]
	v_cvt_pk_bf16_f32 v116, v84, v85
	v_cvt_pk_bf16_f32 v117, v94, v95
	v_cvt_pk_bf16_f32 v118, v90, v91
	v_pk_mul_f32 v[84:85], v[98:99], v[0:1] op_sel_hi:[1,0]
	v_pk_mul_f32 v[88:89], v[88:89], v[0:1] op_sel_hi:[1,0]
	v_pk_mul_f32 v[94:95], v[108:109], v[0:1] op_sel_hi:[1,0]
	v_pk_mul_f32 v[90:91], v[104:105], v[0:1] op_sel_hi:[1,0]
	v_cvt_pk_bf16_f32 v88, v88, v89
	v_cvt_pk_bf16_f32 v89, v84, v85
	v_cvt_pk_bf16_f32 v90, v90, v91
	v_cvt_pk_bf16_f32 v91, v94, v95
	global_store_dwordx4 v[120:121], v[88:91], off offset:256 sc0 sc1
	ds_read_b128 v[88:91], v192 offset:4608
	v_pk_mul_f32 v[100:101], v[100:101], v[0:1] op_sel_hi:[1,0]
	s_waitcnt lgkmcnt(0)
	v_mov_b32_e32 v84, v89
	v_mov_b32_e32 v85, v90
	v_mov_b32_e32 v89, v91
	v_pk_add_f32 v[84:85], v[84:85], v[88:89]
	v_cvt_pk_bf16_f32 v119, v100, v101
	v_add_f32_e32 v0, v84, v85
	v_div_scale_f32 v84, s[0:1], v0, v0, 1.0
	v_rcp_f32_e32 v85, v84
	global_store_dwordx4 v[120:121], v[116:119], off sc0 sc1
	v_fma_f32 v88, -v84, v85, 1.0
	v_fmac_f32_e32 v85, v88, v85
	v_div_scale_f32 v88, vcc, 1.0, v0, 1.0
	v_mul_f32_e32 v89, v88, v85
	v_fma_f32 v90, -v84, v89, v88
	v_fmac_f32_e32 v89, v90, v85
	v_fma_f32 v84, -v84, v89, v88
	v_div_fmas_f32 v84, v84, v85, v89
	v_div_fixup_f32 v0, v84, v0, 1.0
	v_or_b32_e32 v84, 32, v130
	v_ashrrev_i32_e32 v85, 31, v84
	v_lshlrev_b64 v[84:85], 11, v[84:85]
	v_lshl_add_u64 v[88:89], v[134:135], 0, v[84:85]
	v_pk_mul_f32 v[90:91], v[92:93], v[0:1] op_sel_hi:[1,0]
	v_pk_mul_f32 v[84:85], v[86:87], v[0:1] op_sel_hi:[1,0]
	v_pk_mul_f32 v[92:93], v[102:103], v[0:1] op_sel_hi:[1,0]
	v_pk_mul_f32 v[86:87], v[96:97], v[0:1] op_sel_hi:[1,0]
	v_cvt_pk_bf16_f32 v84, v84, v85
	v_cvt_pk_bf16_f32 v85, v90, v91
	v_cvt_pk_bf16_f32 v86, v86, v87
	v_cvt_pk_bf16_f32 v87, v92, v93
	global_store_dwordx4 v[88:89], v[84:87], off sc0 sc1
	v_pk_mul_f32 v[90:91], v[114:115], v[0:1] op_sel_hi:[1,0]
	v_pk_mul_f32 v[92:93], v[112:113], v[0:1] op_sel_hi:[1,0]
	v_pk_mul_f32 v[86:87], v[110:111], v[0:1] op_sel_hi:[1,0]
	v_pk_mul_f32 v[84:85], v[106:107], v[0:1] op_sel_hi:[1,0]
	s_nop 0
	v_cvt_pk_bf16_f32 v84, v84, v85
	v_cvt_pk_bf16_f32 v85, v86, v87
	v_cvt_pk_bf16_f32 v86, v92, v93
	v_cvt_pk_bf16_f32 v87, v90, v91
	global_store_dwordx4 v[88:89], v[84:87], off offset:256 sc0 sc1
	ds_read_b128 v[84:87], v192 offset:4864
	s_waitcnt lgkmcnt(0)
	v_mov_b32_e32 v88, v85
	v_mov_b32_e32 v89, v86
	v_mov_b32_e32 v85, v87
	v_pk_add_f32 v[84:85], v[88:89], v[84:85]
	s_nop 0
	v_add_f32_e32 v0, v84, v85
	v_div_scale_f32 v84, s[0:1], v0, v0, 1.0
	v_rcp_f32_e32 v85, v84
	s_nop 0
	v_fma_f32 v86, -v84, v85, 1.0
	v_fmac_f32_e32 v85, v86, v85
	v_div_scale_f32 v86, vcc, 1.0, v0, 1.0
	v_mul_f32_e32 v87, v86, v85
	v_fma_f32 v88, -v84, v87, v86
	v_fmac_f32_e32 v87, v88, v85
	v_fma_f32 v84, -v84, v87, v86
	v_div_fmas_f32 v84, v84, v85, v87
	v_div_fixup_f32 v0, v84, v0, 1.0
	v_or_b32_e32 v84, 48, v130
	v_ashrrev_i32_e32 v85, 31, v84
	v_lshlrev_b64 v[84:85], 11, v[84:85]
	v_pk_mul_f32 v[60:61], v[60:61], v[0:1] op_sel_hi:[1,0]
	v_pk_mul_f32 v[52:53], v[52:53], v[0:1] op_sel_hi:[1,0]
	v_pk_mul_f32 v[56:57], v[56:57], v[0:1] op_sel_hi:[1,0]
	v_lshl_add_u64 v[88:89], v[134:135], 0, v[84:85]
	v_cvt_pk_bf16_f32 v84, v52, v53
	v_cvt_pk_bf16_f32 v85, v60, v61
	v_cvt_pk_bf16_f32 v86, v56, v57
	v_pk_mul_f32 v[56:57], v[66:67], v[0:1] op_sel_hi:[1,0]
	v_pk_mul_f32 v[52:53], v[54:55], v[0:1] op_sel_hi:[1,0]
	v_pk_mul_f32 v[60:61], v[76:77], v[0:1] op_sel_hi:[1,0]
	v_pk_mul_f32 v[54:55], v[70:71], v[0:1] op_sel_hi:[1,0]
	v_cvt_pk_bf16_f32 v52, v52, v53
	v_cvt_pk_bf16_f32 v53, v56, v57
	v_cvt_pk_bf16_f32 v54, v54, v55
	v_cvt_pk_bf16_f32 v55, v60, v61
	global_store_dwordx4 v[88:89], v[52:55], off offset:256 sc0 sc1
	ds_read_b128 v[52:55], v192 offset:6144
	v_pk_mul_f32 v[68:69], v[68:69], v[0:1] op_sel_hi:[1,0]
	s_waitcnt lgkmcnt(0)
	v_mov_b32_e32 v56, v53
	v_mov_b32_e32 v57, v54
	v_mov_b32_e32 v53, v55
	v_pk_add_f32 v[52:53], v[56:57], v[52:53]
	v_cvt_pk_bf16_f32 v87, v68, v69
	v_add_f32_e32 v0, v52, v53
	v_div_scale_f32 v52, s[0:1], v0, v0, 1.0
	v_rcp_f32_e32 v53, v52
	s_mov_b32 s0, 0x40000
	global_store_dwordx4 v[88:89], v[84:87], off sc0 sc1
	v_fma_f32 v54, -v52, v53, 1.0
	v_fmac_f32_e32 v53, v54, v53
	v_div_scale_f32 v54, vcc, 1.0, v0, 1.0
	v_mul_f32_e32 v55, v54, v53
	v_fma_f32 v56, -v52, v55, v54
	v_fmac_f32_e32 v55, v56, v53
	v_fma_f32 v52, -v52, v55, v54
	v_div_fmas_f32 v52, v52, v53, v55
	v_div_fixup_f32 v0, v52, v0, 1.0
	v_pk_mul_f32 v[54:55], v[62:63], v[0:1] op_sel_hi:[1,0]
	v_pk_mul_f32 v[52:53], v[58:59], v[0:1] op_sel_hi:[1,0]
	v_pk_mul_f32 v[58:59], v[74:75], v[0:1] op_sel_hi:[1,0]
	v_pk_mul_f32 v[60:61], v[64:65], v[0:1] op_sel_hi:[1,0]
	v_cvt_pk_bf16_f32 v52, v52, v53
	v_cvt_pk_bf16_f32 v53, v54, v55
	v_cvt_pk_bf16_f32 v55, v58, v59
	v_add_co_u32_e32 v58, vcc, s0, v18
	v_cvt_pk_bf16_f32 v54, v60, v61
	s_nop 0
	v_addc_co_u32_e32 v59, vcc, 0, v19, vcc
	global_store_dwordx4 v[58:59], v[52:55], off sc0 sc1
	v_pk_mul_f32 v[58:59], v[82:83], v[0:1] op_sel_hi:[1,0]
	v_pk_mul_f32 v[60:61], v[80:81], v[0:1] op_sel_hi:[1,0]
	v_pk_mul_f32 v[54:55], v[78:79], v[0:1] op_sel_hi:[1,0]
	v_pk_mul_f32 v[52:53], v[72:73], v[0:1] op_sel_hi:[1,0]
	v_lshl_add_u64 v[56:57], v[18:19], 0, s[20:21]
	v_cvt_pk_bf16_f32 v52, v52, v53
	v_cvt_pk_bf16_f32 v53, v54, v55
	v_cvt_pk_bf16_f32 v54, v60, v61
	v_cvt_pk_bf16_f32 v55, v58, v59
	global_store_dwordx4 v[56:57], v[52:55], off offset:256 sc0 sc1
	ds_read_b128 v[52:55], v192 offset:6400
	s_waitcnt lgkmcnt(0)
	v_mov_b32_e32 v56, v53
	v_mov_b32_e32 v57, v54
	v_mov_b32_e32 v53, v55
	v_pk_add_f32 v[52:53], v[56:57], v[52:53]
	s_nop 0
	v_add_f32_e32 v0, v52, v53
	v_div_scale_f32 v52, s[0:1], v0, v0, 1.0
	v_rcp_f32_e32 v53, v52
	s_mov_b64 s[0:1], 0x48000
	v_fma_f32 v54, -v52, v53, 1.0
	v_fmac_f32_e32 v53, v54, v53
	v_div_scale_f32 v54, vcc, 1.0, v0, 1.0
	v_mul_f32_e32 v55, v54, v53
	v_fma_f32 v56, -v52, v55, v54
	v_fmac_f32_e32 v55, v56, v53
	v_fma_f32 v52, -v52, v55, v54
	v_div_fmas_f32 v52, v52, v53, v55
	v_div_fixup_f32 v0, v52, v0, 1.0
	v_lshl_add_u64 v[52:53], v[18:19], 0, s[0:1]
	v_pk_mul_f32 v[24:25], v[24:25], v[0:1] op_sel_hi:[1,0]
	s_mov_b32 s0, 0x48000
	v_pk_mul_f32 v[30:31], v[30:31], v[0:1] op_sel_hi:[1,0]
	v_pk_mul_f32 v[40:41], v[40:41], v[0:1] op_sel_hi:[1,0]
	v_pk_mul_f32 v[54:55], v[28:29], v[0:1] op_sel_hi:[1,0]
	v_cvt_pk_bf16_f32 v28, v24, v25
	v_add_co_u32_e32 v24, vcc, s0, v18
	v_cvt_pk_bf16_f32 v29, v30, v31
	v_cvt_pk_bf16_f32 v30, v54, v55
	v_cvt_pk_bf16_f32 v31, v40, v41
	v_addc_co_u32_e32 v25, vcc, 0, v19, vcc
	global_store_dwordx4 v[24:25], v[28:31], off sc0 sc1
	v_pk_mul_f32 v[24:25], v[34:35], v[0:1] op_sel_hi:[1,0]
	v_pk_mul_f32 v[20:21], v[20:21], v[0:1] op_sel_hi:[1,0]
	v_pk_mul_f32 v[34:35], v[44:45], v[0:1] op_sel_hi:[1,0]
	v_pk_mul_f32 v[30:31], v[36:37], v[0:1] op_sel_hi:[1,0]
	v_cvt_pk_bf16_f32 v28, v20, v21
	v_cvt_pk_bf16_f32 v29, v24, v25
	v_cvt_pk_bf16_f32 v30, v30, v31
	v_cvt_pk_bf16_f32 v31, v34, v35
	global_store_dwordx4 v[52:53], v[28:31], off offset:256 sc0 sc1
	ds_read_b128 v[28:31], v192 offset:6656
	s_waitcnt lgkmcnt(0)
	v_mov_b32_e32 v20, v29
	v_mov_b32_e32 v21, v30
	v_mov_b32_e32 v29, v31
	v_pk_add_f32 v[20:21], v[20:21], v[28:29]
	s_nop 0
	v_add_f32_e32 v0, v20, v21
	v_div_scale_f32 v20, s[0:1], v0, v0, 1.0
	v_rcp_f32_e32 v21, v20
	s_mov_b32 s0, 0x50000
	v_fma_f32 v24, -v20, v21, 1.0
	v_fmac_f32_e32 v21, v24, v21
	v_div_scale_f32 v24, vcc, 1.0, v0, 1.0
	v_mul_f32_e32 v25, v24, v21
	v_fma_f32 v28, -v20, v25, v24
	v_fmac_f32_e32 v25, v28, v21
	v_fma_f32 v20, -v20, v25, v24
	v_div_fmas_f32 v20, v20, v21, v25
	v_div_fixup_f32 v0, v20, v0, 1.0
	v_pk_mul_f32 v[26:27], v[26:27], v[0:1] op_sel_hi:[1,0]
	v_pk_mul_f32 v[20:21], v[22:23], v[0:1] op_sel_hi:[1,0]
	v_pk_mul_f32 v[28:29], v[42:43], v[0:1] op_sel_hi:[1,0]
	v_pk_mul_f32 v[22:23], v[32:33], v[0:1] op_sel_hi:[1,0]
	v_cvt_pk_bf16_f32 v20, v20, v21
	v_cvt_pk_bf16_f32 v21, v26, v27
	v_add_co_u32_e32 v26, vcc, s0, v18
	v_cvt_pk_bf16_f32 v22, v22, v23
	v_cvt_pk_bf16_f32 v23, v28, v29
	v_addc_co_u32_e32 v27, vcc, 0, v19, vcc
	global_store_dwordx4 v[26:27], v[20:23], off sc0 sc1
	v_pk_mul_f32 v[26:27], v[50:51], v[0:1] op_sel_hi:[1,0]
	v_pk_mul_f32 v[28:29], v[48:49], v[0:1] op_sel_hi:[1,0]
	v_pk_mul_f32 v[22:23], v[46:47], v[0:1] op_sel_hi:[1,0]
	v_pk_mul_f32 v[20:21], v[38:39], v[0:1] op_sel_hi:[1,0]
	v_lshl_add_u64 v[24:25], v[18:19], 0, s[22:23]
	v_cvt_pk_bf16_f32 v20, v20, v21
	v_cvt_pk_bf16_f32 v21, v22, v23
	v_cvt_pk_bf16_f32 v22, v28, v29
	v_cvt_pk_bf16_f32 v23, v26, v27
	global_store_dwordx4 v[24:25], v[20:23], off offset:256 sc0 sc1
	ds_read_b128 v[20:23], v192 offset:6912
	s_waitcnt lgkmcnt(0)
	v_mov_b32_e32 v24, v21
	v_mov_b32_e32 v25, v22
	v_mov_b32_e32 v21, v23
	v_pk_add_f32 v[20:21], v[24:25], v[20:21]
	s_nop 0
	v_add_f32_e32 v0, v20, v21
	v_div_scale_f32 v20, s[0:1], v0, v0, 1.0
	v_rcp_f32_e32 v21, v20
	s_mov_b64 s[0:1], 0x58000
	v_fma_f32 v22, -v20, v21, 1.0
	v_fmac_f32_e32 v21, v22, v21
	v_div_scale_f32 v22, vcc, 1.0, v0, 1.0
	v_mul_f32_e32 v23, v22, v21
	v_fma_f32 v24, -v20, v23, v22
	v_fmac_f32_e32 v23, v24, v21
	v_fma_f32 v20, -v20, v23, v22
	v_div_fmas_f32 v20, v20, v21, v23
	v_div_fixup_f32 v0, v20, v0, 1.0
	v_lshl_add_u64 v[20:21], v[18:19], 0, s[0:1]
	v_pk_mul_f32 v[8:9], v[8:9], v[0:1] op_sel_hi:[1,0]
	v_pk_mul_f32 v[4:5], v[4:5], v[0:1] op_sel_hi:[1,0]
	s_mov_b32 s0, 0x58000
	v_pk_mul_f32 v[14:15], v[14:15], v[0:1] op_sel_hi:[1,0]
	v_pk_mul_f32 v[6:7], v[6:7], v[0:1] op_sel_hi:[1,0]
	v_cvt_pk_bf16_f32 v4, v4, v5
	v_cvt_pk_bf16_f32 v5, v8, v9
	v_add_co_u32_e32 v8, vcc, s0, v18
	v_cvt_pk_bf16_f32 v6, v6, v7
	v_cvt_pk_bf16_f32 v7, v14, v15
	v_addc_co_u32_e32 v9, vcc, 0, v19, vcc
	global_store_dwordx4 v[8:9], v[4:7], off sc0 sc1
	v_pk_mul_f32 v[2:3], v[2:3], v[0:1] op_sel_hi:[1,0]
	v_pk_mul_f32 v[8:9], v[10:11], v[0:1] op_sel_hi:[1,0]
	v_pk_mul_f32 v[4:5], v[12:13], v[0:1] op_sel_hi:[1,0]
	v_pk_mul_f32 v[6:7], v[16:17], v[0:1] op_sel_hi:[1,0]
	v_cvt_pk_bf16_f32 v2, v2, v3
	v_cvt_pk_bf16_f32 v3, v4, v5
	v_cvt_pk_bf16_f32 v4, v8, v9
	v_cvt_pk_bf16_f32 v5, v6, v7
	global_store_dwordx4 v[20:21], v[2:5], off offset:256 sc0 sc1
	s_waitcnt lgkmcnt(0)
	s_barrier

.LBB0_503:
	s_mov_b32 s0, -1
	s_add_u32 s14, s74, 0x8800000
	s_waitcnt vmcnt(0)
	s_barrier
	s_addc_u32 s15, s75, 0
	v_mbcnt_lo_u32_b32 v0, s0, 0
	v_mbcnt_hi_u32_b32 v166, s0, v0
	s_lshl_b32 s0, s90, 8
	v_and_b32_e32 v130, 15, v166
	s_add_i32 s17, s0, s65
	v_or_b32_e32 v156, s17, v130
	s_ashr_i32 s17, s16, 31
	s_lshl_b32 s1, s64, 5
	s_lshl_b64 s[16:17], s[16:17], 8
	v_lshrrev_b32_e32 v0, 1, v166
	s_or_b32 s16, s16, s1
	v_and_b32_e32 v0, 56, v0
	v_and_b32_e32 v131, 64, v231
	v_lshl_add_u64 v[154:155], s[16:17], 0, v[0:1]
	v_xor_b32_e32 v0, 16, v231
	v_add_u32_e32 v131, 64, v131
	v_cmp_lt_i32_e32 vcc, v0, v131
	v_readlane_b32 s16, v253, 34
	v_lshlrev_b64 v[178:179], 1, v[154:155]
	v_cndmask_b32_e32 v0, v231, v0, vcc
	v_lshlrev_b32_e32 v168, 2, v0
	v_xor_b32_e32 v0, 32, v231
	v_cmp_lt_i32_e32 vcc, v0, v131
	v_readlane_b32 s17, v253, 35
	v_ashrrev_i32_e32 v157, 31, v156
	v_cndmask_b32_e32 v0, v231, v0, vcc
	v_lshl_add_u64 v[158:159], s[16:17], 0, v[178:179]
	v_lshlrev_b64 v[180:181], 11, v[156:157]
	v_lshlrev_b32_e32 v167, 2, v0
	v_or_b32_e32 v0, s65, v130
	v_lshl_add_u64 v[130:131], v[158:159], 0, v[180:181]
	global_load_dwordx4 v[170:173], v[130:131], off
	global_load_dwordx4 v[174:177], v[130:131], off offset:256
	v_or_b32_e32 v130, 16, v156
	v_ashrrev_i32_e32 v131, 31, v130
	v_lshlrev_b64 v[164:165], 11, v[130:131]
	v_lshl_add_u64 v[130:131], v[158:159], 0, v[164:165]
	global_load_dwordx4 v[150:153], v[130:131], off
	global_load_dwordx4 v[146:149], v[130:131], off offset:256
	v_or_b32_e32 v130, 32, v156
	v_ashrrev_i32_e32 v131, 31, v130
	v_lshlrev_b64 v[162:163], 11, v[130:131]
	v_lshl_add_u64 v[130:131], v[158:159], 0, v[162:163]
	global_load_dwordx4 v[142:145], v[130:131], off
	global_load_dwordx4 v[138:141], v[130:131], off offset:256
	v_or_b32_e32 v130, 48, v156
	v_ashrrev_i32_e32 v131, 31, v130
	v_lshlrev_b64 v[160:161], 11, v[130:131]
	v_lshl_add_u64 v[130:131], v[158:159], 0, v[160:161]
	global_load_dwordx4 v[134:137], v[130:131], off
	s_nop 0
	global_load_dwordx4 v[130:133], v[130:131], off offset:256
	v_lshl_add_u64 v[180:181], s[14:15], 0, v[180:181]
	v_lshl_add_u64 v[178:179], v[180:181], 0, v[178:179]
	v_cmp_gt_u32_e32 vcc, 16, v166
	s_lshl_b32 s1, s64, 2
	s_waitcnt vmcnt(0)
	v_lshlrev_b32_e32 v182, 16, v170
	v_and_b32_e32 v183, 0xffff0000, v170
	v_lshlrev_b32_e32 v170, 16, v171
	v_and_b32_e32 v171, 0xffff0000, v171
	v_pk_add_f32 v[128:129], v[128:129], v[170:171]
	v_lshlrev_b32_e32 v170, 16, v172
	v_and_b32_e32 v171, 0xffff0000, v172
	v_pk_add_f32 v[170:171], v[122:123], v[170:171]
	v_lshlrev_b32_e32 v122, 16, v173
	v_and_b32_e32 v123, 0xffff0000, v173
	v_pk_add_f32 v[126:127], v[126:127], v[182:183]
	v_pk_add_f32 v[172:173], v[124:125], v[122:123]
	v_cvt_pk_bf16_f32 v122, v126, v127
	v_cvt_pk_bf16_f32 v123, v128, v129
	v_cvt_pk_bf16_f32 v124, v170, v171
	v_cvt_pk_bf16_f32 v125, v172, v173
	global_store_dwordx4 v[178:179], v[122:125], off sc0 sc1
	s_nop 1
	v_pk_mul_f32 v[122:123], v[126:127], v[126:127]
	v_pk_mul_f32 v[126:127], v[170:171], v[170:171]
	v_lshlrev_b32_e32 v170, 16, v174
	v_and_b32_e32 v171, 0xffff0000, v174
	v_pk_add_f32 v[118:119], v[118:119], v[170:171]
	v_lshlrev_b32_e32 v170, 16, v175
	v_and_b32_e32 v171, 0xffff0000, v175
	v_pk_add_f32 v[120:121], v[120:121], v[170:171]
	v_lshlrev_b32_e32 v170, 16, v176
	v_and_b32_e32 v171, 0xffff0000, v176
	v_pk_add_f32 v[170:171], v[114:115], v[170:171]
	v_lshlrev_b32_e32 v114, 16, v177
	v_and_b32_e32 v115, 0xffff0000, v177
	v_pk_mul_f32 v[124:125], v[128:129], v[128:129]
	v_pk_mul_f32 v[128:129], v[172:173], v[172:173]
	v_pk_add_f32 v[172:173], v[116:117], v[114:115]
	v_cvt_pk_bf16_f32 v114, v118, v119
	v_cvt_pk_bf16_f32 v115, v120, v121
	v_cvt_pk_bf16_f32 v116, v170, v171
	v_cvt_pk_bf16_f32 v117, v172, v173
	global_store_dwordx4 v[178:179], v[114:117], off offset:256 sc0 sc1
	s_nop 1
	v_pk_mul_f32 v[114:115], v[118:119], v[118:119]
	v_pk_mul_f32 v[116:117], v[120:121], v[120:121]
	v_add_f32_e32 v114, v114, v115
	v_add_f32_e32 v116, v116, v117
	v_pk_mul_f32 v[118:119], v[170:171], v[170:171]
	v_pk_mul_f32 v[120:121], v[172:173], v[172:173]
	v_add_f32_e32 v114, v114, v116
	v_add_f32_e32 v115, v128, v129
	v_add_f32_e32 v116, v126, v127
	v_add_f32_e32 v120, v120, v121
	v_add_f32_e32 v118, v118, v119
	v_add_f32_e32 v115, v116, v115
	v_add_f32_e32 v116, v124, v125
	v_add_f32_e32 v117, v122, v123
	v_add_f32_e32 v118, v118, v120
	v_add_f32_e32 v116, v117, v116
	v_add_f32_e32 v114, v114, v118
	v_add_f32_e32 v115, v116, v115
	v_add_f32_e32 v114, v115, v114
	ds_bpermute_b32 v115, v168, v114
	s_waitcnt lgkmcnt(0)
	v_add_f32_e32 v114, v114, v115
	ds_bpermute_b32 v115, v167, v114
	s_and_saveexec_b64 s[16:17], vcc
	s_cbranch_execz .LBB0_505
	v_lshl_or_b32 v116, v0, 4, s1
	s_waitcnt lgkmcnt(0)
	v_add_f32_e32 v114, v114, v115
	ds_write_b32 v116, v114
.LBB0_505:
	s_or_b64 exec, exec, s[16:17]
	v_lshlrev_b32_e32 v114, 16, v150
	s_waitcnt lgkmcnt(0)
	v_and_b32_e32 v115, 0xffff0000, v150
	v_pk_add_f32 v[110:111], v[110:111], v[114:115]
	v_lshlrev_b32_e32 v114, 16, v151
	v_and_b32_e32 v115, 0xffff0000, v151
	v_pk_add_f32 v[112:113], v[112:113], v[114:115]
	v_lshlrev_b32_e32 v114, 16, v152
	v_and_b32_e32 v115, 0xffff0000, v152
	v_pk_add_f32 v[114:115], v[106:107], v[114:115]
	v_lshlrev_b32_e32 v106, 16, v153
	v_and_b32_e32 v107, 0xffff0000, v153
	v_pk_add_f32 v[116:117], v[108:109], v[106:107]
	v_lshl_add_u64 v[118:119], s[14:15], 0, v[164:165]
	v_cvt_pk_bf16_f32 v106, v110, v111
	v_cvt_pk_bf16_f32 v107, v112, v113
	v_cvt_pk_bf16_f32 v108, v114, v115
	v_cvt_pk_bf16_f32 v109, v116, v117
	v_lshl_add_u64 v[118:119], v[154:155], 1, v[118:119]
	global_store_dwordx4 v[118:119], v[106:109], off sc0 sc1
	s_nop 1
	v_pk_mul_f32 v[106:107], v[110:111], v[110:111]
	v_pk_mul_f32 v[110:111], v[114:115], v[114:115]
	v_lshlrev_b32_e32 v114, 16, v146
	v_and_b32_e32 v115, 0xffff0000, v146
	v_pk_add_f32 v[102:103], v[102:103], v[114:115]
	v_lshlrev_b32_e32 v114, 16, v147
	v_and_b32_e32 v115, 0xffff0000, v147
	v_pk_add_f32 v[104:105], v[104:105], v[114:115]
	v_lshlrev_b32_e32 v114, 16, v148
	v_and_b32_e32 v115, 0xffff0000, v148
	v_pk_add_f32 v[114:115], v[98:99], v[114:115]
	v_lshlrev_b32_e32 v98, 16, v149
	v_and_b32_e32 v99, 0xffff0000, v149
	v_pk_mul_f32 v[108:109], v[112:113], v[112:113]
	v_pk_mul_f32 v[112:113], v[116:117], v[116:117]
	v_pk_add_f32 v[116:117], v[100:101], v[98:99]
	v_cvt_pk_bf16_f32 v98, v102, v103
	v_cvt_pk_bf16_f32 v99, v104, v105
	v_cvt_pk_bf16_f32 v100, v114, v115
	v_cvt_pk_bf16_f32 v101, v116, v117
	global_store_dwordx4 v[118:119], v[98:101], off offset:256 sc0 sc1
	s_nop 1
	v_pk_mul_f32 v[98:99], v[102:103], v[102:103]
	v_pk_mul_f32 v[100:101], v[104:105], v[104:105]
	v_add_f32_e32 v98, v98, v99
	v_add_f32_e32 v100, v100, v101
	v_pk_mul_f32 v[102:103], v[114:115], v[114:115]
	v_pk_mul_f32 v[104:105], v[116:117], v[116:117]
	v_add_f32_e32 v98, v98, v100
	v_add_f32_e32 v99, v112, v113
	v_add_f32_e32 v100, v110, v111
	v_add_f32_e32 v104, v104, v105
	v_add_f32_e32 v102, v102, v103
	v_add_f32_e32 v99, v100, v99
	v_add_f32_e32 v100, v108, v109
	v_add_f32_e32 v101, v106, v107
	v_add_f32_e32 v102, v102, v104
	v_add_f32_e32 v100, v101, v100
	v_add_f32_e32 v98, v98, v102
	v_add_f32_e32 v99, v100, v99
	v_add_f32_e32 v98, v99, v98
	ds_bpermute_b32 v99, v168, v98
	s_waitcnt lgkmcnt(0)
	v_add_f32_e32 v98, v98, v99
	ds_bpermute_b32 v99, v167, v98
	s_and_saveexec_b64 s[16:17], vcc
	v_readlane_b32 s38, v253, 47
	v_readlane_b32 s91, v253, 27
	s_mov_b32 s89, 0x2e8ba2e9
	s_movk_i32 s90, 0xfea0
	s_mov_b32 s29, 0x47800000
	v_readlane_b32 s39, v253, 48
	s_cbranch_execz .LBB0_507
	v_lshl_or_b32 v100, v0, 4, s1
	s_waitcnt lgkmcnt(0)
	v_add_f32_e32 v98, v98, v99
	ds_write_b32 v100, v98 offset:256

.LBB0_545:
	s_mov_b32 s0, -1
	s_add_u32 s16, s74, 0x8800000
	s_waitcnt vmcnt(0)
	s_barrier
	s_addc_u32 s17, s75, 0
	v_mbcnt_lo_u32_b32 v0, s0, 0
	v_mbcnt_hi_u32_b32 v190, s0, v0
	s_lshl_b32 s14, s90, 8
	v_and_b32_e32 v193, 15, v190
	s_add_i32 s0, s14, s60
	s_ashr_i32 s37, s36, 31
	s_lshl_b32 s15, s61, 5
	v_or_b32_e32 v180, s0, v193
	s_lshl_b64 s[0:1], s[36:37], 8
	v_lshrrev_b32_e32 v0, 1, v190
	s_or_b32 s0, s0, s15
	v_and_b32_e32 v0, 56, v0
	v_lshl_add_u64 v[178:179], s[0:1], 0, v[0:1]
	v_readlane_b32 s0, v253, 47
	v_readlane_b32 s1, v253, 48
	v_ashrrev_i32_e32 v181, 31, v180
	v_lshlrev_b64 v[130:131], 12, v[180:181]
	v_lshl_add_u64 v[182:183], v[178:179], 2, s[0:1]
	v_lshl_add_u64 v[130:131], v[182:183], 0, v[130:131]
	global_load_dwordx4 v[200:203], v[130:131], off
	global_load_dwordx4 v[204:207], v[130:131], off offset:16
	global_load_dwordx4 v[208:211], v[130:131], off offset:512
	global_load_dwordx4 v[212:215], v[130:131], off offset:528
	v_or_b32_e32 v188, 16, v180
	v_or_b32_e32 v186, 32, v180
	v_or_b32_e32 v184, 48, v180
	v_ashrrev_i32_e32 v189, 31, v188
	v_ashrrev_i32_e32 v187, 31, v186
	v_ashrrev_i32_e32 v185, 31, v184
	v_lshlrev_b64 v[130:131], 12, v[188:189]
	v_lshlrev_b64 v[132:133], 12, v[186:187]
	v_lshlrev_b64 v[134:135], 12, v[184:185]
	v_lshl_add_u64 v[130:131], v[182:183], 0, v[130:131]
	v_lshl_add_u64 v[132:133], v[182:183], 0, v[132:133]
	v_lshl_add_u64 v[134:135], v[182:183], 0, v[134:135]
	global_load_dwordx4 v[170:173], v[130:131], off offset:16
	global_load_dwordx4 v[174:177], v[130:131], off
	global_load_dwordx4 v[162:165], v[130:131], off offset:528
	global_load_dwordx4 v[166:169], v[130:131], off offset:512
	global_load_dwordx4 v[154:157], v[132:133], off offset:16
	global_load_dwordx4 v[158:161], v[132:133], off
	global_load_dwordx4 v[146:149], v[132:133], off offset:528
	global_load_dwordx4 v[150:153], v[132:133], off offset:512
	global_load_dwordx4 v[138:141], v[134:135], off offset:16
	global_load_dwordx4 v[142:145], v[134:135], off
	s_nop 0
	global_load_dwordx4 v[130:133], v[134:135], off offset:528
	s_nop 0
	global_load_dwordx4 v[134:137], v[134:135], off offset:512
	v_and_b32_e32 v191, 64, v231
	v_xor_b32_e32 v0, 16, v231
	v_add_u32_e32 v191, 64, v191
	v_xor_b32_e32 v192, 32, v231
	v_cmp_lt_i32_e32 vcc, v0, v191
	v_lshlrev_b64 v[194:195], 11, v[180:181]
	s_lshl_b32 s15, s61, 2
	v_cndmask_b32_e32 v0, v231, v0, vcc
	v_cmp_lt_i32_e32 vcc, v192, v191
	s_waitcnt vmcnt(0)
	v_pk_add_f32 v[128:129], v[128:129], v[202:203]
	v_pk_add_f32 v[126:127], v[126:127], v[200:201]
	v_pk_add_f32 v[124:125], v[124:125], v[206:207]
	v_pk_add_f32 v[122:123], v[122:123], v[204:205]
	v_pk_add_f32 v[200:201], v[116:117], v[214:215]
	v_pk_add_f32 v[202:203], v[114:115], v[212:213]
	v_cvt_pk_bf16_f32 v114, v126, v127
	v_cvt_pk_bf16_f32 v115, v128, v129
	v_cvt_pk_bf16_f32 v116, v122, v123
	v_cvt_pk_bf16_f32 v117, v124, v125
	v_mul_f32_e32 v127, v127, v127
	v_mul_f32_e32 v129, v129, v129
	v_mul_f32_e32 v123, v123, v123
	v_mul_f32_e32 v125, v125, v125
	v_fmac_f32_e32 v127, v126, v126
	v_fmac_f32_e32 v129, v128, v128
	v_fmac_f32_e32 v123, v122, v122
	v_fmac_f32_e32 v125, v124, v124
	v_pk_add_f32 v[120:121], v[120:121], v[210:211]
	v_pk_add_f32 v[118:119], v[118:119], v[208:209]
	v_add_f32_e32 v122, v127, v129
	v_add_f32_e32 v123, v123, v125
	v_cndmask_b32_e32 v191, v231, v192, vcc
	v_lshlrev_b32_e32 v192, 2, v0
	v_or_b32_e32 v0, s60, v193
	v_mul_f32_e32 v181, v119, v119
	v_mul_f32_e32 v193, v121, v121
	v_mul_f32_e32 v204, v203, v203
	v_add_f32_e32 v122, v122, v123
	v_mul_f32_e32 v123, v201, v201
	v_fmac_f32_e32 v181, v118, v118
	v_fmac_f32_e32 v193, v120, v120
	v_fmac_f32_e32 v204, v202, v202
	v_fmac_f32_e32 v123, v200, v200
	v_add_f32_e32 v124, v181, v193
	v_add_f32_e32 v123, v204, v123
	v_add_f32_e32 v123, v124, v123
	v_add_f32_e32 v124, v122, v123
	ds_bpermute_b32 v125, v192, v124
	v_lshl_add_u64 v[122:123], s[16:17], 0, v[194:195]
	v_lshl_add_u64 v[122:123], v[178:179], 1, v[122:123]
	v_lshlrev_b32_e32 v191, 2, v191
	global_store_dwordx4 v[122:123], v[114:117], off sc0 sc1
	v_cmp_gt_u32_e32 vcc, 16, v190
	s_waitcnt lgkmcnt(0)
	v_add_f32_e32 v114, v124, v125
	ds_bpermute_b32 v115, v191, v114
	v_cvt_pk_bf16_f32 v116, v118, v119
	v_cvt_pk_bf16_f32 v117, v120, v121
	v_cvt_pk_bf16_f32 v118, v202, v203
	v_cvt_pk_bf16_f32 v119, v200, v201
	global_store_dwordx4 v[122:123], v[116:119], off offset:256 sc0 sc1
	s_and_saveexec_b64 s[0:1], vcc
	s_cbranch_execz .LBB0_547
	v_lshl_or_b32 v116, v0, 4, s15
	s_waitcnt lgkmcnt(0)
	v_add_f32_e32 v114, v114, v115
	ds_write_b32 v116, v114
.LBB0_547:
	s_or_b64 exec, exec, s[0:1]
	v_pk_add_f32 v[110:111], v[110:111], v[174:175]
	v_pk_add_f32 v[112:113], v[112:113], v[176:177]
	v_pk_add_f32 v[118:119], v[106:107], v[170:171]
	v_cvt_pk_bf16_f32 v106, v110, v111
	v_mul_f32_e32 v111, v111, v111
	v_fmac_f32_e32 v111, v110, v110
	v_mul_f32_e32 v110, v113, v113
	v_pk_add_f32 v[116:117], v[108:109], v[172:173]
	v_fmac_f32_e32 v110, v112, v112
	v_cvt_pk_bf16_f32 v107, v112, v113
	v_add_f32_e32 v110, v111, v110
	v_mul_f32_e32 v111, v119, v119
	v_mul_f32_e32 v112, v117, v117
	v_fmac_f32_e32 v111, v118, v118
	v_fmac_f32_e32 v112, v116, v116
	v_pk_add_f32 v[104:105], v[104:105], v[168:169]
	v_pk_add_f32 v[102:103], v[102:103], v[166:167]
	v_add_f32_e32 v111, v111, v112
	v_pk_add_f32 v[112:113], v[98:99], v[162:163]
	v_mul_f32_e32 v98, v103, v103
	v_mul_f32_e32 v99, v105, v105
	v_cvt_pk_bf16_f32 v109, v116, v117
	v_add_f32_e32 v116, v110, v111
	v_pk_add_f32 v[110:111], v[100:101], v[164:165]
	v_fmac_f32_e32 v98, v102, v102
	v_fmac_f32_e32 v99, v104, v104
	v_add_f32_e32 v98, v98, v99
	v_mul_f32_e32 v99, v113, v113
	v_mul_f32_e32 v100, v111, v111
	v_fmac_f32_e32 v99, v112, v112
	v_fmac_f32_e32 v100, v110, v110
	v_add_f32_e32 v99, v99, v100
	v_add_f32_e32 v98, v98, v99
	v_add_f32_e32 v101, v116, v98
	ds_bpermute_b32 v116, v192, v101
	s_waitcnt lgkmcnt(1)
	v_lshlrev_b64 v[114:115], 11, v[188:189]
	v_lshl_add_u64 v[98:99], s[16:17], 0, v[114:115]
	v_lshl_add_u64 v[114:115], v[178:179], 1, v[98:99]
	v_cvt_pk_bf16_f32 v108, v118, v119
	s_waitcnt lgkmcnt(0)
	v_add_f32_e32 v98, v101, v116
	ds_bpermute_b32 v99, v191, v98
	v_cvt_pk_bf16_f32 v100, v102, v103
	v_cvt_pk_bf16_f32 v101, v104, v105
	v_cvt_pk_bf16_f32 v102, v112, v113
	v_cvt_pk_bf16_f32 v103, v110, v111
	global_store_dwordx4 v[114:115], v[106:109], off sc0 sc1
	global_store_dwordx4 v[114:115], v[100:103], off offset:256 sc0 sc1
	s_and_saveexec_b64 s[0:1], vcc
	v_readlane_b32 s91, v253, 27
	s_mov_b32 s89, 0x2e8ba2e9
	s_movk_i32 s90, 0xfea0
	s_mov_b32 s29, 0x47800000
	s_cbranch_execz .LBB0_549
	v_lshl_or_b32 v100, v0, 4, s15
	s_waitcnt lgkmcnt(0)
	v_add_f32_e32 v98, v98, v99
	ds_write_b32 v100, v98 offset:256
.LBB0_549:
	s_or_b64 exec, exec, s[0:1]
	v_pk_add_f32 v[94:95], v[94:95], v[158:159]
	v_pk_add_f32 v[96:97], v[96:97], v[160:161]
	v_pk_add_f32 v[102:103], v[90:91], v[154:155]
	v_cvt_pk_bf16_f32 v90, v94, v95
	v_mul_f32_e32 v95, v95, v95
	v_fmac_f32_e32 v95, v94, v94
	v_mul_f32_e32 v94, v97, v97
	v_pk_add_f32 v[100:101], v[92:93], v[156:157]
	v_fmac_f32_e32 v94, v96, v96
	v_cvt_pk_bf16_f32 v91, v96, v97
	v_add_f32_e32 v94, v95, v94
	v_mul_f32_e32 v95, v103, v103
	v_mul_f32_e32 v96, v101, v101
	v_fmac_f32_e32 v95, v102, v102
	v_fmac_f32_e32 v96, v100, v100
	v_pk_add_f32 v[88:89], v[88:89], v[152:153]
	v_pk_add_f32 v[86:87], v[86:87], v[150:151]
	v_add_f32_e32 v95, v95, v96
	v_pk_add_f32 v[96:97], v[82:83], v[146:147]
	v_mul_f32_e32 v82, v87, v87
	v_mul_f32_e32 v83, v89, v89
	v_cvt_pk_bf16_f32 v93, v100, v101
	v_add_f32_e32 v100, v94, v95
	v_pk_add_f32 v[94:95], v[84:85], v[148:149]
	v_fmac_f32_e32 v82, v86, v86
	v_fmac_f32_e32 v83, v88, v88
	v_add_f32_e32 v82, v82, v83
	v_mul_f32_e32 v83, v97, v97
	v_mul_f32_e32 v84, v95, v95
	v_fmac_f32_e32 v83, v96, v96
	v_fmac_f32_e32 v84, v94, v94
	v_add_f32_e32 v83, v83, v84
	v_add_f32_e32 v82, v82, v83
	v_add_f32_e32 v85, v100, v82
	ds_bpermute_b32 v100, v192, v85
	s_waitcnt lgkmcnt(1)
	v_lshlrev_b64 v[98:99], 11, v[186:187]
	v_lshl_add_u64 v[82:83], s[16:17], 0, v[98:99]
	v_lshl_add_u64 v[98:99], v[178:179], 1, v[82:83]
	v_cvt_pk_bf16_f32 v92, v102, v103
	s_waitcnt lgkmcnt(0)
	v_add_f32_e32 v82, v85, v100
	ds_bpermute_b32 v83, v191, v82
	v_cvt_pk_bf16_f32 v84, v86, v87
	v_cvt_pk_bf16_f32 v85, v88, v89
	v_cvt_pk_bf16_f32 v86, v96, v97
	v_cvt_pk_bf16_f32 v87, v94, v95
	global_store_dwordx4 v[98:99], v[90:93], off sc0 sc1
	global_store_dwordx4 v[98:99], v[84:87], off offset:256 sc0 sc1
	s_and_saveexec_b64 s[0:1], vcc
	s_cbranch_execz .LBB0_551
	v_lshl_or_b32 v84, v0, 4, s15
	s_waitcnt lgkmcnt(0)
	v_add_f32_e32 v82, v82, v83
	ds_write_b32 v84, v82 offset:512
.LBB0_551:
	s_or_b64 exec, exec, s[0:1]
	v_pk_add_f32 v[78:79], v[78:79], v[142:143]
	v_pk_add_f32 v[80:81], v[80:81], v[144:145]
	v_pk_add_f32 v[86:87], v[74:75], v[138:139]
	v_cvt_pk_bf16_f32 v74, v78, v79
	v_mul_f32_e32 v79, v79, v79
	v_fmac_f32_e32 v79, v78, v78
	v_mul_f32_e32 v78, v81, v81
	v_pk_add_f32 v[84:85], v[76:77], v[140:141]
	v_fmac_f32_e32 v78, v80, v80
	v_cvt_pk_bf16_f32 v75, v80, v81
	v_add_f32_e32 v78, v79, v78
	v_mul_f32_e32 v79, v87, v87
	v_mul_f32_e32 v80, v85, v85
	v_fmac_f32_e32 v79, v86, v86
	v_fmac_f32_e32 v80, v84, v84
	v_pk_add_f32 v[72:73], v[72:73], v[136:137]
	v_pk_add_f32 v[70:71], v[70:71], v[134:135]
	v_add_f32_e32 v79, v79, v80
	v_pk_add_f32 v[80:81], v[66:67], v[130:131]
	v_mul_f32_e32 v66, v71, v71
	v_mul_f32_e32 v67, v73, v73
	v_cvt_pk_bf16_f32 v77, v84, v85
	v_add_f32_e32 v84, v78, v79
	v_pk_add_f32 v[78:79], v[68:69], v[132:133]
	v_fmac_f32_e32 v66, v70, v70
	v_fmac_f32_e32 v67, v72, v72
	v_add_f32_e32 v66, v66, v67
	v_mul_f32_e32 v67, v81, v81
	v_mul_f32_e32 v68, v79, v79
	v_fmac_f32_e32 v67, v80, v80
	v_fmac_f32_e32 v68, v78, v78
	v_add_f32_e32 v67, v67, v68
	v_add_f32_e32 v66, v66, v67
	v_add_f32_e32 v69, v84, v66
	ds_bpermute_b32 v84, v192, v69
	s_waitcnt lgkmcnt(1)
	v_lshlrev_b64 v[82:83], 11, v[184:185]
	v_lshl_add_u64 v[66:67], s[16:17], 0, v[82:83]
	v_lshl_add_u64 v[82:83], v[178:179], 1, v[66:67]
	v_cvt_pk_bf16_f32 v76, v86, v87
	s_waitcnt lgkmcnt(0)
	v_add_f32_e32 v66, v69, v84
	ds_bpermute_b32 v67, v191, v66
	v_cvt_pk_bf16_f32 v68, v70, v71
	v_cvt_pk_bf16_f32 v69, v72, v73
	v_cvt_pk_bf16_f32 v70, v80, v81
	v_cvt_pk_bf16_f32 v71, v78, v79
	global_store_dwordx4 v[82:83], v[74:77], off sc0 sc1
	global_store_dwordx4 v[82:83], v[68:71], off offset:256 sc0 sc1
	s_and_saveexec_b64 s[0:1], vcc
	s_cbranch_execz .LBB0_553
	v_lshl_or_b32 v68, v0, 4, s15
	s_waitcnt lgkmcnt(0)
	v_add_f32_e32 v66, v66, v67
	ds_write_b32 v68, v66 offset:768
.LBB0_553:
	s_or_b64 exec, exec, s[0:1]
	v_add_u32_e32 v136, 0x80, v180
	v_ashrrev_i32_e32 v137, 31, v136
	s_waitcnt lgkmcnt(0)
	v_lshlrev_b64 v[66:67], 12, v[136:137]
	v_lshl_add_u64 v[66:67], v[182:183], 0, v[66:67]
	global_load_dwordx4 v[120:123], v[66:67], off
	global_load_dwordx4 v[124:127], v[66:67], off offset:16
	global_load_dwordx4 v[128:131], v[66:67], off offset:512
	global_load_dwordx4 v[132:135], v[66:67], off offset:528
	v_add_u32_e32 v118, 0x90, v180
	v_add_u32_e32 v116, 0xa0, v180
	v_add_u32_e32 v114, 0xb0, v180
	v_ashrrev_i32_e32 v119, 31, v118
	v_ashrrev_i32_e32 v117, 31, v116
	v_ashrrev_i32_e32 v115, 31, v114
	v_lshlrev_b64 v[66:67], 12, v[118:119]
	v_lshlrev_b64 v[68:69], 12, v[116:117]
	v_lshlrev_b64 v[70:71], 12, v[114:115]
	v_lshl_add_u64 v[66:67], v[182:183], 0, v[66:67]
	v_lshl_add_u64 v[68:69], v[182:183], 0, v[68:69]
	v_lshl_add_u64 v[70:71], v[182:183], 0, v[70:71]
	global_load_dwordx4 v[106:109], v[66:67], off offset:16
	global_load_dwordx4 v[110:113], v[66:67], off
	global_load_dwordx4 v[98:101], v[66:67], off offset:528
	global_load_dwordx4 v[102:105], v[66:67], off offset:512
	global_load_dwordx4 v[90:93], v[68:69], off offset:16
	global_load_dwordx4 v[94:97], v[68:69], off
	global_load_dwordx4 v[82:85], v[68:69], off offset:528
	global_load_dwordx4 v[86:89], v[68:69], off offset:512
	global_load_dwordx4 v[74:77], v[70:71], off offset:16
	global_load_dwordx4 v[78:81], v[70:71], off
	s_nop 0
	global_load_dwordx4 v[66:69], v[70:71], off offset:528
	s_nop 0
	global_load_dwordx4 v[70:73], v[70:71], off offset:512
	v_lshlrev_b64 v[136:137], 11, v[136:137]
	s_waitcnt vmcnt(15)
	v_pk_add_f32 v[64:65], v[64:65], v[122:123]
	v_pk_add_f32 v[62:63], v[62:63], v[120:121]
	s_waitcnt vmcnt(14)
	v_pk_add_f32 v[60:61], v[60:61], v[126:127]
	v_pk_add_f32 v[58:59], v[58:59], v[124:125]
	s_waitcnt vmcnt(13)
	v_pk_add_f32 v[56:57], v[56:57], v[130:131]
	v_pk_add_f32 v[54:55], v[54:55], v[128:129]
	s_waitcnt vmcnt(12)
	v_pk_add_f32 v[120:121], v[52:53], v[134:135]
	v_pk_add_f32 v[122:123], v[50:51], v[132:133]
	v_cvt_pk_bf16_f32 v50, v62, v63
	v_cvt_pk_bf16_f32 v51, v64, v65
	v_cvt_pk_bf16_f32 v52, v58, v59
	v_cvt_pk_bf16_f32 v53, v60, v61
	v_mul_f32_e32 v63, v63, v63
	v_mul_f32_e32 v65, v65, v65
	v_mul_f32_e32 v59, v59, v59
	v_mul_f32_e32 v61, v61, v61
	v_mul_f32_e32 v124, v55, v55
	v_mul_f32_e32 v125, v57, v57
	v_mul_f32_e32 v126, v123, v123
	v_mul_f32_e32 v127, v121, v121
	v_fmac_f32_e32 v63, v62, v62
	v_fmac_f32_e32 v65, v64, v64
	v_fmac_f32_e32 v59, v58, v58
	v_fmac_f32_e32 v61, v60, v60
	v_fmac_f32_e32 v124, v54, v54
	v_fmac_f32_e32 v125, v56, v56
	v_fmac_f32_e32 v126, v122, v122
	v_fmac_f32_e32 v127, v120, v120
	v_add_f32_e32 v58, v63, v65
	v_add_f32_e32 v59, v59, v61
	v_add_f32_e32 v60, v124, v125
	v_add_f32_e32 v61, v126, v127
	v_add_f32_e32 v58, v58, v59
	v_add_f32_e32 v59, v60, v61
	v_add_f32_e32 v60, v58, v59
	ds_bpermute_b32 v61, v192, v60
	v_lshl_add_u64 v[58:59], s[16:17], 0, v[136:137]
	v_lshl_add_u64 v[58:59], v[178:179], 1, v[58:59]
	global_store_dwordx4 v[58:59], v[50:53], off sc0 sc1
	s_waitcnt lgkmcnt(0)
	s_nop 0
	v_add_f32_e32 v50, v60, v61
	ds_bpermute_b32 v51, v191, v50
	v_cvt_pk_bf16_f32 v52, v54, v55
	v_cvt_pk_bf16_f32 v53, v56, v57
	v_cvt_pk_bf16_f32 v54, v122, v123
	v_cvt_pk_bf16_f32 v55, v120, v121
	global_store_dwordx4 v[58:59], v[52:55], off offset:256 sc0 sc1
	s_and_saveexec_b64 s[0:1], vcc
	s_cbranch_execz .LBB0_555
	v_lshl_or_b32 v52, v0, 4, s15
	s_waitcnt lgkmcnt(0)
	v_add_f32_e32 v50, v50, v51
	ds_write_b32 v52, v50 offset:2048
.LBB0_555:
	s_or_b64 exec, exec, s[0:1]
	s_waitcnt vmcnt(12)
	v_pk_add_f32 v[46:47], v[46:47], v[110:111]
	v_pk_add_f32 v[48:49], v[48:49], v[112:113]
	v_pk_add_f32 v[54:55], v[42:43], v[106:107]
	v_cvt_pk_bf16_f32 v42, v46, v47
	v_mul_f32_e32 v47, v47, v47
	v_fmac_f32_e32 v47, v46, v46
	v_mul_f32_e32 v46, v49, v49
	v_pk_add_f32 v[52:53], v[44:45], v[108:109]
	v_fmac_f32_e32 v46, v48, v48
	v_cvt_pk_bf16_f32 v43, v48, v49
	v_add_f32_e32 v46, v47, v46
	v_mul_f32_e32 v47, v55, v55
	v_mul_f32_e32 v48, v53, v53
	v_fmac_f32_e32 v47, v54, v54
	v_fmac_f32_e32 v48, v52, v52
	s_waitcnt vmcnt(10)
	v_pk_add_f32 v[40:41], v[40:41], v[104:105]
	v_pk_add_f32 v[38:39], v[38:39], v[102:103]
	v_add_f32_e32 v47, v47, v48
	v_pk_add_f32 v[48:49], v[34:35], v[98:99]
	v_mul_f32_e32 v34, v39, v39
	v_mul_f32_e32 v35, v41, v41
	v_cvt_pk_bf16_f32 v45, v52, v53
	v_add_f32_e32 v52, v46, v47
	v_pk_add_f32 v[46:47], v[36:37], v[100:101]
	v_fmac_f32_e32 v34, v38, v38
	v_fmac_f32_e32 v35, v40, v40
	v_add_f32_e32 v34, v34, v35
	v_mul_f32_e32 v35, v49, v49
	v_mul_f32_e32 v36, v47, v47
	v_fmac_f32_e32 v35, v48, v48
	v_fmac_f32_e32 v36, v46, v46
	v_add_f32_e32 v35, v35, v36
	v_add_f32_e32 v34, v34, v35
	v_add_f32_e32 v37, v52, v34
	ds_bpermute_b32 v52, v192, v37
	s_waitcnt lgkmcnt(1)
	v_lshlrev_b64 v[50:51], 11, v[118:119]
	v_lshl_add_u64 v[34:35], s[16:17], 0, v[50:51]
	v_lshl_add_u64 v[50:51], v[178:179], 1, v[34:35]
	v_cvt_pk_bf16_f32 v44, v54, v55
	s_waitcnt lgkmcnt(0)
	v_add_f32_e32 v34, v37, v52
	ds_bpermute_b32 v35, v191, v34
	v_cvt_pk_bf16_f32 v36, v38, v39
	v_cvt_pk_bf16_f32 v37, v40, v41
	v_cvt_pk_bf16_f32 v38, v48, v49
	v_cvt_pk_bf16_f32 v39, v46, v47
	global_store_dwordx4 v[50:51], v[42:45], off sc0 sc1
	global_store_dwordx4 v[50:51], v[36:39], off offset:256 sc0 sc1
	s_and_saveexec_b64 s[0:1], vcc
	s_cbranch_execz .LBB0_557
	v_lshl_or_b32 v36, v0, 4, s15
	s_waitcnt lgkmcnt(0)
	v_add_f32_e32 v34, v34, v35
	ds_write_b32 v36, v34 offset:2304
.LBB0_557:
	s_or_b64 exec, exec, s[0:1]
	s_waitcnt vmcnt(10)
	v_pk_add_f32 v[30:31], v[30:31], v[94:95]
	v_pk_add_f32 v[32:33], v[32:33], v[96:97]
	v_pk_add_f32 v[38:39], v[26:27], v[90:91]
	v_cvt_pk_bf16_f32 v26, v30, v31
	v_mul_f32_e32 v31, v31, v31
	v_fmac_f32_e32 v31, v30, v30
	v_mul_f32_e32 v30, v33, v33
	v_pk_add_f32 v[36:37], v[28:29], v[92:93]
	v_fmac_f32_e32 v30, v32, v32
	v_cvt_pk_bf16_f32 v27, v32, v33
	v_add_f32_e32 v30, v31, v30
	v_mul_f32_e32 v31, v39, v39
	v_mul_f32_e32 v32, v37, v37
	v_fmac_f32_e32 v31, v38, v38
	v_fmac_f32_e32 v32, v36, v36
	s_waitcnt vmcnt(8)
	v_pk_add_f32 v[24:25], v[24:25], v[88:89]
	v_pk_add_f32 v[22:23], v[22:23], v[86:87]
	v_add_f32_e32 v31, v31, v32
	v_pk_add_f32 v[32:33], v[18:19], v[82:83]
	v_mul_f32_e32 v18, v23, v23
	v_mul_f32_e32 v19, v25, v25
	v_cvt_pk_bf16_f32 v29, v36, v37
	v_add_f32_e32 v36, v30, v31
	v_pk_add_f32 v[30:31], v[20:21], v[84:85]
	v_fmac_f32_e32 v18, v22, v22
	v_fmac_f32_e32 v19, v24, v24
	v_add_f32_e32 v18, v18, v19
	v_mul_f32_e32 v19, v33, v33
	v_mul_f32_e32 v20, v31, v31
	v_fmac_f32_e32 v19, v32, v32
	v_fmac_f32_e32 v20, v30, v30
	v_add_f32_e32 v19, v19, v20
	v_add_f32_e32 v18, v18, v19
	v_add_f32_e32 v21, v36, v18
	ds_bpermute_b32 v36, v192, v21
	s_waitcnt lgkmcnt(1)
	v_lshlrev_b64 v[34:35], 11, v[116:117]
	v_lshl_add_u64 v[18:19], s[16:17], 0, v[34:35]
	v_lshl_add_u64 v[34:35], v[178:179], 1, v[18:19]
	v_cvt_pk_bf16_f32 v28, v38, v39
	s_waitcnt lgkmcnt(0)
	v_add_f32_e32 v18, v21, v36
	ds_bpermute_b32 v19, v191, v18
	v_cvt_pk_bf16_f32 v20, v22, v23
	v_cvt_pk_bf16_f32 v21, v24, v25
	v_cvt_pk_bf16_f32 v22, v32, v33
	v_cvt_pk_bf16_f32 v23, v30, v31
	global_store_dwordx4 v[34:35], v[26:29], off sc0 sc1
	global_store_dwordx4 v[34:35], v[20:23], off offset:256 sc0 sc1
	s_and_saveexec_b64 s[0:1], vcc
	s_cbranch_execz .LBB0_559
	v_lshl_or_b32 v20, v0, 4, s15
	s_waitcnt lgkmcnt(0)
	v_add_f32_e32 v18, v18, v19
	ds_write_b32 v20, v18 offset:2560
.LBB0_559:
	s_or_b64 exec, exec, s[0:1]
	s_waitcnt vmcnt(8)
	v_pk_add_f32 v[14:15], v[14:15], v[78:79]
	v_pk_add_f32 v[16:17], v[16:17], v[80:81]
	v_pk_add_f32 v[22:23], v[10:11], v[74:75]
	v_cvt_pk_bf16_f32 v10, v14, v15
	v_mul_f32_e32 v15, v15, v15
	v_fmac_f32_e32 v15, v14, v14
	v_mul_f32_e32 v14, v17, v17
	v_pk_add_f32 v[20:21], v[12:13], v[76:77]
	v_fmac_f32_e32 v14, v16, v16
	v_cvt_pk_bf16_f32 v11, v16, v17
	v_add_f32_e32 v14, v15, v14
	v_mul_f32_e32 v15, v23, v23
	v_mul_f32_e32 v16, v21, v21
	v_fmac_f32_e32 v15, v22, v22
	v_fmac_f32_e32 v16, v20, v20
	s_waitcnt vmcnt(6)
	v_pk_add_f32 v[8:9], v[8:9], v[72:73]
	v_pk_add_f32 v[6:7], v[6:7], v[70:71]
	v_add_f32_e32 v15, v15, v16
	v_pk_add_f32 v[16:17], v[2:3], v[66:67]
	v_mul_f32_e32 v2, v7, v7
	v_mul_f32_e32 v3, v9, v9
	v_cvt_pk_bf16_f32 v13, v20, v21
	v_add_f32_e32 v20, v14, v15
	v_pk_add_f32 v[14:15], v[4:5], v[68:69]
	v_fmac_f32_e32 v2, v6, v6
	v_fmac_f32_e32 v3, v8, v8
	v_add_f32_e32 v2, v2, v3
	v_mul_f32_e32 v3, v17, v17
	v_mul_f32_e32 v4, v15, v15
	v_fmac_f32_e32 v3, v16, v16
	v_fmac_f32_e32 v4, v14, v14
	v_add_f32_e32 v3, v3, v4
	v_add_f32_e32 v2, v2, v3
	v_add_f32_e32 v5, v20, v2
	ds_bpermute_b32 v20, v192, v5
	s_waitcnt lgkmcnt(1)
	v_lshlrev_b64 v[18:19], 11, v[114:115]
	v_lshl_add_u64 v[2:3], s[16:17], 0, v[18:19]
	v_lshl_add_u64 v[18:19], v[178:179], 1, v[2:3]
	v_cvt_pk_bf16_f32 v12, v22, v23
	s_waitcnt lgkmcnt(0)
	v_add_f32_e32 v2, v5, v20
	ds_bpermute_b32 v3, v191, v2
	v_cvt_pk_bf16_f32 v4, v6, v7
	v_cvt_pk_bf16_f32 v5, v8, v9
	v_cvt_pk_bf16_f32 v6, v16, v17
	v_cvt_pk_bf16_f32 v7, v14, v15
	global_store_dwordx4 v[18:19], v[10:13], off sc0 sc1
	global_store_dwordx4 v[18:19], v[4:7], off offset:256 sc0 sc1
	s_and_saveexec_b64 s[0:1], vcc
	s_cbranch_execz .LBB0_561
	v_lshl_or_b32 v0, v0, 4, s15
	s_waitcnt lgkmcnt(0)
	v_add_f32_e32 v2, v2, v3
	ds_write_b32 v0, v2 offset:2816

.LBB0_582:
	v_lshrrev_b64 v[8:9], 8, v[6:7]
	v_and_b32_e32 v8, -4, v8
	v_lshl_add_u64 v[8:9], s[48:49], 0, v[8:9]
	global_load_dword v0, v[8:9], off
	s_nop 0
	global_load_dwordx4 v[8:11], v[2:3], off nt
	v_lshl_add_u64 v[6:7], v[6:7], 0, s[4:5]
	s_mov_b64 s[54:55], 0xfffff
	v_cmp_lt_u64_e32 vcc, s[54:55], v[6:7]
	v_lshl_add_u64 v[2:3], v[2:3], 0, s[68:69]
	s_or_b64 s[50:51], vcc, s[50:51]
	s_waitcnt vmcnt(0)
	v_pk_mul_f32 v[8:9], v[0:1], v[8:9] op_sel_hi:[0,1]
	v_pk_mul_f32 v[10:11], v[0:1], v[10:11] op_sel_hi:[0,1]
	v_cvt_pk_bf16_f32 v8, v8, v9
	v_cvt_pk_bf16_f32 v9, v10, v11
	global_store_dwordx2 v[4:5], v[8:9], off sc0 sc1
	v_lshl_add_u64 v[4:5], v[4:5], 0, s[8:9]
	s_andn2_b64 exec, exec, s[50:51]
	s_cbranch_execnz .LBB0_582

.LBB0_585:
	s_ashr_i32 s35, s29, 31
	s_lshr_b32 s35, s35, 27
	s_add_i32 s35, s29, s35
	s_ashr_i32 s35, s35, 5
	s_lshl_b32 s48, s35, 6
	s_lshl_b32 s35, s35, 10
	s_sub_i32 s46, s31, s35
	v_or_b32_e32 v38, s48, v102
	s_ashr_i32 s47, s46, 31
	v_ashrrev_i32_e32 v39, 31, v38
	v_or_b32_e32 v10, 8, v38
	v_lshl_add_u64 v[54:55], s[46:47], 2, v[2:3]
	v_lshlrev_b64 v[6:7], 12, v[38:39]
	v_ashrrev_i32_e32 v11, 31, v10
	v_lshl_add_u64 v[6:7], v[54:55], 0, v[6:7]
	v_lshlrev_b64 v[10:11], 12, v[10:11]
	v_or_b32_e32 v14, 16, v38
	global_load_dwordx4 v[6:9], v[6:7], off nt
	v_lshl_add_u64 v[10:11], v[54:55], 0, v[10:11]
	v_ashrrev_i32_e32 v15, 31, v14
	global_load_dwordx4 v[10:13], v[10:11], off nt
	v_lshlrev_b64 v[14:15], 12, v[14:15]
	v_or_b32_e32 v34, 24, v38
	v_lshl_add_u64 v[14:15], v[54:55], 0, v[14:15]
	v_ashrrev_i32_e32 v35, 31, v34
	global_load_dwordx4 v[14:17], v[14:15], off nt
	v_lshlrev_b64 v[34:35], 12, v[34:35]
	v_or_b32_e32 v42, 32, v38
	v_lshl_add_u64 v[34:35], v[54:55], 0, v[34:35]
	v_ashrrev_i32_e32 v43, 31, v42
	global_load_dwordx4 v[34:37], v[34:35], off nt
	v_lshlrev_b64 v[42:43], 12, v[42:43]
	v_or_b32_e32 v46, 40, v38
	v_lshl_add_u64 v[42:43], v[54:55], 0, v[42:43]
	v_ashrrev_i32_e32 v47, 31, v46
	global_load_dwordx4 v[42:45], v[42:43], off nt
	v_lshlrev_b64 v[46:47], 12, v[46:47]
	v_or_b32_e32 v50, 48, v38
	v_lshl_add_u64 v[46:47], v[54:55], 0, v[46:47]
	v_ashrrev_i32_e32 v51, 31, v50
	global_load_dwordx4 v[46:49], v[46:47], off nt
	v_lshlrev_b64 v[50:51], 12, v[50:51]
	v_or_b32_e32 v38, 56, v38
	v_lshl_add_u64 v[50:51], v[54:55], 0, v[50:51]
	v_ashrrev_i32_e32 v39, 31, v38
	global_load_dwordx4 v[50:53], v[50:51], off nt
	v_lshlrev_b64 v[38:39], 12, v[38:39]
	v_lshl_add_u64 v[38:39], v[54:55], 0, v[38:39]
	global_load_dwordx4 v[54:57], v[38:39], off nt
	v_add_u32_e32 v0, v40, v71
	s_ashr_i32 s49, s48, 31
	s_add_i32 s29, s29, s72
	s_add_i32 s31, s31, s28
	s_cmpk_lt_i32 s29, 0x200
	s_waitcnt vmcnt(7)
	ds_write2_b32 v0, v6, v7 offset1:1
	ds_write2_b32 v0, v8, v9 offset0:2 offset1:3
	v_add_u32_e32 v6, 0x420, v0
	s_waitcnt vmcnt(6)
	ds_write2_b32 v6, v10, v11 offset1:1
	v_add_u32_e32 v6, 0x428, v0
	ds_write2_b32 v6, v12, v13 offset1:1
	v_add_u32_e32 v6, 0x840, v0
	v_lshl_add_u64 v[10:11], s[48:49], 1, v[4:5]
	s_waitcnt vmcnt(5)
	ds_write2_b32 v6, v14, v15 offset1:1
	v_add_u32_e32 v6, 0x848, v0
	ds_write2_b32 v6, v16, v17 offset1:1
	v_add_u32_e32 v6, 0xc60, v0
	s_waitcnt vmcnt(4)
	ds_write2_b32 v6, v34, v35 offset1:1
	v_add_u32_e32 v6, 0xc68, v0
	ds_write2_b32 v6, v36, v37 offset1:1
	v_add_u32_e32 v6, 0x1080, v0
	s_waitcnt vmcnt(3)
	ds_write2_b32 v6, v42, v43 offset1:1
	v_add_u32_e32 v6, 0x1088, v0
	ds_write2_b32 v6, v44, v45 offset1:1
	v_add_u32_e32 v6, 0x14a0, v0
	s_waitcnt vmcnt(2)
	ds_write2_b32 v6, v46, v47 offset1:1
	v_add_u32_e32 v6, 0x14a8, v0
	ds_write2_b32 v6, v48, v49 offset1:1
	v_add_u32_e32 v6, 0x18c0, v0
	v_add_u32_e32 v46, s46, v102
	s_waitcnt vmcnt(1)
	ds_write2_b32 v6, v50, v51 offset1:1
	v_add_u32_e32 v6, 0x18c8, v0
	ds_write2_b32 v6, v52, v53 offset1:1
	v_add_u32_e32 v6, 0x1ce0, v0
	v_add_u32_e32 v0, 0x1ce8, v0
	s_waitcnt vmcnt(0)
	ds_write2_b32 v6, v54, v55 offset1:1
	ds_write2_b32 v0, v56, v57 offset1:1
	s_waitcnt lgkmcnt(0)
	ds_read2_b32 v[12:13], v41 offset0:33 offset1:41
	ds_read2_b32 v[14:15], v41 offset1:8
	ds_read2_b32 v[16:17], v41 offset0:66 offset1:74
	ds_read2_b32 v[34:35], v41 offset0:99 offset1:107
	ds_read2_b32 v[36:37], v41 offset0:132 offset1:140
	ds_read2_b32 v[38:39], v41 offset0:165 offset1:173
	ds_read2_b32 v[42:43], v41 offset0:198 offset1:206
	ds_read2_b32 v[44:45], v41 offset0:231 offset1:239
	v_ashrrev_i32_e32 v47, 31, v46
	v_lshlrev_b64 v[48:49], 11, v[46:47]
	s_waitcnt lgkmcnt(6)
	v_cvt_pk_bf16_f32 v6, v14, v12
	s_waitcnt lgkmcnt(4)
	v_cvt_pk_bf16_f32 v7, v16, v34
	s_waitcnt lgkmcnt(2)
	v_cvt_pk_bf16_f32 v8, v36, v38
	s_waitcnt lgkmcnt(0)
	v_cvt_pk_bf16_f32 v9, v42, v44
	v_lshl_add_u64 v[48:49], v[10:11], 0, v[48:49]
	v_add_u32_e32 v12, 8, v46
	global_store_dwordx4 v[48:49], v[6:9], off sc0 sc1
	v_add_u32_e32 v48, 16, v46
	v_ashrrev_i32_e32 v49, 31, v48
	v_cvt_pk_bf16_f32 v6, v15, v13
	v_ashrrev_i32_e32 v13, 31, v12
	v_lshlrev_b64 v[12:13], 11, v[12:13]
	v_cvt_pk_bf16_f32 v7, v17, v35
	v_cvt_pk_bf16_f32 v8, v37, v39
	v_cvt_pk_bf16_f32 v9, v43, v45
	v_lshl_add_u64 v[12:13], v[10:11], 0, v[12:13]
	global_store_dwordx4 v[12:13], v[6:9], off sc0 sc1
	ds_read2_b32 v[12:13], v41 offset0:49 offset1:57
	ds_read2_b32 v[14:15], v41 offset0:16 offset1:24
	ds_read2_b32 v[16:17], v41 offset0:82 offset1:90
	ds_read2_b32 v[34:35], v41 offset0:115 offset1:123
	ds_read2_b32 v[36:37], v41 offset0:148 offset1:156
	ds_read2_b32 v[38:39], v41 offset0:181 offset1:189
	ds_read2_b32 v[42:43], v41 offset0:214 offset1:222
	ds_read2_b32 v[44:45], v41 offset0:247 offset1:255
	v_lshlrev_b64 v[48:49], 11, v[48:49]
	s_waitcnt lgkmcnt(6)
	v_cvt_pk_bf16_f32 v6, v14, v12
	s_waitcnt lgkmcnt(4)
	v_cvt_pk_bf16_f32 v7, v16, v34
	s_waitcnt lgkmcnt(2)
	v_cvt_pk_bf16_f32 v8, v36, v38
	s_waitcnt lgkmcnt(0)
	v_cvt_pk_bf16_f32 v9, v42, v44
	v_lshl_add_u64 v[48:49], v[10:11], 0, v[48:49]
	v_add_u32_e32 v12, 24, v46
	global_store_dwordx4 v[48:49], v[6:9], off sc0 sc1
	s_nop 1
	v_cvt_pk_bf16_f32 v6, v15, v13
	v_ashrrev_i32_e32 v13, 31, v12
	v_lshlrev_b64 v[12:13], 11, v[12:13]
	v_cvt_pk_bf16_f32 v7, v17, v35
	v_cvt_pk_bf16_f32 v8, v37, v39
	v_cvt_pk_bf16_f32 v9, v43, v45
	v_lshl_add_u64 v[10:11], v[10:11], 0, v[12:13]
	global_store_dwordx4 v[10:11], v[6:9], off sc0 sc1
	s_waitcnt lgkmcnt(0)
	s_cbranch_scc1 .LBB0_585

.LBB0_588:
	s_ashr_i32 s46, s29, 31
	s_lshr_b32 s46, s46, 26
	s_add_i32 s46, s29, s46
	s_and_b32 s48, s46, 0xffffffc0
	s_lshl_b32 s46, s46, 5
	s_and_b32 s46, s46, 0xfffff800
	s_sub_i32 s46, s35, s46
	v_or_b32_e32 v38, s48, v102
	s_ashr_i32 s47, s46, 31
	v_ashrrev_i32_e32 v39, 31, v38
	v_or_b32_e32 v10, 8, v38
	v_lshl_add_u64 v[54:55], s[46:47], 2, v[4:5]
	v_lshlrev_b64 v[6:7], 13, v[38:39]
	v_ashrrev_i32_e32 v11, 31, v10
	v_lshl_add_u64 v[6:7], v[54:55], 0, v[6:7]
	v_lshlrev_b64 v[10:11], 13, v[10:11]
	v_or_b32_e32 v14, 16, v38
	global_load_dwordx4 v[6:9], v[6:7], off nt
	v_lshl_add_u64 v[10:11], v[54:55], 0, v[10:11]
	v_ashrrev_i32_e32 v15, 31, v14
	global_load_dwordx4 v[10:13], v[10:11], off nt
	v_lshlrev_b64 v[14:15], 13, v[14:15]
	v_or_b32_e32 v34, 24, v38
	v_lshl_add_u64 v[14:15], v[54:55], 0, v[14:15]
	v_ashrrev_i32_e32 v35, 31, v34
	global_load_dwordx4 v[14:17], v[14:15], off nt
	v_lshlrev_b64 v[34:35], 13, v[34:35]
	v_or_b32_e32 v42, 32, v38
	v_lshl_add_u64 v[34:35], v[54:55], 0, v[34:35]
	v_ashrrev_i32_e32 v43, 31, v42
	global_load_dwordx4 v[34:37], v[34:35], off nt
	v_lshlrev_b64 v[42:43], 13, v[42:43]
	v_or_b32_e32 v46, 40, v38
	v_lshl_add_u64 v[42:43], v[54:55], 0, v[42:43]
	v_ashrrev_i32_e32 v47, 31, v46
	global_load_dwordx4 v[42:45], v[42:43], off nt
	v_lshlrev_b64 v[46:47], 13, v[46:47]
	v_or_b32_e32 v50, 48, v38
	v_lshl_add_u64 v[46:47], v[54:55], 0, v[46:47]
	v_ashrrev_i32_e32 v51, 31, v50
	global_load_dwordx4 v[46:49], v[46:47], off nt
	v_lshlrev_b64 v[50:51], 13, v[50:51]
	v_or_b32_e32 v38, 56, v38
	v_lshl_add_u64 v[50:51], v[54:55], 0, v[50:51]
	v_ashrrev_i32_e32 v39, 31, v38
	global_load_dwordx4 v[50:53], v[50:51], off nt
	v_lshlrev_b64 v[38:39], 13, v[38:39]
	v_lshl_add_u64 v[38:39], v[54:55], 0, v[38:39]
	global_load_dwordx4 v[54:57], v[38:39], off nt
	v_add_u32_e32 v0, v40, v71
	s_ashr_i32 s49, s48, 31
	s_add_i32 s29, s29, s72
	s_add_i32 s35, s35, s28
	s_cmpk_lt_i32 s29, 0x400
	s_waitcnt vmcnt(7)
	ds_write2_b32 v0, v6, v7 offset1:1
	ds_write2_b32 v0, v8, v9 offset0:2 offset1:3
	v_add_u32_e32 v6, 0x420, v0
	s_waitcnt vmcnt(6)
	ds_write2_b32 v6, v10, v11 offset1:1
	v_add_u32_e32 v6, 0x428, v0
	ds_write2_b32 v6, v12, v13 offset1:1
	v_add_u32_e32 v6, 0x840, v0
	v_lshl_add_u64 v[10:11], s[48:49], 1, v[2:3]
	s_waitcnt vmcnt(5)
	ds_write2_b32 v6, v14, v15 offset1:1
	v_add_u32_e32 v6, 0x848, v0
	ds_write2_b32 v6, v16, v17 offset1:1
	v_add_u32_e32 v6, 0xc60, v0
	s_waitcnt vmcnt(4)
	ds_write2_b32 v6, v34, v35 offset1:1
	v_add_u32_e32 v6, 0xc68, v0
	ds_write2_b32 v6, v36, v37 offset1:1
	v_add_u32_e32 v6, 0x1080, v0
	s_waitcnt vmcnt(3)
	ds_write2_b32 v6, v42, v43 offset1:1
	v_add_u32_e32 v6, 0x1088, v0
	ds_write2_b32 v6, v44, v45 offset1:1
	v_add_u32_e32 v6, 0x14a0, v0
	s_waitcnt vmcnt(2)
	ds_write2_b32 v6, v46, v47 offset1:1
	v_add_u32_e32 v6, 0x14a8, v0
	ds_write2_b32 v6, v48, v49 offset1:1
	v_add_u32_e32 v6, 0x18c0, v0
	v_add_u32_e32 v46, s46, v102
	s_waitcnt vmcnt(1)
	ds_write2_b32 v6, v50, v51 offset1:1
	v_add_u32_e32 v6, 0x18c8, v0
	ds_write2_b32 v6, v52, v53 offset1:1
	v_add_u32_e32 v6, 0x1ce0, v0
	v_add_u32_e32 v0, 0x1ce8, v0
	s_waitcnt vmcnt(0)
	ds_write2_b32 v6, v54, v55 offset1:1
	ds_write2_b32 v0, v56, v57 offset1:1
	s_waitcnt lgkmcnt(0)
	ds_read2_b32 v[12:13], v41 offset0:33 offset1:41
	ds_read2_b32 v[14:15], v41 offset1:8
	ds_read2_b32 v[16:17], v41 offset0:66 offset1:74
	ds_read2_b32 v[34:35], v41 offset0:99 offset1:107
	ds_read2_b32 v[36:37], v41 offset0:132 offset1:140
	ds_read2_b32 v[38:39], v41 offset0:165 offset1:173
	ds_read2_b32 v[42:43], v41 offset0:198 offset1:206
	ds_read2_b32 v[44:45], v41 offset0:231 offset1:239
	v_ashrrev_i32_e32 v47, 31, v46
	v_lshlrev_b64 v[48:49], 11, v[46:47]
	s_waitcnt lgkmcnt(6)
	v_cvt_pk_bf16_f32 v6, v14, v12
	s_waitcnt lgkmcnt(4)
	v_cvt_pk_bf16_f32 v7, v16, v34
	s_waitcnt lgkmcnt(2)
	v_cvt_pk_bf16_f32 v8, v36, v38
	s_waitcnt lgkmcnt(0)
	v_cvt_pk_bf16_f32 v9, v42, v44
	v_lshl_add_u64 v[48:49], v[10:11], 0, v[48:49]
	v_add_u32_e32 v12, 8, v46
	global_store_dwordx4 v[48:49], v[6:9], off sc0 sc1
	v_add_u32_e32 v48, 16, v46
	v_ashrrev_i32_e32 v49, 31, v48
	v_cvt_pk_bf16_f32 v6, v15, v13
	v_ashrrev_i32_e32 v13, 31, v12
	v_lshlrev_b64 v[12:13], 11, v[12:13]
	v_cvt_pk_bf16_f32 v7, v17, v35
	v_cvt_pk_bf16_f32 v8, v37, v39
	v_cvt_pk_bf16_f32 v9, v43, v45
	v_lshl_add_u64 v[12:13], v[10:11], 0, v[12:13]
	global_store_dwordx4 v[12:13], v[6:9], off sc0 sc1
	ds_read2_b32 v[12:13], v41 offset0:49 offset1:57
	ds_read2_b32 v[14:15], v41 offset0:16 offset1:24
	ds_read2_b32 v[16:17], v41 offset0:82 offset1:90
	ds_read2_b32 v[34:35], v41 offset0:115 offset1:123
	ds_read2_b32 v[36:37], v41 offset0:148 offset1:156
	ds_read2_b32 v[38:39], v41 offset0:181 offset1:189
	ds_read2_b32 v[42:43], v41 offset0:214 offset1:222
	ds_read2_b32 v[44:45], v41 offset0:247 offset1:255
	v_lshlrev_b64 v[48:49], 11, v[48:49]
	s_waitcnt lgkmcnt(6)
	v_cvt_pk_bf16_f32 v6, v14, v12
	s_waitcnt lgkmcnt(4)
	v_cvt_pk_bf16_f32 v7, v16, v34
	s_waitcnt lgkmcnt(2)
	v_cvt_pk_bf16_f32 v8, v36, v38
	s_waitcnt lgkmcnt(0)
	v_cvt_pk_bf16_f32 v9, v42, v44
	v_lshl_add_u64 v[48:49], v[10:11], 0, v[48:49]
	v_add_u32_e32 v12, 24, v46
	global_store_dwordx4 v[48:49], v[6:9], off sc0 sc1
	s_nop 1
	v_cvt_pk_bf16_f32 v6, v15, v13
	v_ashrrev_i32_e32 v13, 31, v12
	v_lshlrev_b64 v[12:13], 11, v[12:13]
	v_cvt_pk_bf16_f32 v7, v17, v35
	v_cvt_pk_bf16_f32 v8, v37, v39
	v_cvt_pk_bf16_f32 v9, v43, v45
	v_lshl_add_u64 v[10:11], v[10:11], 0, v[12:13]
	global_store_dwordx4 v[10:11], v[6:9], off sc0 sc1
	s_waitcnt lgkmcnt(0)
	s_cbranch_scc1 .LBB0_588

.LBB0_591:
	global_load_dwordx4 v[2:5], v[36:37], off offset:-2048 nt
	s_add_i32 s29, s29, s72
	s_cmpk_lt_i32 s29, 0x200
	s_waitcnt vmcnt(0)
	v_pk_mul_f32 v[6:7], v[4:5], v[4:5]
	v_pk_mul_f32 v[8:9], v[2:3], v[2:3]
	s_nop 0
	v_pk_mov_b32 v[10:11], v[8:9], v[6:7] op_sel:[1,0]
	v_mov_b32_e32 v9, v7
	v_pk_add_f32 v[48:49], v[10:11], v[8:9]
	global_load_dwordx4 v[10:13], v[36:37], off offset:-1024 nt
	v_pk_add_f32 v[48:49], v[48:49], v[48:49] op_sel:[0,1] op_sel_hi:[1,0]
	s_waitcnt vmcnt(0)
	v_pk_mul_f32 v[6:7], v[12:13], v[12:13]
	v_pk_mul_f32 v[8:9], v[10:11], v[10:11]
	s_nop 0
	v_pk_mov_b32 v[14:15], v[8:9], v[6:7] op_sel:[1,0]
	v_mov_b32_e32 v9, v7
	v_pk_add_f32 v[50:51], v[14:15], v[8:9]
	global_load_dwordx4 v[14:17], v[36:37], off nt
	global_load_dwordx4 v[6:9], v[36:37], off offset:1024 nt
	v_pk_add_f32 v[50:51], v[50:51], v[50:51] op_sel:[0,1] op_sel_hi:[1,0]
	v_lshl_add_u64 v[36:37], v[36:37], 0, s[76:77]
	s_waitcnt vmcnt(0)
	v_mul_f32_e32 v0, v6, v6
	v_mul_f32_e32 v52, v7, v7
	v_mov_b32_e32 v49, v0
	v_mov_b32_e32 v51, v52
	v_mul_f32_e32 v0, v15, v15
	v_mul_f32_e32 v53, v8, v8
	v_pk_add_f32 v[48:49], v[48:49], v[50:51]
	v_pk_fma_f32 v[50:51], v[14:15], v[14:15], v[0:1] op_sel_hi:[1,1,0]
	v_mul_f32_e32 v0, v17, v17
	v_mul_f32_e32 v54, v9, v9
	v_mov_b32_e32 v51, v53
	v_pk_fma_f32 v[52:53], v[16:17], v[16:17], v[0:1] op_sel_hi:[1,1,0]
	s_nop 0
	v_mov_b32_e32 v53, v54
	v_pk_add_f32 v[50:51], v[50:51], v[52:53]
	s_nop 0
	v_pk_add_f32 v[48:49], v[48:49], v[50:51]
	s_nop 0
	v_add_f32_e32 v0, v48, v49
	ds_bpermute_b32 v48, v42, v0
	s_waitcnt lgkmcnt(0)
	v_add_f32_e32 v0, v0, v48
	ds_bpermute_b32 v48, v43, v0
	s_waitcnt lgkmcnt(0)
	v_add_f32_e32 v0, v0, v48
	ds_bpermute_b32 v48, v44, v0
	s_waitcnt lgkmcnt(0)
	v_add_f32_e32 v0, v0, v48
	ds_bpermute_b32 v48, v45, v0
	s_waitcnt lgkmcnt(0)
	v_add_f32_e32 v0, v0, v48
	ds_bpermute_b32 v48, v46, v0
	s_waitcnt lgkmcnt(0)
	v_add_f32_e32 v0, v0, v48
	ds_bpermute_b32 v48, v47, v0
	s_waitcnt lgkmcnt(0)
	v_add_f32_e32 v0, v0, v48
	v_fmamk_f32 v0, v0, 0x3a800000, v196
	v_cmp_gt_f32_e32 vcc, s96, v0
	v_mul_f32_e32 v48, 0x4b800000, v0
	s_nop 0
	v_cndmask_b32_e32 v0, v0, v48, vcc
	v_rsq_f32_e32 v0, v0
	s_nop 0
	v_mul_f32_e32 v48, 0x45800000, v0
	v_cndmask_b32_e32 v0, v0, v48, vcc
	global_load_dwordx4 v[48:51], v[34:35], off nt
	v_pk_mul_f32 v[2:3], v[2:3], v[0:1] op_sel_hi:[1,0]
	v_pk_mul_f32 v[4:5], v[4:5], v[0:1] op_sel_hi:[1,0]
	v_pk_mul_f32 v[10:11], v[10:11], v[0:1] op_sel_hi:[1,0]
	v_pk_mul_f32 v[6:7], v[6:7], v[0:1] op_sel_hi:[1,0]
	s_waitcnt vmcnt(0)
	v_pk_mul_f32 v[2:3], v[48:49], v[2:3]
	v_pk_mul_f32 v[4:5], v[50:51], v[4:5]
	v_cvt_pk_bf16_f32 v2, v2, v3
	v_cvt_pk_bf16_f32 v3, v4, v5
	global_store_dwordx2 v[38:39], v[2:3], off offset:-1024 sc0 sc1
	global_load_dwordx4 v[2:5], v[34:35], off offset:1024 nt
	s_waitcnt vmcnt(0)
	v_pk_mul_f32 v[2:3], v[2:3], v[10:11]
	v_pk_mul_f32 v[10:11], v[12:13], v[0:1] op_sel_hi:[1,0]
	v_cvt_pk_bf16_f32 v2, v2, v3
	v_pk_mul_f32 v[4:5], v[4:5], v[10:11]
	v_pk_mul_f32 v[10:11], v[14:15], v[0:1] op_sel_hi:[1,0]
	v_cvt_pk_bf16_f32 v3, v4, v5
	global_store_dwordx2 v[38:39], v[2:3], off offset:-512 sc0 sc1
	global_load_dwordx4 v[2:5], v[34:35], off offset:2048 nt
	s_waitcnt vmcnt(0)
	v_pk_mul_f32 v[2:3], v[2:3], v[10:11]
	v_pk_mul_f32 v[10:11], v[16:17], v[0:1] op_sel_hi:[1,0]
	v_cvt_pk_bf16_f32 v2, v2, v3
	v_pk_mul_f32 v[4:5], v[4:5], v[10:11]
	s_nop 0
	v_cvt_pk_bf16_f32 v3, v4, v5
	global_store_dwordx2 v[38:39], v[2:3], off sc0 sc1
	global_load_dwordx4 v[2:5], v[34:35], off offset:3072 nt
	s_waitcnt vmcnt(0)
	v_pk_mul_f32 v[2:3], v[2:3], v[6:7]
	v_pk_mul_f32 v[6:7], v[8:9], v[0:1] op_sel_hi:[1,0]
	v_cvt_pk_bf16_f32 v2, v2, v3
	v_pk_mul_f32 v[4:5], v[4:5], v[6:7]
	s_nop 0
	v_cvt_pk_bf16_f32 v3, v4, v5
	global_store_dwordx2 v[38:39], v[2:3], off offset:512 sc0 sc1
	v_lshl_add_u64 v[38:39], v[38:39], 0, s[78:79]
	s_cbranch_scc1 .LBB0_591
	s_branch .LBB0_579

.LBB0_622:
	v_or_b32_e32 v110, 8, v102
	v_or_b32_e32 v108, 16, v102
	s_andn2_b64 vcc, exec, s[46:47]
	v_or_b32_e32 v106, 24, v102
	s_cbranch_vccnz .LBB0_626
	s_and_b64 vcc, exec, s[36:37]
	s_cbranch_vccnz .LBB0_625
	v_and_b32_e32 v0, 7, v235
	v_lshlrev_b32_e32 v112, 4, v0
	v_add3_u32 v67, s34, v112, v71
	s_waitcnt vmcnt(7)
	v_pk_mul_f32 v[30:31], v[30:31], v[68:69] op_sel_hi:[1,0]
	ds_write2_b32 v67, v30, v31 offset1:1
	v_pk_mul_f32 v[30:31], v[32:33], v[68:69] op_sel_hi:[1,0]
	ds_write2_b32 v67, v30, v31 offset0:2 offset1:3
	v_add_u32_e32 v32, 0x420, v67
	s_waitcnt vmcnt(6)
	v_pk_mul_f32 v[30:31], v[38:39], v[66:67] op_sel_hi:[1,0]
	ds_write2_b32 v32, v30, v31 offset1:1
	v_add_u32_e32 v32, 0x428, v67
	v_pk_mul_f32 v[30:31], v[40:41], v[66:67] op_sel_hi:[1,0]
	ds_write2_b32 v32, v30, v31 offset1:1
	v_add_u32_e32 v32, 0x840, v67
	s_waitcnt vmcnt(5)
	v_pk_mul_f32 v[30:31], v[34:35], v[76:77] op_sel_hi:[1,0]
	ds_write2_b32 v32, v30, v31 offset1:1
	v_add_u32_e32 v32, 0x848, v67
	v_pk_mul_f32 v[30:31], v[36:37], v[76:77] op_sel_hi:[1,0]
	ds_write2_b32 v32, v30, v31 offset1:1
	v_add_u32_e32 v32, 0xc60, v67
	s_waitcnt vmcnt(4)
	v_pk_mul_f32 v[30:31], v[46:47], v[74:75] op_sel_hi:[1,0]
	ds_write2_b32 v32, v30, v31 offset1:1
	v_add_u32_e32 v32, 0xc68, v67
	v_pk_mul_f32 v[30:31], v[48:49], v[74:75] op_sel_hi:[1,0]
	ds_write2_b32 v32, v30, v31 offset1:1
	v_add_u32_e32 v32, 0x1080, v67
	s_waitcnt vmcnt(3)
	v_pk_mul_f32 v[30:31], v[42:43], v[84:85] op_sel_hi:[1,0]
	ds_write2_b32 v32, v30, v31 offset1:1
	v_add_u32_e32 v32, 0x1088, v67
	v_pk_mul_f32 v[30:31], v[44:45], v[84:85] op_sel_hi:[1,0]
	ds_write2_b32 v32, v30, v31 offset1:1
	v_add_u32_e32 v32, 0x14a0, v67
	s_waitcnt vmcnt(2)
	v_pk_mul_f32 v[30:31], v[54:55], v[82:83] op_sel_hi:[1,0]
	ds_write2_b32 v32, v30, v31 offset1:1
	v_add_u32_e32 v32, 0x14a8, v67
	v_pk_mul_f32 v[30:31], v[56:57], v[82:83] op_sel_hi:[1,0]
	ds_write2_b32 v32, v30, v31 offset1:1
	v_add_u32_e32 v32, 0x18c0, v67
	s_waitcnt vmcnt(1)
	v_pk_mul_f32 v[30:31], v[50:51], v[92:93] op_sel_hi:[1,0]
	ds_write2_b32 v32, v30, v31 offset1:1
	v_add_u32_e32 v32, 0x18c8, v67
	v_pk_mul_f32 v[30:31], v[52:53], v[92:93] op_sel_hi:[1,0]
	ds_write2_b32 v32, v30, v31 offset1:1
	v_add_u32_e32 v32, 0x1ce0, v67
	s_waitcnt vmcnt(0)
	v_pk_mul_f32 v[30:31], v[58:59], v[90:91] op_sel_hi:[1,0]
	ds_write2_b32 v32, v30, v31 offset1:1
	v_add_u32_e32 v32, 0x1ce8, v67
	v_pk_mul_f32 v[30:31], v[60:61], v[90:91] op_sel_hi:[1,0]
	ds_write2_b32 v32, v30, v31 offset1:1
	s_waitcnt lgkmcnt(0)
	v_mul_u32_u24_e32 v0, 0x420, v0
	v_add3_u32 v52, s34, v0, v73
	ds_read2_b32 v[34:35], v52 offset0:33 offset1:41
	ds_read2_b32 v[36:37], v52 offset1:8
	ds_read2_b32 v[38:39], v52 offset0:66 offset1:74
	ds_read2_b32 v[40:41], v52 offset0:99 offset1:107
	ds_read2_b32 v[42:43], v52 offset0:132 offset1:140
	ds_read2_b32 v[44:45], v52 offset0:165 offset1:173
	ds_read2_b32 v[46:47], v52 offset0:198 offset1:206
	ds_read2_b32 v[48:49], v52 offset0:231 offset1:239
	v_lshlrev_b32_e32 v0, 11, v102
	v_lshl_add_u64 v[50:51], s[16:17], 0, v[0:1]
	v_mov_b32_e32 v113, v1
	s_waitcnt lgkmcnt(0)
	v_cvt_pk_bf16_f32 v30, v36, v34
	v_cvt_pk_bf16_f32 v31, v38, v40
	v_cvt_pk_bf16_f32 v32, v42, v44
	v_cvt_pk_bf16_f32 v33, v46, v48
	v_lshl_add_u64 v[50:51], v[50:51], 0, v[112:113]
	global_store_dwordx4 v[50:51], v[30:33], off sc0 sc1
	v_lshlrev_b32_e32 v0, 11, v110
	s_nop 0
	v_cvt_pk_bf16_f32 v30, v37, v35
	v_cvt_pk_bf16_f32 v31, v39, v41
	v_cvt_pk_bf16_f32 v32, v43, v45
	v_cvt_pk_bf16_f32 v33, v47, v49
	ds_read2_b32 v[36:37], v52 offset0:49 offset1:57
	ds_read2_b32 v[38:39], v52 offset0:16 offset1:24
	ds_read2_b32 v[40:41], v52 offset0:82 offset1:90
	ds_read2_b32 v[42:43], v52 offset0:115 offset1:123
	ds_read2_b32 v[44:45], v52 offset0:148 offset1:156
	ds_read2_b32 v[46:47], v52 offset0:181 offset1:189
	ds_read2_b32 v[48:49], v52 offset0:214 offset1:222
	ds_read2_b32 v[50:51], v52 offset0:247 offset1:255
	v_lshl_add_u64 v[34:35], s[16:17], 0, v[0:1]
	v_lshl_add_u64 v[34:35], v[34:35], 0, v[112:113]
	v_lshlrev_b32_e32 v0, 11, v108
	global_store_dwordx4 v[34:35], v[30:33], off sc0 sc1
	v_lshl_add_u64 v[34:35], s[16:17], 0, v[0:1]
	v_lshl_add_u64 v[34:35], v[34:35], 0, v[112:113]
	s_waitcnt lgkmcnt(6)
	v_cvt_pk_bf16_f32 v30, v38, v36
	s_waitcnt lgkmcnt(4)
	v_cvt_pk_bf16_f32 v31, v40, v42
	s_waitcnt lgkmcnt(2)
	v_cvt_pk_bf16_f32 v32, v44, v46
	s_waitcnt lgkmcnt(0)
	v_cvt_pk_bf16_f32 v33, v48, v50
	v_lshlrev_b32_e32 v0, 11, v106
	global_store_dwordx4 v[34:35], v[30:33], off sc0 sc1
	v_lshl_add_u64 v[34:35], s[16:17], 0, v[0:1]
	v_lshl_add_u64 v[34:35], v[34:35], 0, v[112:113]
	v_cvt_pk_bf16_f32 v30, v39, v37
	v_cvt_pk_bf16_f32 v31, v41, v43
	v_cvt_pk_bf16_f32 v32, v45, v47
	v_cvt_pk_bf16_f32 v33, v49, v51
	global_store_dwordx4 v[34:35], v[30:33], off sc0 sc1
	s_waitcnt lgkmcnt(0)

.LBB0_641:
	s_andn2_b64 vcc, exec, s[38:39]
	s_cbranch_vccnz .LBB0_645
	s_cmp_eq_u32 s31, 0
	s_cbranch_scc1 .LBB0_644
	v_and_b32_e32 v0, 7, v235
	s_waitcnt vmcnt(7)
	v_lshlrev_b32_e32 v30, 4, v0
	v_add3_u32 v31, s34, v30, v71
	v_pk_mul_f32 v[2:3], v[2:3], v[72:73] op_sel_hi:[1,0]
	ds_write2_b32 v31, v2, v3 offset1:1
	v_pk_mul_f32 v[2:3], v[4:5], v[72:73] op_sel_hi:[1,0]
	ds_write2_b32 v31, v2, v3 offset0:2 offset1:3
	v_add_u32_e32 v4, 0x420, v31
	s_waitcnt vmcnt(6)
	v_pk_mul_f32 v[2:3], v[10:11], v[70:71] op_sel_hi:[1,0]
	ds_write2_b32 v4, v2, v3 offset1:1
	v_add_u32_e32 v4, 0x428, v31
	v_pk_mul_f32 v[2:3], v[12:13], v[70:71] op_sel_hi:[1,0]
	ds_write2_b32 v4, v2, v3 offset1:1
	v_add_u32_e32 v4, 0x840, v31
	s_waitcnt vmcnt(5)
	v_pk_mul_f32 v[2:3], v[6:7], v[80:81] op_sel_hi:[1,0]
	ds_write2_b32 v4, v2, v3 offset1:1
	v_add_u32_e32 v4, 0x848, v31
	v_pk_mul_f32 v[2:3], v[8:9], v[80:81] op_sel_hi:[1,0]
	ds_write2_b32 v4, v2, v3 offset1:1
	v_add_u32_e32 v4, 0xc60, v31
	s_waitcnt vmcnt(4)
	v_pk_mul_f32 v[2:3], v[18:19], v[78:79] op_sel_hi:[1,0]
	ds_write2_b32 v4, v2, v3 offset1:1
	v_add_u32_e32 v4, 0xc68, v31
	v_pk_mul_f32 v[2:3], v[20:21], v[78:79] op_sel_hi:[1,0]
	ds_write2_b32 v4, v2, v3 offset1:1
	v_add_u32_e32 v4, 0x1080, v31
	s_waitcnt vmcnt(3)
	v_pk_mul_f32 v[2:3], v[14:15], v[88:89] op_sel_hi:[1,0]
	ds_write2_b32 v4, v2, v3 offset1:1
	v_add_u32_e32 v4, 0x1088, v31
	v_pk_mul_f32 v[2:3], v[16:17], v[88:89] op_sel_hi:[1,0]
	ds_write2_b32 v4, v2, v3 offset1:1
	v_add_u32_e32 v4, 0x14a0, v31
	s_waitcnt vmcnt(2)
	v_pk_mul_f32 v[2:3], v[26:27], v[86:87] op_sel_hi:[1,0]
	ds_write2_b32 v4, v2, v3 offset1:1
	v_add_u32_e32 v4, 0x14a8, v31
	v_pk_mul_f32 v[2:3], v[28:29], v[86:87] op_sel_hi:[1,0]
	ds_write2_b32 v4, v2, v3 offset1:1
	v_add_u32_e32 v4, 0x18c0, v31
	s_waitcnt vmcnt(1)
	v_pk_mul_f32 v[2:3], v[22:23], v[96:97] op_sel_hi:[1,0]
	ds_write2_b32 v4, v2, v3 offset1:1
	v_add_u32_e32 v4, 0x18c8, v31
	v_pk_mul_f32 v[2:3], v[24:25], v[96:97] op_sel_hi:[1,0]
	ds_write2_b32 v4, v2, v3 offset1:1
	v_add_u32_e32 v4, 0x1ce0, v31
	s_waitcnt vmcnt(0)
	v_pk_mul_f32 v[2:3], v[62:63], v[94:95] op_sel_hi:[1,0]
	ds_write2_b32 v4, v2, v3 offset1:1
	v_add_u32_e32 v4, 0x1ce8, v31
	v_pk_mul_f32 v[2:3], v[64:65], v[94:95] op_sel_hi:[1,0]
	ds_write2_b32 v4, v2, v3 offset1:1
	s_waitcnt lgkmcnt(0)
	v_mul_u32_u24_e32 v0, 0x420, v0
	v_add3_u32 v24, s34, v0, v73
	ds_read2_b32 v[6:7], v24 offset0:33 offset1:41
	ds_read2_b32 v[8:9], v24 offset1:8
	ds_read2_b32 v[10:11], v24 offset0:66 offset1:74
	ds_read2_b32 v[12:13], v24 offset0:99 offset1:107
	ds_read2_b32 v[14:15], v24 offset0:132 offset1:140
	ds_read2_b32 v[16:17], v24 offset0:165 offset1:173
	ds_read2_b32 v[18:19], v24 offset0:198 offset1:206
	ds_read2_b32 v[20:21], v24 offset0:231 offset1:239
	v_lshlrev_b32_e32 v0, 11, v102
	v_lshl_add_u64 v[22:23], s[14:15], 0, v[0:1]
	v_mov_b32_e32 v31, v1
	s_waitcnt lgkmcnt(0)
	v_cvt_pk_bf16_f32 v2, v8, v6
	v_cvt_pk_bf16_f32 v3, v10, v12
	v_cvt_pk_bf16_f32 v4, v14, v16
	v_cvt_pk_bf16_f32 v5, v18, v20
	v_lshl_add_u64 v[22:23], v[22:23], 0, v[30:31]
	global_store_dwordx4 v[22:23], v[2:5], off sc0 sc1
	v_lshlrev_b32_e32 v0, 11, v110
	s_nop 0
	v_cvt_pk_bf16_f32 v2, v9, v7
	v_cvt_pk_bf16_f32 v3, v11, v13
	v_cvt_pk_bf16_f32 v4, v15, v17
	v_cvt_pk_bf16_f32 v5, v19, v21
	ds_read2_b32 v[8:9], v24 offset0:49 offset1:57
	ds_read2_b32 v[10:11], v24 offset0:16 offset1:24
	ds_read2_b32 v[12:13], v24 offset0:82 offset1:90
	ds_read2_b32 v[14:15], v24 offset0:115 offset1:123
	ds_read2_b32 v[16:17], v24 offset0:148 offset1:156
	ds_read2_b32 v[18:19], v24 offset0:181 offset1:189
	ds_read2_b32 v[20:21], v24 offset0:214 offset1:222
	ds_read2_b32 v[22:23], v24 offset0:247 offset1:255
	v_lshl_add_u64 v[6:7], s[14:15], 0, v[0:1]
	v_lshl_add_u64 v[6:7], v[6:7], 0, v[30:31]
	v_lshlrev_b32_e32 v0, 11, v108
	global_store_dwordx4 v[6:7], v[2:5], off sc0 sc1
	v_lshl_add_u64 v[6:7], s[14:15], 0, v[0:1]
	v_lshl_add_u64 v[6:7], v[6:7], 0, v[30:31]
	s_waitcnt lgkmcnt(6)
	v_cvt_pk_bf16_f32 v2, v10, v8
	s_waitcnt lgkmcnt(4)
	v_cvt_pk_bf16_f32 v3, v12, v14
	s_waitcnt lgkmcnt(2)
	v_cvt_pk_bf16_f32 v4, v16, v18
	s_waitcnt lgkmcnt(0)
	v_cvt_pk_bf16_f32 v5, v20, v22
	v_lshlrev_b32_e32 v0, 11, v106
	global_store_dwordx4 v[6:7], v[2:5], off sc0 sc1
	v_lshl_add_u64 v[6:7], s[14:15], 0, v[0:1]
	v_lshl_add_u64 v[6:7], v[6:7], 0, v[30:31]
	v_cvt_pk_bf16_f32 v2, v11, v9
	v_cvt_pk_bf16_f32 v3, v13, v15
	v_cvt_pk_bf16_f32 v4, v17, v19
	v_cvt_pk_bf16_f32 v5, v21, v23
	global_store_dwordx4 v[6:7], v[2:5], off sc0 sc1
	s_waitcnt lgkmcnt(0)

.LBB0_660:
	s_andn2_b64 vcc, exec, s[38:39]
	s_cbranch_vccnz .LBB0_664
	s_cmp_eq_u32 s31, 0
	s_cbranch_scc1 .LBB0_663
	v_and_b32_e32 v0, 7, v235
	s_waitcnt vmcnt(0)
	v_lshlrev_b32_e32 v62, 4, v0
	v_add3_u32 v63, s34, v62, v71
	v_pk_mul_f32 v[34:35], v[34:35], v[76:77] op_sel_hi:[1,0]
	ds_write2_b32 v63, v34, v35 offset1:1
	v_pk_mul_f32 v[34:35], v[36:37], v[76:77] op_sel_hi:[1,0]
	ds_write2_b32 v63, v34, v35 offset0:2 offset1:3
	v_add_u32_e32 v36, 0x420, v63
	v_pk_mul_f32 v[34:35], v[42:43], v[74:75] op_sel_hi:[1,0]
	ds_write2_b32 v36, v34, v35 offset1:1
	v_add_u32_e32 v36, 0x428, v63
	v_pk_mul_f32 v[34:35], v[44:45], v[74:75] op_sel_hi:[1,0]
	ds_write2_b32 v36, v34, v35 offset1:1
	v_add_u32_e32 v36, 0x840, v63
	v_pk_mul_f32 v[34:35], v[38:39], v[84:85] op_sel_hi:[1,0]
	ds_write2_b32 v36, v34, v35 offset1:1
	v_add_u32_e32 v36, 0x848, v63
	v_pk_mul_f32 v[34:35], v[40:41], v[84:85] op_sel_hi:[1,0]
	ds_write2_b32 v36, v34, v35 offset1:1
	v_add_u32_e32 v36, 0xc60, v63
	v_pk_mul_f32 v[34:35], v[50:51], v[82:83] op_sel_hi:[1,0]
	ds_write2_b32 v36, v34, v35 offset1:1
	v_add_u32_e32 v36, 0xc68, v63
	v_pk_mul_f32 v[34:35], v[52:53], v[82:83] op_sel_hi:[1,0]
	ds_write2_b32 v36, v34, v35 offset1:1
	v_add_u32_e32 v36, 0x1080, v63
	v_pk_mul_f32 v[34:35], v[46:47], v[92:93] op_sel_hi:[1,0]
	ds_write2_b32 v36, v34, v35 offset1:1
	v_add_u32_e32 v36, 0x1088, v63
	v_pk_mul_f32 v[34:35], v[48:49], v[92:93] op_sel_hi:[1,0]
	ds_write2_b32 v36, v34, v35 offset1:1
	v_add_u32_e32 v36, 0x14a0, v63
	v_pk_mul_f32 v[34:35], v[58:59], v[90:91] op_sel_hi:[1,0]
	ds_write2_b32 v36, v34, v35 offset1:1
	v_add_u32_e32 v36, 0x14a8, v63
	v_pk_mul_f32 v[34:35], v[60:61], v[90:91] op_sel_hi:[1,0]
	ds_write2_b32 v36, v34, v35 offset1:1
	v_add_u32_e32 v36, 0x18c0, v63
	v_pk_mul_f32 v[34:35], v[54:55], v[114:115] op_sel_hi:[1,0]
	ds_write2_b32 v36, v34, v35 offset1:1
	v_add_u32_e32 v36, 0x18c8, v63
	v_pk_mul_f32 v[34:35], v[56:57], v[114:115] op_sel_hi:[1,0]
	ds_write2_b32 v36, v34, v35 offset1:1
	v_add_u32_e32 v36, 0x1ce0, v63
	v_pk_mul_f32 v[34:35], v[66:67], v[112:113] op_sel_hi:[1,0]
	ds_write2_b32 v36, v34, v35 offset1:1
	v_add_u32_e32 v36, 0x1ce8, v63
	v_pk_mul_f32 v[34:35], v[68:69], v[112:113] op_sel_hi:[1,0]
	ds_write2_b32 v36, v34, v35 offset1:1
	s_waitcnt lgkmcnt(0)
	v_mul_u32_u24_e32 v0, 0x420, v0
	v_add3_u32 v56, s34, v0, v73
	ds_read2_b32 v[38:39], v56 offset0:33 offset1:41
	ds_read2_b32 v[40:41], v56 offset1:8
	ds_read2_b32 v[42:43], v56 offset0:66 offset1:74
	ds_read2_b32 v[44:45], v56 offset0:99 offset1:107
	ds_read2_b32 v[46:47], v56 offset0:132 offset1:140
	ds_read2_b32 v[48:49], v56 offset0:165 offset1:173
	ds_read2_b32 v[50:51], v56 offset0:198 offset1:206
	ds_read2_b32 v[52:53], v56 offset0:231 offset1:239
	v_lshlrev_b32_e32 v0, 11, v102
	v_lshl_add_u64 v[54:55], s[16:17], 0, v[0:1]
	v_mov_b32_e32 v63, v1
	s_waitcnt lgkmcnt(0)
	v_cvt_pk_bf16_f32 v34, v40, v38
	v_cvt_pk_bf16_f32 v35, v42, v44
	v_cvt_pk_bf16_f32 v36, v46, v48
	v_cvt_pk_bf16_f32 v37, v50, v52
	v_lshl_add_u64 v[54:55], v[54:55], 0, v[62:63]
	global_store_dwordx4 v[54:55], v[34:37], off sc0 sc1
	v_lshlrev_b32_e32 v0, 11, v110
	s_nop 0
	v_cvt_pk_bf16_f32 v34, v41, v39
	v_cvt_pk_bf16_f32 v35, v43, v45
	v_cvt_pk_bf16_f32 v36, v47, v49
	v_cvt_pk_bf16_f32 v37, v51, v53
	ds_read2_b32 v[40:41], v56 offset0:49 offset1:57
	ds_read2_b32 v[42:43], v56 offset0:16 offset1:24
	ds_read2_b32 v[44:45], v56 offset0:82 offset1:90
	ds_read2_b32 v[46:47], v56 offset0:115 offset1:123
	ds_read2_b32 v[48:49], v56 offset0:148 offset1:156
	ds_read2_b32 v[50:51], v56 offset0:181 offset1:189
	ds_read2_b32 v[52:53], v56 offset0:214 offset1:222
	ds_read2_b32 v[54:55], v56 offset0:247 offset1:255
	v_lshl_add_u64 v[38:39], s[16:17], 0, v[0:1]
	v_lshl_add_u64 v[38:39], v[38:39], 0, v[62:63]
	v_lshlrev_b32_e32 v0, 11, v108
	global_store_dwordx4 v[38:39], v[34:37], off sc0 sc1
	v_lshl_add_u64 v[38:39], s[16:17], 0, v[0:1]
	v_lshl_add_u64 v[38:39], v[38:39], 0, v[62:63]
	s_waitcnt lgkmcnt(6)
	v_cvt_pk_bf16_f32 v34, v42, v40
	s_waitcnt lgkmcnt(4)
	v_cvt_pk_bf16_f32 v35, v44, v46
	s_waitcnt lgkmcnt(2)
	v_cvt_pk_bf16_f32 v36, v48, v50
	s_waitcnt lgkmcnt(0)
	v_cvt_pk_bf16_f32 v37, v52, v54
	v_lshlrev_b32_e32 v0, 11, v106
	global_store_dwordx4 v[38:39], v[34:37], off sc0 sc1
	v_lshl_add_u64 v[38:39], s[16:17], 0, v[0:1]
	v_lshl_add_u64 v[38:39], v[38:39], 0, v[62:63]
	v_cvt_pk_bf16_f32 v34, v43, v41
	v_cvt_pk_bf16_f32 v35, v45, v47
	v_cvt_pk_bf16_f32 v36, v49, v51
	v_cvt_pk_bf16_f32 v37, v53, v55
	global_store_dwordx4 v[38:39], v[34:37], off sc0 sc1
	s_waitcnt lgkmcnt(0)

.LBB0_682:
	s_andn2_b64 vcc, exec, s[50:51]
	s_cbranch_vccnz .LBB0_686
	s_cmp_eq_u32 s31, 0
	s_cbranch_scc1 .LBB0_685
	s_waitcnt vmcnt(6)
	v_pk_mul_f32 v[2:3], v[126:127], v[2:3] op_sel_hi:[0,1]
	ds_write2_b32 v103, v2, v3 offset1:1
	v_pk_mul_f32 v[2:3], v[126:127], v[4:5] op_sel_hi:[0,1]
	ds_write2_b32 v103, v2, v3 offset0:2 offset1:3
	s_waitcnt vmcnt(5)
	v_pk_mul_f32 v[2:3], v[120:121], v[14:15] op_sel_hi:[0,1]
	v_add_u32_e32 v0, 0x420, v103
	ds_write2_b32 v0, v2, v3 offset1:1
	v_pk_mul_f32 v[2:3], v[120:121], v[16:17] op_sel_hi:[0,1]
	v_add_u32_e32 v0, 0x428, v103
	ds_write2_b32 v0, v2, v3 offset1:1
	s_waitcnt vmcnt(3)
	v_pk_mul_f32 v[2:3], v[132:133], v[6:7] op_sel_hi:[0,1]
	v_add_u32_e32 v0, 0x840, v103
	ds_write2_b32 v0, v2, v3 offset1:1
	v_pk_mul_f32 v[2:3], v[132:133], v[8:9] op_sel_hi:[0,1]
	v_add_u32_e32 v0, 0x848, v103
	ds_write2_b32 v0, v2, v3 offset1:1
	s_waitcnt vmcnt(5)
	v_pk_mul_f32 v[2:3], v[128:129], v[22:23] op_sel_hi:[0,1]
	v_add_u32_e32 v0, 0xc60, v103
	ds_write2_b32 v0, v2, v3 offset1:1
	v_pk_mul_f32 v[2:3], v[128:129], v[24:25] op_sel_hi:[0,1]
	v_add_u32_e32 v0, 0xc68, v103
	ds_write2_b32 v0, v2, v3 offset1:1
	s_waitcnt vmcnt(3)
	v_pk_mul_f32 v[2:3], v[136:137], v[10:11] op_sel_hi:[0,1]
	v_add_u32_e32 v0, 0x1080, v103
	ds_write2_b32 v0, v2, v3 offset1:1
	v_pk_mul_f32 v[2:3], v[136:137], v[12:13] op_sel_hi:[0,1]
	v_add_u32_e32 v0, 0x1088, v103
	ds_write2_b32 v0, v2, v3 offset1:1
	v_pk_mul_f32 v[2:3], v[130:131], v[26:27] op_sel_hi:[0,1]
	v_add_u32_e32 v0, 0x14a0, v103
	ds_write2_b32 v0, v2, v3 offset1:1
	v_pk_mul_f32 v[2:3], v[130:131], v[28:29] op_sel_hi:[0,1]
	v_add_u32_e32 v0, 0x14a8, v103
	ds_write2_b32 v0, v2, v3 offset1:1
	s_waitcnt vmcnt(2)
	v_pk_mul_f32 v[2:3], v[138:139], v[18:19] op_sel_hi:[0,1]
	v_add_u32_e32 v0, 0x18c0, v103
	ds_write2_b32 v0, v2, v3 offset1:1
	v_pk_mul_f32 v[2:3], v[138:139], v[20:21] op_sel_hi:[0,1]
	v_add_u32_e32 v0, 0x18c8, v103
	ds_write2_b32 v0, v2, v3 offset1:1
	s_waitcnt vmcnt(0)
	v_pk_mul_f32 v[2:3], v[134:135], v[30:31] op_sel_hi:[0,1]
	v_add_u32_e32 v0, 0x1ce0, v103
	ds_write2_b32 v0, v2, v3 offset1:1
	v_pk_mul_f32 v[2:3], v[134:135], v[32:33] op_sel_hi:[0,1]
	v_add_u32_e32 v0, 0x1ce8, v103
	ds_write2_b32 v0, v2, v3 offset1:1
	s_waitcnt lgkmcnt(0)
	ds_read2_b32 v[6:7], v99 offset0:33 offset1:41
	ds_read2_b32 v[8:9], v99 offset1:8
	ds_read2_b32 v[10:11], v99 offset0:66 offset1:74
	ds_read2_b32 v[12:13], v99 offset0:99 offset1:107
	ds_read2_b32 v[14:15], v99 offset0:132 offset1:140
	ds_read2_b32 v[16:17], v99 offset0:165 offset1:173
	ds_read2_b32 v[18:19], v99 offset0:198 offset1:206
	ds_read2_b32 v[20:21], v99 offset0:231 offset1:239
	v_lshl_add_u64 v[22:23], s[14:15], 0, v[124:125]
	v_lshlrev_b32_e32 v0, 1, v112
	s_waitcnt lgkmcnt(6)
	v_cvt_pk_bf16_f32 v2, v8, v6
	s_waitcnt lgkmcnt(4)
	v_cvt_pk_bf16_f32 v3, v10, v12
	s_waitcnt lgkmcnt(2)
	v_cvt_pk_bf16_f32 v4, v14, v16
	s_waitcnt lgkmcnt(0)
	v_cvt_pk_bf16_f32 v5, v18, v20
	v_lshl_add_u64 v[22:23], v[22:23], 0, v[0:1]
	global_store_dwordx4 v[22:23], v[2:5], off sc0 sc1
	s_nop 1
	v_cvt_pk_bf16_f32 v2, v9, v7
	v_cvt_pk_bf16_f32 v3, v11, v13
	v_cvt_pk_bf16_f32 v4, v15, v17
	v_cvt_pk_bf16_f32 v5, v19, v21
	ds_read2_b32 v[8:9], v99 offset0:49 offset1:57
	ds_read2_b32 v[10:11], v99 offset0:16 offset1:24
	ds_read2_b32 v[12:13], v99 offset0:82 offset1:90
	ds_read2_b32 v[14:15], v99 offset0:115 offset1:123
	ds_read2_b32 v[16:17], v99 offset0:148 offset1:156
	ds_read2_b32 v[18:19], v99 offset0:181 offset1:189
	ds_read2_b32 v[20:21], v99 offset0:214 offset1:222
	ds_read2_b32 v[22:23], v99 offset0:247 offset1:255
	v_lshl_add_u64 v[6:7], s[14:15], 0, v[122:123]
	v_lshl_add_u64 v[6:7], v[6:7], 0, v[0:1]
	global_store_dwordx4 v[6:7], v[2:5], off sc0 sc1
	v_lshl_add_u64 v[6:7], s[14:15], 0, v[118:119]
	v_lshl_add_u64 v[6:7], v[6:7], 0, v[0:1]
	s_waitcnt lgkmcnt(6)
	v_cvt_pk_bf16_f32 v2, v10, v8
	s_waitcnt lgkmcnt(4)
	v_cvt_pk_bf16_f32 v3, v12, v14
	s_waitcnt lgkmcnt(2)
	v_cvt_pk_bf16_f32 v4, v16, v18
	s_waitcnt lgkmcnt(0)
	v_cvt_pk_bf16_f32 v5, v20, v22
	global_store_dwordx4 v[6:7], v[2:5], off sc0 sc1
	v_lshl_add_u64 v[6:7], s[14:15], 0, v[116:117]
	v_lshl_add_u64 v[6:7], v[6:7], 0, v[0:1]
	v_cvt_pk_bf16_f32 v2, v11, v9
	v_cvt_pk_bf16_f32 v3, v13, v15
	v_cvt_pk_bf16_f32 v4, v17, v19
	v_cvt_pk_bf16_f32 v5, v21, v23
	global_store_dwordx4 v[6:7], v[2:5], off sc0 sc1
	s_waitcnt lgkmcnt(0)

.LBB0_700:
	s_andn2_b64 vcc, exec, s[50:51]
	s_cbranch_vccnz .LBB0_667
	s_cmp_eq_u32 s31, 0
	s_cbranch_scc1 .LBB0_666
	s_waitcnt vmcnt(6)
	v_pk_mul_f32 v[2:3], v[2:3], v[126:127] op_sel_hi:[1,0]
	ds_write2_b32 v103, v2, v3 offset1:1
	v_pk_mul_f32 v[2:3], v[4:5], v[126:127] op_sel_hi:[1,0]
	ds_write2_b32 v103, v2, v3 offset0:2 offset1:3
	s_waitcnt vmcnt(5)
	v_pk_mul_f32 v[2:3], v[14:15], v[120:121] op_sel_hi:[1,0]
	v_add_u32_e32 v0, 0x420, v103
	ds_write2_b32 v0, v2, v3 offset1:1
	v_pk_mul_f32 v[2:3], v[16:17], v[120:121] op_sel_hi:[1,0]
	v_add_u32_e32 v0, 0x428, v103
	ds_write2_b32 v0, v2, v3 offset1:1
	s_waitcnt vmcnt(3)
	v_pk_mul_f32 v[2:3], v[6:7], v[132:133] op_sel_hi:[1,0]
	v_add_u32_e32 v0, 0x840, v103
	ds_write2_b32 v0, v2, v3 offset1:1
	v_pk_mul_f32 v[2:3], v[8:9], v[132:133] op_sel_hi:[1,0]
	v_add_u32_e32 v0, 0x848, v103
	ds_write2_b32 v0, v2, v3 offset1:1
	v_pk_mul_f32 v[2:3], v[22:23], v[128:129] op_sel_hi:[1,0]
	v_add_u32_e32 v0, 0xc60, v103
	ds_write2_b32 v0, v2, v3 offset1:1
	v_pk_mul_f32 v[2:3], v[24:25], v[128:129] op_sel_hi:[1,0]
	v_add_u32_e32 v0, 0xc68, v103
	ds_write2_b32 v0, v2, v3 offset1:1
	v_pk_mul_f32 v[2:3], v[10:11], v[136:137] op_sel_hi:[1,0]
	v_add_u32_e32 v0, 0x1080, v103
	ds_write2_b32 v0, v2, v3 offset1:1
	v_pk_mul_f32 v[2:3], v[12:13], v[136:137] op_sel_hi:[1,0]
	v_add_u32_e32 v0, 0x1088, v103
	ds_write2_b32 v0, v2, v3 offset1:1
	v_pk_mul_f32 v[2:3], v[26:27], v[130:131] op_sel_hi:[1,0]
	v_add_u32_e32 v0, 0x14a0, v103
	ds_write2_b32 v0, v2, v3 offset1:1
	v_pk_mul_f32 v[2:3], v[28:29], v[130:131] op_sel_hi:[1,0]
	v_add_u32_e32 v0, 0x14a8, v103
	ds_write2_b32 v0, v2, v3 offset1:1
	s_waitcnt vmcnt(2)
	v_pk_mul_f32 v[2:3], v[18:19], v[138:139] op_sel_hi:[1,0]
	v_add_u32_e32 v0, 0x18c0, v103
	ds_write2_b32 v0, v2, v3 offset1:1
	v_pk_mul_f32 v[2:3], v[20:21], v[138:139] op_sel_hi:[1,0]
	v_add_u32_e32 v0, 0x18c8, v103
	ds_write2_b32 v0, v2, v3 offset1:1
	s_waitcnt vmcnt(0)
	v_pk_mul_f32 v[2:3], v[30:31], v[134:135] op_sel_hi:[1,0]
	v_add_u32_e32 v0, 0x1ce0, v103
	ds_write2_b32 v0, v2, v3 offset1:1
	v_pk_mul_f32 v[2:3], v[32:33], v[134:135] op_sel_hi:[1,0]
	v_add_u32_e32 v0, 0x1ce8, v103
	ds_write2_b32 v0, v2, v3 offset1:1
	s_waitcnt lgkmcnt(0)
	ds_read2_b32 v[6:7], v99 offset0:33 offset1:41
	ds_read2_b32 v[8:9], v99 offset1:8
	ds_read2_b32 v[10:11], v99 offset0:66 offset1:74
	ds_read2_b32 v[12:13], v99 offset0:99 offset1:107
	ds_read2_b32 v[14:15], v99 offset0:132 offset1:140
	ds_read2_b32 v[16:17], v99 offset0:165 offset1:173
	ds_read2_b32 v[18:19], v99 offset0:198 offset1:206
	ds_read2_b32 v[20:21], v99 offset0:231 offset1:239
	v_lshl_add_u64 v[22:23], s[14:15], 0, v[124:125]
	v_lshlrev_b32_e32 v0, 1, v112
	s_waitcnt lgkmcnt(6)
	v_cvt_pk_bf16_f32 v2, v8, v6
	s_waitcnt lgkmcnt(4)
	v_cvt_pk_bf16_f32 v3, v10, v12
	s_waitcnt lgkmcnt(2)
	v_cvt_pk_bf16_f32 v4, v14, v16
	s_waitcnt lgkmcnt(0)
	v_cvt_pk_bf16_f32 v5, v18, v20
	v_lshl_add_u64 v[22:23], v[22:23], 0, v[0:1]
	global_store_dwordx4 v[22:23], v[2:5], off sc0 sc1
	s_nop 1
	v_cvt_pk_bf16_f32 v2, v9, v7
	v_cvt_pk_bf16_f32 v3, v11, v13
	v_cvt_pk_bf16_f32 v4, v15, v17
	v_cvt_pk_bf16_f32 v5, v19, v21
	ds_read2_b32 v[8:9], v99 offset0:49 offset1:57
	ds_read2_b32 v[10:11], v99 offset0:16 offset1:24
	ds_read2_b32 v[12:13], v99 offset0:82 offset1:90
	ds_read2_b32 v[14:15], v99 offset0:115 offset1:123
	ds_read2_b32 v[16:17], v99 offset0:148 offset1:156
	ds_read2_b32 v[18:19], v99 offset0:181 offset1:189
	ds_read2_b32 v[20:21], v99 offset0:214 offset1:222
	ds_read2_b32 v[22:23], v99 offset0:247 offset1:255
	v_lshl_add_u64 v[6:7], s[14:15], 0, v[122:123]
	v_lshl_add_u64 v[6:7], v[6:7], 0, v[0:1]
	global_store_dwordx4 v[6:7], v[2:5], off sc0 sc1
	v_lshl_add_u64 v[6:7], s[14:15], 0, v[118:119]
	v_lshl_add_u64 v[6:7], v[6:7], 0, v[0:1]
	s_waitcnt lgkmcnt(6)
	v_cvt_pk_bf16_f32 v2, v10, v8
	s_waitcnt lgkmcnt(4)
	v_cvt_pk_bf16_f32 v3, v12, v14
	s_waitcnt lgkmcnt(2)
	v_cvt_pk_bf16_f32 v4, v16, v18
	s_waitcnt lgkmcnt(0)
	v_cvt_pk_bf16_f32 v5, v20, v22
	global_store_dwordx4 v[6:7], v[2:5], off sc0 sc1
	v_lshl_add_u64 v[6:7], s[14:15], 0, v[116:117]
	v_lshl_add_u64 v[6:7], v[6:7], 0, v[0:1]
	v_cvt_pk_bf16_f32 v2, v11, v9
	v_cvt_pk_bf16_f32 v3, v13, v15
	v_cvt_pk_bf16_f32 v4, v17, v19
	v_cvt_pk_bf16_f32 v5, v21, v23
	global_store_dwordx4 v[6:7], v[2:5], off sc0 sc1
	s_waitcnt lgkmcnt(0)
	s_branch .LBB0_666

.LBB0_725:
	s_and_b64 vcc, exec, s[46:47]
	s_cbranch_vccz .LBB0_729
	s_cmp_eq_u32 s31, 0
	s_cbranch_scc1 .LBB0_728
	s_waitcnt vmcnt(6)
	v_pk_mul_f32 v[2:3], v[2:3], v[126:127] op_sel_hi:[1,0]
	ds_write2_b32 v103, v2, v3 offset1:1
	v_pk_mul_f32 v[2:3], v[4:5], v[126:127] op_sel_hi:[1,0]
	ds_write2_b32 v103, v2, v3 offset0:2 offset1:3
	s_waitcnt vmcnt(5)
	v_pk_mul_f32 v[2:3], v[14:15], v[120:121] op_sel_hi:[1,0]
	v_add_u32_e32 v0, 0x420, v103
	ds_write2_b32 v0, v2, v3 offset1:1
	v_pk_mul_f32 v[2:3], v[16:17], v[120:121] op_sel_hi:[1,0]
	v_add_u32_e32 v0, 0x428, v103
	ds_write2_b32 v0, v2, v3 offset1:1
	s_waitcnt vmcnt(3)
	v_pk_mul_f32 v[2:3], v[6:7], v[132:133] op_sel_hi:[1,0]
	v_add_u32_e32 v0, 0x840, v103
	ds_write2_b32 v0, v2, v3 offset1:1
	v_pk_mul_f32 v[2:3], v[8:9], v[132:133] op_sel_hi:[1,0]
	v_add_u32_e32 v0, 0x848, v103
	ds_write2_b32 v0, v2, v3 offset1:1
	v_pk_mul_f32 v[2:3], v[22:23], v[128:129] op_sel_hi:[1,0]
	v_add_u32_e32 v0, 0xc60, v103
	ds_write2_b32 v0, v2, v3 offset1:1
	v_pk_mul_f32 v[2:3], v[24:25], v[128:129] op_sel_hi:[1,0]
	v_add_u32_e32 v0, 0xc68, v103
	ds_write2_b32 v0, v2, v3 offset1:1
	v_pk_mul_f32 v[2:3], v[10:11], v[136:137] op_sel_hi:[1,0]
	v_add_u32_e32 v0, 0x1080, v103
	ds_write2_b32 v0, v2, v3 offset1:1
	v_pk_mul_f32 v[2:3], v[12:13], v[136:137] op_sel_hi:[1,0]
	v_add_u32_e32 v0, 0x1088, v103
	ds_write2_b32 v0, v2, v3 offset1:1
	v_pk_mul_f32 v[2:3], v[26:27], v[130:131] op_sel_hi:[1,0]
	v_add_u32_e32 v0, 0x14a0, v103
	ds_write2_b32 v0, v2, v3 offset1:1
	v_pk_mul_f32 v[2:3], v[28:29], v[130:131] op_sel_hi:[1,0]
	v_add_u32_e32 v0, 0x14a8, v103
	ds_write2_b32 v0, v2, v3 offset1:1
	s_waitcnt vmcnt(2)
	v_pk_mul_f32 v[2:3], v[18:19], v[138:139] op_sel_hi:[1,0]
	v_add_u32_e32 v0, 0x18c0, v103
	ds_write2_b32 v0, v2, v3 offset1:1
	v_pk_mul_f32 v[2:3], v[20:21], v[138:139] op_sel_hi:[1,0]
	v_add_u32_e32 v0, 0x18c8, v103
	ds_write2_b32 v0, v2, v3 offset1:1
	s_waitcnt vmcnt(0)
	v_pk_mul_f32 v[2:3], v[30:31], v[134:135] op_sel_hi:[1,0]
	v_add_u32_e32 v0, 0x1ce0, v103
	ds_write2_b32 v0, v2, v3 offset1:1
	v_pk_mul_f32 v[2:3], v[32:33], v[134:135] op_sel_hi:[1,0]
	v_add_u32_e32 v0, 0x1ce8, v103
	ds_write2_b32 v0, v2, v3 offset1:1
	s_waitcnt lgkmcnt(0)
	ds_read2_b32 v[6:7], v99 offset0:33 offset1:41
	ds_read2_b32 v[8:9], v99 offset1:8
	ds_read2_b32 v[10:11], v99 offset0:66 offset1:74
	ds_read2_b32 v[12:13], v99 offset0:99 offset1:107
	ds_read2_b32 v[14:15], v99 offset0:132 offset1:140
	ds_read2_b32 v[16:17], v99 offset0:165 offset1:173
	ds_read2_b32 v[18:19], v99 offset0:198 offset1:206
	ds_read2_b32 v[20:21], v99 offset0:231 offset1:239
	v_lshl_add_u64 v[22:23], s[14:15], 0, v[124:125]
	v_lshlrev_b32_e32 v0, 1, v112
	s_waitcnt lgkmcnt(6)
	v_cvt_pk_bf16_f32 v2, v8, v6
	s_waitcnt lgkmcnt(4)
	v_cvt_pk_bf16_f32 v3, v10, v12
	s_waitcnt lgkmcnt(2)
	v_cvt_pk_bf16_f32 v4, v14, v16
	s_waitcnt lgkmcnt(0)
	v_cvt_pk_bf16_f32 v5, v18, v20
	v_lshl_add_u64 v[22:23], v[22:23], 0, v[0:1]
	global_store_dwordx4 v[22:23], v[2:5], off sc0 sc1
	s_nop 1
	v_cvt_pk_bf16_f32 v2, v9, v7
	v_cvt_pk_bf16_f32 v3, v11, v13
	v_cvt_pk_bf16_f32 v4, v15, v17
	v_cvt_pk_bf16_f32 v5, v19, v21
	ds_read2_b32 v[8:9], v99 offset0:49 offset1:57
	ds_read2_b32 v[10:11], v99 offset0:16 offset1:24
	ds_read2_b32 v[12:13], v99 offset0:82 offset1:90
	ds_read2_b32 v[14:15], v99 offset0:115 offset1:123
	ds_read2_b32 v[16:17], v99 offset0:148 offset1:156
	ds_read2_b32 v[18:19], v99 offset0:181 offset1:189
	ds_read2_b32 v[20:21], v99 offset0:214 offset1:222
	ds_read2_b32 v[22:23], v99 offset0:247 offset1:255
	v_lshl_add_u64 v[6:7], s[14:15], 0, v[122:123]
	v_lshl_add_u64 v[6:7], v[6:7], 0, v[0:1]
	global_store_dwordx4 v[6:7], v[2:5], off sc0 sc1
	v_lshl_add_u64 v[6:7], s[14:15], 0, v[118:119]
	v_lshl_add_u64 v[6:7], v[6:7], 0, v[0:1]
	s_waitcnt lgkmcnt(6)
	v_cvt_pk_bf16_f32 v2, v10, v8
	s_waitcnt lgkmcnt(4)
	v_cvt_pk_bf16_f32 v3, v12, v14
	s_waitcnt lgkmcnt(2)
	v_cvt_pk_bf16_f32 v4, v16, v18
	s_waitcnt lgkmcnt(0)
	v_cvt_pk_bf16_f32 v5, v20, v22
	global_store_dwordx4 v[6:7], v[2:5], off sc0 sc1
	v_lshl_add_u64 v[6:7], s[14:15], 0, v[116:117]
	v_lshl_add_u64 v[6:7], v[6:7], 0, v[0:1]
	v_cvt_pk_bf16_f32 v2, v11, v9
	v_cvt_pk_bf16_f32 v3, v13, v15
	v_cvt_pk_bf16_f32 v4, v17, v19
	v_cvt_pk_bf16_f32 v5, v21, v23
	global_store_dwordx4 v[6:7], v[2:5], off sc0 sc1
	s_waitcnt lgkmcnt(0)

.LBB0_744:
	s_andn2_b64 vcc, exec, s[46:47]
	s_cbranch_vccnz .LBB0_748
	s_cmp_eq_u32 s31, 0
	s_cbranch_scc1 .LBB0_747
	s_waitcnt vmcnt(0)
	v_pk_mul_f32 v[2:3], v[62:63], v[140:141] op_sel_hi:[1,0]
	ds_write2_b32 v103, v2, v3 offset1:1
	v_pk_mul_f32 v[2:3], v[64:65], v[140:141] op_sel_hi:[1,0]
	ds_write2_b32 v103, v2, v3 offset0:2 offset1:3
	v_pk_mul_f32 v[2:3], v[74:75], v[142:143] op_sel_hi:[1,0]
	v_add_u32_e32 v0, 0x420, v103
	ds_write2_b32 v0, v2, v3 offset1:1
	v_pk_mul_f32 v[2:3], v[76:77], v[142:143] op_sel_hi:[1,0]
	v_add_u32_e32 v0, 0x428, v103
	ds_write2_b32 v0, v2, v3 offset1:1
	v_pk_mul_f32 v[2:3], v[70:71], v[146:147] op_sel_hi:[1,0]
	v_add_u32_e32 v0, 0x840, v103
	ds_write2_b32 v0, v2, v3 offset1:1
	v_pk_mul_f32 v[2:3], v[72:73], v[146:147] op_sel_hi:[1,0]
	v_add_u32_e32 v0, 0x848, v103
	ds_write2_b32 v0, v2, v3 offset1:1
	v_pk_mul_f32 v[2:3], v[82:83], v[144:145] op_sel_hi:[1,0]
	v_add_u32_e32 v0, 0xc60, v103
	ds_write2_b32 v0, v2, v3 offset1:1
	v_pk_mul_f32 v[2:3], v[84:85], v[144:145] op_sel_hi:[1,0]
	v_add_u32_e32 v0, 0xc68, v103
	ds_write2_b32 v0, v2, v3 offset1:1
	v_pk_mul_f32 v[2:3], v[78:79], v[150:151] op_sel_hi:[1,0]
	v_add_u32_e32 v0, 0x1080, v103
	ds_write2_b32 v0, v2, v3 offset1:1
	v_pk_mul_f32 v[2:3], v[80:81], v[150:151] op_sel_hi:[1,0]
	v_add_u32_e32 v0, 0x1088, v103
	ds_write2_b32 v0, v2, v3 offset1:1
	v_pk_mul_f32 v[2:3], v[90:91], v[148:149] op_sel_hi:[1,0]
	v_add_u32_e32 v0, 0x14a0, v103
	ds_write2_b32 v0, v2, v3 offset1:1
	v_pk_mul_f32 v[2:3], v[92:93], v[148:149] op_sel_hi:[1,0]
	v_add_u32_e32 v0, 0x14a8, v103
	ds_write2_b32 v0, v2, v3 offset1:1
	v_pk_mul_f32 v[2:3], v[86:87], v[154:155] op_sel_hi:[1,0]
	v_add_u32_e32 v0, 0x18c0, v103
	ds_write2_b32 v0, v2, v3 offset1:1
	v_pk_mul_f32 v[2:3], v[88:89], v[154:155] op_sel_hi:[1,0]
	v_add_u32_e32 v0, 0x18c8, v103
	ds_write2_b32 v0, v2, v3 offset1:1
	v_pk_mul_f32 v[2:3], v[94:95], v[152:153] op_sel_hi:[1,0]
	v_add_u32_e32 v0, 0x1ce0, v103
	ds_write2_b32 v0, v2, v3 offset1:1
	v_pk_mul_f32 v[2:3], v[96:97], v[152:153] op_sel_hi:[1,0]
	v_add_u32_e32 v0, 0x1ce8, v103
	ds_write2_b32 v0, v2, v3 offset1:1
	s_waitcnt lgkmcnt(0)
	ds_read2_b32 v[6:7], v99 offset0:33 offset1:41
	ds_read2_b32 v[8:9], v99 offset1:8
	ds_read2_b32 v[10:11], v99 offset0:66 offset1:74
	ds_read2_b32 v[12:13], v99 offset0:99 offset1:107
	ds_read2_b32 v[14:15], v99 offset0:132 offset1:140
	ds_read2_b32 v[16:17], v99 offset0:165 offset1:173
	ds_read2_b32 v[18:19], v99 offset0:198 offset1:206
	ds_read2_b32 v[20:21], v99 offset0:231 offset1:239
	v_lshl_add_u64 v[22:23], s[38:39], 0, v[124:125]
	v_lshlrev_b32_e32 v0, 1, v112
	s_waitcnt lgkmcnt(6)
	v_cvt_pk_bf16_f32 v2, v8, v6
	s_waitcnt lgkmcnt(4)
	v_cvt_pk_bf16_f32 v3, v10, v12
	s_waitcnt lgkmcnt(2)
	v_cvt_pk_bf16_f32 v4, v14, v16
	s_waitcnt lgkmcnt(0)
	v_cvt_pk_bf16_f32 v5, v18, v20
	v_lshl_add_u64 v[22:23], v[22:23], 0, v[0:1]
	global_store_dwordx4 v[22:23], v[2:5], off sc0 sc1
	s_nop 1
	v_cvt_pk_bf16_f32 v2, v9, v7
	v_cvt_pk_bf16_f32 v3, v11, v13
	v_cvt_pk_bf16_f32 v4, v15, v17
	v_cvt_pk_bf16_f32 v5, v19, v21
	ds_read2_b32 v[8:9], v99 offset0:49 offset1:57
	ds_read2_b32 v[10:11], v99 offset0:16 offset1:24
	ds_read2_b32 v[12:13], v99 offset0:82 offset1:90
	ds_read2_b32 v[14:15], v99 offset0:115 offset1:123
	ds_read2_b32 v[16:17], v99 offset0:148 offset1:156
	ds_read2_b32 v[18:19], v99 offset0:181 offset1:189
	ds_read2_b32 v[20:21], v99 offset0:214 offset1:222
	ds_read2_b32 v[22:23], v99 offset0:247 offset1:255
	v_lshl_add_u64 v[6:7], s[38:39], 0, v[122:123]
	v_lshl_add_u64 v[6:7], v[6:7], 0, v[0:1]
	global_store_dwordx4 v[6:7], v[2:5], off sc0 sc1
	v_lshl_add_u64 v[6:7], s[38:39], 0, v[118:119]
	v_lshl_add_u64 v[6:7], v[6:7], 0, v[0:1]
	s_waitcnt lgkmcnt(6)
	v_cvt_pk_bf16_f32 v2, v10, v8
	s_waitcnt lgkmcnt(4)
	v_cvt_pk_bf16_f32 v3, v12, v14
	s_waitcnt lgkmcnt(2)
	v_cvt_pk_bf16_f32 v4, v16, v18
	s_waitcnt lgkmcnt(0)
	v_cvt_pk_bf16_f32 v5, v20, v22
	global_store_dwordx4 v[6:7], v[2:5], off sc0 sc1
	v_lshl_add_u64 v[6:7], s[38:39], 0, v[116:117]
	v_lshl_add_u64 v[6:7], v[6:7], 0, v[0:1]
	v_cvt_pk_bf16_f32 v2, v11, v9
	v_cvt_pk_bf16_f32 v3, v13, v15
	v_cvt_pk_bf16_f32 v4, v17, v19
	v_cvt_pk_bf16_f32 v5, v21, v23
	global_store_dwordx4 v[6:7], v[2:5], off sc0 sc1
	s_waitcnt lgkmcnt(0)

.LBB0_754:
	s_andn2_b64 vcc, exec, s[36:37]
	s_cbranch_vccnz .LBB0_751
	s_cmp_eq_u32 s31, 0
	s_cbranch_scc1 .LBB0_750
	s_waitcnt vmcnt(3)
	v_pk_mul_f32 v[34:35], v[136:137], v[34:35] op_sel_hi:[0,1]
	ds_write2_b32 v103, v34, v35 offset1:1
	v_pk_mul_f32 v[34:35], v[136:137], v[36:37] op_sel_hi:[0,1]
	ds_write2_b32 v103, v34, v35 offset0:2 offset1:3
	v_pk_mul_f32 v[34:35], v[134:135], v[42:43] op_sel_hi:[0,1]
	v_add_u32_e32 v0, 0x420, v103
	ds_write2_b32 v0, v34, v35 offset1:1
	v_pk_mul_f32 v[34:35], v[134:135], v[44:45] op_sel_hi:[0,1]
	v_add_u32_e32 v0, 0x428, v103
	ds_write2_b32 v0, v34, v35 offset1:1
	s_waitcnt vmcnt(2)
	v_pk_mul_f32 v[34:35], v[138:139], v[38:39] op_sel_hi:[0,1]
	v_add_u32_e32 v0, 0x840, v103
	ds_write2_b32 v0, v34, v35 offset1:1
	v_pk_mul_f32 v[34:35], v[138:139], v[40:41] op_sel_hi:[0,1]
	v_add_u32_e32 v0, 0x848, v103
	ds_write2_b32 v0, v34, v35 offset1:1
	v_pk_mul_f32 v[34:35], v[130:131], v[50:51] op_sel_hi:[0,1]
	v_add_u32_e32 v0, 0xc60, v103
	ds_write2_b32 v0, v34, v35 offset1:1
	v_pk_mul_f32 v[34:35], v[130:131], v[52:53] op_sel_hi:[0,1]
	v_add_u32_e32 v0, 0xc68, v103
	ds_write2_b32 v0, v34, v35 offset1:1
	v_pk_mul_f32 v[34:35], v[132:133], v[46:47] op_sel_hi:[0,1]
	v_add_u32_e32 v0, 0x1080, v103
	ds_write2_b32 v0, v34, v35 offset1:1
	v_pk_mul_f32 v[34:35], v[132:133], v[48:49] op_sel_hi:[0,1]
	v_add_u32_e32 v0, 0x1088, v103
	ds_write2_b32 v0, v34, v35 offset1:1
	s_waitcnt vmcnt(0)
	v_pk_mul_f32 v[34:35], v[126:127], v[58:59] op_sel_hi:[0,1]
	v_add_u32_e32 v0, 0x14a0, v103
	ds_write2_b32 v0, v34, v35 offset1:1
	v_pk_mul_f32 v[34:35], v[126:127], v[60:61] op_sel_hi:[0,1]
	v_add_u32_e32 v0, 0x14a8, v103
	ds_write2_b32 v0, v34, v35 offset1:1
	v_pk_mul_f32 v[34:35], v[128:129], v[54:55] op_sel_hi:[0,1]
	v_add_u32_e32 v0, 0x18c0, v103
	ds_write2_b32 v0, v34, v35 offset1:1
	v_pk_mul_f32 v[34:35], v[128:129], v[56:57] op_sel_hi:[0,1]
	v_add_u32_e32 v0, 0x18c8, v103
	ds_write2_b32 v0, v34, v35 offset1:1
	v_pk_mul_f32 v[34:35], v[120:121], v[66:67] op_sel_hi:[0,1]
	v_add_u32_e32 v0, 0x1ce0, v103
	ds_write2_b32 v0, v34, v35 offset1:1
	v_pk_mul_f32 v[34:35], v[120:121], v[68:69] op_sel_hi:[0,1]
	v_add_u32_e32 v0, 0x1ce8, v103
	ds_write2_b32 v0, v34, v35 offset1:1
	s_waitcnt lgkmcnt(0)
	ds_read2_b32 v[38:39], v99 offset0:33 offset1:41
	ds_read2_b32 v[40:41], v99 offset1:8
	ds_read2_b32 v[42:43], v99 offset0:66 offset1:74
	ds_read2_b32 v[44:45], v99 offset0:99 offset1:107
	ds_read2_b32 v[46:47], v99 offset0:132 offset1:140
	ds_read2_b32 v[48:49], v99 offset0:165 offset1:173
	ds_read2_b32 v[50:51], v99 offset0:198 offset1:206
	ds_read2_b32 v[52:53], v99 offset0:231 offset1:239
	v_mad_u64_u32 v[54:55], s[36:37], s34, v102, 0
	v_lshl_add_u64 v[54:55], v[54:55], 1, s[14:15]
	v_lshlrev_b32_e32 v0, 1, v112
	s_waitcnt lgkmcnt(6)
	v_cvt_pk_bf16_f32 v34, v40, v38
	s_waitcnt lgkmcnt(4)
	v_cvt_pk_bf16_f32 v35, v42, v44
	s_waitcnt lgkmcnt(2)
	v_cvt_pk_bf16_f32 v36, v46, v48
	s_waitcnt lgkmcnt(0)
	v_cvt_pk_bf16_f32 v37, v50, v52
	v_lshl_add_u64 v[54:55], v[54:55], 0, v[0:1]
	global_store_dwordx4 v[54:55], v[34:37], off sc0 sc1
	s_nop 1
	v_cvt_pk_bf16_f32 v34, v41, v39
	v_cvt_pk_bf16_f32 v35, v43, v45
	v_cvt_pk_bf16_f32 v36, v47, v49
	v_cvt_pk_bf16_f32 v37, v51, v53
	v_mad_u64_u32 v[38:39], s[36:37], s34, v110, 0
	ds_read2_b32 v[40:41], v99 offset0:16 offset1:24
	ds_read2_b32 v[42:43], v99 offset0:49 offset1:57
	ds_read2_b32 v[44:45], v99 offset0:82 offset1:90
	ds_read2_b32 v[46:47], v99 offset0:115 offset1:123
	ds_read2_b32 v[48:49], v99 offset0:148 offset1:156
	ds_read2_b32 v[50:51], v99 offset0:181 offset1:189
	ds_read2_b32 v[52:53], v99 offset0:214 offset1:222
	ds_read2_b32 v[54:55], v99 offset0:247 offset1:255
	v_lshl_add_u64 v[38:39], v[38:39], 1, s[14:15]
	v_lshl_add_u64 v[38:39], v[38:39], 0, v[0:1]
	global_store_dwordx4 v[38:39], v[34:37], off sc0 sc1
	v_mad_u64_u32 v[38:39], s[36:37], s34, v108, 0
	v_lshl_add_u64 v[38:39], v[38:39], 1, s[14:15]
	s_waitcnt lgkmcnt(6)
	v_cvt_pk_bf16_f32 v34, v40, v42
	s_waitcnt lgkmcnt(4)
	v_cvt_pk_bf16_f32 v35, v44, v46
	s_waitcnt lgkmcnt(2)
	v_cvt_pk_bf16_f32 v36, v48, v50
	s_waitcnt lgkmcnt(0)
	v_cvt_pk_bf16_f32 v37, v52, v54
	v_lshl_add_u64 v[38:39], v[38:39], 0, v[0:1]
	global_store_dwordx4 v[38:39], v[34:37], off sc0 sc1
	v_mad_u64_u32 v[38:39], s[36:37], s34, v106, 0
	v_lshl_add_u64 v[38:39], v[38:39], 1, s[14:15]
	v_cvt_pk_bf16_f32 v34, v41, v43
	v_cvt_pk_bf16_f32 v35, v45, v47
	v_cvt_pk_bf16_f32 v36, v49, v51
	v_cvt_pk_bf16_f32 v37, v53, v55
	v_lshl_add_u64 v[38:39], v[38:39], 0, v[0:1]
	global_store_dwordx4 v[38:39], v[34:37], off sc0 sc1
	s_waitcnt lgkmcnt(0)
	s_branch .LBB0_750

.LBB0_759:
	s_and_b64 vcc, exec, s[16:17]
	s_cbranch_vccz .LBB0_763
	s_cmp_eq_u32 s31, 0
	s_cbranch_scc1 .LBB0_762
	s_waitcnt vmcnt(3)
	v_pk_mul_f32 v[34:35], v[34:35], v[136:137] op_sel_hi:[1,0]
	ds_write2_b32 v103, v34, v35 offset1:1
	v_pk_mul_f32 v[34:35], v[36:37], v[136:137] op_sel_hi:[1,0]
	ds_write2_b32 v103, v34, v35 offset0:2 offset1:3
	v_pk_mul_f32 v[34:35], v[42:43], v[134:135] op_sel_hi:[1,0]
	v_add_u32_e32 v0, 0x420, v103
	ds_write2_b32 v0, v34, v35 offset1:1
	v_pk_mul_f32 v[34:35], v[44:45], v[134:135] op_sel_hi:[1,0]
	v_add_u32_e32 v0, 0x428, v103
	ds_write2_b32 v0, v34, v35 offset1:1
	s_waitcnt vmcnt(2)
	v_pk_mul_f32 v[34:35], v[38:39], v[138:139] op_sel_hi:[1,0]
	v_add_u32_e32 v0, 0x840, v103
	ds_write2_b32 v0, v34, v35 offset1:1
	v_pk_mul_f32 v[34:35], v[40:41], v[138:139] op_sel_hi:[1,0]
	v_add_u32_e32 v0, 0x848, v103
	ds_write2_b32 v0, v34, v35 offset1:1
	v_pk_mul_f32 v[34:35], v[50:51], v[130:131] op_sel_hi:[1,0]
	v_add_u32_e32 v0, 0xc60, v103
	ds_write2_b32 v0, v34, v35 offset1:1
	v_pk_mul_f32 v[34:35], v[52:53], v[130:131] op_sel_hi:[1,0]
	v_add_u32_e32 v0, 0xc68, v103
	ds_write2_b32 v0, v34, v35 offset1:1
	v_pk_mul_f32 v[34:35], v[46:47], v[132:133] op_sel_hi:[1,0]
	v_add_u32_e32 v0, 0x1080, v103
	ds_write2_b32 v0, v34, v35 offset1:1
	v_pk_mul_f32 v[34:35], v[48:49], v[132:133] op_sel_hi:[1,0]
	v_add_u32_e32 v0, 0x1088, v103
	ds_write2_b32 v0, v34, v35 offset1:1
	s_waitcnt vmcnt(0)
	v_pk_mul_f32 v[34:35], v[58:59], v[126:127] op_sel_hi:[1,0]
	v_add_u32_e32 v0, 0x14a0, v103
	ds_write2_b32 v0, v34, v35 offset1:1
	v_pk_mul_f32 v[34:35], v[60:61], v[126:127] op_sel_hi:[1,0]
	v_add_u32_e32 v0, 0x14a8, v103
	ds_write2_b32 v0, v34, v35 offset1:1
	v_pk_mul_f32 v[34:35], v[54:55], v[128:129] op_sel_hi:[1,0]
	v_add_u32_e32 v0, 0x18c0, v103
	ds_write2_b32 v0, v34, v35 offset1:1
	v_pk_mul_f32 v[34:35], v[56:57], v[128:129] op_sel_hi:[1,0]
	v_add_u32_e32 v0, 0x18c8, v103
	ds_write2_b32 v0, v34, v35 offset1:1
	v_pk_mul_f32 v[34:35], v[66:67], v[120:121] op_sel_hi:[1,0]
	v_add_u32_e32 v0, 0x1ce0, v103
	ds_write2_b32 v0, v34, v35 offset1:1
	v_pk_mul_f32 v[34:35], v[68:69], v[120:121] op_sel_hi:[1,0]
	v_add_u32_e32 v0, 0x1ce8, v103
	ds_write2_b32 v0, v34, v35 offset1:1
	s_waitcnt lgkmcnt(0)
	ds_read2_b32 v[38:39], v99 offset0:33 offset1:41
	ds_read2_b32 v[40:41], v99 offset1:8
	ds_read2_b32 v[42:43], v99 offset0:66 offset1:74
	ds_read2_b32 v[44:45], v99 offset0:99 offset1:107
	ds_read2_b32 v[46:47], v99 offset0:132 offset1:140
	ds_read2_b32 v[48:49], v99 offset0:165 offset1:173
	ds_read2_b32 v[50:51], v99 offset0:198 offset1:206
	ds_read2_b32 v[52:53], v99 offset0:231 offset1:239
	v_mul_u32_u24_e32 v0, s34, v102
	v_lshlrev_b32_e32 v0, 1, v0
	v_lshl_add_u64 v[54:55], s[14:15], 0, v[0:1]
	v_lshlrev_b32_e32 v0, 1, v112
	s_lshl_b32 s14, s34, 3
	s_waitcnt lgkmcnt(6)
	v_cvt_pk_bf16_f32 v34, v40, v38
	s_waitcnt lgkmcnt(4)
	v_cvt_pk_bf16_f32 v35, v42, v44
	s_waitcnt lgkmcnt(2)
	v_cvt_pk_bf16_f32 v36, v46, v48
	s_waitcnt lgkmcnt(0)
	v_cvt_pk_bf16_f32 v37, v50, v52
	v_lshl_add_u64 v[56:57], v[54:55], 0, v[0:1]
	s_ashr_i32 s15, s14, 31
	global_store_dwordx4 v[56:57], v[34:37], off sc0 sc1
	s_lshl_b64 s[14:15], s[14:15], 1
	s_nop 0
	v_cvt_pk_bf16_f32 v34, v41, v39
	v_cvt_pk_bf16_f32 v35, v43, v45
	v_cvt_pk_bf16_f32 v36, v47, v49
	v_cvt_pk_bf16_f32 v37, v51, v53
	v_lshl_add_u64 v[38:39], v[54:55], 0, s[14:15]
	ds_read2_b32 v[42:43], v99 offset0:16 offset1:24
	ds_read2_b32 v[44:45], v99 offset0:49 offset1:57
	ds_read2_b32 v[46:47], v99 offset0:82 offset1:90
	ds_read2_b32 v[48:49], v99 offset0:115 offset1:123
	ds_read2_b32 v[50:51], v99 offset0:148 offset1:156
	ds_read2_b32 v[52:53], v99 offset0:181 offset1:189
	ds_read2_b32 v[54:55], v99 offset0:214 offset1:222
	ds_read2_b32 v[56:57], v99 offset0:247 offset1:255
	v_lshl_add_u64 v[40:41], v[38:39], 0, v[0:1]
	v_lshl_add_u64 v[38:39], v[38:39], 0, s[14:15]
	global_store_dwordx4 v[40:41], v[34:37], off sc0 sc1
	v_lshl_add_u64 v[40:41], v[38:39], 0, v[0:1]
	v_lshl_add_u64 v[38:39], v[38:39], 0, s[14:15]
	s_waitcnt lgkmcnt(6)
	v_cvt_pk_bf16_f32 v34, v42, v44
	s_waitcnt lgkmcnt(4)
	v_cvt_pk_bf16_f32 v35, v46, v48
	s_waitcnt lgkmcnt(2)
	v_cvt_pk_bf16_f32 v36, v50, v52
	s_waitcnt lgkmcnt(0)
	v_cvt_pk_bf16_f32 v37, v54, v56
	global_store_dwordx4 v[40:41], v[34:37], off sc0 sc1
	v_lshl_add_u64 v[38:39], v[38:39], 0, v[0:1]
	s_nop 0
	v_cvt_pk_bf16_f32 v34, v43, v45
	v_cvt_pk_bf16_f32 v35, v47, v49
	v_cvt_pk_bf16_f32 v36, v51, v53
	v_cvt_pk_bf16_f32 v37, v55, v57
	global_store_dwordx4 v[38:39], v[34:37], off sc0 sc1
	s_waitcnt lgkmcnt(0)

.LBB0_781:
	s_andn2_b64 vcc, exec, s[46:47]
	s_cbranch_vccnz .LBB0_785
	s_cmp_eq_u32 s31, 0
	s_cbranch_scc1 .LBB0_784
	v_pk_mul_f32 v[26:27], v[134:135], v[26:27] op_sel_hi:[0,1]
	v_add_u32_e32 v0, 0x420, v103
	ds_write2_b32 v0, v26, v27 offset1:1
	v_pk_mul_f32 v[26:27], v[134:135], v[28:29] op_sel_hi:[0,1]
	v_add_u32_e32 v0, 0x428, v103
	ds_write2_b32 v0, v26, v27 offset1:1
	v_pk_mul_f32 v[22:23], v[138:139], v[22:23] op_sel_hi:[0,1]
	v_add_u32_e32 v0, 0x840, v103
	ds_write2_b32 v0, v22, v23 offset1:1
	v_pk_mul_f32 v[22:23], v[138:139], v[24:25] op_sel_hi:[0,1]
	v_add_u32_e32 v0, 0x848, v103
	ds_write2_b32 v0, v22, v23 offset1:1
	v_pk_mul_f32 v[18:19], v[130:131], v[18:19] op_sel_hi:[0,1]
	v_add_u32_e32 v0, 0xc60, v103
	ds_write2_b32 v0, v18, v19 offset1:1
	v_pk_mul_f32 v[18:19], v[130:131], v[20:21] op_sel_hi:[0,1]
	v_add_u32_e32 v0, 0xc68, v103
	ds_write2_b32 v0, v18, v19 offset1:1
	v_pk_mul_f32 v[14:15], v[132:133], v[14:15] op_sel_hi:[0,1]
	v_add_u32_e32 v0, 0x1080, v103
	ds_write2_b32 v0, v14, v15 offset1:1
	v_pk_mul_f32 v[14:15], v[132:133], v[16:17] op_sel_hi:[0,1]
	v_add_u32_e32 v0, 0x1088, v103
	ds_write2_b32 v0, v14, v15 offset1:1
	s_waitcnt vmcnt(2)
	v_pk_mul_f32 v[10:11], v[126:127], v[10:11] op_sel_hi:[0,1]
	v_add_u32_e32 v0, 0x14a0, v103
	ds_write2_b32 v0, v10, v11 offset1:1
	v_pk_mul_f32 v[10:11], v[126:127], v[12:13] op_sel_hi:[0,1]
	v_add_u32_e32 v0, 0x14a8, v103
	ds_write2_b32 v0, v10, v11 offset1:1
	s_waitcnt vmcnt(1)
	v_pk_mul_f32 v[6:7], v[128:129], v[6:7] op_sel_hi:[0,1]
	v_add_u32_e32 v0, 0x18c0, v103
	ds_write2_b32 v0, v6, v7 offset1:1
	v_pk_mul_f32 v[6:7], v[128:129], v[8:9] op_sel_hi:[0,1]
	v_add_u32_e32 v0, 0x18c8, v103
	s_waitcnt vmcnt(0)
	v_pk_mul_f32 v[30:31], v[136:137], v[30:31] op_sel_hi:[0,1]
	ds_write2_b32 v0, v6, v7 offset1:1
	v_pk_mul_f32 v[2:3], v[120:121], v[2:3] op_sel_hi:[0,1]
	v_add_u32_e32 v0, 0x1ce0, v103
	ds_write2_b32 v103, v30, v31 offset1:1
	v_pk_mul_f32 v[30:31], v[136:137], v[32:33] op_sel_hi:[0,1]
	ds_write2_b32 v0, v2, v3 offset1:1
	v_pk_mul_f32 v[2:3], v[120:121], v[4:5] op_sel_hi:[0,1]
	v_add_u32_e32 v0, 0x1ce8, v103
	ds_write2_b32 v103, v30, v31 offset0:2 offset1:3
	ds_write2_b32 v0, v2, v3 offset1:1
	s_waitcnt lgkmcnt(0)
	ds_read2_b32 v[6:7], v99 offset0:33 offset1:41
	ds_read2_b32 v[8:9], v99 offset1:8
	ds_read2_b32 v[10:11], v99 offset0:66 offset1:74
	ds_read2_b32 v[12:13], v99 offset0:99 offset1:107
	ds_read2_b32 v[14:15], v99 offset0:132 offset1:140
	ds_read2_b32 v[16:17], v99 offset0:165 offset1:173
	ds_read2_b32 v[18:19], v99 offset0:198 offset1:206
	ds_read2_b32 v[20:21], v99 offset0:231 offset1:239
	v_mad_u64_u32 v[22:23], s[36:37], s34, v102, 0
	v_lshl_add_u64 v[22:23], v[22:23], 1, s[0:1]
	v_lshlrev_b32_e32 v0, 1, v112
	s_waitcnt lgkmcnt(6)
	v_cvt_pk_bf16_f32 v2, v8, v6
	s_waitcnt lgkmcnt(4)
	v_cvt_pk_bf16_f32 v3, v10, v12
	s_waitcnt lgkmcnt(2)
	v_cvt_pk_bf16_f32 v4, v14, v16
	s_waitcnt lgkmcnt(0)
	v_cvt_pk_bf16_f32 v5, v18, v20
	v_lshl_add_u64 v[22:23], v[22:23], 0, v[0:1]
	global_store_dwordx4 v[22:23], v[2:5], off sc0 sc1
	s_nop 1
	v_cvt_pk_bf16_f32 v2, v9, v7
	v_cvt_pk_bf16_f32 v3, v11, v13
	v_cvt_pk_bf16_f32 v4, v15, v17
	v_cvt_pk_bf16_f32 v5, v19, v21
	v_mad_u64_u32 v[6:7], s[36:37], s34, v110, 0
	ds_read2_b32 v[8:9], v99 offset0:16 offset1:24
	ds_read2_b32 v[10:11], v99 offset0:49 offset1:57
	ds_read2_b32 v[12:13], v99 offset0:82 offset1:90
	ds_read2_b32 v[14:15], v99 offset0:115 offset1:123
	ds_read2_b32 v[16:17], v99 offset0:148 offset1:156
	ds_read2_b32 v[18:19], v99 offset0:181 offset1:189
	ds_read2_b32 v[20:21], v99 offset0:214 offset1:222
	ds_read2_b32 v[22:23], v99 offset0:247 offset1:255
	v_lshl_add_u64 v[6:7], v[6:7], 1, s[0:1]
	v_lshl_add_u64 v[6:7], v[6:7], 0, v[0:1]
	global_store_dwordx4 v[6:7], v[2:5], off sc0 sc1
	v_mad_u64_u32 v[6:7], s[36:37], s34, v108, 0
	v_lshl_add_u64 v[6:7], v[6:7], 1, s[0:1]
	s_waitcnt lgkmcnt(6)
	v_cvt_pk_bf16_f32 v2, v8, v10
	s_waitcnt lgkmcnt(4)
	v_cvt_pk_bf16_f32 v3, v12, v14
	s_waitcnt lgkmcnt(2)
	v_cvt_pk_bf16_f32 v4, v16, v18
	s_waitcnt lgkmcnt(0)
	v_cvt_pk_bf16_f32 v5, v20, v22
	v_lshl_add_u64 v[6:7], v[6:7], 0, v[0:1]
	global_store_dwordx4 v[6:7], v[2:5], off sc0 sc1
	v_mad_u64_u32 v[6:7], s[36:37], s34, v106, 0
	v_lshl_add_u64 v[6:7], v[6:7], 1, s[0:1]
	v_cvt_pk_bf16_f32 v2, v9, v11
	v_cvt_pk_bf16_f32 v3, v13, v15
	v_cvt_pk_bf16_f32 v4, v17, v19
	v_cvt_pk_bf16_f32 v5, v21, v23
	v_lshl_add_u64 v[6:7], v[6:7], 0, v[0:1]
	global_store_dwordx4 v[6:7], v[2:5], off sc0 sc1
	s_waitcnt lgkmcnt(0)

.LBB0_799:
	s_andn2_b64 vcc, exec, s[46:47]
	s_cbranch_vccnz .LBB0_766
	s_cmp_eq_u32 s31, 0
	s_cbranch_scc1 .LBB0_765
	v_pk_mul_f32 v[26:27], v[26:27], v[134:135] op_sel_hi:[1,0]
	v_add_u32_e32 v0, 0x420, v103
	ds_write2_b32 v0, v26, v27 offset1:1
	v_pk_mul_f32 v[26:27], v[28:29], v[134:135] op_sel_hi:[1,0]
	v_add_u32_e32 v0, 0x428, v103
	ds_write2_b32 v0, v26, v27 offset1:1
	v_pk_mul_f32 v[22:23], v[22:23], v[138:139] op_sel_hi:[1,0]
	v_add_u32_e32 v0, 0x840, v103
	ds_write2_b32 v0, v22, v23 offset1:1
	v_pk_mul_f32 v[22:23], v[24:25], v[138:139] op_sel_hi:[1,0]
	v_add_u32_e32 v0, 0x848, v103
	ds_write2_b32 v0, v22, v23 offset1:1
	v_pk_mul_f32 v[18:19], v[18:19], v[130:131] op_sel_hi:[1,0]
	v_add_u32_e32 v0, 0xc60, v103
	ds_write2_b32 v0, v18, v19 offset1:1
	v_pk_mul_f32 v[18:19], v[20:21], v[130:131] op_sel_hi:[1,0]
	v_add_u32_e32 v0, 0xc68, v103
	ds_write2_b32 v0, v18, v19 offset1:1
	v_pk_mul_f32 v[14:15], v[14:15], v[132:133] op_sel_hi:[1,0]
	v_add_u32_e32 v0, 0x1080, v103
	ds_write2_b32 v0, v14, v15 offset1:1
	v_pk_mul_f32 v[14:15], v[16:17], v[132:133] op_sel_hi:[1,0]
	v_add_u32_e32 v0, 0x1088, v103
	ds_write2_b32 v0, v14, v15 offset1:1
	s_waitcnt vmcnt(2)
	v_pk_mul_f32 v[10:11], v[10:11], v[126:127] op_sel_hi:[1,0]
	v_add_u32_e32 v0, 0x14a0, v103
	ds_write2_b32 v0, v10, v11 offset1:1
	v_pk_mul_f32 v[10:11], v[12:13], v[126:127] op_sel_hi:[1,0]
	v_add_u32_e32 v0, 0x14a8, v103
	ds_write2_b32 v0, v10, v11 offset1:1
	s_waitcnt vmcnt(1)
	v_pk_mul_f32 v[6:7], v[6:7], v[128:129] op_sel_hi:[1,0]
	v_add_u32_e32 v0, 0x18c0, v103
	ds_write2_b32 v0, v6, v7 offset1:1
	v_pk_mul_f32 v[6:7], v[8:9], v[128:129] op_sel_hi:[1,0]
	v_add_u32_e32 v0, 0x18c8, v103
	s_waitcnt vmcnt(0)
	v_pk_mul_f32 v[30:31], v[30:31], v[136:137] op_sel_hi:[1,0]
	ds_write2_b32 v0, v6, v7 offset1:1
	v_pk_mul_f32 v[2:3], v[2:3], v[120:121] op_sel_hi:[1,0]
	v_add_u32_e32 v0, 0x1ce0, v103
	ds_write2_b32 v103, v30, v31 offset1:1
	v_pk_mul_f32 v[30:31], v[32:33], v[136:137] op_sel_hi:[1,0]
	ds_write2_b32 v0, v2, v3 offset1:1
	v_pk_mul_f32 v[2:3], v[4:5], v[120:121] op_sel_hi:[1,0]
	v_add_u32_e32 v0, 0x1ce8, v103
	ds_write2_b32 v103, v30, v31 offset0:2 offset1:3
	ds_write2_b32 v0, v2, v3 offset1:1
	s_waitcnt lgkmcnt(0)
	ds_read2_b32 v[6:7], v99 offset0:33 offset1:41
	ds_read2_b32 v[8:9], v99 offset1:8
	ds_read2_b32 v[10:11], v99 offset0:66 offset1:74
	ds_read2_b32 v[12:13], v99 offset0:99 offset1:107
	ds_read2_b32 v[14:15], v99 offset0:132 offset1:140
	ds_read2_b32 v[16:17], v99 offset0:165 offset1:173
	ds_read2_b32 v[18:19], v99 offset0:198 offset1:206
	ds_read2_b32 v[20:21], v99 offset0:231 offset1:239
	v_mad_u64_u32 v[22:23], s[36:37], s34, v102, 0
	v_lshl_add_u64 v[22:23], v[22:23], 1, s[0:1]
	v_lshlrev_b32_e32 v0, 1, v112
	s_waitcnt lgkmcnt(6)
	v_cvt_pk_bf16_f32 v2, v8, v6
	s_waitcnt lgkmcnt(4)
	v_cvt_pk_bf16_f32 v3, v10, v12
	s_waitcnt lgkmcnt(2)
	v_cvt_pk_bf16_f32 v4, v14, v16
	s_waitcnt lgkmcnt(0)
	v_cvt_pk_bf16_f32 v5, v18, v20
	v_lshl_add_u64 v[22:23], v[22:23], 0, v[0:1]
	global_store_dwordx4 v[22:23], v[2:5], off sc0 sc1
	s_nop 1
	v_cvt_pk_bf16_f32 v2, v9, v7
	v_cvt_pk_bf16_f32 v3, v11, v13
	v_cvt_pk_bf16_f32 v4, v15, v17
	v_cvt_pk_bf16_f32 v5, v19, v21
	v_mad_u64_u32 v[6:7], s[36:37], s34, v110, 0
	ds_read2_b32 v[8:9], v99 offset0:16 offset1:24
	ds_read2_b32 v[10:11], v99 offset0:49 offset1:57
	ds_read2_b32 v[12:13], v99 offset0:82 offset1:90
	ds_read2_b32 v[14:15], v99 offset0:115 offset1:123
	ds_read2_b32 v[16:17], v99 offset0:148 offset1:156
	ds_read2_b32 v[18:19], v99 offset0:181 offset1:189
	ds_read2_b32 v[20:21], v99 offset0:214 offset1:222
	ds_read2_b32 v[22:23], v99 offset0:247 offset1:255
	v_lshl_add_u64 v[6:7], v[6:7], 1, s[0:1]
	v_lshl_add_u64 v[6:7], v[6:7], 0, v[0:1]
	global_store_dwordx4 v[6:7], v[2:5], off sc0 sc1
	v_mad_u64_u32 v[6:7], s[36:37], s34, v108, 0
	v_lshl_add_u64 v[6:7], v[6:7], 1, s[0:1]
	s_waitcnt lgkmcnt(6)
	v_cvt_pk_bf16_f32 v2, v8, v10
	s_waitcnt lgkmcnt(4)
	v_cvt_pk_bf16_f32 v3, v12, v14
	s_waitcnt lgkmcnt(2)
	v_cvt_pk_bf16_f32 v4, v16, v18
	s_waitcnt lgkmcnt(0)
	v_cvt_pk_bf16_f32 v5, v20, v22
	v_lshl_add_u64 v[6:7], v[6:7], 0, v[0:1]
	global_store_dwordx4 v[6:7], v[2:5], off sc0 sc1
	v_mad_u64_u32 v[6:7], s[36:37], s34, v106, 0
	v_lshl_add_u64 v[6:7], v[6:7], 1, s[0:1]
	v_cvt_pk_bf16_f32 v2, v9, v11
	v_cvt_pk_bf16_f32 v3, v13, v15
	v_cvt_pk_bf16_f32 v4, v17, v19
	v_cvt_pk_bf16_f32 v5, v21, v23
	v_lshl_add_u64 v[6:7], v[6:7], 0, v[0:1]
	global_store_dwordx4 v[6:7], v[2:5], off sc0 sc1
	s_waitcnt lgkmcnt(0)
	s_branch .LBB0_765

.LBB0_812:
	s_andn2_b64 vcc, exec, s[16:17]
	s_cbranch_vccnz .LBB0_816
	s_cmp_eq_u32 s31, 0
	s_cbranch_scc1 .LBB0_815
	v_pk_mul_f32 v[26:27], v[26:27], v[134:135] op_sel_hi:[1,0]
	v_add_u32_e32 v0, 0x420, v103
	ds_write2_b32 v0, v26, v27 offset1:1
	v_pk_mul_f32 v[26:27], v[28:29], v[134:135] op_sel_hi:[1,0]
	v_add_u32_e32 v0, 0x428, v103
	ds_write2_b32 v0, v26, v27 offset1:1
	v_pk_mul_f32 v[22:23], v[22:23], v[138:139] op_sel_hi:[1,0]
	v_add_u32_e32 v0, 0x840, v103
	ds_write2_b32 v0, v22, v23 offset1:1
	v_pk_mul_f32 v[22:23], v[24:25], v[138:139] op_sel_hi:[1,0]
	v_add_u32_e32 v0, 0x848, v103
	ds_write2_b32 v0, v22, v23 offset1:1
	v_pk_mul_f32 v[18:19], v[18:19], v[130:131] op_sel_hi:[1,0]
	v_add_u32_e32 v0, 0xc60, v103
	ds_write2_b32 v0, v18, v19 offset1:1
	v_pk_mul_f32 v[18:19], v[20:21], v[130:131] op_sel_hi:[1,0]
	v_add_u32_e32 v0, 0xc68, v103
	ds_write2_b32 v0, v18, v19 offset1:1
	v_pk_mul_f32 v[14:15], v[14:15], v[132:133] op_sel_hi:[1,0]
	v_add_u32_e32 v0, 0x1080, v103
	ds_write2_b32 v0, v14, v15 offset1:1
	v_pk_mul_f32 v[14:15], v[16:17], v[132:133] op_sel_hi:[1,0]
	v_add_u32_e32 v0, 0x1088, v103
	ds_write2_b32 v0, v14, v15 offset1:1
	s_waitcnt vmcnt(2)
	v_pk_mul_f32 v[10:11], v[10:11], v[126:127] op_sel_hi:[1,0]
	v_add_u32_e32 v0, 0x14a0, v103
	ds_write2_b32 v0, v10, v11 offset1:1
	v_pk_mul_f32 v[10:11], v[12:13], v[126:127] op_sel_hi:[1,0]
	v_add_u32_e32 v0, 0x14a8, v103
	ds_write2_b32 v0, v10, v11 offset1:1
	s_waitcnt vmcnt(1)
	v_pk_mul_f32 v[6:7], v[6:7], v[128:129] op_sel_hi:[1,0]
	v_add_u32_e32 v0, 0x18c0, v103
	ds_write2_b32 v0, v6, v7 offset1:1
	v_pk_mul_f32 v[6:7], v[8:9], v[128:129] op_sel_hi:[1,0]
	v_add_u32_e32 v0, 0x18c8, v103
	s_waitcnt vmcnt(0)
	v_pk_mul_f32 v[30:31], v[30:31], v[136:137] op_sel_hi:[1,0]
	ds_write2_b32 v0, v6, v7 offset1:1
	v_pk_mul_f32 v[2:3], v[2:3], v[120:121] op_sel_hi:[1,0]
	v_add_u32_e32 v0, 0x1ce0, v103
	ds_write2_b32 v103, v30, v31 offset1:1
	v_pk_mul_f32 v[30:31], v[32:33], v[136:137] op_sel_hi:[1,0]
	ds_write2_b32 v0, v2, v3 offset1:1
	v_pk_mul_f32 v[2:3], v[4:5], v[120:121] op_sel_hi:[1,0]
	v_add_u32_e32 v0, 0x1ce8, v103
	ds_write2_b32 v103, v30, v31 offset0:2 offset1:3
	ds_write2_b32 v0, v2, v3 offset1:1
	s_waitcnt lgkmcnt(0)
	ds_read2_b32 v[6:7], v99 offset0:33 offset1:41
	ds_read2_b32 v[8:9], v99 offset1:8
	ds_read2_b32 v[10:11], v99 offset0:66 offset1:74
	ds_read2_b32 v[12:13], v99 offset0:99 offset1:107
	ds_read2_b32 v[14:15], v99 offset0:132 offset1:140
	ds_read2_b32 v[16:17], v99 offset0:165 offset1:173
	ds_read2_b32 v[18:19], v99 offset0:198 offset1:206
	ds_read2_b32 v[20:21], v99 offset0:231 offset1:239
	v_mad_u64_u32 v[22:23], s[16:17], s34, v102, 0
	v_lshl_add_u64 v[22:23], v[22:23], 1, s[0:1]
	v_lshlrev_b32_e32 v0, 1, v112
	s_waitcnt lgkmcnt(6)
	v_cvt_pk_bf16_f32 v2, v8, v6
	s_waitcnt lgkmcnt(4)
	v_cvt_pk_bf16_f32 v3, v10, v12
	s_waitcnt lgkmcnt(2)
	v_cvt_pk_bf16_f32 v4, v14, v16
	s_waitcnt lgkmcnt(0)
	v_cvt_pk_bf16_f32 v5, v18, v20
	v_lshl_add_u64 v[22:23], v[22:23], 0, v[0:1]
	global_store_dwordx4 v[22:23], v[2:5], off sc0 sc1
	s_nop 1
	v_cvt_pk_bf16_f32 v2, v9, v7
	v_cvt_pk_bf16_f32 v3, v11, v13
	v_cvt_pk_bf16_f32 v4, v15, v17
	v_cvt_pk_bf16_f32 v5, v19, v21
	v_mad_u64_u32 v[6:7], s[16:17], s34, v110, 0
	ds_read2_b32 v[8:9], v99 offset0:16 offset1:24
	ds_read2_b32 v[10:11], v99 offset0:49 offset1:57
	ds_read2_b32 v[12:13], v99 offset0:82 offset1:90
	ds_read2_b32 v[14:15], v99 offset0:115 offset1:123
	ds_read2_b32 v[16:17], v99 offset0:148 offset1:156
	ds_read2_b32 v[18:19], v99 offset0:181 offset1:189
	ds_read2_b32 v[20:21], v99 offset0:214 offset1:222
	ds_read2_b32 v[22:23], v99 offset0:247 offset1:255
	v_lshl_add_u64 v[6:7], v[6:7], 1, s[0:1]
	v_lshl_add_u64 v[6:7], v[6:7], 0, v[0:1]
	global_store_dwordx4 v[6:7], v[2:5], off sc0 sc1
	v_mad_u64_u32 v[6:7], s[16:17], s34, v108, 0
	v_lshl_add_u64 v[6:7], v[6:7], 1, s[0:1]
	s_waitcnt lgkmcnt(6)
	v_cvt_pk_bf16_f32 v2, v8, v10
	s_waitcnt lgkmcnt(4)
	v_cvt_pk_bf16_f32 v3, v12, v14
	s_waitcnt lgkmcnt(2)
	v_cvt_pk_bf16_f32 v4, v16, v18
	s_waitcnt lgkmcnt(0)
	v_cvt_pk_bf16_f32 v5, v20, v22
	v_lshl_add_u64 v[6:7], v[6:7], 0, v[0:1]
	global_store_dwordx4 v[6:7], v[2:5], off sc0 sc1
	v_mad_u64_u32 v[6:7], s[16:17], s34, v106, 0
	v_lshl_add_u64 v[6:7], v[6:7], 1, s[0:1]
	v_cvt_pk_bf16_f32 v2, v9, v11
	v_cvt_pk_bf16_f32 v3, v13, v15
	v_cvt_pk_bf16_f32 v4, v17, v19
	v_cvt_pk_bf16_f32 v5, v21, v23
	v_lshl_add_u64 v[6:7], v[6:7], 0, v[0:1]
	global_store_dwordx4 v[6:7], v[2:5], off sc0 sc1
	s_waitcnt lgkmcnt(0)

.LBB0_817:
	s_waitcnt vmcnt(0)
	v_pk_mul_f32 v[2:3], v[62:63], v[136:137] op_sel_hi:[1,0]
	ds_write2_b32 v103, v2, v3 offset1:1
	v_pk_mul_f32 v[2:3], v[64:65], v[136:137] op_sel_hi:[1,0]
	ds_write2_b32 v103, v2, v3 offset0:2 offset1:3
	v_pk_mul_f32 v[2:3], v[50:51], v[134:135] op_sel_hi:[1,0]
	v_add_u32_e32 v0, 0x420, v103
	ds_write2_b32 v0, v2, v3 offset1:1
	v_pk_mul_f32 v[2:3], v[52:53], v[134:135] op_sel_hi:[1,0]
	v_add_u32_e32 v0, 0x428, v103
	ds_write2_b32 v0, v2, v3 offset1:1
	v_pk_mul_f32 v[2:3], v[58:59], v[138:139] op_sel_hi:[1,0]
	v_add_u32_e32 v0, 0x840, v103
	ds_write2_b32 v0, v2, v3 offset1:1
	v_pk_mul_f32 v[2:3], v[60:61], v[138:139] op_sel_hi:[1,0]
	v_add_u32_e32 v0, 0x848, v103
	ds_write2_b32 v0, v2, v3 offset1:1
	v_pk_mul_f32 v[2:3], v[42:43], v[130:131] op_sel_hi:[1,0]
	v_add_u32_e32 v0, 0xc60, v103
	ds_write2_b32 v0, v2, v3 offset1:1
	v_pk_mul_f32 v[2:3], v[44:45], v[130:131] op_sel_hi:[1,0]
	v_add_u32_e32 v0, 0xc68, v103
	ds_write2_b32 v0, v2, v3 offset1:1
	v_pk_mul_f32 v[2:3], v[54:55], v[132:133] op_sel_hi:[1,0]
	v_add_u32_e32 v0, 0x1080, v103
	ds_write2_b32 v0, v2, v3 offset1:1
	v_pk_mul_f32 v[2:3], v[56:57], v[132:133] op_sel_hi:[1,0]
	v_add_u32_e32 v0, 0x1088, v103
	ds_write2_b32 v0, v2, v3 offset1:1
	v_pk_mul_f32 v[2:3], v[38:39], v[126:127] op_sel_hi:[1,0]
	v_add_u32_e32 v0, 0x14a0, v103
	ds_write2_b32 v0, v2, v3 offset1:1
	v_pk_mul_f32 v[2:3], v[40:41], v[126:127] op_sel_hi:[1,0]
	v_add_u32_e32 v0, 0x14a8, v103
	ds_write2_b32 v0, v2, v3 offset1:1
	v_pk_mul_f32 v[2:3], v[46:47], v[128:129] op_sel_hi:[1,0]
	v_add_u32_e32 v0, 0x18c0, v103
	ds_write2_b32 v0, v2, v3 offset1:1
	v_pk_mul_f32 v[2:3], v[48:49], v[128:129] op_sel_hi:[1,0]
	v_add_u32_e32 v0, 0x18c8, v103
	ds_write2_b32 v0, v2, v3 offset1:1
	v_pk_mul_f32 v[2:3], v[34:35], v[120:121] op_sel_hi:[1,0]
	v_add_u32_e32 v0, 0x1ce0, v103
	ds_write2_b32 v0, v2, v3 offset1:1
	v_pk_mul_f32 v[2:3], v[36:37], v[120:121] op_sel_hi:[1,0]
	v_add_u32_e32 v0, 0x1ce8, v103
	ds_write2_b32 v0, v2, v3 offset1:1
	s_waitcnt lgkmcnt(0)
	ds_read2_b32 v[6:7], v99 offset0:33 offset1:41
	ds_read2_b32 v[8:9], v99 offset1:8
	ds_read2_b32 v[10:11], v99 offset0:66 offset1:74
	ds_read2_b32 v[12:13], v99 offset0:99 offset1:107
	ds_read2_b32 v[14:15], v99 offset0:132 offset1:140
	ds_read2_b32 v[16:17], v99 offset0:165 offset1:173
	ds_read2_b32 v[18:19], v99 offset0:198 offset1:206
	ds_read2_b32 v[20:21], v99 offset0:231 offset1:239
	v_mad_u64_u32 v[22:23], s[0:1], s34, v102, 0
	v_lshl_add_u64 v[22:23], v[22:23], 1, s[14:15]
	v_lshlrev_b32_e32 v0, 1, v112
	s_waitcnt lgkmcnt(6)
	v_cvt_pk_bf16_f32 v2, v8, v6
	s_waitcnt lgkmcnt(4)
	v_cvt_pk_bf16_f32 v3, v10, v12
	s_waitcnt lgkmcnt(2)
	v_cvt_pk_bf16_f32 v4, v14, v16
	s_waitcnt lgkmcnt(0)
	v_cvt_pk_bf16_f32 v5, v18, v20
	v_lshl_add_u64 v[22:23], v[22:23], 0, v[0:1]
	global_store_dwordx4 v[22:23], v[2:5], off sc0 sc1
	s_nop 1
	v_cvt_pk_bf16_f32 v2, v9, v7
	v_cvt_pk_bf16_f32 v3, v11, v13
	v_cvt_pk_bf16_f32 v4, v15, v17
	v_cvt_pk_bf16_f32 v5, v19, v21
	v_mad_u64_u32 v[6:7], s[0:1], s34, v110, 0
	ds_read2_b32 v[8:9], v99 offset0:16 offset1:24
	ds_read2_b32 v[10:11], v99 offset0:49 offset1:57
	ds_read2_b32 v[12:13], v99 offset0:82 offset1:90
	ds_read2_b32 v[14:15], v99 offset0:115 offset1:123
	ds_read2_b32 v[16:17], v99 offset0:148 offset1:156
	ds_read2_b32 v[18:19], v99 offset0:181 offset1:189
	ds_read2_b32 v[20:21], v99 offset0:214 offset1:222
	ds_read2_b32 v[22:23], v99 offset0:247 offset1:255
	v_lshl_add_u64 v[6:7], v[6:7], 1, s[14:15]
	v_lshl_add_u64 v[6:7], v[6:7], 0, v[0:1]
	global_store_dwordx4 v[6:7], v[2:5], off sc0 sc1
	v_mad_u64_u32 v[6:7], s[0:1], s34, v108, 0
	v_lshl_add_u64 v[6:7], v[6:7], 1, s[14:15]
	s_waitcnt lgkmcnt(6)
	v_cvt_pk_bf16_f32 v2, v8, v10
	s_waitcnt lgkmcnt(4)
	v_cvt_pk_bf16_f32 v3, v12, v14
	s_waitcnt lgkmcnt(2)
	v_cvt_pk_bf16_f32 v4, v16, v18
	s_waitcnt lgkmcnt(0)
	v_cvt_pk_bf16_f32 v5, v20, v22
	v_lshl_add_u64 v[6:7], v[6:7], 0, v[0:1]
	global_store_dwordx4 v[6:7], v[2:5], off sc0 sc1
	v_mad_u64_u32 v[6:7], s[0:1], s34, v106, 0
	v_lshl_add_u64 v[6:7], v[6:7], 1, s[14:15]
	v_cvt_pk_bf16_f32 v2, v9, v11
	v_cvt_pk_bf16_f32 v3, v13, v15
	v_cvt_pk_bf16_f32 v4, v17, v19
	v_cvt_pk_bf16_f32 v5, v21, v23
	v_lshl_add_u64 v[6:7], v[6:7], 0, v[0:1]
	global_store_dwordx4 v[6:7], v[2:5], off sc0 sc1
	s_waitcnt lgkmcnt(0)

.LBB0_820:
	v_add_u32_e32 v98, s92, v98
	s_mov_b32 s16, 0xbfff
	v_cmp_lt_i32_e32 vcc, s16, v98
	global_store_dwordx4 v[6:7], v[2:5], off sc0 sc1
	s_or_b64 s[14:15], vcc, s[14:15]
	v_lshl_add_u64 v[6:7], v[6:7], 0, s[34:35]
	s_andn2_b64 exec, exec, s[14:15]
	s_cbranch_execnz .LBB0_820

.LBB0_824:
	s_ashr_i32 s31, s30, 31
	s_lshl_b64 s[0:1], s[30:31], 12
	s_waitcnt lgkmcnt(0)
	v_lshl_add_u64 v[2:3], v[54:55], 0, s[0:1]
	global_load_dwordx4 v[64:67], v[2:3], off nt
	global_load_dwordx4 v[68:71], v[2:3], off offset:1024 nt
	global_load_dwordx4 v[72:75], v[2:3], off offset:2048 nt
	global_load_dwordx4 v[50:53], v[2:3], off offset:3072 nt
	s_add_i32 s0, s30, s72
	s_ashr_i32 s1, s0, 31
	s_add_i32 s16, s37, s30
	s_lshl_b64 s[14:15], s[0:1], 12
	s_ashr_i32 s17, s16, 31
	v_lshl_add_u64 v[2:3], v[54:55], 0, s[14:15]
	s_lshl_b64 s[14:15], s[16:17], 12
	global_load_dwordx4 v[46:49], v[2:3], off nt
	global_load_dwordx4 v[42:45], v[2:3], off offset:1024 nt
	global_load_dwordx4 v[38:41], v[2:3], off offset:2048 nt
	global_load_dwordx4 v[34:37], v[2:3], off offset:3072 nt
	v_lshl_add_u64 v[2:3], v[54:55], 0, s[14:15]
	s_mul_i32 s14, s91, 24
	s_add_i32 s14, s14, s30
	s_ashr_i32 s15, s14, 31
	s_lshl_b64 s[34:35], s[14:15], 12
	global_load_dwordx4 v[30:33], v[2:3], off nt
	global_load_dwordx4 v[26:29], v[2:3], off offset:1024 nt
	global_load_dwordx4 v[22:25], v[2:3], off offset:2048 nt
	global_load_dwordx4 v[18:21], v[2:3], off offset:3072 nt
	v_lshl_add_u64 v[2:3], v[54:55], 0, s[34:35]
	global_load_dwordx4 v[14:17], v[2:3], off nt
	global_load_dwordx4 v[10:13], v[2:3], off offset:1024 nt
	global_load_dwordx4 v[6:9], v[2:3], off offset:2048 nt
	s_nop 0
	global_load_dwordx4 v[2:5], v[2:3], off offset:3072 nt
	s_lshl_b64 s[34:35], s[30:31], 11
	s_waitcnt vmcnt(15)
	v_mul_f32_e32 v0, v65, v65
	v_mul_f32_e32 v76, v67, v67
	v_fmac_f32_e32 v0, v64, v64
	v_fmac_f32_e32 v76, v66, v66
	v_cvt_pk_bf16_f32 v64, v64, v65
	v_cvt_pk_bf16_f32 v65, v66, v67
	v_lshl_add_u64 v[66:67], v[56:57], 0, s[34:35]
	global_store_dwordx2 v[66:67], v[64:65], off sc0 sc1
	s_waitcnt vmcnt(15)
	v_mul_f32_e32 v64, v69, v69
	v_mul_f32_e32 v65, v71, v71
	v_fmac_f32_e32 v64, v68, v68
	v_fmac_f32_e32 v65, v70, v70
	v_add_f32_e32 v0, v0, v76
	v_add_f32_e32 v64, v64, v65
	v_add_f32_e32 v0, v0, v64
	v_cvt_pk_bf16_f32 v64, v68, v69
	v_cvt_pk_bf16_f32 v65, v70, v71
	global_store_dwordx2 v[66:67], v[64:65], off offset:512 sc0 sc1
	s_waitcnt vmcnt(15)
	v_mul_f32_e32 v64, v73, v73
	v_mul_f32_e32 v65, v75, v75
	v_fmac_f32_e32 v64, v72, v72
	v_fmac_f32_e32 v65, v74, v74
	v_add_f32_e32 v64, v64, v65
	v_add_f32_e32 v0, v0, v64
	v_cvt_pk_bf16_f32 v64, v72, v73
	v_cvt_pk_bf16_f32 v65, v74, v75
	global_store_dwordx2 v[66:67], v[64:65], off offset:1024 sc0 sc1
	s_waitcnt vmcnt(15)
	v_mul_f32_e32 v64, v51, v51
	v_mul_f32_e32 v65, v53, v53
	v_fmac_f32_e32 v64, v50, v50
	v_fmac_f32_e32 v65, v52, v52
	v_add_f32_e32 v64, v64, v65
	v_add_f32_e32 v0, v0, v64
	v_cvt_pk_bf16_f32 v50, v50, v51
	v_cvt_pk_bf16_f32 v51, v52, v53
	global_store_dwordx2 v[66:67], v[50:51], off offset:1536 sc0 sc1
	ds_bpermute_b32 v50, v58, v0
	s_waitcnt lgkmcnt(0)
	v_add_f32_e32 v0, v0, v50
	ds_bpermute_b32 v50, v59, v0
	s_waitcnt lgkmcnt(0)
	v_add_f32_e32 v0, v0, v50
	ds_bpermute_b32 v50, v60, v0
	s_waitcnt lgkmcnt(0)
	v_add_f32_e32 v0, v0, v50
	ds_bpermute_b32 v50, v61, v0
	s_waitcnt lgkmcnt(0)
	v_add_f32_e32 v0, v0, v50
	ds_bpermute_b32 v50, v62, v0
	s_waitcnt lgkmcnt(0)
	v_add_f32_e32 v0, v0, v50
	ds_bpermute_b32 v50, v63, v0
	s_and_saveexec_b64 s[34:35], vcc
	s_cbranch_execz .LBB0_826
	s_waitcnt lgkmcnt(0)
	v_add_f32_e32 v0, v0, v50
	v_fma_f32 v0, v0, s40, 0.5
	v_trunc_f32_e32 v0, v0
	v_mul_f32_e32 v50, 0x2f800000, v0
	v_floor_f32_e32 v51, v50
	v_fmac_f32_e32 v0, 0xcf800000, v51
	v_cvt_u32_f32_e32 v50, v0
	v_cvt_u32_f32_e32 v51, v51
	s_lshl_b64 s[30:31], s[30:31], 3
	s_add_u32 s30, s29, s30
	s_addc_u32 s31, s36, s31
	global_store_dwordx2 v1, v[50:51], s[30:31] sc0 sc1
.LBB0_826:
	s_or_b64 exec, exec, s[34:35]
	s_lshl_b64 s[30:31], s[0:1], 11
	s_waitcnt vmcnt(15)
	v_mul_f32_e32 v0, v47, v47
	s_waitcnt lgkmcnt(0)
	v_mul_f32_e32 v50, v49, v49
	v_fmac_f32_e32 v0, v46, v46
	v_fmac_f32_e32 v50, v48, v48
	v_cvt_pk_bf16_f32 v46, v46, v47
	v_cvt_pk_bf16_f32 v47, v48, v49
	v_lshl_add_u64 v[48:49], v[56:57], 0, s[30:31]
	global_store_dwordx2 v[48:49], v[46:47], off sc0 sc1
	s_waitcnt vmcnt(15)
	v_mul_f32_e32 v46, v43, v43
	v_fmac_f32_e32 v46, v42, v42
	v_cvt_pk_bf16_f32 v42, v42, v43
	v_cvt_pk_bf16_f32 v43, v44, v45
	v_mul_f32_e32 v47, v45, v45
	global_store_dwordx2 v[48:49], v[42:43], off offset:512 sc0 sc1
	s_waitcnt vmcnt(15)
	v_mul_f32_e32 v42, v39, v39
	v_fmac_f32_e32 v47, v44, v44
	v_fmac_f32_e32 v42, v38, v38
	v_mul_f32_e32 v43, v41, v41
	v_cvt_pk_bf16_f32 v38, v38, v39
	v_cvt_pk_bf16_f32 v39, v40, v41
	v_add_f32_e32 v0, v0, v50
	v_add_f32_e32 v46, v46, v47
	v_fmac_f32_e32 v43, v40, v40
	global_store_dwordx2 v[48:49], v[38:39], off offset:1024 sc0 sc1
	s_waitcnt vmcnt(15)
	v_mul_f32_e32 v38, v35, v35
	v_mul_f32_e32 v39, v37, v37
	v_add_f32_e32 v0, v0, v46
	v_add_f32_e32 v42, v42, v43
	v_fmac_f32_e32 v38, v34, v34
	v_fmac_f32_e32 v39, v36, v36
	v_add_f32_e32 v0, v0, v42
	v_add_f32_e32 v38, v38, v39
	v_add_f32_e32 v0, v0, v38
	v_cvt_pk_bf16_f32 v34, v34, v35
	v_cvt_pk_bf16_f32 v35, v36, v37
	global_store_dwordx2 v[48:49], v[34:35], off offset:1536 sc0 sc1
	ds_bpermute_b32 v34, v58, v0
	s_waitcnt lgkmcnt(0)
	v_add_f32_e32 v0, v0, v34
	ds_bpermute_b32 v34, v59, v0
	s_waitcnt lgkmcnt(0)
	v_add_f32_e32 v0, v0, v34
	ds_bpermute_b32 v34, v60, v0
	s_waitcnt lgkmcnt(0)
	v_add_f32_e32 v0, v0, v34
	ds_bpermute_b32 v34, v61, v0
	s_waitcnt lgkmcnt(0)
	v_add_f32_e32 v0, v0, v34
	ds_bpermute_b32 v34, v62, v0
	s_waitcnt lgkmcnt(0)
	v_add_f32_e32 v0, v0, v34
	ds_bpermute_b32 v34, v63, v0
	s_and_saveexec_b64 s[30:31], vcc
	s_cbranch_execz .LBB0_828
	s_waitcnt lgkmcnt(0)
	v_add_f32_e32 v0, v0, v34
	v_fma_f32 v0, v0, s40, 0.5
	v_trunc_f32_e32 v0, v0
	v_mul_f32_e32 v34, 0x2f800000, v0
	v_floor_f32_e32 v35, v34
	v_fmac_f32_e32 v0, 0xcf800000, v35
	v_cvt_u32_f32_e32 v34, v0
	v_cvt_u32_f32_e32 v35, v35
	s_lshl_b64 s[34:35], s[0:1], 3
	s_add_u32 s34, s29, s34
	s_addc_u32 s35, s36, s35
	global_store_dwordx2 v1, v[34:35], s[34:35] sc0 sc1
.LBB0_828:
	s_or_b64 exec, exec, s[30:31]
	s_lshl_b64 s[30:31], s[16:17], 11
	s_waitcnt vmcnt(15)
	v_mul_f32_e32 v0, v31, v31
	s_waitcnt lgkmcnt(0)
	v_mul_f32_e32 v34, v33, v33
	v_fmac_f32_e32 v0, v30, v30
	v_fmac_f32_e32 v34, v32, v32
	v_cvt_pk_bf16_f32 v30, v30, v31
	v_cvt_pk_bf16_f32 v31, v32, v33
	v_lshl_add_u64 v[32:33], v[56:57], 0, s[30:31]
	global_store_dwordx2 v[32:33], v[30:31], off sc0 sc1
	s_waitcnt vmcnt(15)
	v_mul_f32_e32 v30, v27, v27
	v_fmac_f32_e32 v30, v26, v26
	v_cvt_pk_bf16_f32 v26, v26, v27
	v_cvt_pk_bf16_f32 v27, v28, v29
	v_mul_f32_e32 v31, v29, v29
	global_store_dwordx2 v[32:33], v[26:27], off offset:512 sc0 sc1
	s_waitcnt vmcnt(15)
	v_mul_f32_e32 v26, v23, v23
	v_fmac_f32_e32 v31, v28, v28
	v_fmac_f32_e32 v26, v22, v22
	v_mul_f32_e32 v27, v25, v25
	v_cvt_pk_bf16_f32 v22, v22, v23
	v_cvt_pk_bf16_f32 v23, v24, v25
	v_add_f32_e32 v0, v0, v34
	v_add_f32_e32 v30, v30, v31
	v_fmac_f32_e32 v27, v24, v24
	global_store_dwordx2 v[32:33], v[22:23], off offset:1024 sc0 sc1
	s_waitcnt vmcnt(15)
	v_mul_f32_e32 v22, v19, v19
	v_mul_f32_e32 v23, v21, v21
	v_add_f32_e32 v0, v0, v30
	v_add_f32_e32 v26, v26, v27
	v_fmac_f32_e32 v22, v18, v18
	v_fmac_f32_e32 v23, v20, v20
	v_add_f32_e32 v0, v0, v26
	v_add_f32_e32 v22, v22, v23
	v_add_f32_e32 v0, v0, v22
	v_cvt_pk_bf16_f32 v18, v18, v19
	v_cvt_pk_bf16_f32 v19, v20, v21
	global_store_dwordx2 v[32:33], v[18:19], off offset:1536 sc0 sc1
	ds_bpermute_b32 v18, v58, v0
	s_waitcnt lgkmcnt(0)
	v_add_f32_e32 v0, v0, v18
	ds_bpermute_b32 v18, v59, v0
	s_waitcnt lgkmcnt(0)
	v_add_f32_e32 v0, v0, v18
	ds_bpermute_b32 v18, v60, v0
	s_waitcnt lgkmcnt(0)
	v_add_f32_e32 v0, v0, v18
	ds_bpermute_b32 v18, v61, v0
	s_waitcnt lgkmcnt(0)
	v_add_f32_e32 v0, v0, v18
	ds_bpermute_b32 v18, v62, v0
	s_waitcnt lgkmcnt(0)
	v_add_f32_e32 v0, v0, v18
	ds_bpermute_b32 v18, v63, v0
	s_and_saveexec_b64 s[30:31], vcc
	s_cbranch_execz .LBB0_830
	s_waitcnt lgkmcnt(0)
	v_add_f32_e32 v0, v0, v18
	v_fma_f32 v0, v0, s40, 0.5
	v_trunc_f32_e32 v0, v0
	v_mul_f32_e32 v18, 0x2f800000, v0
	v_floor_f32_e32 v19, v18
	v_fmac_f32_e32 v0, 0xcf800000, v19
	v_cvt_u32_f32_e32 v18, v0
	v_cvt_u32_f32_e32 v19, v19
	s_lshl_b64 s[16:17], s[16:17], 3
	s_add_u32 s16, s29, s16
	s_addc_u32 s17, s36, s17
	global_store_dwordx2 v1, v[18:19], s[16:17] sc0 sc1
.LBB0_830:
	s_or_b64 exec, exec, s[30:31]
	s_lshl_b64 s[16:17], s[14:15], 11
	s_waitcnt vmcnt(15)
	v_mul_f32_e32 v0, v15, v15
	s_waitcnt lgkmcnt(0)
	v_mul_f32_e32 v18, v17, v17
	v_fmac_f32_e32 v0, v14, v14
	v_fmac_f32_e32 v18, v16, v16
	v_cvt_pk_bf16_f32 v14, v14, v15
	v_cvt_pk_bf16_f32 v15, v16, v17
	v_lshl_add_u64 v[16:17], v[56:57], 0, s[16:17]
	global_store_dwordx2 v[16:17], v[14:15], off sc0 sc1
	s_waitcnt vmcnt(15)
	v_mul_f32_e32 v14, v11, v11
	v_fmac_f32_e32 v14, v10, v10
	v_cvt_pk_bf16_f32 v10, v10, v11
	v_cvt_pk_bf16_f32 v11, v12, v13
	v_mul_f32_e32 v15, v13, v13
	global_store_dwordx2 v[16:17], v[10:11], off offset:512 sc0 sc1
	s_waitcnt vmcnt(15)
	v_mul_f32_e32 v10, v7, v7
	v_fmac_f32_e32 v15, v12, v12
	v_fmac_f32_e32 v10, v6, v6
	v_mul_f32_e32 v11, v9, v9
	v_cvt_pk_bf16_f32 v6, v6, v7
	v_cvt_pk_bf16_f32 v7, v8, v9
	v_add_f32_e32 v0, v0, v18
	v_add_f32_e32 v14, v14, v15
	v_fmac_f32_e32 v11, v8, v8
	global_store_dwordx2 v[16:17], v[6:7], off offset:1024 sc0 sc1
	s_waitcnt vmcnt(15)
	v_mul_f32_e32 v6, v3, v3
	v_mul_f32_e32 v7, v5, v5
	v_add_f32_e32 v0, v0, v14
	v_add_f32_e32 v10, v10, v11
	v_fmac_f32_e32 v6, v2, v2
	v_fmac_f32_e32 v7, v4, v4
	v_add_f32_e32 v0, v0, v10
	v_add_f32_e32 v6, v6, v7
	v_add_f32_e32 v0, v0, v6
	v_cvt_pk_bf16_f32 v2, v2, v3
	v_cvt_pk_bf16_f32 v3, v4, v5
	global_store_dwordx2 v[16:17], v[2:3], off offset:1536 sc0 sc1
	ds_bpermute_b32 v2, v58, v0
	s_waitcnt lgkmcnt(0)
	v_add_f32_e32 v0, v0, v2
	ds_bpermute_b32 v2, v59, v0
	s_waitcnt lgkmcnt(0)
	v_add_f32_e32 v0, v0, v2
	ds_bpermute_b32 v2, v60, v0
	s_waitcnt lgkmcnt(0)
	v_add_f32_e32 v0, v0, v2
	ds_bpermute_b32 v2, v61, v0
	s_waitcnt lgkmcnt(0)
	v_add_f32_e32 v0, v0, v2
	ds_bpermute_b32 v2, v62, v0
	s_waitcnt lgkmcnt(0)
	v_add_f32_e32 v0, v0, v2
	ds_bpermute_b32 v2, v63, v0
	s_and_saveexec_b64 s[16:17], vcc
	s_cbranch_execz .LBB0_823
	s_waitcnt lgkmcnt(0)
	v_add_f32_e32 v0, v0, v2
	v_fma_f32 v0, v0, s40, 0.5
	v_trunc_f32_e32 v0, v0
	v_mul_f32_e32 v2, 0x2f800000, v0
	v_floor_f32_e32 v3, v2
	v_fmac_f32_e32 v0, 0xcf800000, v3
	v_cvt_u32_f32_e32 v2, v0
	v_cvt_u32_f32_e32 v3, v3
	s_lshl_b64 s[14:15], s[14:15], 3
	s_add_u32 s14, s29, s14
	s_addc_u32 s15, s36, s15
	global_store_dwordx2 v1, v[2:3], s[14:15] sc0 sc1
	s_branch .LBB0_823

.LBB0_872:
	v_lshlrev_b64 v[226:227], 11, v[212:213]
	v_pk_mul_f32 v[122:123], v[122:123], v[190:191]
	v_cndmask_b32_e64 v0, 0, 1, s[56:57]
	v_lshl_add_u64 v[190:191], s[14:15], 0, v[226:227]
	v_pk_mul_f32 v[128:129], v[128:129], v[222:223]
	v_pk_mul_f32 v[126:127], v[126:127], v[220:221]
	v_pk_mul_f32 v[124:125], v[124:125], v[192:193]
	v_cmp_ne_u32_e64 s[40:41], 1, v0
	s_andn2_b64 vcc, exec, s[56:57]
	v_lshl_add_u64 v[190:191], v[210:211], 1, v[190:191]
	s_cbranch_vccnz .LBB0_874
	v_cvt_pk_bf16_f32 v220, v126, v127
	v_cvt_pk_bf16_f32 v221, v128, v129
	v_cvt_pk_bf16_f32 v222, v122, v123
	v_cvt_pk_bf16_f32 v223, v124, v125
	global_store_dwordx4 v[190:191], v[220:223], off sc0 sc1

.LBB0_876:
	v_pk_mul_f32 v[96:97], v[96:97], v[220:221]
	v_pk_mul_f32 v[94:95], v[94:95], v[192:193]
	v_pk_mul_f32 v[92:93], v[92:93], v[188:189]
	s_and_b64 vcc, exec, s[40:41]
	v_pk_mul_f32 v[90:91], v[90:91], v[186:187]
	s_cbranch_vccnz .LBB0_878
	v_cvt_pk_bf16_f32 v186, v94, v95
	v_cvt_pk_bf16_f32 v187, v96, v97
	v_cvt_pk_bf16_f32 v188, v90, v91
	v_cvt_pk_bf16_f32 v189, v92, v93
	global_store_dwordx4 v[190:191], v[186:189], off offset:256 sc0 sc1

.LBB0_880:
	v_lshlrev_b64 v[190:191], 11, v[218:219]
	v_pk_mul_f32 v[114:115], v[114:115], v[182:183]
	v_lshl_add_u64 v[182:183], s[14:15], 0, v[190:191]
	v_pk_mul_f32 v[120:121], v[120:121], v[188:189]
	v_pk_mul_f32 v[118:119], v[118:119], v[186:187]
	v_pk_mul_f32 v[116:117], v[116:117], v[184:185]
	s_and_b64 vcc, exec, s[40:41]
	v_lshl_add_u64 v[182:183], v[210:211], 1, v[182:183]
	s_cbranch_vccnz .LBB0_882
	v_cvt_pk_bf16_f32 v184, v118, v119
	v_cvt_pk_bf16_f32 v185, v120, v121
	v_cvt_pk_bf16_f32 v186, v114, v115
	v_cvt_pk_bf16_f32 v187, v116, v117
	global_store_dwordx4 v[182:183], v[184:187], off sc0 sc1

.LBB0_884:
	v_pk_mul_f32 v[88:89], v[88:89], v[186:187]
	v_pk_mul_f32 v[86:87], v[86:87], v[184:185]
	v_pk_mul_f32 v[84:85], v[84:85], v[180:181]
	s_and_b64 vcc, exec, s[40:41]
	v_pk_mul_f32 v[82:83], v[82:83], v[178:179]
	s_cbranch_vccnz .LBB0_886
	v_cvt_pk_bf16_f32 v178, v86, v87
	v_cvt_pk_bf16_f32 v179, v88, v89
	v_cvt_pk_bf16_f32 v180, v82, v83
	v_cvt_pk_bf16_f32 v181, v84, v85
	global_store_dwordx4 v[182:183], v[178:181], off offset:256 sc0 sc1

.LBB0_888:
	v_lshlrev_b64 v[182:183], 11, v[216:217]
	v_pk_mul_f32 v[106:107], v[106:107], v[174:175]
	v_lshl_add_u64 v[174:175], s[14:15], 0, v[182:183]
	v_pk_mul_f32 v[112:113], v[112:113], v[180:181]
	v_pk_mul_f32 v[110:111], v[110:111], v[178:179]
	v_pk_mul_f32 v[108:109], v[108:109], v[176:177]
	s_and_b64 vcc, exec, s[40:41]
	v_lshl_add_u64 v[174:175], v[210:211], 1, v[174:175]
	s_cbranch_vccnz .LBB0_890
	v_cvt_pk_bf16_f32 v176, v110, v111
	v_cvt_pk_bf16_f32 v177, v112, v113
	v_cvt_pk_bf16_f32 v178, v106, v107
	v_cvt_pk_bf16_f32 v179, v108, v109
	global_store_dwordx4 v[174:175], v[176:179], off sc0 sc1

.LBB0_892:
	v_pk_mul_f32 v[80:81], v[80:81], v[178:179]
	v_pk_mul_f32 v[78:79], v[78:79], v[176:177]
	v_pk_mul_f32 v[76:77], v[76:77], v[172:173]
	s_and_b64 vcc, exec, s[40:41]
	v_pk_mul_f32 v[74:75], v[74:75], v[170:171]
	s_cbranch_vccnz .LBB0_894
	v_cvt_pk_bf16_f32 v170, v78, v79
	v_cvt_pk_bf16_f32 v171, v80, v81
	v_cvt_pk_bf16_f32 v172, v74, v75
	v_cvt_pk_bf16_f32 v173, v76, v77
	global_store_dwordx4 v[174:175], v[170:173], off offset:256 sc0 sc1

.LBB0_896:
	v_lshlrev_b64 v[174:175], 11, v[214:215]
	v_pk_mul_f32 v[98:99], v[98:99], v[166:167]
	v_lshl_add_u64 v[166:167], s[14:15], 0, v[174:175]
	v_pk_mul_f32 v[104:105], v[104:105], v[172:173]
	v_pk_mul_f32 v[102:103], v[102:103], v[170:171]
	v_pk_mul_f32 v[100:101], v[100:101], v[168:169]
	s_and_b64 vcc, exec, s[40:41]
	v_lshl_add_u64 v[166:167], v[210:211], 1, v[166:167]
	s_cbranch_vccnz .LBB0_898
	v_cvt_pk_bf16_f32 v168, v102, v103
	v_cvt_pk_bf16_f32 v169, v104, v105
	v_cvt_pk_bf16_f32 v170, v98, v99
	v_cvt_pk_bf16_f32 v171, v100, v101
	global_store_dwordx4 v[166:167], v[168:171], off sc0 sc1

.LBB0_900:
	v_pk_mul_f32 v[72:73], v[72:73], v[170:171]
	v_pk_mul_f32 v[70:71], v[70:71], v[168:169]
	v_pk_mul_f32 v[68:69], v[68:69], v[164:165]
	s_and_b64 vcc, exec, s[40:41]
	v_pk_mul_f32 v[66:67], v[66:67], v[162:163]
	s_cbranch_vccnz .LBB0_902
	v_cvt_pk_bf16_f32 v162, v70, v71
	v_cvt_pk_bf16_f32 v163, v72, v73
	v_cvt_pk_bf16_f32 v164, v66, v67
	v_cvt_pk_bf16_f32 v165, v68, v69
	global_store_dwordx4 v[166:167], v[162:165], off offset:256 sc0 sc1

.LBB0_920:
	v_lshlrev_b64 v[158:159], 11, v[218:219]
	v_lshl_add_u64 v[158:159], s[14:15], 0, v[158:159]
	v_pk_mul_f32 v[64:65], v[64:65], v[222:223]
	v_pk_mul_f32 v[62:63], v[62:63], v[220:221]
	v_pk_mul_f32 v[60:61], v[60:61], v[192:193]
	v_pk_mul_f32 v[58:59], v[58:59], v[190:191]
	s_and_b64 vcc, exec, s[40:41]
	v_lshl_add_u64 v[158:159], v[210:211], 1, v[158:159]
	s_cbranch_vccnz .LBB0_922
	v_cvt_pk_bf16_f32 v190, v62, v63
	v_cvt_pk_bf16_f32 v191, v64, v65
	v_cvt_pk_bf16_f32 v192, v58, v59
	v_cvt_pk_bf16_f32 v193, v60, v61
	global_store_dwordx4 v[158:159], v[190:193], off sc0 sc1

.LBB0_924:
	v_pk_mul_f32 v[32:33], v[32:33], v[190:191]
	v_pk_mul_f32 v[30:31], v[30:31], v[160:161]
	v_pk_mul_f32 v[28:29], v[28:29], v[188:189]
	s_and_b64 vcc, exec, s[40:41]
	v_pk_mul_f32 v[26:27], v[26:27], v[186:187]
	s_cbranch_vccnz .LBB0_926
	v_cvt_pk_bf16_f32 v154, v30, v31
	v_cvt_pk_bf16_f32 v155, v32, v33
	v_cvt_pk_bf16_f32 v156, v26, v27
	v_cvt_pk_bf16_f32 v157, v28, v29
	global_store_dwordx4 v[158:159], v[154:157], off offset:256 sc0 sc1

.LBB0_928:
	v_lshlrev_b64 v[150:151], 11, v[216:217]
	v_lshl_add_u64 v[150:151], s[14:15], 0, v[150:151]
	v_pk_mul_f32 v[56:57], v[56:57], v[158:159]
	v_pk_mul_f32 v[54:55], v[54:55], v[154:155]
	v_pk_mul_f32 v[52:53], v[52:53], v[160:161]
	v_pk_mul_f32 v[50:51], v[50:51], v[156:157]
	s_and_b64 vcc, exec, s[40:41]
	v_lshl_add_u64 v[150:151], v[210:211], 1, v[150:151]
	s_cbranch_vccnz .LBB0_930
	v_cvt_pk_bf16_f32 v152, v54, v55
	v_cvt_pk_bf16_f32 v153, v56, v57
	v_cvt_pk_bf16_f32 v154, v50, v51
	v_cvt_pk_bf16_f32 v155, v52, v53
	global_store_dwordx4 v[150:151], v[152:155], off sc0 sc1

.LBB0_932:
	v_pk_mul_f32 v[24:25], v[24:25], v[156:157]
	v_pk_mul_f32 v[22:23], v[22:23], v[152:153]
	v_pk_mul_f32 v[20:21], v[20:21], v[158:159]
	s_and_b64 vcc, exec, s[40:41]
	v_pk_mul_f32 v[18:19], v[18:19], v[154:155]
	s_cbranch_vccnz .LBB0_934
	v_cvt_pk_bf16_f32 v146, v22, v23
	v_cvt_pk_bf16_f32 v147, v24, v25
	v_cvt_pk_bf16_f32 v148, v18, v19
	v_cvt_pk_bf16_f32 v149, v20, v21
	global_store_dwordx4 v[150:151], v[146:149], off offset:256 sc0 sc1

.LBB0_936:
	v_lshlrev_b64 v[142:143], 11, v[214:215]
	v_lshl_add_u64 v[142:143], s[14:15], 0, v[142:143]
	v_pk_mul_f32 v[48:49], v[48:49], v[150:151]
	v_pk_mul_f32 v[46:47], v[46:47], v[146:147]
	v_pk_mul_f32 v[44:45], v[44:45], v[152:153]
	v_pk_mul_f32 v[42:43], v[42:43], v[148:149]
	s_and_b64 vcc, exec, s[40:41]
	v_lshl_add_u64 v[142:143], v[210:211], 1, v[142:143]
	s_cbranch_vccnz .LBB0_938
	v_cvt_pk_bf16_f32 v144, v46, v47
	v_cvt_pk_bf16_f32 v145, v48, v49
	v_cvt_pk_bf16_f32 v146, v42, v43
	v_cvt_pk_bf16_f32 v147, v44, v45
	global_store_dwordx4 v[142:143], v[144:147], off sc0 sc1

.LBB0_940:
	v_pk_mul_f32 v[16:17], v[16:17], v[148:149]
	v_pk_mul_f32 v[14:15], v[14:15], v[144:145]
	v_pk_mul_f32 v[12:13], v[12:13], v[150:151]
	s_and_b64 vcc, exec, s[40:41]
	v_pk_mul_f32 v[10:11], v[10:11], v[146:147]
	s_cbranch_vccnz .LBB0_942
	v_cvt_pk_bf16_f32 v138, v14, v15
	v_cvt_pk_bf16_f32 v139, v16, v17
	v_cvt_pk_bf16_f32 v140, v10, v11
	v_cvt_pk_bf16_f32 v141, v12, v13
	global_store_dwordx4 v[142:143], v[138:141], off offset:256 sc0 sc1

.LBB0_944:
	v_lshlrev_b64 v[134:135], 11, v[212:213]
	v_lshl_add_u64 v[134:135], s[14:15], 0, v[134:135]
	v_pk_mul_f32 v[40:41], v[40:41], v[142:143]
	v_pk_mul_f32 v[38:39], v[38:39], v[138:139]
	v_pk_mul_f32 v[36:37], v[36:37], v[144:145]
	v_pk_mul_f32 v[34:35], v[34:35], v[140:141]
	s_and_b64 vcc, exec, s[40:41]
	v_lshl_add_u64 v[134:135], v[210:211], 1, v[134:135]
	s_cbranch_vccnz .LBB0_946
	v_cvt_pk_bf16_f32 v136, v38, v39
	v_cvt_pk_bf16_f32 v137, v40, v41
	v_cvt_pk_bf16_f32 v138, v34, v35
	v_cvt_pk_bf16_f32 v139, v36, v37
	global_store_dwordx4 v[134:135], v[136:139], off sc0 sc1

.LBB0_948:
	v_pk_mul_f32 v[8:9], v[8:9], v[140:141]
	v_pk_mul_f32 v[6:7], v[6:7], v[136:137]
	v_pk_mul_f32 v[4:5], v[4:5], v[142:143]
	s_and_b64 vcc, exec, s[40:41]
	v_pk_mul_f32 v[2:3], v[2:3], v[138:139]
	s_cbranch_vccnz .LBB0_950
	v_cvt_pk_bf16_f32 v130, v6, v7
	v_cvt_pk_bf16_f32 v131, v8, v9
	v_cvt_pk_bf16_f32 v132, v2, v3
	v_cvt_pk_bf16_f32 v133, v4, v5
	global_store_dwordx4 v[134:135], v[130:133], off offset:256 sc0 sc1

.LBB0_1061:
	s_waitcnt vmcnt(0)
	v_ffbh_u32_e32 v159, v157
	v_min_u32_e32 v159, 32, v159
	v_lshlrev_b64 v[156:157], v159, v[156:157]
	v_min_u32_e32 v156, 1, v156
	v_or_b32_e32 v156, v157, v156
	v_cvt_f32_u32_e32 v156, v156
	v_sub_u32_e32 v157, 32, v159
	s_mov_b32 s36, 0x358637bd
	v_mov_b64_e32 v[164:165], s[36:37]
	v_ldexp_f32 v157, v156, v157
	v_ffbh_u32_e32 v156, v155
	v_min_u32_e32 v156, 32, v156
	v_lshlrev_b64 v[154:155], v156, v[154:155]
	v_min_u32_e32 v154, 1, v154
	v_or_b32_e32 v154, v155, v154
	v_cvt_f32_u32_e32 v154, v154
	v_sub_u32_e32 v155, 32, v156
	s_mov_b32 s48, 0x32800000
	s_mov_b32 s29, -1
	v_ldexp_f32 v156, v154, v155
	v_pk_fma_f32 v[154:155], v[156:157], s[48:49], v[164:165] op_sel_hi:[1,0,0]
	v_readlane_b32 s92, v253, 28
	v_mul_f32_e32 v156, 0x4b800000, v155
	v_cmp_gt_f32_e64 s[36:37], s96, v155
	v_cmp_gt_f32_e32 vcc, s96, v154
	v_mbcnt_lo_u32_b32 v0, s29, 0
	v_cndmask_b32_e64 v155, v155, v156, s[36:37]
	v_rsq_f32_e32 v155, v155
	v_mbcnt_hi_u32_b32 v0, s29, v0
	s_lshl_b32 s29, s84, 8
	s_add_i32 s29, s29, s52
	v_mul_f32_e32 v156, 0x45800000, v155
	v_cndmask_b32_e64 v155, v155, v156, s[36:37]
	v_mul_f32_e32 v156, 0x4b800000, v154
	v_cndmask_b32_e32 v154, v154, v156, vcc
	v_rsq_f32_e32 v154, v154
	v_and_or_b32 v158, v0, 15, s29
	v_and_b32_e32 v0, 0x70, v0
	v_ashrrev_i32_e32 v159, 31, v158
	v_mul_f32_e32 v156, 0x45800000, v154
	v_cndmask_b32_e32 v154, v154, v156, vcc
	v_ffbh_u32_e32 v156, v153
	v_min_u32_e32 v156, 32, v156
	v_lshlrev_b64 v[152:153], v156, v[152:153]
	v_min_u32_e32 v152, 1, v152
	v_or_b32_e32 v152, v153, v152
	v_cvt_f32_u32_e32 v152, v152
	v_sub_u32_e32 v153, 32, v156
	s_mov_b32 s89, 0x2e8ba2e9
	s_movk_i32 s90, 0xfea0
	v_ldexp_f32 v153, v152, v153
	v_ffbh_u32_e32 v152, v151
	v_min_u32_e32 v152, 32, v152
	v_lshlrev_b64 v[150:151], v152, v[150:151]
	v_min_u32_e32 v150, 1, v150
	v_or_b32_e32 v150, v151, v150
	v_cvt_f32_u32_e32 v150, v150
	v_sub_u32_e32 v151, 32, v152
	v_readlane_b32 s93, v253, 29
	v_ldexp_f32 v152, v150, v151
	v_pk_fma_f32 v[150:151], v[152:153], s[48:49], v[164:165] op_sel_hi:[1,0,0]
	s_nop 0
	v_mul_f32_e32 v152, 0x4b800000, v151
	v_cmp_gt_f32_e64 s[36:37], s96, v151
	v_cmp_gt_f32_e32 vcc, s96, v150
	s_nop 0
	v_cndmask_b32_e64 v151, v151, v152, s[36:37]
	v_rsq_f32_e32 v151, v151
	s_nop 0
	v_mul_f32_e32 v152, 0x45800000, v151
	v_cndmask_b32_e64 v151, v151, v152, s[36:37]
	v_mul_f32_e32 v152, 0x4b800000, v150
	v_cndmask_b32_e32 v150, v150, v152, vcc
	v_rsq_f32_e32 v150, v150
	s_nop 0
	v_mul_f32_e32 v152, 0x45800000, v150
	v_cndmask_b32_e32 v150, v150, v152, vcc
	v_ffbh_u32_e32 v152, v149
	v_min_u32_e32 v152, 32, v152
	v_lshlrev_b64 v[148:149], v152, v[148:149]
	v_min_u32_e32 v148, 1, v148
	v_or_b32_e32 v148, v149, v148
	v_cvt_f32_u32_e32 v148, v148
	v_sub_u32_e32 v149, 32, v152
	v_ldexp_f32 v149, v148, v149
	v_ffbh_u32_e32 v148, v147
	v_min_u32_e32 v148, 32, v148
	v_lshlrev_b64 v[146:147], v148, v[146:147]
	v_min_u32_e32 v146, 1, v146
	v_or_b32_e32 v146, v147, v146
	v_cvt_f32_u32_e32 v146, v146
	v_sub_u32_e32 v147, 32, v148
	v_ldexp_f32 v148, v146, v147
	v_pk_fma_f32 v[146:147], v[148:149], s[48:49], v[164:165] op_sel_hi:[1,0,0]
	s_nop 0
	v_mul_f32_e32 v148, 0x4b800000, v147
	v_cmp_gt_f32_e64 s[36:37], s96, v147
	v_cmp_gt_f32_e32 vcc, s96, v146
	s_nop 0
	v_cndmask_b32_e64 v147, v147, v148, s[36:37]
	v_rsq_f32_e32 v147, v147
	s_nop 0
	v_mul_f32_e32 v148, 0x45800000, v147
	v_cndmask_b32_e64 v149, v147, v148, s[36:37]
	v_mul_f32_e32 v147, 0x4b800000, v146
	v_cndmask_b32_e32 v146, v146, v147, vcc
	v_rsq_f32_e32 v146, v146
	s_nop 0
	v_mul_f32_e32 v147, 0x45800000, v146
	v_cndmask_b32_e32 v148, v146, v147, vcc
	v_ffbh_u32_e32 v146, v145
	v_min_u32_e32 v146, 32, v146
	v_lshlrev_b64 v[144:145], v146, v[144:145]
	v_min_u32_e32 v144, 1, v144
	v_or_b32_e32 v144, v145, v144
	v_cvt_f32_u32_e32 v144, v144
	v_sub_u32_e32 v145, 32, v146
	v_ldexp_f32 v145, v144, v145
	v_ffbh_u32_e32 v144, v143
	v_min_u32_e32 v144, 32, v144
	v_lshlrev_b64 v[142:143], v144, v[142:143]
	v_min_u32_e32 v142, 1, v142
	v_or_b32_e32 v142, v143, v142
	v_cvt_f32_u32_e32 v142, v142
	v_sub_u32_e32 v143, 32, v144
	v_ldexp_f32 v144, v142, v143
	v_pk_fma_f32 v[142:143], v[144:145], s[48:49], v[164:165] op_sel_hi:[1,0,0]
	s_nop 0
	v_mul_f32_e32 v144, 0x4b800000, v143
	v_cmp_gt_f32_e64 s[36:37], s96, v143
	v_cmp_gt_f32_e32 vcc, s96, v142
	s_nop 0
	v_cndmask_b32_e64 v143, v143, v144, s[36:37]
	v_rsq_f32_e32 v143, v143
	s_nop 0
	v_mul_f32_e32 v144, 0x45800000, v143
	v_cndmask_b32_e64 v147, v143, v144, s[36:37]
	s_ashr_i32 s36, s83, 2
	s_ashr_i32 s37, s36, 31
	s_lshl_b64 s[36:37], s[36:37], 25
	s_add_u32 s29, s60, s36
	s_addc_u32 s36, s61, s37
	s_lshl_b32 s37, s83, 9
	s_and_b32 s37, s37, 0x600
	s_add_u32 s29, s29, s37
	s_addc_u32 s37, s36, 0
	s_add_u32 s36, s29, s82
	s_addc_u32 s37, s37, 0
	v_lshl_add_u64 v[144:145], s[36:37], 0, v[0:1]
	v_mul_f32_e32 v0, 0xbfb8aa3b, v155
	v_pk_mul_f32 v[122:123], v[0:1], v[122:123] op_sel_hi:[0,1]
	v_exp_f32_e32 v122, v122
	v_pk_mul_f32 v[124:125], v[0:1], v[124:125] op_sel_hi:[0,1]
	v_pk_mul_f32 v[128:129], v[0:1], v[128:129] op_sel_hi:[0,1]
	v_pk_mul_f32 v[126:127], v[0:1], v[126:127] op_sel_hi:[0,1]
	v_add_f32_e32 v122, 1.0, v122
	v_rcp_f32_e32 v152, v122
	v_exp_f32_e32 v122, v123
	v_exp_f32_e32 v126, v126
	v_exp_f32_e32 v127, v127
	v_exp_f32_e32 v128, v128
	v_add_f32_e32 v122, 1.0, v122
	v_rcp_f32_e32 v153, v122
	v_exp_f32_e32 v122, v124
	v_exp_f32_e32 v129, v129
	v_mul_f32_e32 v143, 0x4b800000, v142
	v_cndmask_b32_e32 v142, v142, v143, vcc
	v_add_f32_e32 v122, 1.0, v122
	v_rcp_f32_e32 v155, v122
	v_exp_f32_e32 v122, v125
	v_rsq_f32_e32 v142, v142
	v_add_f32_e32 v126, 1.0, v126
	v_add_f32_e32 v127, 1.0, v127
	v_add_f32_e32 v128, 1.0, v128
	v_add_f32_e32 v129, 1.0, v129
	v_add_f32_e32 v122, 1.0, v122
	v_pk_mul_f32 v[114:115], v[0:1], v[114:115] op_sel_hi:[0,1]
	v_rcp_f32_e32 v126, v126
	v_rcp_f32_e32 v127, v127
	v_rcp_f32_e32 v128, v128
	v_rcp_f32_e32 v129, v129
	v_rcp_f32_e32 v125, v122
	v_pk_mul_f32 v[120:121], v[0:1], v[120:121] op_sel_hi:[0,1]
	v_pk_mul_f32 v[118:119], v[0:1], v[118:119] op_sel_hi:[0,1]
	v_pk_mul_f32 v[116:117], v[0:1], v[116:117] op_sel_hi:[0,1]
	v_exp_f32_e32 v0, v114
	v_exp_f32_e32 v114, v115
	v_mul_f32_e32 v143, 0x45800000, v142
	v_cndmask_b32_e32 v146, v142, v143, vcc
	v_lshlrev_b64 v[142:143], 11, v[158:159]
	v_lshl_add_u64 v[142:143], v[144:145], 0, v[142:143]
	v_cvt_pk_bf16_f32 v122, v126, v127
	v_cvt_pk_bf16_f32 v123, v128, v129
	v_cvt_pk_bf16_f32 v124, v152, v153
	v_cvt_pk_bf16_f32 v125, v155, v125
	v_add_f32_e32 v114, 1.0, v114
	global_store_dwordx4 v[142:143], v[122:125], off sc0 sc1
	v_add_f32_e32 v0, 1.0, v0
	v_rcp_f32_e32 v0, v0
	v_rcp_f32_e32 v122, v114
	v_exp_f32_e32 v114, v116
	v_exp_f32_e32 v118, v118
	v_exp_f32_e32 v119, v119
	v_exp_f32_e32 v120, v120
	v_add_f32_e32 v114, 1.0, v114
	v_exp_f32_e32 v121, v121
	v_rcp_f32_e32 v123, v114
	v_exp_f32_e32 v114, v117
	v_cvt_pk_bf16_f32 v116, v0, v122
	v_mul_f32_e32 v0, 0xbfb8aa3b, v154
	v_add_f32_e32 v118, 1.0, v118
	v_add_f32_e32 v119, 1.0, v119
	v_add_f32_e32 v120, 1.0, v120
	v_add_f32_e32 v121, 1.0, v121
	v_add_f32_e32 v114, 1.0, v114
	v_pk_mul_f32 v[106:107], v[0:1], v[106:107] op_sel_hi:[0,1]
	v_rcp_f32_e32 v118, v118
	v_rcp_f32_e32 v119, v119
	v_rcp_f32_e32 v120, v120
	v_rcp_f32_e32 v121, v121
	v_rcp_f32_e32 v117, v114
	v_exp_f32_e32 v106, v106
	v_cvt_pk_bf16_f32 v114, v118, v119
	v_cvt_pk_bf16_f32 v115, v120, v121
	v_cvt_pk_bf16_f32 v117, v123, v117
	v_add_f32_e32 v106, 1.0, v106
	global_store_dwordx4 v[142:143], v[114:117], off offset:256 sc0 sc1
	v_pk_mul_f32 v[108:109], v[0:1], v[108:109] op_sel_hi:[0,1]
	v_pk_mul_f32 v[112:113], v[0:1], v[112:113] op_sel_hi:[0,1]
	v_rcp_f32_e32 v116, v106
	v_exp_f32_e32 v106, v107
	v_pk_mul_f32 v[110:111], v[0:1], v[110:111] op_sel_hi:[0,1]
	v_exp_f32_e32 v110, v110
	v_exp_f32_e32 v111, v111
	v_add_f32_e32 v106, 1.0, v106
	v_rcp_f32_e32 v117, v106
	v_exp_f32_e32 v106, v108
	v_exp_f32_e32 v112, v112
	v_exp_f32_e32 v113, v113
	v_add_f32_e32 v110, 1.0, v110
	v_add_f32_e32 v106, 1.0, v106
	v_rcp_f32_e32 v118, v106
	v_exp_f32_e32 v106, v109
	v_add_f32_e32 v111, 1.0, v111
	v_add_f32_e32 v112, 1.0, v112
	v_add_f32_e32 v113, 1.0, v113
	v_add_f32_e32 v106, 1.0, v106
	v_pk_mul_f32 v[98:99], v[0:1], v[98:99] op_sel_hi:[0,1]
	v_rcp_f32_e32 v110, v110
	v_rcp_f32_e32 v111, v111
	v_rcp_f32_e32 v112, v112
	v_rcp_f32_e32 v113, v113
	v_rcp_f32_e32 v109, v106
	v_pk_mul_f32 v[104:105], v[0:1], v[104:105] op_sel_hi:[0,1]
	v_pk_mul_f32 v[102:103], v[0:1], v[102:103] op_sel_hi:[0,1]
	v_pk_mul_f32 v[100:101], v[0:1], v[100:101] op_sel_hi:[0,1]
	v_exp_f32_e32 v0, v98
	v_exp_f32_e32 v98, v99
	v_or_b32_e32 v114, 16, v158
	v_ashrrev_i32_e32 v115, 31, v114
	v_lshlrev_b64 v[114:115], 11, v[114:115]
	v_lshl_add_u64 v[114:115], v[144:145], 0, v[114:115]
	v_cvt_pk_bf16_f32 v106, v110, v111
	v_cvt_pk_bf16_f32 v107, v112, v113
	v_cvt_pk_bf16_f32 v108, v116, v117
	v_cvt_pk_bf16_f32 v109, v118, v109
	v_add_f32_e32 v98, 1.0, v98
	global_store_dwordx4 v[114:115], v[106:109], off sc0 sc1
	v_add_f32_e32 v0, 1.0, v0
	v_rcp_f32_e32 v0, v0
	v_rcp_f32_e32 v106, v98
	v_exp_f32_e32 v98, v100
	v_exp_f32_e32 v102, v102
	v_exp_f32_e32 v103, v103
	v_exp_f32_e32 v104, v104
	v_add_f32_e32 v98, 1.0, v98
	v_exp_f32_e32 v105, v105
	v_rcp_f32_e32 v107, v98
	v_exp_f32_e32 v98, v101
	v_cvt_pk_bf16_f32 v100, v0, v106
	v_mul_f32_e32 v0, 0xbfb8aa3b, v151
	v_add_f32_e32 v102, 1.0, v102
	v_add_f32_e32 v103, 1.0, v103
	v_add_f32_e32 v104, 1.0, v104
	v_add_f32_e32 v105, 1.0, v105
	v_add_f32_e32 v98, 1.0, v98
	v_pk_mul_f32 v[90:91], v[0:1], v[90:91] op_sel_hi:[0,1]
	v_rcp_f32_e32 v102, v102
	v_rcp_f32_e32 v103, v103
	v_rcp_f32_e32 v104, v104
	v_rcp_f32_e32 v105, v105
	v_rcp_f32_e32 v101, v98
	v_exp_f32_e32 v90, v90
	v_cvt_pk_bf16_f32 v98, v102, v103
	v_cvt_pk_bf16_f32 v99, v104, v105
	v_cvt_pk_bf16_f32 v101, v107, v101
	v_add_f32_e32 v90, 1.0, v90
	global_store_dwordx4 v[114:115], v[98:101], off offset:256 sc0 sc1
	v_pk_mul_f32 v[92:93], v[0:1], v[92:93] op_sel_hi:[0,1]
	v_pk_mul_f32 v[96:97], v[0:1], v[96:97] op_sel_hi:[0,1]
	v_rcp_f32_e32 v100, v90
	v_exp_f32_e32 v90, v91
	v_pk_mul_f32 v[94:95], v[0:1], v[94:95] op_sel_hi:[0,1]
	v_exp_f32_e32 v94, v94
	v_exp_f32_e32 v95, v95
	v_add_f32_e32 v90, 1.0, v90
	v_rcp_f32_e32 v101, v90
	v_exp_f32_e32 v90, v92
	v_exp_f32_e32 v96, v96
	v_exp_f32_e32 v97, v97
	v_add_f32_e32 v94, 1.0, v94
	v_add_f32_e32 v90, 1.0, v90
	v_rcp_f32_e32 v102, v90
	v_exp_f32_e32 v90, v93
	v_add_f32_e32 v95, 1.0, v95
	v_add_f32_e32 v96, 1.0, v96
	v_add_f32_e32 v97, 1.0, v97
	v_add_f32_e32 v90, 1.0, v90
	v_pk_mul_f32 v[82:83], v[0:1], v[82:83] op_sel_hi:[0,1]
	v_rcp_f32_e32 v94, v94
	v_rcp_f32_e32 v95, v95
	v_rcp_f32_e32 v96, v96
	v_rcp_f32_e32 v97, v97
	v_rcp_f32_e32 v93, v90
	v_pk_mul_f32 v[88:89], v[0:1], v[88:89] op_sel_hi:[0,1]
	v_pk_mul_f32 v[86:87], v[0:1], v[86:87] op_sel_hi:[0,1]
	v_pk_mul_f32 v[84:85], v[0:1], v[84:85] op_sel_hi:[0,1]
	v_exp_f32_e32 v0, v82
	v_exp_f32_e32 v82, v83
	v_or_b32_e32 v98, 32, v158
	v_ashrrev_i32_e32 v99, 31, v98
	v_lshlrev_b64 v[98:99], 11, v[98:99]
	v_lshl_add_u64 v[98:99], v[144:145], 0, v[98:99]
	v_cvt_pk_bf16_f32 v90, v94, v95
	v_cvt_pk_bf16_f32 v91, v96, v97
	v_cvt_pk_bf16_f32 v92, v100, v101
	v_cvt_pk_bf16_f32 v93, v102, v93
	v_add_f32_e32 v82, 1.0, v82
	global_store_dwordx4 v[98:99], v[90:93], off sc0 sc1
	v_add_f32_e32 v0, 1.0, v0
	v_rcp_f32_e32 v0, v0
	v_rcp_f32_e32 v90, v82
	v_exp_f32_e32 v82, v84
	v_exp_f32_e32 v86, v86
	v_exp_f32_e32 v87, v87
	v_exp_f32_e32 v88, v88
	v_add_f32_e32 v82, 1.0, v82
	v_exp_f32_e32 v89, v89
	v_rcp_f32_e32 v91, v82
	v_exp_f32_e32 v82, v85
	v_cvt_pk_bf16_f32 v84, v0, v90
	v_mul_f32_e32 v0, 0xbfb8aa3b, v150
	v_add_f32_e32 v86, 1.0, v86
	v_add_f32_e32 v87, 1.0, v87
	v_add_f32_e32 v88, 1.0, v88
	v_add_f32_e32 v89, 1.0, v89
	v_add_f32_e32 v82, 1.0, v82
	v_pk_mul_f32 v[74:75], v[0:1], v[74:75] op_sel_hi:[0,1]
	v_rcp_f32_e32 v86, v86
	v_rcp_f32_e32 v87, v87
	v_rcp_f32_e32 v88, v88
	v_rcp_f32_e32 v89, v89
	v_rcp_f32_e32 v85, v82
	v_exp_f32_e32 v74, v74
	v_cvt_pk_bf16_f32 v82, v86, v87
	v_cvt_pk_bf16_f32 v83, v88, v89
	v_cvt_pk_bf16_f32 v85, v91, v85
	v_add_f32_e32 v74, 1.0, v74
	global_store_dwordx4 v[98:99], v[82:85], off offset:256 sc0 sc1
	v_pk_mul_f32 v[76:77], v[0:1], v[76:77] op_sel_hi:[0,1]
	v_pk_mul_f32 v[80:81], v[0:1], v[80:81] op_sel_hi:[0,1]
	v_rcp_f32_e32 v84, v74
	v_exp_f32_e32 v74, v75
	v_pk_mul_f32 v[78:79], v[0:1], v[78:79] op_sel_hi:[0,1]
	v_exp_f32_e32 v78, v78
	v_exp_f32_e32 v79, v79
	v_add_f32_e32 v74, 1.0, v74
	v_rcp_f32_e32 v85, v74
	v_exp_f32_e32 v74, v76
	v_exp_f32_e32 v80, v80
	v_exp_f32_e32 v81, v81
	v_add_f32_e32 v78, 1.0, v78
	v_add_f32_e32 v74, 1.0, v74
	v_rcp_f32_e32 v86, v74
	v_exp_f32_e32 v74, v77
	v_add_f32_e32 v79, 1.0, v79
	v_add_f32_e32 v80, 1.0, v80
	v_add_f32_e32 v81, 1.0, v81
	v_add_f32_e32 v74, 1.0, v74
	v_pk_mul_f32 v[66:67], v[0:1], v[66:67] op_sel_hi:[0,1]
	v_rcp_f32_e32 v78, v78
	v_rcp_f32_e32 v79, v79
	v_rcp_f32_e32 v80, v80
	v_rcp_f32_e32 v81, v81
	v_rcp_f32_e32 v77, v74
	v_pk_mul_f32 v[72:73], v[0:1], v[72:73] op_sel_hi:[0,1]
	v_pk_mul_f32 v[70:71], v[0:1], v[70:71] op_sel_hi:[0,1]
	v_pk_mul_f32 v[68:69], v[0:1], v[68:69] op_sel_hi:[0,1]
	v_exp_f32_e32 v0, v66
	v_exp_f32_e32 v66, v67
	v_or_b32_e32 v82, 48, v158
	v_ashrrev_i32_e32 v83, 31, v82
	v_lshlrev_b64 v[82:83], 11, v[82:83]
	v_lshl_add_u64 v[82:83], v[144:145], 0, v[82:83]
	v_cvt_pk_bf16_f32 v74, v78, v79
	v_cvt_pk_bf16_f32 v75, v80, v81
	v_cvt_pk_bf16_f32 v76, v84, v85
	v_cvt_pk_bf16_f32 v77, v86, v77
	v_add_f32_e32 v66, 1.0, v66
	global_store_dwordx4 v[82:83], v[74:77], off sc0 sc1
	v_add_f32_e32 v0, 1.0, v0
	v_rcp_f32_e32 v0, v0
	v_rcp_f32_e32 v74, v66
	v_exp_f32_e32 v66, v68
	v_exp_f32_e32 v70, v70
	v_exp_f32_e32 v71, v71
	v_exp_f32_e32 v72, v72
	v_add_f32_e32 v66, 1.0, v66
	v_exp_f32_e32 v73, v73
	v_rcp_f32_e32 v75, v66
	v_exp_f32_e32 v66, v69
	v_cvt_pk_bf16_f32 v68, v0, v74
	v_mul_f32_e32 v0, 0xbfb8aa3b, v149
	v_add_f32_e32 v70, 1.0, v70
	v_add_f32_e32 v71, 1.0, v71
	v_add_f32_e32 v72, 1.0, v72
	v_add_f32_e32 v73, 1.0, v73
	v_add_f32_e32 v66, 1.0, v66
	v_pk_mul_f32 v[58:59], v[0:1], v[58:59] op_sel_hi:[0,1]
	v_rcp_f32_e32 v70, v70
	v_rcp_f32_e32 v71, v71
	v_rcp_f32_e32 v72, v72
	v_rcp_f32_e32 v73, v73
	v_rcp_f32_e32 v69, v66
	v_exp_f32_e32 v58, v58
	v_cvt_pk_bf16_f32 v66, v70, v71
	v_cvt_pk_bf16_f32 v67, v72, v73
	v_cvt_pk_bf16_f32 v69, v75, v69
	v_add_f32_e32 v58, 1.0, v58
	global_store_dwordx4 v[82:83], v[66:69], off offset:256 sc0 sc1
	v_pk_mul_f32 v[60:61], v[0:1], v[60:61] op_sel_hi:[0,1]
	v_pk_mul_f32 v[62:63], v[0:1], v[62:63] op_sel_hi:[0,1]
	v_rcp_f32_e32 v68, v58
	v_exp_f32_e32 v58, v59
	v_pk_mul_f32 v[64:65], v[0:1], v[64:65] op_sel_hi:[0,1]
	v_exp_f32_e32 v62, v62
	v_exp_f32_e32 v63, v63
	v_add_f32_e32 v58, 1.0, v58
	v_rcp_f32_e32 v69, v58
	v_exp_f32_e32 v58, v60
	v_exp_f32_e32 v64, v64
	v_exp_f32_e32 v65, v65
	v_add_f32_e32 v62, 1.0, v62
	v_add_f32_e32 v58, 1.0, v58
	v_rcp_f32_e32 v70, v58
	v_exp_f32_e32 v58, v61
	v_add_f32_e32 v63, 1.0, v63
	v_rcp_f32_e32 v62, v62
	v_rcp_f32_e32 v63, v63
	v_add_f32_e32 v64, 1.0, v64
	v_add_f32_e32 v65, 1.0, v65
	v_add_f32_e32 v58, 1.0, v58
	v_pk_mul_f32 v[50:51], v[0:1], v[50:51] op_sel_hi:[0,1]
	v_rcp_f32_e32 v64, v64
	v_rcp_f32_e32 v65, v65
	v_rcp_f32_e32 v61, v58
	v_pk_mul_f32 v[56:57], v[0:1], v[56:57] op_sel_hi:[0,1]
	v_pk_mul_f32 v[54:55], v[0:1], v[54:55] op_sel_hi:[0,1]
	v_pk_mul_f32 v[52:53], v[0:1], v[52:53] op_sel_hi:[0,1]
	v_exp_f32_e32 v0, v50
	v_exp_f32_e32 v50, v51
	s_mov_b32 s29, 0x40000
	v_cvt_pk_bf16_f32 v58, v62, v63
	v_add_co_u32_e32 v62, vcc, s29, v142
	v_cvt_pk_bf16_f32 v59, v64, v65
	v_cvt_pk_bf16_f32 v60, v68, v69
	v_cvt_pk_bf16_f32 v61, v70, v61
	v_addc_co_u32_e32 v63, vcc, 0, v143, vcc
	v_add_f32_e32 v50, 1.0, v50
	global_store_dwordx4 v[62:63], v[58:61], off sc0 sc1
	v_add_f32_e32 v0, 1.0, v0
	v_rcp_f32_e32 v0, v0
	v_rcp_f32_e32 v58, v50
	v_exp_f32_e32 v50, v52
	v_exp_f32_e32 v54, v54
	v_exp_f32_e32 v55, v55
	v_exp_f32_e32 v56, v56
	v_add_f32_e32 v50, 1.0, v50
	v_exp_f32_e32 v57, v57
	v_rcp_f32_e32 v59, v50
	v_exp_f32_e32 v50, v53
	v_cvt_pk_bf16_f32 v52, v0, v58
	v_mul_f32_e32 v0, 0xbfb8aa3b, v148
	v_add_f32_e32 v54, 1.0, v54
	v_add_f32_e32 v55, 1.0, v55
	v_add_f32_e32 v56, 1.0, v56
	v_add_f32_e32 v57, 1.0, v57
	v_add_f32_e32 v50, 1.0, v50
	v_pk_mul_f32 v[42:43], v[0:1], v[42:43] op_sel_hi:[0,1]
	v_rcp_f32_e32 v54, v54
	v_rcp_f32_e32 v55, v55
	v_rcp_f32_e32 v56, v56
	v_rcp_f32_e32 v57, v57
	v_rcp_f32_e32 v53, v50
	v_exp_f32_e32 v42, v42
	v_lshl_add_u64 v[66:67], v[142:143], 0, s[20:21]
	v_cvt_pk_bf16_f32 v50, v54, v55
	v_cvt_pk_bf16_f32 v51, v56, v57
	v_cvt_pk_bf16_f32 v53, v59, v53
	v_add_f32_e32 v42, 1.0, v42
	global_store_dwordx4 v[66:67], v[50:53], off offset:256 sc0 sc1
	v_pk_mul_f32 v[44:45], v[0:1], v[44:45] op_sel_hi:[0,1]
	v_pk_mul_f32 v[46:47], v[0:1], v[46:47] op_sel_hi:[0,1]
	v_rcp_f32_e32 v52, v42
	v_exp_f32_e32 v42, v43
	v_pk_mul_f32 v[48:49], v[0:1], v[48:49] op_sel_hi:[0,1]
	v_exp_f32_e32 v46, v46
	v_exp_f32_e32 v47, v47
	v_add_f32_e32 v42, 1.0, v42
	v_rcp_f32_e32 v53, v42
	v_exp_f32_e32 v42, v44
	v_exp_f32_e32 v48, v48
	v_exp_f32_e32 v49, v49
	v_add_f32_e32 v46, 1.0, v46
	v_add_f32_e32 v42, 1.0, v42
	v_rcp_f32_e32 v54, v42
	v_exp_f32_e32 v42, v45
	v_add_f32_e32 v47, 1.0, v47
	v_rcp_f32_e32 v46, v46
	v_rcp_f32_e32 v47, v47
	v_add_f32_e32 v48, 1.0, v48
	v_add_f32_e32 v49, 1.0, v49
	v_add_f32_e32 v42, 1.0, v42
	v_pk_mul_f32 v[34:35], v[0:1], v[34:35] op_sel_hi:[0,1]
	v_rcp_f32_e32 v48, v48
	v_rcp_f32_e32 v49, v49
	v_rcp_f32_e32 v45, v42
	v_pk_mul_f32 v[40:41], v[0:1], v[40:41] op_sel_hi:[0,1]
	v_pk_mul_f32 v[38:39], v[0:1], v[38:39] op_sel_hi:[0,1]
	v_pk_mul_f32 v[36:37], v[0:1], v[36:37] op_sel_hi:[0,1]
	v_exp_f32_e32 v0, v34
	v_exp_f32_e32 v34, v35
	s_mov_b32 s29, 0x48000
	v_cvt_pk_bf16_f32 v42, v46, v47
	v_add_co_u32_e32 v46, vcc, s29, v142
	v_cvt_pk_bf16_f32 v43, v48, v49
	v_cvt_pk_bf16_f32 v44, v52, v53
	v_cvt_pk_bf16_f32 v45, v54, v45
	v_addc_co_u32_e32 v47, vcc, 0, v143, vcc
	v_add_f32_e32 v34, 1.0, v34
	global_store_dwordx4 v[46:47], v[42:45], off sc0 sc1
	v_add_f32_e32 v0, 1.0, v0
	v_rcp_f32_e32 v0, v0
	v_rcp_f32_e32 v42, v34
	v_exp_f32_e32 v34, v36
	v_exp_f32_e32 v38, v38
	v_exp_f32_e32 v39, v39
	v_exp_f32_e32 v40, v40
	v_add_f32_e32 v34, 1.0, v34
	v_exp_f32_e32 v41, v41
	v_rcp_f32_e32 v43, v34
	v_exp_f32_e32 v34, v37
	v_cvt_pk_bf16_f32 v36, v0, v42
	v_mul_f32_e32 v0, 0xbfb8aa3b, v147
	v_add_f32_e32 v38, 1.0, v38
	v_add_f32_e32 v39, 1.0, v39
	v_add_f32_e32 v40, 1.0, v40
	v_add_f32_e32 v41, 1.0, v41
	v_add_f32_e32 v34, 1.0, v34
	v_pk_mul_f32 v[26:27], v[0:1], v[26:27] op_sel_hi:[0,1]
	v_rcp_f32_e32 v38, v38
	v_rcp_f32_e32 v39, v39
	v_rcp_f32_e32 v40, v40
	v_rcp_f32_e32 v41, v41
	v_rcp_f32_e32 v37, v34
	v_exp_f32_e32 v26, v26
	s_mov_b64 s[36:37], 0x48000
	v_lshl_add_u64 v[50:51], v[142:143], 0, s[36:37]
	v_cvt_pk_bf16_f32 v34, v38, v39
	v_cvt_pk_bf16_f32 v35, v40, v41
	v_cvt_pk_bf16_f32 v37, v43, v37
	v_add_f32_e32 v26, 1.0, v26
	global_store_dwordx4 v[50:51], v[34:37], off offset:256 sc0 sc1
	v_pk_mul_f32 v[28:29], v[0:1], v[28:29] op_sel_hi:[0,1]
	v_pk_mul_f32 v[30:31], v[0:1], v[30:31] op_sel_hi:[0,1]
	v_rcp_f32_e32 v36, v26
	v_exp_f32_e32 v26, v27
	v_pk_mul_f32 v[32:33], v[0:1], v[32:33] op_sel_hi:[0,1]
	v_exp_f32_e32 v30, v30
	v_exp_f32_e32 v31, v31
	v_add_f32_e32 v26, 1.0, v26
	v_rcp_f32_e32 v37, v26
	v_exp_f32_e32 v26, v28
	v_exp_f32_e32 v32, v32
	v_exp_f32_e32 v33, v33
	v_add_f32_e32 v30, 1.0, v30
	v_add_f32_e32 v26, 1.0, v26
	v_rcp_f32_e32 v38, v26
	v_exp_f32_e32 v26, v29
	v_add_f32_e32 v31, 1.0, v31
	v_rcp_f32_e32 v30, v30
	v_rcp_f32_e32 v31, v31
	v_add_f32_e32 v32, 1.0, v32
	v_add_f32_e32 v33, 1.0, v33
	v_add_f32_e32 v26, 1.0, v26
	v_pk_mul_f32 v[18:19], v[0:1], v[18:19] op_sel_hi:[0,1]
	v_rcp_f32_e32 v32, v32
	v_rcp_f32_e32 v33, v33
	v_rcp_f32_e32 v29, v26
	v_pk_mul_f32 v[24:25], v[0:1], v[24:25] op_sel_hi:[0,1]
	v_pk_mul_f32 v[22:23], v[0:1], v[22:23] op_sel_hi:[0,1]
	v_pk_mul_f32 v[20:21], v[0:1], v[20:21] op_sel_hi:[0,1]
	v_exp_f32_e32 v0, v18
	v_exp_f32_e32 v18, v19
	s_mov_b32 s29, 0x50000
	v_cvt_pk_bf16_f32 v26, v30, v31
	v_add_co_u32_e32 v30, vcc, s29, v142
	v_cvt_pk_bf16_f32 v27, v32, v33
	v_cvt_pk_bf16_f32 v28, v36, v37
	v_cvt_pk_bf16_f32 v29, v38, v29
	v_addc_co_u32_e32 v31, vcc, 0, v143, vcc
	v_add_f32_e32 v18, 1.0, v18
	global_store_dwordx4 v[30:31], v[26:29], off sc0 sc1
	v_add_f32_e32 v0, 1.0, v0
	v_rcp_f32_e32 v0, v0
	v_rcp_f32_e32 v26, v18
	v_exp_f32_e32 v18, v20
	v_exp_f32_e32 v22, v22
	v_exp_f32_e32 v23, v23
	v_exp_f32_e32 v24, v24
	v_add_f32_e32 v18, 1.0, v18
	v_exp_f32_e32 v25, v25
	v_rcp_f32_e32 v27, v18
	v_exp_f32_e32 v18, v21
	v_cvt_pk_bf16_f32 v20, v0, v26
	v_mul_f32_e32 v0, 0xbfb8aa3b, v146
	v_add_f32_e32 v22, 1.0, v22
	v_add_f32_e32 v23, 1.0, v23
	v_add_f32_e32 v24, 1.0, v24
	v_add_f32_e32 v25, 1.0, v25
	v_add_f32_e32 v18, 1.0, v18
	v_pk_mul_f32 v[10:11], v[0:1], v[10:11] op_sel_hi:[0,1]
	v_rcp_f32_e32 v22, v22
	v_rcp_f32_e32 v23, v23
	v_rcp_f32_e32 v24, v24
	v_rcp_f32_e32 v25, v25
	v_rcp_f32_e32 v21, v18
	v_exp_f32_e32 v10, v10
	v_lshl_add_u64 v[34:35], v[142:143], 0, s[22:23]
	v_cvt_pk_bf16_f32 v18, v22, v23
	v_cvt_pk_bf16_f32 v19, v24, v25
	v_cvt_pk_bf16_f32 v21, v27, v21
	v_add_f32_e32 v10, 1.0, v10
	global_store_dwordx4 v[34:35], v[18:21], off offset:256 sc0 sc1
	v_pk_mul_f32 v[12:13], v[0:1], v[12:13] op_sel_hi:[0,1]
	v_pk_mul_f32 v[14:15], v[0:1], v[14:15] op_sel_hi:[0,1]
	v_rcp_f32_e32 v20, v10
	v_exp_f32_e32 v10, v11
	v_pk_mul_f32 v[16:17], v[0:1], v[16:17] op_sel_hi:[0,1]
	v_exp_f32_e32 v14, v14
	v_exp_f32_e32 v15, v15
	v_add_f32_e32 v10, 1.0, v10
	v_rcp_f32_e32 v21, v10
	v_exp_f32_e32 v10, v12
	v_exp_f32_e32 v16, v16
	v_exp_f32_e32 v17, v17
	v_add_f32_e32 v14, 1.0, v14
	v_add_f32_e32 v10, 1.0, v10
	v_rcp_f32_e32 v22, v10
	v_exp_f32_e32 v10, v13
	v_add_f32_e32 v15, 1.0, v15
	v_rcp_f32_e32 v14, v14
	v_rcp_f32_e32 v15, v15
	v_add_f32_e32 v16, 1.0, v16
	v_add_f32_e32 v17, 1.0, v17
	v_add_f32_e32 v10, 1.0, v10
	v_pk_mul_f32 v[2:3], v[0:1], v[2:3] op_sel_hi:[0,1]
	v_rcp_f32_e32 v16, v16
	v_rcp_f32_e32 v17, v17
	v_rcp_f32_e32 v13, v10
	v_pk_mul_f32 v[8:9], v[0:1], v[8:9] op_sel_hi:[0,1]
	v_pk_mul_f32 v[6:7], v[0:1], v[6:7] op_sel_hi:[0,1]
	v_pk_mul_f32 v[4:5], v[0:1], v[4:5] op_sel_hi:[0,1]
	v_exp_f32_e32 v0, v2
	v_exp_f32_e32 v2, v3
	s_mov_b32 s29, 0x58000
	v_cvt_pk_bf16_f32 v10, v14, v15
	v_add_co_u32_e32 v14, vcc, s29, v142
	v_cvt_pk_bf16_f32 v11, v16, v17
	v_cvt_pk_bf16_f32 v12, v20, v21
	v_cvt_pk_bf16_f32 v13, v22, v13
	v_addc_co_u32_e32 v15, vcc, 0, v143, vcc
	v_add_f32_e32 v2, 1.0, v2
	global_store_dwordx4 v[14:15], v[10:13], off sc0 sc1
	v_exp_f32_e32 v6, v6
	v_exp_f32_e32 v7, v7
	v_rcp_f32_e32 v10, v2
	v_exp_f32_e32 v2, v4
	v_exp_f32_e32 v8, v8
	v_exp_f32_e32 v9, v9
	v_add_f32_e32 v6, 1.0, v6
	v_add_f32_e32 v2, 1.0, v2
	v_rcp_f32_e32 v11, v2
	v_exp_f32_e32 v2, v5
	v_add_f32_e32 v7, 1.0, v7
	v_add_f32_e32 v8, 1.0, v8
	v_add_f32_e32 v9, 1.0, v9
	v_add_f32_e32 v0, 1.0, v0
	v_add_f32_e32 v2, 1.0, v2
	v_rcp_f32_e32 v6, v6
	v_rcp_f32_e32 v7, v7
	v_rcp_f32_e32 v8, v8
	v_rcp_f32_e32 v9, v9
	v_rcp_f32_e32 v0, v0
	v_rcp_f32_e32 v5, v2
	s_mov_b64 s[36:37], 0x58000
	v_lshl_add_u64 v[18:19], v[142:143], 0, s[36:37]
	v_cvt_pk_bf16_f32 v2, v6, v7
	v_cvt_pk_bf16_f32 v3, v8, v9
	v_cvt_pk_bf16_f32 v4, v0, v10
	v_cvt_pk_bf16_f32 v5, v11, v5
	s_mov_b64 s[36:37], -1
	s_andn2_b64 vcc, exec, s[46:47]
	global_store_dwordx4 v[18:19], v[2:5], off offset:256 sc0 sc1
	s_cbranch_vccnz .LBB0_1054
	s_nop 0
	v_lshl_add_u32 v2, s38, 8, v160
	v_ashrrev_i32_e32 v3, 31, v2
	v_lshl_add_u64 v[2:3], v[2:3], 3, s[0:1]
	global_load_dwordx2 v[156:157], v[2:3], off nt
	global_load_dwordx2 v[154:155], v[2:3], off offset:128 nt
	global_load_dwordx2 v[152:153], v[2:3], off offset:256 nt
	global_load_dwordx2 v[150:151], v[2:3], off offset:384 nt
	global_load_dwordx2 v[148:149], v[2:3], off offset:1024 nt
	global_load_dwordx2 v[146:147], v[2:3], off offset:1152 nt
	global_load_dwordx2 v[144:145], v[2:3], off offset:1280 nt
	global_load_dwordx2 v[142:143], v[2:3], off offset:1408 nt
	s_andn2_b64 vcc, exec, s[14:15]
	s_cbranch_vccnz .LBB0_1053
	s_barrier
	s_branch .LBB0_1053

.LBB0_1071:
	s_or_b64 exec, exec, s[38:39]
	s_waitcnt lgkmcnt(0)
	ds_read_b128 v[2:5], v203 offset:49280
	ds_read_b128 v[6:9], v203 offset:49312
	s_lshl_b32 s29, s31, 12
	v_lshl_or_b32 v49, v236, 1, s29
	v_add_u32_e32 v49, v49, v242
	s_waitcnt lgkmcnt(1)
	v_rcp_f32_e32 v0, v2
	v_rcp_f32_e32 v10, v3
	v_rcp_f32_e32 v11, v4
	v_rcp_f32_e32 v12, v5
	v_mul_f32_e32 v32, v32, v0
	v_mul_f32_e32 v0, v16, v0
	v_cvt_pk_bf16_f32 v0, v0, s0
	s_waitcnt lgkmcnt(0)
	v_rcp_f32_e32 v13, v6
	ds_read_b128 v[2:5], v203 offset:49344
	v_rcp_f32_e32 v14, v7
	v_rcp_f32_e32 v15, v8
	v_rcp_f32_e32 v48, v9
	ds_read_b128 v[6:9], v203 offset:49376
	ds_write_b16 v49, v0 offset:51264
	v_mul_f32_e32 v0, v33, v10
	v_cvt_pk_bf16_f32 v0, v0, s0
	ds_write_b16 v49, v0 offset:51328
	v_mul_f32_e32 v0, v17, v10
	v_cvt_pk_bf16_f32 v0, v0, s0
	ds_write_b16 v49, v0 offset:51392
	v_mul_f32_e32 v0, v34, v11
	v_cvt_pk_bf16_f32 v0, v0, s0
	ds_write_b16 v49, v0 offset:51456
	v_mul_f32_e32 v0, v18, v11
	v_cvt_pk_bf16_f32 v0, v0, s0
	ds_write_b16 v49, v0 offset:51520
	v_mul_f32_e32 v0, v35, v12
	v_cvt_pk_bf16_f32 v0, v0, s0
	ds_write_b16 v49, v0 offset:51584
	v_mul_f32_e32 v0, v19, v12
	v_cvt_pk_bf16_f32 v0, v0, s0
	ds_write_b16 v49, v0 offset:51648
	v_mul_f32_e32 v0, v36, v13
	v_cvt_pk_bf16_f32 v0, v0, s0
	ds_write_b16 v49, v0 offset:52224
	v_mul_f32_e32 v0, v20, v13
	v_cvt_pk_bf16_f32 v0, v0, s0
	ds_write_b16 v49, v0 offset:52288
	v_mul_f32_e32 v0, v37, v14
	v_cvt_pk_bf16_f32 v0, v0, s0
	ds_write_b16 v49, v0 offset:52352
	v_mul_f32_e32 v0, v21, v14
	v_cvt_pk_bf16_f32 v0, v0, s0
	ds_write_b16 v49, v0 offset:52416
	v_mul_f32_e32 v0, v38, v15
	v_cvt_pk_bf16_f32 v0, v0, s0
	ds_write_b16 v49, v0 offset:52480
	v_mul_f32_e32 v0, v22, v15
	v_cvt_pk_bf16_f32 v0, v0, s0
	s_waitcnt lgkmcnt(13)
	v_rcp_f32_e32 v2, v2
	ds_write_b16 v49, v0 offset:52544
	v_mul_f32_e32 v0, v39, v48
	v_cvt_pk_bf16_f32 v0, v0, s0
	ds_write_b16 v49, v0 offset:52608
	v_mul_f32_e32 v0, v23, v48
	v_cvt_pk_bf16_f32 v0, v0, s0
	v_rcp_f32_e32 v3, v3
	ds_write_b16 v49, v0 offset:52672
	v_mul_f32_e32 v0, v40, v2
	v_cvt_pk_bf16_f32 v0, v0, s0
	ds_write_b16 v49, v0 offset:53248
	v_mul_f32_e32 v0, v24, v2
	v_cvt_pk_bf16_f32 v0, v0, s0
	v_rcp_f32_e32 v4, v4
	ds_write_b16 v49, v0 offset:53312
	v_mul_f32_e32 v0, v41, v3
	v_cvt_pk_bf16_f32 v0, v0, s0
	ds_write_b16 v49, v0 offset:53376
	v_mul_f32_e32 v0, v25, v3
	v_cvt_pk_bf16_f32 v0, v0, s0
	v_rcp_f32_e32 v5, v5
	ds_write_b16 v49, v0 offset:53440
	v_mul_f32_e32 v0, v42, v4
	v_cvt_pk_bf16_f32 v0, v0, s0
	ds_write_b16 v49, v0 offset:53504
	v_mul_f32_e32 v0, v26, v4
	v_cvt_pk_bf16_f32 v0, v0, s0
	s_waitcnt lgkmcnt(14)
	v_rcp_f32_e32 v6, v6
	ds_write_b16 v49, v0 offset:53568
	v_mul_f32_e32 v0, v43, v5
	v_cvt_pk_bf16_f32 v0, v0, s0
	ds_write_b16 v49, v0 offset:53632
	v_mul_f32_e32 v0, v27, v5
	v_cvt_pk_bf16_f32 v0, v0, s0
	v_rcp_f32_e32 v7, v7
	ds_write_b16 v49, v0 offset:53696
	v_mul_f32_e32 v0, v44, v6
	v_cvt_pk_bf16_f32 v0, v0, s0
	ds_write_b16 v49, v0 offset:54272
	v_mul_f32_e32 v0, v28, v6
	v_cvt_pk_bf16_f32 v0, v0, s0
	v_rcp_f32_e32 v8, v8
	ds_write_b16 v49, v0 offset:54336
	v_mul_f32_e32 v0, v45, v7
	v_cvt_pk_bf16_f32 v0, v0, s0
	ds_write_b16 v49, v0 offset:54400
	v_mul_f32_e32 v0, v29, v7
	v_cvt_pk_bf16_f32 v0, v0, s0
	v_rcp_f32_e32 v9, v9
	ds_write_b16 v49, v0 offset:54464
	v_mul_f32_e32 v0, v46, v8
	v_cvt_pk_bf16_f32 v0, v0, s0
	ds_write_b16 v49, v0 offset:54528
	v_mul_f32_e32 v0, v30, v8
	v_cvt_pk_bf16_f32 v0, v0, s0
	ds_write_b16 v49, v0 offset:54592
	v_mul_f32_e32 v0, v47, v9
	v_cvt_pk_bf16_f32 v0, v0, s0
	ds_write_b16 v49, v0 offset:54656
	v_mul_f32_e32 v0, v31, v9
	v_cvt_pk_bf16_f32 v32, v32, s0
	v_cvt_pk_bf16_f32 v0, v0, s0
	ds_write_b16 v49, v32 offset:51200
	ds_write_b16 v49, v0 offset:54720
	v_or_b32_e32 v0, s29, v204
	s_waitcnt lgkmcnt(0)
	v_add_u32_e32 v2, v0, v243
	ds_read_b128 v[2:5], v2 offset:51200
	v_add_u32_e32 v6, v0, v244
	ds_read_b128 v[6:9], v6 offset:51200
	v_mov_b32_e32 v205, v1
	v_lshl_add_u64 v[10:11], s[50:51], 0, v[204:205]
	v_mov_b32_e32 v207, v1
	v_lshl_add_u64 v[12:13], v[10:11], 0, v[206:207]
	v_mov_b32_e32 v209, v1
	s_waitcnt lgkmcnt(1)
	global_store_dwordx4 v[12:13], v[2:5], off sc0 sc1
	v_mov_b32_e32 v211, v1
	v_lshl_add_u64 v[12:13], v[10:11], 0, v[210:211]
	v_lshl_add_u64 v[2:3], v[10:11], 0, v[208:209]
	s_waitcnt lgkmcnt(0)
	global_store_dwordx4 v[2:3], v[6:9], off sc0 sc1
	v_add_u32_e32 v2, v0, v245
	ds_read_b128 v[2:5], v2 offset:51200
	v_add_u32_e32 v0, v0, v246
	ds_read_b128 v[6:9], v0 offset:51200
	v_mov_b32_e32 v213, v1
	s_mov_b64 s[52:53], 0
	s_waitcnt lgkmcnt(1)
	global_store_dwordx4 v[12:13], v[2:5], off sc0 sc1
	s_and_b64 vcc, exec, s[54:55]
	s_nop 0
	v_lshl_add_u64 v[2:3], v[10:11], 0, v[212:213]
	s_waitcnt lgkmcnt(0)
	global_store_dwordx4 v[2:3], v[6:9], off sc0 sc1
	s_waitcnt lgkmcnt(0)
	s_barrier
	s_cbranch_vccnz .LBB0_1069

.LBB0_1171:
	s_add_i32 s35, s31, s34
	s_add_u32 s29, s14, s35
	s_addc_u32 s38, s15, 0
	v_mov_b32_e32 v35, s38
	v_or_b32_e32 v34, s29, v116
	v_lshlrev_b64 v[34:35], 10, v[34:35]
	v_lshl_add_u64 v[42:43], v[140:141], 0, v[34:35]
	global_load_dwordx4 v[34:37], v[42:43], off
	v_add_co_u32_e32 v44, vcc, s10, v42
	v_add_u32_e32 v167, s34, v119
	s_nop 0
	v_addc_co_u32_e32 v45, vcc, 0, v43, vcc
	global_load_dwordx4 v[38:41], v[44:45], off
	global_load_dwordx4 v[168:171], v[42:43], off offset:32
	global_load_dwordx4 v[172:175], v[44:45], off offset:32
	global_load_dwordx4 v[176:179], v[42:43], off offset:64
	global_load_dwordx4 v[180:183], v[44:45], off offset:64
	global_load_dwordx4 v[184:187], v[42:43], off offset:96
	global_load_dwordx4 v[188:191], v[44:45], off offset:96
	v_mov_b32_e32 v43, s38
	v_or_b32_e32 v42, s29, v118
	v_lshlrev_b64 v[42:43], 10, v[42:43]
	v_lshl_add_u64 v[42:43], v[142:143], 0, v[42:43]
	global_load_dwordx4 v[82:85], v[42:43], off
	v_mov_b32_e32 v43, s38
	v_or_b32_e32 v42, s29, v124
	v_lshlrev_b64 v[42:43], 10, v[42:43]
	v_lshl_add_u64 v[42:43], v[142:143], 0, v[42:43]
	global_load_dwordx4 v[86:89], v[42:43], off
	v_mov_b32_e32 v43, s38
	v_or_b32_e32 v42, s29, v126
	v_lshlrev_b64 v[42:43], 10, v[42:43]
	v_lshl_add_u64 v[42:43], v[142:143], 0, v[42:43]
	global_load_dwordx4 v[90:93], v[42:43], off
	v_mov_b32_e32 v43, s38
	v_or_b32_e32 v42, s29, v128
	v_lshlrev_b64 v[42:43], 10, v[42:43]
	v_lshl_add_u64 v[42:43], v[142:143], 0, v[42:43]
	global_load_dwordx4 v[94:97], v[42:43], off
	v_mov_b32_e32 v43, s38
	v_or_b32_e32 v42, s29, v130
	v_lshlrev_b64 v[42:43], 10, v[42:43]
	v_lshl_add_u64 v[42:43], v[142:143], 0, v[42:43]
	global_load_dwordx4 v[98:101], v[42:43], off
	v_mov_b32_e32 v43, s38
	v_or_b32_e32 v42, s29, v132
	v_lshlrev_b64 v[42:43], 10, v[42:43]
	v_lshl_add_u64 v[42:43], v[142:143], 0, v[42:43]
	global_load_dwordx4 v[102:105], v[42:43], off
	v_mov_b32_e32 v43, s38
	v_or_b32_e32 v42, s29, v134
	v_lshlrev_b64 v[42:43], 10, v[42:43]
	v_lshl_add_u64 v[42:43], v[142:143], 0, v[42:43]
	global_load_dwordx4 v[106:109], v[42:43], off
	v_mov_b32_e32 v43, s38
	s_cmp_eq_u32 s34, 0
	v_cmp_lt_u32_e64 s[38:39], v167, v125
	s_cselect_b64 vcc, -1, 0
	v_or_b32_e32 v42, s29, v136
	v_lshlrev_b64 v[42:43], 10, v[42:43]
	v_lshl_add_u64 v[42:43], v[142:143], 0, v[42:43]
	global_load_dwordx4 v[110:113], v[42:43], off
	s_mov_b32 s29, 0xd7d1fdd
	s_waitcnt vmcnt(15)
	v_mfma_f32_32x32x16_bf16 v[50:65], v[34:37], v[66:69], 0
	s_waitcnt vmcnt(7)
	ds_write_b128 v115, v[82:85]
	s_waitcnt vmcnt(6)
	ds_write_b128 v115, v[86:89] offset:1536
	s_waitcnt vmcnt(5)
	ds_write_b128 v115, v[90:93] offset:3072
	s_waitcnt vmcnt(4)
	ds_write_b128 v115, v[94:97] offset:4608
	s_waitcnt vmcnt(3)
	ds_write_b128 v115, v[98:101] offset:6144
	s_waitcnt vmcnt(2)
	ds_write_b128 v115, v[102:105] offset:7680
	s_waitcnt vmcnt(1)
	ds_write_b128 v115, v[106:109] offset:9216
	s_waitcnt vmcnt(0)
	ds_write_b128 v115, v[110:113] offset:10752
	v_mfma_f32_32x32x16_bf16 v[50:65], v[168:171], v[70:73], v[50:65]
	v_mfma_f32_32x32x16_bf16 v[50:65], v[176:179], v[74:77], v[50:65]
	v_mfma_f32_32x32x16_bf16 v[50:65], v[184:187], v[78:81], v[50:65]
	v_mfma_f32_32x32x16_bf16 v[34:49], v[38:41], v[66:69], 0
	s_nop 10
	v_max_f32_e32 v50, v50, v50
	v_min_f32_e32 v50, 0x42fc0000, v50
	v_exp_f32_e32 v50, v50
	s_nop 0
	v_add_f32_e32 v50, 1.0, v50
	v_rcp_f32_e32 v50, v50
	v_mfma_f32_32x32x16_bf16 v[34:49], v[172:175], v[70:73], v[34:49]
	v_cndmask_b32_e64 v168, 1.0, v50, s[38:39]
	v_cndmask_b32_e32 v168, v50, v168, vcc
	v_max_f32_e32 v50, v51, v51
	v_min_f32_e32 v50, 0x42fc0000, v50
	v_exp_f32_e32 v50, v50
	v_add_u32_e32 v51, 1, v167
	v_cmp_lt_u32_e64 s[38:39], v51, v125
	v_mfma_f32_32x32x16_bf16 v[34:49], v[180:183], v[74:77], v[34:49]
	v_add_f32_e32 v50, 1.0, v50
	v_rcp_f32_e32 v50, v50
	s_nop 0
	v_cndmask_b32_e64 v51, 1.0, v50, s[38:39]
	v_cndmask_b32_e32 v169, v50, v51, vcc
	v_max_f32_e32 v50, v52, v52
	v_min_f32_e32 v50, 0x42fc0000, v50
	v_exp_f32_e32 v50, v50
	v_add_u32_e32 v51, 2, v167
	v_cmp_lt_u32_e64 s[38:39], v51, v125
	v_mfma_f32_32x32x16_bf16 v[34:49], v[188:191], v[78:81], v[34:49]
	v_add_f32_e32 v50, 1.0, v50
	v_rcp_f32_e32 v50, v50
	s_nop 0
	v_cndmask_b32_e64 v51, 1.0, v50, s[38:39]
	v_cndmask_b32_e32 v52, v50, v51, vcc
	v_max_f32_e32 v50, v53, v53
	v_min_f32_e32 v50, 0x42fc0000, v50
	v_exp_f32_e32 v50, v50
	v_add_u32_e32 v51, 3, v167
	v_cmp_lt_u32_e64 s[38:39], v51, v125
	s_nop 1
	v_max_f32_e32 v34, v34, v34
	v_add_f32_e32 v50, 1.0, v50
	v_rcp_f32_e32 v50, v50
	v_min_f32_e32 v34, 0x42fc0000, v34
	v_max_f32_e32 v35, v35, v35
	v_exp_f32_e32 v34, v34
	v_cndmask_b32_e64 v51, 1.0, v50, s[38:39]
	v_cndmask_b32_e32 v53, v50, v51, vcc
	v_max_f32_e32 v50, v54, v54
	v_min_f32_e32 v50, 0x42fc0000, v50
	v_exp_f32_e32 v50, v50
	v_cmp_lt_i32_e64 s[38:39], v167, v127
	v_min_f32_e32 v35, 0x42fc0000, v35
	v_max_f32_e32 v36, v36, v36
	v_add_f32_e32 v50, 1.0, v50
	v_rcp_f32_e32 v50, v50
	v_exp_f32_e32 v35, v35
	v_min_f32_e32 v36, 0x42fc0000, v36
	v_max_f32_e32 v37, v37, v37
	v_cndmask_b32_e64 v51, 1.0, v50, s[38:39]
	v_cndmask_b32_e32 v54, v50, v51, vcc
	v_max_f32_e32 v50, v55, v55
	v_min_f32_e32 v50, 0x42fc0000, v50
	v_exp_f32_e32 v50, v50
	v_cmp_lt_i32_e64 s[38:39], v167, v129
	v_exp_f32_e32 v36, v36
	v_min_f32_e32 v37, 0x42fc0000, v37
	v_add_f32_e32 v50, 1.0, v50
	v_rcp_f32_e32 v50, v50
	v_max_f32_e32 v38, v38, v38
	v_exp_f32_e32 v37, v37
	v_min_f32_e32 v38, 0x42fc0000, v38
	v_cndmask_b32_e64 v51, 1.0, v50, s[38:39]
	v_cndmask_b32_e32 v55, v50, v51, vcc
	v_max_f32_e32 v50, v56, v56
	v_min_f32_e32 v50, 0x42fc0000, v50
	v_exp_f32_e32 v50, v50
	v_cmp_lt_i32_e64 s[38:39], v167, v131
	v_add_f32_e32 v34, 1.0, v34
	v_exp_f32_e32 v38, v38
	v_add_f32_e32 v50, 1.0, v50
	v_rcp_f32_e32 v50, v50
	v_rcp_f32_e32 v34, v34
	v_add_f32_e32 v35, 1.0, v35
	v_rcp_f32_e32 v35, v35
	v_cndmask_b32_e64 v51, 1.0, v50, s[38:39]
	v_cndmask_b32_e32 v56, v50, v51, vcc
	v_max_f32_e32 v50, v57, v57
	v_min_f32_e32 v50, 0x42fc0000, v50
	v_exp_f32_e32 v50, v50
	v_cmp_lt_i32_e64 s[38:39], v167, v133
	v_add_f32_e32 v36, 1.0, v36
	v_rcp_f32_e32 v36, v36
	v_add_f32_e32 v50, 1.0, v50
	v_rcp_f32_e32 v50, v50
	v_add_f32_e32 v37, 1.0, v37
	v_rcp_f32_e32 v37, v37
	v_add_f32_e32 v38, 1.0, v38
	v_cndmask_b32_e64 v51, 1.0, v50, s[38:39]
	v_cndmask_b32_e32 v57, v50, v51, vcc
	v_max_f32_e32 v50, v58, v58
	v_min_f32_e32 v50, 0x42fc0000, v50
	v_exp_f32_e32 v50, v50
	v_cmp_lt_i32_e64 s[38:39], v167, v135
	v_rcp_f32_e32 v38, v38
	v_add_f32_e32 v50, 1.0, v50
	v_rcp_f32_e32 v50, v50
	s_nop 0
	v_cndmask_b32_e64 v51, 1.0, v50, s[38:39]
	v_cndmask_b32_e32 v58, v50, v51, vcc
	v_max_f32_e32 v50, v59, v59
	v_min_f32_e32 v50, 0x42fc0000, v50
	v_exp_f32_e32 v50, v50
	v_cmp_lt_i32_e64 s[38:39], v167, v137
	v_add_f32_e32 v50, 1.0, v50
	v_rcp_f32_e32 v50, v50
	s_nop 0
	v_cndmask_b32_e64 v51, 1.0, v50, s[38:39]
	v_cndmask_b32_e32 v59, v50, v51, vcc
	v_max_f32_e32 v50, v60, v60
	v_min_f32_e32 v50, 0x42fc0000, v50
	v_exp_f32_e32 v50, v50
	v_cmp_lt_i32_e64 s[38:39], v167, v144
	v_add_f32_e32 v50, 1.0, v50
	v_rcp_f32_e32 v50, v50
	s_nop 0
	v_cndmask_b32_e64 v51, 1.0, v50, s[38:39]
	v_cndmask_b32_e32 v60, v50, v51, vcc
	v_max_f32_e32 v50, v61, v61
	v_min_f32_e32 v50, 0x42fc0000, v50
	v_exp_f32_e32 v50, v50
	v_cmp_lt_i32_e64 s[38:39], v167, v145
	v_add_f32_e32 v50, 1.0, v50
	v_rcp_f32_e32 v50, v50
	s_nop 0
	v_cndmask_b32_e64 v51, 1.0, v50, s[38:39]
	v_cndmask_b32_e32 v61, v50, v51, vcc
	v_max_f32_e32 v50, v62, v62
	v_min_f32_e32 v50, 0x42fc0000, v50
	v_exp_f32_e32 v50, v50
	v_cmp_lt_i32_e64 s[38:39], v167, v146
	v_add_f32_e32 v50, 1.0, v50
	v_rcp_f32_e32 v50, v50
	s_nop 0
	v_cndmask_b32_e64 v51, 1.0, v50, s[38:39]
	v_cndmask_b32_e32 v62, v50, v51, vcc
	v_max_f32_e32 v50, v63, v63
	v_min_f32_e32 v50, 0x42fc0000, v50
	v_exp_f32_e32 v50, v50
	v_cmp_lt_i32_e64 s[38:39], v167, v147
	v_add_f32_e32 v50, 1.0, v50
	v_rcp_f32_e32 v50, v50
	s_nop 0
	v_cndmask_b32_e64 v51, 1.0, v50, s[38:39]
	v_cndmask_b32_e32 v63, v50, v51, vcc
	v_max_f32_e32 v50, v64, v64
	v_min_f32_e32 v50, 0x42fc0000, v50
	v_exp_f32_e32 v50, v50
	v_cmp_lt_i32_e64 s[38:39], v167, v148
	v_add_f32_e32 v50, 1.0, v50
	v_rcp_f32_e32 v50, v50
	s_nop 0
	v_cndmask_b32_e64 v51, 1.0, v50, s[38:39]
	v_cndmask_b32_e32 v64, v50, v51, vcc
	v_max_f32_e32 v50, v65, v65
	v_min_f32_e32 v50, 0x42fc0000, v50
	v_exp_f32_e32 v50, v50
	v_cmp_lt_i32_e64 s[38:39], v167, v149
	v_add_f32_e32 v50, 1.0, v50
	v_rcp_f32_e32 v50, v50
	s_nop 0
	v_cndmask_b32_e64 v51, 1.0, v50, s[38:39]
	v_cmp_lt_i32_e64 s[38:39], v167, v150
	v_cndmask_b32_e32 v65, v50, v51, vcc
	s_nop 0
	v_cndmask_b32_e64 v50, 1.0, v34, s[38:39]
	v_cmp_lt_i32_e64 s[38:39], v167, v151
	v_cndmask_b32_e32 v34, v34, v50, vcc
	s_nop 0
	v_cndmask_b32_e64 v50, 1.0, v35, s[38:39]
	v_cmp_lt_i32_e64 s[38:39], v167, v152
	v_cndmask_b32_e32 v35, v35, v50, vcc
	s_nop 0
	v_cndmask_b32_e64 v50, 1.0, v36, s[38:39]
	v_cmp_lt_i32_e64 s[38:39], v167, v153
	v_cndmask_b32_e32 v36, v36, v50, vcc
	s_nop 0
	v_cndmask_b32_e64 v50, 1.0, v37, s[38:39]
	v_cmp_lt_i32_e64 s[38:39], v167, v154
	v_cndmask_b32_e32 v37, v37, v50, vcc
	v_mul_f32_e32 v51, v36, v37
	v_cndmask_b32_e64 v50, 1.0, v38, s[38:39]
	v_cndmask_b32_e32 v170, v38, v50, vcc
	v_max_f32_e32 v38, v39, v39
	v_min_f32_e32 v38, 0x42fc0000, v38
	v_exp_f32_e32 v38, v38
	v_cmp_lt_i32_e64 s[38:39], v167, v155
	v_add_f32_e32 v38, 1.0, v38
	v_rcp_f32_e32 v38, v38
	s_nop 0
	v_cndmask_b32_e64 v39, 1.0, v38, s[38:39]
	v_cndmask_b32_e32 v171, v38, v39, vcc
	v_max_f32_e32 v38, v40, v40
	v_min_f32_e32 v38, 0x42fc0000, v38
	v_exp_f32_e32 v38, v38
	v_cmp_lt_i32_e64 s[38:39], v167, v156
	v_mul_f32_e32 v177, v170, v171
	v_mul_f32_e32 v40, v56, v57
	v_add_f32_e32 v38, 1.0, v38
	v_rcp_f32_e32 v38, v38
	s_nop 0
	v_cndmask_b32_e64 v39, 1.0, v38, s[38:39]
	v_cndmask_b32_e32 v172, v38, v39, vcc
	v_max_f32_e32 v38, v41, v41
	v_min_f32_e32 v38, 0x42fc0000, v38
	v_exp_f32_e32 v38, v38
	v_cmp_lt_i32_e64 s[38:39], v167, v157
	v_mul_f32_e32 v41, v58, v59
	v_add_f32_e32 v38, 1.0, v38
	v_rcp_f32_e32 v38, v38
	s_nop 0
	v_cndmask_b32_e64 v39, 1.0, v38, s[38:39]
	v_cndmask_b32_e32 v173, v38, v39, vcc
	v_max_f32_e32 v38, v42, v42
	v_min_f32_e32 v38, 0x42fc0000, v38
	v_exp_f32_e32 v38, v38
	v_cmp_lt_i32_e64 s[38:39], v167, v158
	v_mul_f32_e32 v178, v172, v173
	v_mul_f32_e32 v177, v177, v178
	v_add_f32_e32 v38, 1.0, v38
	v_rcp_f32_e32 v38, v38
	v_mov_b32_e32 v178, v177
	s_nop 1
	v_permlane32_swap_b32_e32 v177, v178
	v_cndmask_b32_e64 v39, 1.0, v38, s[38:39]
	v_cndmask_b32_e32 v42, v38, v39, vcc
	v_max_f32_e32 v38, v43, v43
	v_min_f32_e32 v38, 0x42fc0000, v38
	v_exp_f32_e32 v38, v38
	v_cmp_lt_i32_e64 s[38:39], v167, v159
	v_add_f32_e32 v38, 1.0, v38
	v_rcp_f32_e32 v38, v38
	s_nop 0
	v_cndmask_b32_e64 v39, 1.0, v38, s[38:39]
	v_cndmask_b32_e32 v43, v38, v39, vcc
	v_max_f32_e32 v38, v44, v44
	v_min_f32_e32 v38, 0x42fc0000, v38
	v_exp_f32_e32 v38, v38
	v_cmp_lt_i32_e64 s[38:39], v167, v160
	v_mul_f32_e32 v179, v42, v43
	v_sub_f32_e32 v42, 1.0, v42
	v_add_f32_e32 v38, 1.0, v38
	v_rcp_f32_e32 v38, v38
	s_nop 0
	v_cndmask_b32_e64 v39, 1.0, v38, s[38:39]
	v_cndmask_b32_e32 v44, v38, v39, vcc
	v_max_f32_e32 v38, v45, v45
	v_min_f32_e32 v38, 0x42fc0000, v38
	v_exp_f32_e32 v38, v38
	v_cmp_lt_i32_e64 s[38:39], v167, v161
	v_add_f32_e32 v38, 1.0, v38
	v_rcp_f32_e32 v38, v38
	s_nop 0
	v_cndmask_b32_e64 v39, 1.0, v38, s[38:39]
	v_cndmask_b32_e32 v45, v38, v39, vcc
	v_max_f32_e32 v38, v46, v46
	v_min_f32_e32 v38, 0x42fc0000, v38
	v_exp_f32_e32 v38, v38
	v_cmp_lt_i32_e64 s[38:39], v167, v162
	v_mul_f32_e32 v180, v44, v45
	v_mul_f32_e32 v179, v179, v180
	v_add_f32_e32 v38, 1.0, v38
	v_rcp_f32_e32 v38, v38
	v_mov_b32_e32 v180, v179
	s_nop 1
	v_permlane32_swap_b32_e32 v179, v180
	v_cndmask_b32_e64 v39, 1.0, v38, s[38:39]
	v_cndmask_b32_e32 v174, v38, v39, vcc
	v_max_f32_e32 v38, v47, v47
	v_min_f32_e32 v38, 0x42fc0000, v38
	v_exp_f32_e32 v38, v38
	v_cmp_lt_i32_e64 s[38:39], v167, v163
	v_mul_f32_e32 v47, v62, v63
	v_mul_f32_e32 v46, v60, v61
	v_add_f32_e32 v38, 1.0, v38
	v_rcp_f32_e32 v38, v38
	v_mul_f32_e32 v41, v41, v46
	v_mov_b32_e32 v46, v41
	s_nop 1
	v_permlane32_swap_b32_e32 v41, v46
	v_cndmask_b32_e64 v39, 1.0, v38, s[38:39]
	v_cndmask_b32_e32 v175, v38, v39, vcc
	v_max_f32_e32 v38, v48, v48
	v_min_f32_e32 v38, 0x42fc0000, v38
	v_exp_f32_e32 v38, v38
	v_cmp_lt_i32_e64 s[38:39], v167, v164
	v_mul_f32_e32 v181, v174, v175
	v_mul_f32_e32 v48, v64, v65
	v_add_f32_e32 v38, 1.0, v38
	v_rcp_f32_e32 v38, v38
	v_mul_f32_e32 v47, v47, v48
	v_mov_b32_e32 v48, v47
	s_nop 1
	v_permlane32_swap_b32_e32 v47, v48
	v_cndmask_b32_e64 v39, 1.0, v38, s[38:39]
	v_cndmask_b32_e32 v176, v38, v39, vcc
	v_max_f32_e32 v38, v49, v49
	v_min_f32_e32 v38, 0x42fc0000, v38
	v_exp_f32_e32 v38, v38
	v_cmp_lt_i32_e64 s[38:39], v167, v165
	v_mul_f32_e32 v49, v34, v35
	v_mul_f32_e32 v49, v49, v51
	v_add_f32_e32 v38, 1.0, v38
	v_rcp_f32_e32 v38, v38
	v_mov_b32_e32 v51, v49
	s_nop 1
	v_permlane32_swap_b32_e32 v49, v51
	v_cndmask_b32_e64 v39, 1.0, v38, s[38:39]
	v_cndmask_b32_e32 v167, v38, v39, vcc
	v_mul_f32_e32 v182, v176, v167
	v_mul_f32_e32 v181, v181, v182
	v_mov_b32_e32 v182, v181
	s_nop 1
	v_permlane32_swap_b32_e32 v181, v182
	v_mul_f32_e32 v182, v166, v182
	v_mul_f32_e32 v181, v182, v181
	v_mul_f32_e32 v180, v181, v180
	v_mul_f32_e32 v179, v180, v179
	v_mul_f32_e32 v178, v179, v178
	v_mul_f32_e32 v177, v178, v177
	v_mul_f32_e32 v51, v177, v51
	v_mul_f32_e32 v38, v168, v169
	v_mul_f32_e32 v39, v52, v53
	v_mul_f32_e32 v49, v51, v49
	v_mul_f32_e32 v50, v38, v39
	v_mul_f32_e32 v39, v54, v55
	v_mul_f32_e32 v48, v49, v48
	v_mul_f32_e32 v39, v39, v40
	v_mul_f32_e32 v47, v48, v47
	v_mov_b32_e32 v40, v39
	v_mul_f32_e32 v46, v47, v46
	s_nop 0
	v_permlane32_swap_b32_e32 v39, v40
	v_mul_f32_e32 v41, v46, v41
	v_mov_b32_e32 v38, v50
	v_mul_f32_e32 v40, v41, v40
	s_nop 0
	v_permlane32_swap_b32_e32 v50, v38
	v_mul_f32_e32 v39, v40, v39
	v_cndmask_b32_e64 v177, v177, v51, s[36:37]
	v_mul_f32_e32 v51, v39, v38
	v_cndmask_b32_e64 v38, v39, v51, s[36:37]
	v_mul_f32_e32 v39, v53, v38
	v_cndmask_b32_e64 v40, v41, v40, s[36:37]
	v_mul_f32_e32 v41, v52, v39
	v_cndmask_b32_e64 v180, v181, v180, s[36:37]
	v_cndmask_b32_e64 v181, v47, v46, s[36:37]
	v_mul_f32_e32 v46, v169, v41
	v_sub_f32_e32 v47, 1.0, v168
	v_mul_f32_e32 v46, v47, v46
	v_sub_f32_e32 v47, 1.0, v169
	v_mul_f32_e32 v41, v47, v41
	v_sub_f32_e32 v47, 1.0, v52
	v_mul_f32_e32 v39, v47, v39
	v_sub_f32_e32 v47, 1.0, v53
	v_mul_f32_e32 v38, v47, v38
	v_mul_f32_e32 v47, v57, v40
	v_cndmask_b32_e64 v178, v179, v178, s[36:37]
	v_cndmask_b32_e64 v179, v49, v48, s[36:37]
	v_mul_f32_e32 v48, v56, v47
	v_mul_f32_e32 v49, v55, v48
	v_sub_f32_e32 v52, 1.0, v54
	v_mul_f32_e32 v49, v52, v49
	v_sub_f32_e32 v52, 1.0, v55
	v_mul_f32_e32 v48, v52, v48
	v_sub_f32_e32 v52, 1.0, v56
	v_mul_f32_e32 v52, v52, v47
	v_sub_f32_e32 v47, 1.0, v57
	v_mul_f32_e32 v40, v47, v40
	v_cvt_pk_bf16_f32 v47, v39, v38
	v_mul_f32_e32 v38, v61, v181
	v_mul_f32_e32 v39, v60, v38
	v_cvt_pk_bf16_f32 v46, v46, v41
	v_cvt_pk_bf16_f32 v48, v49, v48
	v_cvt_pk_bf16_f32 v49, v52, v40
	v_mul_f32_e32 v40, v59, v39
	v_sub_f32_e32 v41, 1.0, v58
	v_mul_f32_e32 v40, v41, v40
	v_sub_f32_e32 v41, 1.0, v59
	v_mul_f32_e32 v39, v41, v39
	v_sub_f32_e32 v41, 1.0, v60
	v_mul_f32_e32 v41, v41, v38
	v_sub_f32_e32 v38, 1.0, v61
	v_mul_f32_e32 v52, v38, v181
	v_mul_f32_e32 v38, v65, v179
	v_mul_f32_e32 v53, v64, v38
	v_mul_f32_e32 v54, v63, v53
	v_sub_f32_e32 v55, 1.0, v62
	v_mul_f32_e32 v54, v55, v54
	v_sub_f32_e32 v55, 1.0, v63
	v_mul_f32_e32 v53, v55, v53
	v_sub_f32_e32 v55, 1.0, v64
	v_mul_f32_e32 v55, v55, v38
	v_sub_f32_e32 v38, 1.0, v65
	v_mul_f32_e32 v56, v38, v179
	v_cvt_pk_bf16_f32 v38, v40, v39
	v_cvt_pk_bf16_f32 v39, v41, v52
	v_mul_f32_e32 v52, v37, v177
	v_cvt_pk_bf16_f32 v40, v54, v53
	v_mul_f32_e32 v53, v36, v52
	v_sub_f32_e32 v36, 1.0, v36
	v_mul_f32_e32 v54, v35, v53
	v_sub_f32_e32 v35, 1.0, v35
	v_mul_f32_e32 v36, v36, v52
	v_mul_f32_e32 v52, v173, v178
	v_sub_f32_e32 v34, 1.0, v34
	v_mul_f32_e32 v35, v35, v53
	v_mul_f32_e32 v53, v172, v52
	v_cvt_pk_bf16_f32 v41, v55, v56
	v_mul_f32_e32 v34, v34, v54
	v_mul_f32_e32 v54, v171, v53
	v_sub_f32_e32 v55, 1.0, v170
	v_mul_f32_e32 v54, v55, v54
	v_sub_f32_e32 v55, 1.0, v171
	v_mul_f32_e32 v53, v55, v53
	v_sub_f32_e32 v55, 1.0, v172
	v_sub_f32_e32 v37, 1.0, v37
	v_mul_f32_e32 v52, v55, v52
	v_sub_f32_e32 v55, 1.0, v173
	v_mul_f32_e32 v37, v37, v177
	v_mul_f32_e32 v55, v55, v178
	v_cvt_pk_bf16_f32 v34, v34, v35
	v_cvt_pk_bf16_f32 v35, v36, v37
	v_cvt_pk_bf16_f32 v37, v52, v55
	v_mul_f32_e32 v52, v45, v180
	v_cndmask_b32_e64 v166, v166, v182, s[36:37]
	v_cvt_pk_bf16_f32 v36, v54, v53
	v_mul_f32_e32 v53, v44, v52
	v_sub_f32_e32 v44, 1.0, v44
	v_mul_f32_e32 v54, v43, v53
	v_sub_f32_e32 v43, 1.0, v43
	v_mul_f32_e32 v44, v44, v52
	v_mul_f32_e32 v52, v167, v166
	v_mul_f32_e32 v43, v43, v53
	v_mul_f32_e32 v53, v176, v52
	v_mul_f32_e32 v42, v42, v54
	v_mul_f32_e32 v54, v175, v53
	v_sub_f32_e32 v55, 1.0, v174
	v_mul_f32_e32 v54, v55, v54
	v_sub_f32_e32 v55, 1.0, v175
	v_mul_f32_e32 v53, v55, v53
	v_sub_f32_e32 v55, 1.0, v176
	v_sub_f32_e32 v45, 1.0, v45
	v_mul_f32_e32 v52, v55, v52
	v_sub_f32_e32 v55, 1.0, v167
	v_mul_f32_e32 v45, v45, v180
	v_mul_f32_e32 v55, v55, v166
	v_cvt_pk_bf16_f32 v42, v42, v43
	v_cvt_pk_bf16_f32 v43, v44, v45
	v_cvt_pk_bf16_f32 v44, v54, v53
	v_cvt_pk_bf16_f32 v45, v52, v55
	v_mul_f32_e32 v166, v51, v50
	ds_read_b64_tr_b16 v[50:51], v117
	ds_read_b64_tr_b16 v[52:53], v117 offset:1536
	ds_read_b64_tr_b16 v[54:55], v117 offset:3072
	ds_read_b64_tr_b16 v[56:57], v117 offset:4608
	ds_read_b64_tr_b16 v[58:59], v117 offset:6144
	ds_read_b64_tr_b16 v[60:61], v117 offset:7680
	ds_read_b64_tr_b16 v[62:63], v117 offset:9216
	ds_read_b64_tr_b16 v[64:65], v117 offset:10752
	s_waitcnt lgkmcnt(0)
	s_nop 0
	v_mfma_f32_32x32x16_bf16 v[18:33], v[50:53], v[46:49], v[18:33]
	v_cmp_gt_f32_e32 vcc, s29, v166
	s_cmp_lg_u64 vcc, exec
	s_cselect_b64 s[38:39], -1, 0
	s_cmp_lg_u32 s35, 0
	s_cselect_b64 s[40:41], -1, 0
	s_and_b64 s[38:39], s[40:41], s[38:39]
	s_sub_i32 s34, s34, 64
	v_mfma_f32_32x32x16_bf16 v[18:33], v[54:57], v[38:41], v[18:33]
	s_and_b64 vcc, exec, s[38:39]
	v_mfma_f32_32x32x16_bf16 v[18:33], v[58:61], v[34:37], v[18:33]
	v_mfma_f32_32x32x16_bf16 v[18:33], v[62:65], v[42:45], v[18:33]
	ds_read_b64_tr_b16 v[62:63], v117 offset:64
	ds_read_b64_tr_b16 v[64:65], v117 offset:1600
	ds_read_b64_tr_b16 v[58:59], v117 offset:3136
	ds_read_b64_tr_b16 v[60:61], v117 offset:4672
	ds_read_b64_tr_b16 v[50:51], v117 offset:6208
	ds_read_b64_tr_b16 v[52:53], v117 offset:7744
	ds_read_b64_tr_b16 v[54:55], v117 offset:9280
	ds_read_b64_tr_b16 v[56:57], v117 offset:10816
	s_waitcnt lgkmcnt(0)
	s_nop 0
	v_mfma_f32_32x32x16_bf16 v[2:17], v[62:65], v[46:49], v[2:17]
	v_mfma_f32_32x32x16_bf16 v[2:17], v[58:61], v[38:41], v[2:17]
	v_mfma_f32_32x32x16_bf16 v[2:17], v[50:53], v[34:37], v[2:17]
	v_mfma_f32_32x32x16_bf16 v[2:17], v[54:57], v[42:45], v[2:17]
	s_cbranch_vccnz .LBB0_1171
	v_lshlrev_b32_e32 v34, 1, v114
	v_mov_b32_e32 v35, v1
	v_lshl_add_u64 v[34:35], v[138:139], 0, v[34:35]
	v_cvt_pk_bf16_f32 v18, v18, v19
	v_cvt_pk_bf16_f32 v19, v20, v21
	s_nop 5
	v_cvt_pk_bf16_f32 v2, v2, v3
	v_cvt_pk_bf16_f32 v3, v4, v5
	global_store_dwordx2 v[34:35], v[18:19], off sc0 sc1
	global_store_dwordx2 v[34:35], v[2:3], off offset:64 sc0 sc1
	v_cvt_pk_bf16_f32 v2, v22, v23
	v_cvt_pk_bf16_f32 v3, v24, v25
	v_cvt_pk_bf16_f32 v4, v6, v7
	v_cvt_pk_bf16_f32 v5, v8, v9
	global_store_dwordx2 v[34:35], v[2:3], off offset:16 sc0 sc1
	global_store_dwordx2 v[34:35], v[4:5], off offset:80 sc0 sc1
	v_cvt_pk_bf16_f32 v2, v26, v27
	v_cvt_pk_bf16_f32 v3, v28, v29
	v_cvt_pk_bf16_f32 v4, v10, v11
	v_cvt_pk_bf16_f32 v5, v12, v13
	s_add_i32 s17, s17, s72
	s_add_i32 s16, s16, s72
	global_store_dwordx2 v[34:35], v[2:3], off offset:32 sc0 sc1
	global_store_dwordx2 v[34:35], v[4:5], off offset:96 sc0 sc1
	v_cvt_pk_bf16_f32 v2, v30, v31
	v_cvt_pk_bf16_f32 v3, v32, v33
	v_cvt_pk_bf16_f32 v4, v14, v15
	v_cvt_pk_bf16_f32 v5, v16, v17
	s_cmpk_lt_i32 s17, 0x1000
	global_store_dwordx2 v[34:35], v[2:3], off offset:48 sc0 sc1
	global_store_dwordx2 v[34:35], v[4:5], off offset:112 sc0 sc1
	s_cbranch_scc1 .LBB0_1170

.LBB0_1175:
	s_or_b64 exec, exec, s[16:17]
	v_lshlrev_b64 v[28:29], 9, v[98:99]
	v_lshl_add_u64 v[102:103], v[28:29], 1, v[96:97]
	global_load_dwordx4 v[82:85], v[26:27], off
	global_load_dwordx4 v[110:113], v[102:103], off
	global_load_dwordx4 v[74:77], v[26:27], off offset:1024
	global_load_dwordx4 v[78:81], v[102:103], off offset:1024
	global_load_dwordx4 v[66:69], v[26:27], off offset:2048
	global_load_dwordx4 v[70:73], v[102:103], off offset:2048
	global_load_dwordx4 v[58:61], v[26:27], off offset:3072
	global_load_dwordx4 v[62:65], v[102:103], off offset:3072
	s_movk_i32 s16, 0x1000
	v_add_co_u32_e32 v26, vcc, s16, v26
	s_waitcnt vmcnt(8)
	v_lshlrev_b32_e32 v114, 16, v90
	v_addc_co_u32_e32 v27, vcc, 0, v27, vcc
	global_load_dwordx4 v[50:53], v[26:27], off
	v_add_co_u32_e32 v100, vcc, s16, v102
	v_and_b32_e32 v115, 0xffff0000, v90
	s_nop 0
	v_addc_co_u32_e32 v101, vcc, 0, v103, vcc
	global_load_dwordx4 v[54:57], v[100:101], off
	global_load_dwordx4 v[42:45], v[26:27], off offset:1024
	global_load_dwordx4 v[46:49], v[100:101], off offset:1024
	global_load_dwordx4 v[34:37], v[26:27], off offset:2048
	global_load_dwordx4 v[38:41], v[100:101], off offset:2048
	s_nop 0
	global_load_dwordx4 v[26:29], v[26:27], off offset:3072
	s_nop 0
	global_load_dwordx4 v[30:33], v[100:101], off offset:3072
	v_lshlrev_b32_e32 v104, 16, v86
	v_and_b32_e32 v105, 0xffff0000, v86
	v_pk_mul_f32 v[116:117], v[10:11], v[114:115]
	v_lshlrev_b32_e32 v90, 16, v91
	v_pk_fma_f32 v[116:117], v[18:19], v[104:105], v[116:117]
	v_and_b32_e32 v91, 0xffff0000, v91
	v_lshlrev_b32_e32 v86, 16, v87
	v_and_b32_e32 v87, 0xffff0000, v87
	v_readlane_b32 s16, v253, 8
	v_add_u32_e32 v108, s72, v108
	s_waitcnt vmcnt(15)
	v_lshlrev_b32_e32 v104, 16, v82
	v_and_b32_e32 v105, 0xffff0000, v82
	s_waitcnt vmcnt(14)
	v_lshlrev_b32_e32 v106, 16, v110
	v_and_b32_e32 v107, 0xffff0000, v110
	v_pk_fma_f32 v[116:117], v[2:3], v[104:105], v[116:117]
	v_lshlrev_b32_e32 v82, 16, v83
	v_pk_mul_f32 v[116:117], v[116:117], v[106:107]
	v_lshlrev_b32_e32 v106, 16, v111
	v_and_b32_e32 v107, 0xffff0000, v111
	v_pk_mul_f32 v[110:111], v[12:13], v[90:91]
	v_and_b32_e32 v83, 0xffff0000, v83
	v_pk_fma_f32 v[86:87], v[20:21], v[86:87], v[110:111]
	v_lshlrev_b32_e32 v110, 16, v112
	v_pk_fma_f32 v[86:87], v[4:5], v[82:83], v[86:87]
	v_and_b32_e32 v111, 0xffff0000, v112
	v_pk_mul_f32 v[118:119], v[86:87], v[106:107]
	v_lshlrev_b32_e32 v106, 16, v92
	v_and_b32_e32 v107, 0xffff0000, v92
	v_lshlrev_b32_e32 v86, 16, v88
	v_and_b32_e32 v87, 0xffff0000, v88
	v_pk_mul_f32 v[120:121], v[14:15], v[106:107]
	v_lshlrev_b32_e32 v92, 16, v93
	v_pk_fma_f32 v[120:121], v[22:23], v[86:87], v[120:121]
	v_lshlrev_b32_e32 v86, 16, v84
	v_and_b32_e32 v87, 0xffff0000, v84
	v_pk_fma_f32 v[120:121], v[6:7], v[86:87], v[120:121]
	v_and_b32_e32 v93, 0xffff0000, v93
	v_pk_mul_f32 v[120:121], v[120:121], v[110:111]
	v_lshlrev_b32_e32 v110, 16, v113
	v_and_b32_e32 v111, 0xffff0000, v113
	v_lshlrev_b32_e32 v88, 16, v89
	v_and_b32_e32 v89, 0xffff0000, v89
	v_pk_mul_f32 v[112:113], v[16:17], v[92:93]
	v_lshlrev_b32_e32 v84, 16, v85
	v_pk_fma_f32 v[88:89], v[24:25], v[88:89], v[112:113]
	v_and_b32_e32 v85, 0xffff0000, v85
	v_pk_fma_f32 v[88:89], v[8:9], v[84:85], v[88:89]
	v_cvt_pk_bf16_f32 v112, v120, v121
	v_pk_mul_f32 v[88:89], v[88:89], v[110:111]
	v_cvt_pk_bf16_f32 v110, v116, v117
	v_cvt_pk_bf16_f32 v111, v118, v119
	v_cvt_pk_bf16_f32 v113, v88, v89
	global_store_dwordx4 v[102:103], v[110:113], off sc0 sc1
	s_waitcnt vmcnt(13)
	v_lshlrev_b32_e32 v88, 16, v78
	v_and_b32_e32 v89, 0xffff0000, v78
	v_pk_mul_f32 v[110:111], v[10:11], v[104:105]
	v_lshlrev_b32_e32 v112, 16, v74
	v_pk_fma_f32 v[110:111], v[18:19], v[114:115], v[110:111]
	v_and_b32_e32 v113, 0xffff0000, v74
	v_pk_fma_f32 v[110:111], v[2:3], v[112:113], v[110:111]
	v_lshlrev_b32_e32 v78, 16, v79
	v_pk_mul_f32 v[88:89], v[110:111], v[88:89]
	v_pk_mul_f32 v[110:111], v[12:13], v[82:83]
	v_and_b32_e32 v79, 0xffff0000, v79
	v_pk_fma_f32 v[90:91], v[20:21], v[90:91], v[110:111]
	v_lshlrev_b32_e32 v110, 16, v75
	v_and_b32_e32 v111, 0xffff0000, v75
	v_pk_fma_f32 v[74:75], v[4:5], v[110:111], v[90:91]
	v_pk_mul_f32 v[90:91], v[14:15], v[86:87]
	v_pk_mul_f32 v[78:79], v[74:75], v[78:79]
	v_pk_fma_f32 v[90:91], v[22:23], v[106:107], v[90:91]
	v_lshlrev_b32_e32 v106, 16, v76
	v_and_b32_e32 v107, 0xffff0000, v76
	v_lshlrev_b32_e32 v74, 16, v80
	v_and_b32_e32 v75, 0xffff0000, v80
	v_pk_fma_f32 v[90:91], v[6:7], v[106:107], v[90:91]
	v_add_u32_e32 v98, s16, v98
	v_pk_mul_f32 v[90:91], v[90:91], v[74:75]
	v_lshlrev_b32_e32 v74, 16, v81
	v_and_b32_e32 v75, 0xffff0000, v81
	v_pk_mul_f32 v[80:81], v[16:17], v[84:85]
	s_movk_i32 s16, 0x7ff
	v_pk_fma_f32 v[80:81], v[24:25], v[92:93], v[80:81]
	v_lshlrev_b32_e32 v92, 16, v77
	v_and_b32_e32 v93, 0xffff0000, v77
	v_pk_fma_f32 v[76:77], v[8:9], v[92:93], v[80:81]
	v_cmp_lt_i32_e32 vcc, s16, v108
	v_pk_mul_f32 v[80:81], v[76:77], v[74:75]
	v_cvt_pk_bf16_f32 v74, v88, v89
	v_cvt_pk_bf16_f32 v75, v78, v79
	v_cvt_pk_bf16_f32 v76, v90, v91
	v_cvt_pk_bf16_f32 v77, v80, v81
	global_store_dwordx4 v[102:103], v[74:77], off offset:1024 sc0 sc1
	s_waitcnt vmcnt(13)
	v_lshlrev_b32_e32 v78, 16, v66
	v_and_b32_e32 v79, 0xffff0000, v66
	v_pk_mul_f32 v[76:77], v[10:11], v[112:113]
	s_waitcnt vmcnt(12)
	v_lshlrev_b32_e32 v74, 16, v70
	v_pk_fma_f32 v[76:77], v[18:19], v[104:105], v[76:77]
	v_and_b32_e32 v75, 0xffff0000, v70
	v_pk_fma_f32 v[76:77], v[2:3], v[78:79], v[76:77]
	v_lshlrev_b32_e32 v80, 16, v67
	v_pk_mul_f32 v[74:75], v[76:77], v[74:75]
	v_pk_mul_f32 v[76:77], v[12:13], v[110:111]
	v_and_b32_e32 v81, 0xffff0000, v67
	v_pk_fma_f32 v[76:77], v[20:21], v[82:83], v[76:77]
	v_lshlrev_b32_e32 v70, 16, v71
	v_pk_fma_f32 v[66:67], v[4:5], v[80:81], v[76:77]
	v_pk_mul_f32 v[76:77], v[14:15], v[106:107]
	v_and_b32_e32 v71, 0xffff0000, v71
	v_pk_fma_f32 v[76:77], v[22:23], v[86:87], v[76:77]
	v_lshlrev_b32_e32 v82, 16, v68
	v_and_b32_e32 v83, 0xffff0000, v68
	v_pk_mul_f32 v[70:71], v[66:67], v[70:71]
	v_lshlrev_b32_e32 v66, 16, v72
	v_and_b32_e32 v67, 0xffff0000, v72
	v_pk_fma_f32 v[76:77], v[6:7], v[82:83], v[76:77]
	s_or_b64 s[14:15], vcc, s[14:15]
	v_pk_mul_f32 v[76:77], v[76:77], v[66:67]
	v_lshlrev_b32_e32 v66, 16, v73
	v_and_b32_e32 v67, 0xffff0000, v73
	v_pk_mul_f32 v[72:73], v[16:17], v[92:93]
	s_nop 0
	v_pk_fma_f32 v[72:73], v[24:25], v[84:85], v[72:73]
	v_lshlrev_b32_e32 v84, 16, v69
	v_and_b32_e32 v85, 0xffff0000, v69
	v_pk_fma_f32 v[68:69], v[8:9], v[84:85], v[72:73]
	s_nop 0
	v_pk_mul_f32 v[72:73], v[68:69], v[66:67]
	v_cvt_pk_bf16_f32 v66, v74, v75
	v_cvt_pk_bf16_f32 v67, v70, v71
	v_cvt_pk_bf16_f32 v68, v76, v77
	v_cvt_pk_bf16_f32 v69, v72, v73
	global_store_dwordx4 v[102:103], v[66:69], off offset:2048 sc0 sc1
	s_waitcnt vmcnt(12)
	v_lshlrev_b32_e32 v70, 16, v58
	v_and_b32_e32 v71, 0xffff0000, v58
	v_pk_mul_f32 v[68:69], v[10:11], v[78:79]
	s_waitcnt vmcnt(11)
	v_lshlrev_b32_e32 v66, 16, v62
	v_pk_fma_f32 v[68:69], v[18:19], v[112:113], v[68:69]
	v_and_b32_e32 v67, 0xffff0000, v62
	v_pk_fma_f32 v[68:69], v[2:3], v[70:71], v[68:69]
	v_lshlrev_b32_e32 v72, 16, v59
	v_pk_mul_f32 v[66:67], v[68:69], v[66:67]
	v_pk_mul_f32 v[68:69], v[12:13], v[80:81]
	v_and_b32_e32 v73, 0xffff0000, v59
	v_pk_fma_f32 v[68:69], v[20:21], v[110:111], v[68:69]
	v_lshlrev_b32_e32 v62, 16, v63
	v_pk_fma_f32 v[58:59], v[4:5], v[72:73], v[68:69]
	v_pk_mul_f32 v[68:69], v[14:15], v[82:83]
	v_and_b32_e32 v63, 0xffff0000, v63
	v_pk_fma_f32 v[68:69], v[22:23], v[106:107], v[68:69]
	v_lshlrev_b32_e32 v74, 16, v60
	v_and_b32_e32 v75, 0xffff0000, v60
	v_pk_mul_f32 v[62:63], v[58:59], v[62:63]
	v_lshlrev_b32_e32 v58, 16, v64
	v_and_b32_e32 v59, 0xffff0000, v64
	v_pk_fma_f32 v[68:69], v[6:7], v[74:75], v[68:69]
	v_lshlrev_b32_e32 v76, 16, v61
	v_pk_mul_f32 v[68:69], v[68:69], v[58:59]
	v_lshlrev_b32_e32 v58, 16, v65
	v_and_b32_e32 v59, 0xffff0000, v65
	v_pk_mul_f32 v[64:65], v[16:17], v[84:85]
	v_and_b32_e32 v77, 0xffff0000, v61
	v_pk_fma_f32 v[64:65], v[24:25], v[92:93], v[64:65]
	s_nop 0
	v_pk_fma_f32 v[60:61], v[8:9], v[76:77], v[64:65]
	s_nop 0
	v_pk_mul_f32 v[64:65], v[60:61], v[58:59]
	v_cvt_pk_bf16_f32 v58, v66, v67
	v_cvt_pk_bf16_f32 v59, v62, v63
	v_cvt_pk_bf16_f32 v60, v68, v69
	v_cvt_pk_bf16_f32 v61, v64, v65
	global_store_dwordx4 v[102:103], v[58:61], off offset:3072 sc0 sc1
	s_waitcnt vmcnt(11)
	v_lshlrev_b32_e32 v62, 16, v50
	v_and_b32_e32 v63, 0xffff0000, v50
	v_pk_mul_f32 v[60:61], v[10:11], v[70:71]
	s_waitcnt vmcnt(10)
	v_lshlrev_b32_e32 v58, 16, v54
	v_pk_fma_f32 v[60:61], v[18:19], v[78:79], v[60:61]
	v_and_b32_e32 v59, 0xffff0000, v54
	v_pk_fma_f32 v[60:61], v[2:3], v[62:63], v[60:61]
	v_lshlrev_b32_e32 v64, 16, v51
	v_pk_mul_f32 v[58:59], v[60:61], v[58:59]
	v_pk_mul_f32 v[60:61], v[12:13], v[72:73]
	v_and_b32_e32 v65, 0xffff0000, v51
	v_pk_fma_f32 v[60:61], v[20:21], v[80:81], v[60:61]
	v_lshlrev_b32_e32 v54, 16, v55
	v_pk_fma_f32 v[50:51], v[4:5], v[64:65], v[60:61]
	v_pk_mul_f32 v[60:61], v[14:15], v[74:75]
	v_and_b32_e32 v55, 0xffff0000, v55
	v_pk_fma_f32 v[60:61], v[22:23], v[82:83], v[60:61]
	v_lshlrev_b32_e32 v66, 16, v52
	v_and_b32_e32 v67, 0xffff0000, v52
	v_pk_mul_f32 v[54:55], v[50:51], v[54:55]
	v_lshlrev_b32_e32 v50, 16, v56
	v_and_b32_e32 v51, 0xffff0000, v56
	v_pk_fma_f32 v[60:61], v[6:7], v[66:67], v[60:61]
	v_lshlrev_b32_e32 v68, 16, v53
	v_pk_mul_f32 v[60:61], v[60:61], v[50:51]
	v_lshlrev_b32_e32 v50, 16, v57
	v_and_b32_e32 v51, 0xffff0000, v57
	v_pk_mul_f32 v[56:57], v[16:17], v[76:77]
	v_and_b32_e32 v69, 0xffff0000, v53
	v_pk_fma_f32 v[56:57], v[24:25], v[84:85], v[56:57]
	s_nop 0
	v_pk_fma_f32 v[52:53], v[8:9], v[68:69], v[56:57]
	s_nop 0
	v_pk_mul_f32 v[56:57], v[52:53], v[50:51]
	v_cvt_pk_bf16_f32 v50, v58, v59
	v_cvt_pk_bf16_f32 v51, v54, v55
	v_cvt_pk_bf16_f32 v52, v60, v61
	v_cvt_pk_bf16_f32 v53, v56, v57
	global_store_dwordx4 v[100:101], v[50:53], off sc0 sc1
	s_waitcnt vmcnt(10)
	v_lshlrev_b32_e32 v54, 16, v42
	v_and_b32_e32 v55, 0xffff0000, v42
	v_pk_mul_f32 v[52:53], v[10:11], v[62:63]
	s_waitcnt vmcnt(9)
	v_lshlrev_b32_e32 v50, 16, v46
	v_pk_fma_f32 v[52:53], v[18:19], v[70:71], v[52:53]
	v_and_b32_e32 v51, 0xffff0000, v46
	v_pk_fma_f32 v[52:53], v[2:3], v[54:55], v[52:53]
	v_lshlrev_b32_e32 v56, 16, v43
	v_pk_mul_f32 v[50:51], v[52:53], v[50:51]
	v_pk_mul_f32 v[52:53], v[12:13], v[64:65]
	v_and_b32_e32 v57, 0xffff0000, v43
	v_pk_fma_f32 v[52:53], v[20:21], v[72:73], v[52:53]
	v_lshlrev_b32_e32 v46, 16, v47
	v_pk_fma_f32 v[42:43], v[4:5], v[56:57], v[52:53]
	v_pk_mul_f32 v[52:53], v[14:15], v[66:67]
	v_and_b32_e32 v47, 0xffff0000, v47
	v_pk_fma_f32 v[52:53], v[22:23], v[74:75], v[52:53]
	v_lshlrev_b32_e32 v58, 16, v44
	v_and_b32_e32 v59, 0xffff0000, v44
	v_pk_mul_f32 v[46:47], v[42:43], v[46:47]
	v_lshlrev_b32_e32 v42, 16, v48
	v_and_b32_e32 v43, 0xffff0000, v48
	v_pk_fma_f32 v[52:53], v[6:7], v[58:59], v[52:53]
	v_lshlrev_b32_e32 v60, 16, v45
	v_pk_mul_f32 v[52:53], v[52:53], v[42:43]
	v_lshlrev_b32_e32 v42, 16, v49
	v_and_b32_e32 v43, 0xffff0000, v49
	v_pk_mul_f32 v[48:49], v[16:17], v[68:69]
	v_and_b32_e32 v61, 0xffff0000, v45
	v_pk_fma_f32 v[48:49], v[24:25], v[76:77], v[48:49]
	s_nop 0
	v_pk_fma_f32 v[44:45], v[8:9], v[60:61], v[48:49]
	s_nop 0
	v_pk_mul_f32 v[48:49], v[44:45], v[42:43]
	v_cvt_pk_bf16_f32 v42, v50, v51
	v_cvt_pk_bf16_f32 v43, v46, v47
	v_cvt_pk_bf16_f32 v44, v52, v53
	v_cvt_pk_bf16_f32 v45, v48, v49
	global_store_dwordx4 v[100:101], v[42:45], off offset:1024 sc0 sc1
	s_waitcnt vmcnt(9)
	v_lshlrev_b32_e32 v46, 16, v34
	v_and_b32_e32 v47, 0xffff0000, v34
	v_pk_mul_f32 v[44:45], v[10:11], v[54:55]
	s_waitcnt vmcnt(8)
	v_lshlrev_b32_e32 v42, 16, v38
	v_pk_fma_f32 v[44:45], v[18:19], v[62:63], v[44:45]
	v_and_b32_e32 v43, 0xffff0000, v38
	v_pk_fma_f32 v[44:45], v[2:3], v[46:47], v[44:45]
	v_lshlrev_b32_e32 v48, 16, v35
	v_pk_mul_f32 v[42:43], v[44:45], v[42:43]
	v_pk_mul_f32 v[44:45], v[12:13], v[56:57]
	v_and_b32_e32 v49, 0xffff0000, v35
	v_pk_fma_f32 v[44:45], v[20:21], v[64:65], v[44:45]
	v_lshlrev_b32_e32 v38, 16, v39
	v_pk_fma_f32 v[34:35], v[4:5], v[48:49], v[44:45]
	v_pk_mul_f32 v[44:45], v[14:15], v[58:59]
	v_and_b32_e32 v39, 0xffff0000, v39
	v_pk_fma_f32 v[44:45], v[22:23], v[66:67], v[44:45]
	v_lshlrev_b32_e32 v50, 16, v36
	v_and_b32_e32 v51, 0xffff0000, v36
	v_pk_mul_f32 v[38:39], v[34:35], v[38:39]
	v_lshlrev_b32_e32 v34, 16, v40
	v_and_b32_e32 v35, 0xffff0000, v40
	v_pk_fma_f32 v[44:45], v[6:7], v[50:51], v[44:45]
	v_lshlrev_b32_e32 v52, 16, v37
	v_pk_mul_f32 v[44:45], v[44:45], v[34:35]
	v_lshlrev_b32_e32 v34, 16, v41
	v_and_b32_e32 v35, 0xffff0000, v41
	v_pk_mul_f32 v[40:41], v[16:17], v[60:61]
	v_and_b32_e32 v53, 0xffff0000, v37
	v_pk_fma_f32 v[40:41], v[24:25], v[68:69], v[40:41]
	s_nop 0
	v_pk_fma_f32 v[36:37], v[8:9], v[52:53], v[40:41]
	s_nop 0
	v_pk_mul_f32 v[40:41], v[36:37], v[34:35]
	v_cvt_pk_bf16_f32 v34, v42, v43
	v_cvt_pk_bf16_f32 v35, v38, v39
	v_cvt_pk_bf16_f32 v36, v44, v45
	v_cvt_pk_bf16_f32 v37, v40, v41
	global_store_dwordx4 v[100:101], v[34:37], off offset:2048 sc0 sc1
	s_waitcnt vmcnt(8)
	v_lshlrev_b32_e32 v38, 16, v26
	v_and_b32_e32 v39, 0xffff0000, v26
	v_pk_mul_f32 v[36:37], v[10:11], v[46:47]
	s_waitcnt vmcnt(7)
	v_lshlrev_b32_e32 v34, 16, v30
	v_pk_fma_f32 v[36:37], v[18:19], v[54:55], v[36:37]
	v_and_b32_e32 v35, 0xffff0000, v30
	v_pk_fma_f32 v[36:37], v[2:3], v[38:39], v[36:37]
	v_lshlrev_b32_e32 v26, 16, v27
	v_pk_mul_f32 v[34:35], v[36:37], v[34:35]
	v_pk_mul_f32 v[36:37], v[12:13], v[48:49]
	v_and_b32_e32 v27, 0xffff0000, v27
	v_pk_fma_f32 v[36:37], v[20:21], v[56:57], v[36:37]
	v_lshlrev_b32_e32 v30, 16, v31
	v_pk_fma_f32 v[26:27], v[4:5], v[26:27], v[36:37]
	v_pk_mul_f32 v[36:37], v[14:15], v[50:51]
	v_and_b32_e32 v31, 0xffff0000, v31
	v_pk_fma_f32 v[36:37], v[22:23], v[58:59], v[36:37]
	v_lshlrev_b32_e32 v38, 16, v28
	v_and_b32_e32 v39, 0xffff0000, v28
	v_pk_mul_f32 v[30:31], v[26:27], v[30:31]
	v_lshlrev_b32_e32 v26, 16, v32
	v_and_b32_e32 v27, 0xffff0000, v32
	v_pk_fma_f32 v[36:37], v[6:7], v[38:39], v[36:37]
	v_lshlrev_b32_e32 v28, 16, v29
	v_pk_mul_f32 v[36:37], v[36:37], v[26:27]
	v_lshlrev_b32_e32 v26, 16, v33
	v_and_b32_e32 v27, 0xffff0000, v33
	v_pk_mul_f32 v[32:33], v[16:17], v[52:53]
	v_and_b32_e32 v29, 0xffff0000, v29
	v_pk_fma_f32 v[32:33], v[24:25], v[60:61], v[32:33]
	s_nop 0
	v_pk_fma_f32 v[28:29], v[8:9], v[28:29], v[32:33]
	s_nop 0
	v_pk_mul_f32 v[32:33], v[28:29], v[26:27]
	v_cvt_pk_bf16_f32 v26, v34, v35
	v_cvt_pk_bf16_f32 v27, v30, v31
	v_cvt_pk_bf16_f32 v28, v36, v37
	v_cvt_pk_bf16_f32 v29, v32, v33
	global_store_dwordx4 v[100:101], v[26:29], off offset:3072 sc0 sc1
	s_andn2_b64 exec, exec, s[14:15]
	s_cbranch_execz .LBB0_1178

.LBB0_1198:
	s_ashr_i32 s42, s47, 2
	s_mov_b32 s17, -1
	s_ashr_i32 s43, s42, 31
	s_lshl_b64 s[42:43], s[42:43], 21
	v_mbcnt_lo_u32_b32 v0, s17, 0
	v_mbcnt_hi_u32_b32 v138, s17, v0
	s_add_u32 s17, s93, s42
	s_addc_u32 s29, s94, s43
	s_lshl_b32 s42, s47, 19
	s_and_b32 s42, s42, 0x180000
	s_add_u32 s17, s17, s42
	s_addc_u32 s29, s29, 0
	s_ashr_i32 s47, s46, 31
	s_lshl_b64 s[42:43], s[46:47], 9
	s_add_u32 s17, s17, s42
	s_addc_u32 s29, s29, s43
	s_add_u32 s42, s17, s35
	s_addc_u32 s43, s29, 0
	v_and_b32_e32 v0, 0x70, v138
	v_lshl_add_u64 v[142:143], s[42:43], 0, v[0:1]
	v_and_or_b32 v0, v138, 15, s84
	v_lshl_add_u32 v144, s1, 8, v0
	v_ashrrev_i32_e32 v145, 31, v144
	v_lshlrev_b64 v[138:139], 11, v[144:145]
	v_pk_mul_f32 v[128:129], v[128:129], s[26:27] op_sel_hi:[1,0]
	v_pk_mul_f32 v[126:127], v[126:127], s[26:27] op_sel_hi:[1,0]
	v_pk_mul_f32 v[146:147], v[124:125], s[26:27] op_sel_hi:[1,0]
	v_pk_mul_f32 v[124:125], v[122:123], s[26:27] op_sel_hi:[1,0]
	v_lshl_add_u64 v[138:139], v[142:143], 0, v[138:139]
	v_cvt_pk_bf16_f32 v122, v126, v127
	v_cvt_pk_bf16_f32 v123, v128, v129
	v_cvt_pk_bf16_f32 v124, v124, v125
	v_cvt_pk_bf16_f32 v125, v146, v147
	global_store_dwordx4 v[138:139], v[122:125], off sc0 sc1
	v_pk_mul_f32 v[116:117], v[116:117], s[26:27] op_sel_hi:[1,0]
	v_pk_mul_f32 v[114:115], v[114:115], s[26:27] op_sel_hi:[1,0]
	v_pk_mul_f32 v[122:123], v[108:109], s[26:27] op_sel_hi:[1,0]
	v_pk_mul_f32 v[108:109], v[106:107], s[26:27] op_sel_hi:[1,0]
	v_cvt_pk_bf16_f32 v106, v114, v115
	v_cvt_pk_bf16_f32 v107, v116, v117
	v_cvt_pk_bf16_f32 v108, v108, v109
	v_cvt_pk_bf16_f32 v109, v122, v123
	global_store_dwordx4 v[138:139], v[106:109], off offset:256 sc0 sc1
	v_pk_mul_f32 v[112:113], v[112:113], s[26:27] op_sel_hi:[1,0]
	v_pk_mul_f32 v[110:111], v[110:111], s[26:27] op_sel_hi:[1,0]
	v_or_b32_e32 v106, 16, v144
	v_ashrrev_i32_e32 v107, 31, v106
	v_lshlrev_b64 v[106:107], 11, v[106:107]
	v_lshl_add_u64 v[114:115], v[142:143], 0, v[106:107]
	v_pk_mul_f32 v[108:109], v[120:121], s[26:27] op_sel_hi:[1,0]
	v_pk_mul_f32 v[106:107], v[118:119], s[26:27] op_sel_hi:[1,0]
	v_pk_mul_f32 v[100:101], v[100:101], s[26:27] op_sel_hi:[1,0]
	v_cvt_pk_bf16_f32 v106, v106, v107
	v_cvt_pk_bf16_f32 v107, v108, v109
	v_cvt_pk_bf16_f32 v108, v110, v111
	v_cvt_pk_bf16_f32 v109, v112, v113
	global_store_dwordx4 v[114:115], v[106:109], off sc0 sc1
	v_pk_mul_f32 v[98:99], v[98:99], s[26:27] op_sel_hi:[1,0]
	v_pk_mul_f32 v[96:97], v[96:97], s[26:27] op_sel_hi:[1,0]
	v_pk_mul_f32 v[106:107], v[92:93], s[26:27] op_sel_hi:[1,0]
	v_pk_mul_f32 v[92:93], v[90:91], s[26:27] op_sel_hi:[1,0]
	v_cvt_pk_bf16_f32 v90, v98, v99
	v_cvt_pk_bf16_f32 v91, v100, v101
	v_cvt_pk_bf16_f32 v92, v92, v93
	v_cvt_pk_bf16_f32 v93, v106, v107
	global_store_dwordx4 v[114:115], v[90:93], off offset:256 sc0 sc1
	v_pk_mul_f32 v[94:95], v[94:95], s[26:27] op_sel_hi:[1,0]
	v_pk_mul_f32 v[84:85], v[84:85], s[26:27] op_sel_hi:[1,0]
	v_or_b32_e32 v90, 32, v144
	v_ashrrev_i32_e32 v91, 31, v90
	v_lshlrev_b64 v[90:91], 11, v[90:91]
	v_lshl_add_u64 v[98:99], v[142:143], 0, v[90:91]
	v_pk_mul_f32 v[92:93], v[104:105], s[26:27] op_sel_hi:[1,0]
	v_pk_mul_f32 v[90:91], v[102:103], s[26:27] op_sel_hi:[1,0]
	v_pk_mul_f32 v[82:83], v[82:83], s[26:27] op_sel_hi:[1,0]
	v_cvt_pk_bf16_f32 v90, v90, v91
	v_cvt_pk_bf16_f32 v91, v92, v93
	v_cvt_pk_bf16_f32 v92, v94, v95
	v_cvt_pk_bf16_f32 v93, v96, v97
	global_store_dwordx4 v[98:99], v[90:93], off sc0 sc1
	v_pk_mul_f32 v[80:81], v[80:81], s[26:27] op_sel_hi:[1,0]
	v_pk_mul_f32 v[78:79], v[78:79], s[26:27] op_sel_hi:[1,0]
	v_pk_mul_f32 v[90:91], v[76:77], s[26:27] op_sel_hi:[1,0]
	v_pk_mul_f32 v[76:77], v[74:75], s[26:27] op_sel_hi:[1,0]
	v_cvt_pk_bf16_f32 v74, v82, v83
	v_cvt_pk_bf16_f32 v75, v84, v85
	v_cvt_pk_bf16_f32 v76, v76, v77
	v_cvt_pk_bf16_f32 v77, v90, v91
	global_store_dwordx4 v[98:99], v[74:77], off offset:256 sc0 sc1
	v_pk_mul_f32 v[72:73], v[72:73], s[26:27] op_sel_hi:[1,0]
	v_pk_mul_f32 v[70:71], v[70:71], s[26:27] op_sel_hi:[1,0]
	v_or_b32_e32 v74, 48, v144
	v_ashrrev_i32_e32 v75, 31, v74
	v_lshlrev_b64 v[74:75], 11, v[74:75]
	v_lshl_add_u64 v[82:83], v[142:143], 0, v[74:75]
	v_pk_mul_f32 v[76:77], v[88:89], s[26:27] op_sel_hi:[1,0]
	v_pk_mul_f32 v[74:75], v[86:87], s[26:27] op_sel_hi:[1,0]
	v_pk_mul_f32 v[62:63], v[62:63], s[26:27] op_sel_hi:[1,0]
	v_cvt_pk_bf16_f32 v74, v74, v75
	v_cvt_pk_bf16_f32 v75, v76, v77
	v_cvt_pk_bf16_f32 v76, v78, v79
	v_cvt_pk_bf16_f32 v77, v80, v81
	global_store_dwordx4 v[82:83], v[74:77], off sc0 sc1
	s_mov_b32 s1, 0x40000
	v_pk_mul_f32 v[64:65], v[64:65], s[26:27] op_sel_hi:[1,0]
	v_pk_mul_f32 v[74:75], v[68:69], s[26:27] op_sel_hi:[1,0]
	v_pk_mul_f32 v[68:69], v[66:67], s[26:27] op_sel_hi:[1,0]
	v_cvt_pk_bf16_f32 v66, v70, v71
	v_cvt_pk_bf16_f32 v67, v72, v73
	v_cvt_pk_bf16_f32 v68, v68, v69
	v_cvt_pk_bf16_f32 v69, v74, v75
	global_store_dwordx4 v[82:83], v[66:69], off offset:256 sc0 sc1
	v_pk_mul_f32 v[52:53], v[52:53], s[26:27] op_sel_hi:[1,0]
	v_pk_mul_f32 v[50:51], v[50:51], s[26:27] op_sel_hi:[1,0]
	v_pk_mul_f32 v[68:69], v[60:61], s[26:27] op_sel_hi:[1,0]
	v_pk_mul_f32 v[60:61], v[58:59], s[26:27] op_sel_hi:[1,0]
	v_cvt_pk_bf16_f32 v58, v62, v63
	v_add_co_u32_e32 v62, vcc, s1, v138
	v_cvt_pk_bf16_f32 v59, v64, v65
	v_cvt_pk_bf16_f32 v60, v60, v61
	v_cvt_pk_bf16_f32 v61, v68, v69
	v_addc_co_u32_e32 v63, vcc, 0, v139, vcc
	global_store_dwordx4 v[62:63], v[58:61], off sc0 sc1
	v_lshl_add_u64 v[66:67], v[138:139], 0, s[20:21]
	v_pk_mul_f32 v[46:47], v[46:47], s[26:27] op_sel_hi:[1,0]
	v_pk_mul_f32 v[58:59], v[44:45], s[26:27] op_sel_hi:[1,0]
	v_pk_mul_f32 v[44:45], v[42:43], s[26:27] op_sel_hi:[1,0]
	v_cvt_pk_bf16_f32 v42, v50, v51
	v_cvt_pk_bf16_f32 v43, v52, v53
	v_cvt_pk_bf16_f32 v44, v44, v45
	v_cvt_pk_bf16_f32 v45, v58, v59
	global_store_dwordx4 v[66:67], v[42:45], off offset:256 sc0 sc1
	s_mov_b32 s1, 0x48000
	v_pk_mul_f32 v[48:49], v[48:49], s[26:27] op_sel_hi:[1,0]
	v_pk_mul_f32 v[44:45], v[56:57], s[26:27] op_sel_hi:[1,0]
	v_pk_mul_f32 v[42:43], v[54:55], s[26:27] op_sel_hi:[1,0]
	s_mov_b64 s[42:43], 0x48000
	v_cvt_pk_bf16_f32 v42, v42, v43
	v_cvt_pk_bf16_f32 v43, v44, v45
	v_cvt_pk_bf16_f32 v44, v46, v47
	v_add_co_u32_e32 v46, vcc, s1, v138
	v_cvt_pk_bf16_f32 v45, v48, v49
	s_nop 0
	v_addc_co_u32_e32 v47, vcc, 0, v139, vcc
	global_store_dwordx4 v[46:47], v[42:45], off sc0 sc1
	v_pk_mul_f32 v[36:37], v[36:37], s[26:27] op_sel_hi:[1,0]
	v_pk_mul_f32 v[34:35], v[34:35], s[26:27] op_sel_hi:[1,0]
	v_pk_mul_f32 v[42:43], v[28:29], s[26:27] op_sel_hi:[1,0]
	v_pk_mul_f32 v[28:29], v[26:27], s[26:27] op_sel_hi:[1,0]
	v_lshl_add_u64 v[50:51], v[138:139], 0, s[42:43]
	v_cvt_pk_bf16_f32 v26, v34, v35
	v_cvt_pk_bf16_f32 v27, v36, v37
	v_cvt_pk_bf16_f32 v28, v28, v29
	v_cvt_pk_bf16_f32 v29, v42, v43
	global_store_dwordx4 v[50:51], v[26:29], off offset:256 sc0 sc1
	v_pk_mul_f32 v[30:31], v[30:31], s[26:27] op_sel_hi:[1,0]
	s_mov_b32 s1, 0x50000
	v_pk_mul_f32 v[28:29], v[40:41], s[26:27] op_sel_hi:[1,0]
	v_pk_mul_f32 v[26:27], v[38:39], s[26:27] op_sel_hi:[1,0]
	v_pk_mul_f32 v[32:33], v[32:33], s[26:27] op_sel_hi:[1,0]
	v_cvt_pk_bf16_f32 v26, v26, v27
	v_cvt_pk_bf16_f32 v27, v28, v29
	v_cvt_pk_bf16_f32 v28, v30, v31
	v_add_co_u32_e32 v30, vcc, s1, v138
	v_cvt_pk_bf16_f32 v29, v32, v33
	s_nop 0
	v_addc_co_u32_e32 v31, vcc, 0, v139, vcc
	global_store_dwordx4 v[30:31], v[26:29], off sc0 sc1
	v_pk_mul_f32 v[20:21], v[20:21], s[26:27] op_sel_hi:[1,0]
	v_pk_mul_f32 v[18:19], v[18:19], s[26:27] op_sel_hi:[1,0]
	v_pk_mul_f32 v[26:27], v[12:13], s[26:27] op_sel_hi:[1,0]
	v_pk_mul_f32 v[12:13], v[10:11], s[26:27] op_sel_hi:[1,0]
	v_lshl_add_u64 v[34:35], v[138:139], 0, s[22:23]
	v_cvt_pk_bf16_f32 v10, v18, v19
	v_cvt_pk_bf16_f32 v11, v20, v21
	v_cvt_pk_bf16_f32 v12, v12, v13
	v_cvt_pk_bf16_f32 v13, v26, v27
	global_store_dwordx4 v[34:35], v[10:13], off offset:256 sc0 sc1
	v_pk_mul_f32 v[14:15], v[14:15], s[26:27] op_sel_hi:[1,0]
	s_mov_b32 s1, 0x58000
	v_pk_mul_f32 v[12:13], v[24:25], s[26:27] op_sel_hi:[1,0]
	v_pk_mul_f32 v[10:11], v[22:23], s[26:27] op_sel_hi:[1,0]
	v_pk_mul_f32 v[16:17], v[16:17], s[26:27] op_sel_hi:[1,0]
	v_cvt_pk_bf16_f32 v10, v10, v11
	v_cvt_pk_bf16_f32 v11, v12, v13
	v_cvt_pk_bf16_f32 v12, v14, v15
	v_add_co_u32_e32 v14, vcc, s1, v138
	v_cvt_pk_bf16_f32 v13, v16, v17
	s_nop 0
	v_addc_co_u32_e32 v15, vcc, 0, v139, vcc
	s_mov_b64 s[42:43], 0x58000
	global_store_dwordx4 v[14:15], v[10:13], off sc0 sc1
	v_pk_mul_f32 v[8:9], v[8:9], s[26:27] op_sel_hi:[1,0]
	v_pk_mul_f32 v[6:7], v[6:7], s[26:27] op_sel_hi:[1,0]
	v_pk_mul_f32 v[10:11], v[4:5], s[26:27] op_sel_hi:[1,0]
	v_pk_mul_f32 v[4:5], v[2:3], s[26:27] op_sel_hi:[1,0]
	v_lshl_add_u64 v[18:19], v[138:139], 0, s[42:43]
	v_cvt_pk_bf16_f32 v2, v6, v7
	v_cvt_pk_bf16_f32 v3, v8, v9
	v_cvt_pk_bf16_f32 v4, v4, v5
	v_cvt_pk_bf16_f32 v5, v10, v11
	s_and_b64 vcc, exec, s[36:37]
	s_mov_b64 s[36:37], -1
	global_store_dwordx4 v[18:19], v[2:5], off offset:256 sc0 sc1
	s_cbranch_vccnz .LBB0_1189
	v_readlane_b32 s36, v253, 50
	v_readlane_b32 s37, v253, 51
	s_andn2_b64 vcc, exec, s[36:37]
	s_cbranch_vccnz .LBB0_1188
	s_barrier
	s_branch .LBB0_1188

.LBB0_1216:
	s_ashr_i32 s38, s47, 2
	s_mov_b32 s29, -1
	s_ashr_i32 s39, s38, 31
	s_lshl_b64 s[38:39], s[38:39], 21
	v_mbcnt_lo_u32_b32 v0, s29, 0
	v_mbcnt_hi_u32_b32 v142, s29, v0
	s_add_u32 s29, s93, s38
	s_addc_u32 s37, s94, s39
	s_lshl_b32 s38, s47, 9
	s_and_b32 s38, s38, 0x600
	s_add_u32 s29, s29, s38
	s_addc_u32 s37, s37, 0
	s_ashr_i32 s47, s46, 31
	s_lshl_b64 s[38:39], s[46:47], 9
	s_add_u32 s29, s29, s38
	s_addc_u32 s37, s37, s39
	s_add_u32 s38, s29, s35
	s_addc_u32 s39, s37, 0
	v_and_b32_e32 v0, 0x70, v142
	v_lshl_add_u64 v[140:141], s[38:39], 0, v[0:1]
	v_and_or_b32 v0, v142, 15, s84
	v_lshl_add_u32 v142, s1, 8, v0
	v_ashrrev_i32_e32 v143, 31, v142
	v_lshlrev_b64 v[144:145], 11, v[142:143]
	v_lshl_add_u64 v[144:145], v[140:141], 0, v[144:145]
	s_mov_b32 s1, 0x40000
	v_cvt_pk_bf16_f32 v62, v62, v63
	v_cvt_pk_bf16_f32 v63, v64, v65
	v_cvt_pk_bf16_f32 v64, v58, v59
	v_add_co_u32_e32 v58, vcc, s1, v144
	v_cvt_pk_bf16_f32 v70, v70, v71
	v_cvt_pk_bf16_f32 v71, v72, v73
	v_cvt_pk_bf16_f32 v72, v66, v67
	v_lshl_add_u64 v[66:67], v[144:145], 0, s[20:21]
	v_addc_co_u32_e32 v59, vcc, 0, v145, vcc
	v_cvt_pk_bf16_f32 v46, v46, v47
	v_cvt_pk_bf16_f32 v47, v48, v49
	v_cvt_pk_bf16_f32 v48, v42, v43
	v_cvt_pk_bf16_f32 v49, v44, v45
	s_mov_b32 s1, 0x48000
	global_store_dwordx4 v[66:67], v[46:49], off offset:256 sc0 sc1
	s_mov_b64 s[38:39], 0x48000
	v_cvt_pk_bf16_f32 v110, v110, v111
	v_add_co_u32_e32 v48, vcc, s1, v144
	v_cvt_pk_bf16_f32 v111, v112, v113
	v_cvt_pk_bf16_f32 v112, v106, v107
	v_or_b32_e32 v106, 16, v142
	v_lshl_add_u64 v[46:47], v[144:145], 0, s[38:39]
	v_addc_co_u32_e32 v49, vcc, 0, v145, vcc
	v_cvt_pk_bf16_f32 v30, v30, v31
	v_cvt_pk_bf16_f32 v31, v32, v33
	v_cvt_pk_bf16_f32 v32, v26, v27
	v_cvt_pk_bf16_f32 v33, v28, v29
	s_mov_b32 s1, 0x50000
	v_ashrrev_i32_e32 v107, 31, v106
	v_cvt_pk_bf16_f32 v94, v94, v95
	v_cvt_pk_bf16_f32 v95, v96, v97
	v_cvt_pk_bf16_f32 v96, v90, v91
	v_or_b32_e32 v90, 32, v142
	global_store_dwordx4 v[46:47], v[30:33], off offset:256 sc0 sc1
	v_cvt_pk_bf16_f32 v113, v108, v109
	v_lshlrev_b64 v[106:107], 11, v[106:107]
	v_add_co_u32_e32 v32, vcc, s1, v144
	v_ashrrev_i32_e32 v91, 31, v90
	v_cvt_pk_bf16_f32 v78, v78, v79
	v_cvt_pk_bf16_f32 v79, v80, v81
	v_cvt_pk_bf16_f32 v80, v74, v75
	v_or_b32_e32 v74, 48, v142
	v_lshl_add_u64 v[30:31], v[144:145], 0, s[22:23]
	v_addc_co_u32_e32 v33, vcc, 0, v145, vcc
	v_cvt_pk_bf16_f32 v14, v14, v15
	v_cvt_pk_bf16_f32 v15, v16, v17
	v_cvt_pk_bf16_f32 v16, v10, v11
	v_cvt_pk_bf16_f32 v17, v12, v13
	s_mov_b32 s1, 0x58000
	global_store_dwordx4 v[144:145], v[110:113], off offset:256 sc0 sc1
	v_cvt_pk_bf16_f32 v97, v92, v93
	v_lshlrev_b64 v[90:91], 11, v[90:91]
	v_lshl_add_u64 v[110:111], v[140:141], 0, v[106:107]
	v_ashrrev_i32_e32 v75, 31, v74
	global_store_dwordx4 v[30:31], v[14:17], off offset:256 sc0 sc1
	global_store_dwordx4 v[110:111], v[94:97], off offset:256 sc0 sc1
	v_cvt_pk_bf16_f32 v81, v76, v77
	v_add_co_u32_e32 v16, vcc, s1, v144
	v_lshl_add_u64 v[94:95], v[140:141], 0, v[90:91]
	v_lshlrev_b64 v[74:75], 11, v[74:75]
	s_mov_b64 s[38:39], 0x58000
	v_addc_co_u32_e32 v17, vcc, 0, v145, vcc
	v_cvt_pk_bf16_f32 v126, v126, v127
	v_cvt_pk_bf16_f32 v127, v128, v129
	v_cvt_pk_bf16_f32 v128, v122, v123
	v_cvt_pk_bf16_f32 v129, v124, v125
	v_cvt_pk_bf16_f32 v106, v118, v119
	v_cvt_pk_bf16_f32 v107, v120, v121
	v_cvt_pk_bf16_f32 v108, v114, v115
	v_cvt_pk_bf16_f32 v109, v116, v117
	v_cvt_pk_bf16_f32 v90, v102, v103
	v_cvt_pk_bf16_f32 v91, v104, v105
	v_cvt_pk_bf16_f32 v92, v98, v99
	v_cvt_pk_bf16_f32 v93, v100, v101
	global_store_dwordx4 v[94:95], v[78:81], off offset:256 sc0 sc1
	v_cvt_pk_bf16_f32 v76, v82, v83
	v_cvt_pk_bf16_f32 v77, v84, v85
	v_lshl_add_u64 v[78:79], v[140:141], 0, v[74:75]
	v_cvt_pk_bf16_f32 v74, v86, v87
	v_cvt_pk_bf16_f32 v75, v88, v89
	v_cvt_pk_bf16_f32 v73, v68, v69
	v_cvt_pk_bf16_f32 v65, v60, v61
	v_cvt_pk_bf16_f32 v42, v54, v55
	v_cvt_pk_bf16_f32 v43, v56, v57
	v_cvt_pk_bf16_f32 v44, v50, v51
	v_cvt_pk_bf16_f32 v45, v52, v53
	v_cvt_pk_bf16_f32 v26, v38, v39
	v_cvt_pk_bf16_f32 v27, v40, v41
	v_cvt_pk_bf16_f32 v28, v34, v35
	v_cvt_pk_bf16_f32 v29, v36, v37
	v_lshl_add_u64 v[14:15], v[144:145], 0, s[38:39]
	v_cvt_pk_bf16_f32 v10, v22, v23
	v_cvt_pk_bf16_f32 v11, v24, v25
	v_cvt_pk_bf16_f32 v12, v18, v19
	v_cvt_pk_bf16_f32 v13, v20, v21
	v_cvt_pk_bf16_f32 v6, v6, v7
	v_cvt_pk_bf16_f32 v7, v8, v9
	v_cvt_pk_bf16_f32 v8, v2, v3
	v_cvt_pk_bf16_f32 v9, v4, v5
	s_andn2_b64 vcc, exec, s[16:17]
	s_mov_b64 s[16:17], -1
	global_store_dwordx4 v[144:145], v[126:129], off sc0 sc1
	global_store_dwordx4 v[110:111], v[106:109], off sc0 sc1
	global_store_dwordx4 v[94:95], v[90:93], off sc0 sc1
	global_store_dwordx4 v[78:79], v[74:77], off sc0 sc1
	global_store_dwordx4 v[78:79], v[70:73], off offset:256 sc0 sc1
	global_store_dwordx4 v[58:59], v[62:65], off sc0 sc1
	global_store_dwordx4 v[48:49], v[42:45], off sc0 sc1
	global_store_dwordx4 v[32:33], v[26:29], off sc0 sc1
	global_store_dwordx4 v[16:17], v[10:13], off sc0 sc1
	global_store_dwordx4 v[14:15], v[6:9], off offset:256 sc0 sc1
	s_cbranch_vccnz .LBB0_1207
	v_readlane_b32 s16, v253, 50
	v_readlane_b32 s17, v253, 51
	s_andn2_b64 vcc, exec, s[16:17]
	s_cbranch_vccnz .LBB0_1206
	s_barrier
	s_branch .LBB0_1206

.LBB0_1986:
	v_cndmask_b32_e64 v4, 0, 1, s[46:47]
	v_cmp_ne_u32_e64 s[46:47], 0, v4
	v_cndmask_b32_e64 v4, 0, 1, s[42:43]
	v_cmp_ne_u32_e32 vcc, 0, v4
	s_and_saveexec_b64 s[42:43], s[38:39]
	s_cbranch_execz .LBB0_1983
	v_mov_b32_e32 v4, s46
	v_mov_b32_e32 v5, s47
	v_mov_b32_e32 v6, vcc_lo
	v_mov_b32_e32 v7, vcc_hi
	global_store_dwordx4 v1, v[4:7], s[44:45] sc0 sc1
	s_branch .LBB0_1983

.LBB0_1989:
	s_and_b64 vcc, exec, s[0:1]
	s_cbranch_vccz .LBB0_2111
	v_readlane_b32 s0, v253, 45
	s_cmp_eq_u32 s0, 0
	s_cbranch_scc0 .LBB0_2111
	v_readlane_b32 s0, v253, 41
	v_readlane_b32 s1, v253, 42
	s_andn2_b64 vcc, exec, s[0:1]
	s_cbranch_vccnz .LBB0_1995
	s_abs_i32 s1, s30
	s_mul_hi_u32 s14, s1, s27
	s_mul_i32 s14, s14, s33
	s_sub_i32 s1, s1, s14
	s_ashr_i32 s0, s30, 31
	s_sub_i32 s14, s1, s33
	s_cmp_ge_u32 s1, s33
	s_cselect_b32 s1, s14, s1
	s_sub_i32 s14, s1, s33
	s_cmp_ge_u32 s1, s33
	s_cselect_b32 s1, s14, s1
	s_xor_b32 s1, s1, s0
	s_sub_i32 s0, s1, s0
	s_ashr_i32 s1, s0, 31
	s_and_b32 s1, s1, s72
	s_add_i32 s0, s1, s0
	s_lshr_b32 s1, s0, 3
	s_and_b32 s14, s1, 31
	s_cmp_lt_u32 s14, 8
	s_cbranch_scc1 .LBB0_1994
	s_lshr_b32 s1, s1, 5
	s_mul_i32 s1, s1, 24
	s_add_i32 s1, s1, s14
	s_add_i32 s1, s1, -8
	s_and_b32 s0, s0, 7
	s_lshl_b32 s1, s1, 3
	s_or_b32 s0, s0, s1
	s_cmpk_gt_i32 s0, 0x57f
	s_cbranch_scc1 .LBB0_1994
	v_readlane_b32 s14, v253, 32
	s_lshl_b32 s14, s14, 14
	s_lshl_b64 s[16:17], s[86:87], 3
	v_readlane_b32 s34, v250, 3
	v_readlane_b32 s35, v250, 4
	s_add_u32 s16, s34, s16
	s_addc_u32 s17, s35, s17
	s_load_dwordx2 s[16:17], s[16:17], 0x90
	v_readlane_b32 s15, v253, 33
	v_readlane_b32 s15, v253, 38
	s_mul_hi_u32 s1, s15, 0xb00000
	s_mul_i32 s15, s15, 0xb00000
	s_waitcnt lgkmcnt(0)
	s_add_u32 s15, s16, s15
	s_addc_u32 s17, s17, s1
	s_ashr_i32 s1, s0, 31
	s_lshr_b32 s1, s1, 27
	s_add_i32 s1, s0, s1
	s_ashr_i32 s1, s1, 5
	s_lshl_b32 s16, s1, 6
	s_lshl_b32 s1, s1, 10
	s_lshl_b32 s0, s0, 5
	s_sub_i32 s0, s0, s1
	s_ashr_i32 s1, s0, 31
	s_waitcnt vmcnt(0)
	v_lshrrev_b32_e32 v35, 3, v198
	s_lshl_b64 s[34:35], s[0:1], 2
	s_waitcnt vmcnt(0)
	v_or_b32_e32 v30, s16, v35
	s_add_u32 s34, s15, s34
	v_lshlrev_b32_e32 v0, 4, v198
	s_addc_u32 s35, s17, s35
	v_and_b32_e32 v0, 0x70, v0
	v_ashrrev_i32_e32 v31, 31, v30
	v_or_b32_e32 v6, 8, v30
	v_lshl_add_u64 v[32:33], s[34:35], 0, v[0:1]
	v_lshlrev_b64 v[2:3], 12, v[30:31]
	v_ashrrev_i32_e32 v7, 31, v6
	v_lshl_add_u64 v[2:3], v[32:33], 0, v[2:3]
	v_lshlrev_b64 v[6:7], 12, v[6:7]
	v_or_b32_e32 v10, 16, v30
	global_load_dwordx4 v[2:5], v[2:3], off
	v_lshl_add_u64 v[6:7], v[32:33], 0, v[6:7]
	v_ashrrev_i32_e32 v11, 31, v10
	global_load_dwordx4 v[6:9], v[6:7], off
	v_lshlrev_b64 v[10:11], 12, v[10:11]
	v_or_b32_e32 v14, 24, v30
	v_lshl_add_u64 v[10:11], v[32:33], 0, v[10:11]
	v_ashrrev_i32_e32 v15, 31, v14
	global_load_dwordx4 v[10:13], v[10:11], off
	v_lshlrev_b64 v[14:15], 12, v[14:15]
	v_or_b32_e32 v18, 32, v30
	v_lshl_add_u64 v[14:15], v[32:33], 0, v[14:15]
	v_ashrrev_i32_e32 v19, 31, v18
	global_load_dwordx4 v[14:17], v[14:15], off
	v_lshlrev_b64 v[18:19], 12, v[18:19]
	v_or_b32_e32 v22, 40, v30
	v_lshl_add_u64 v[18:19], v[32:33], 0, v[18:19]
	v_ashrrev_i32_e32 v23, 31, v22
	global_load_dwordx4 v[18:21], v[18:19], off
	v_lshlrev_b64 v[22:23], 12, v[22:23]
	v_or_b32_e32 v26, 48, v30
	v_lshl_add_u64 v[22:23], v[32:33], 0, v[22:23]
	v_ashrrev_i32_e32 v27, 31, v26
	global_load_dwordx4 v[22:25], v[22:23], off
	v_lshlrev_b64 v[26:27], 12, v[26:27]
	v_or_b32_e32 v30, 56, v30
	v_lshl_add_u64 v[26:27], v[32:33], 0, v[26:27]
	v_ashrrev_i32_e32 v31, 31, v30
	global_load_dwordx4 v[26:29], v[26:27], off
	v_lshlrev_b64 v[30:31], 12, v[30:31]
	v_lshl_add_u64 v[30:31], v[32:33], 0, v[30:31]
	global_load_dwordx4 v[30:33], v[30:31], off
	s_mul_hi_i32 s1, s0, 0x1600
	s_mulk_i32 s0, 0x1600
	s_add_u32 s15, s74, s0
	s_addc_u32 s29, s75, s1
	s_ashr_i32 s17, s16, 31
	v_and_b32_e32 v0, 7, v235
	s_lshl_b64 s[0:1], s[16:17], 1
	v_lshlrev_b32_e32 v34, 4, v0
	s_add_u32 s0, s15, s0
	v_or_b32_e32 v36, s14, v34
	s_movk_i32 s15, 0x84
	v_mad_u32_u24 v36, v35, s15, v36
	v_mul_u32_u24_e32 v0, 0x420, v0
	s_addc_u32 s1, s29, s1
	s_waitcnt vmcnt(7)
	ds_write2_b32 v36, v2, v3 offset1:1
	ds_write2_b32 v36, v4, v5 offset0:2 offset1:3
	v_add_u32_e32 v2, 0x420, v36
	s_waitcnt vmcnt(6)
	ds_write2_b32 v2, v6, v7 offset1:1
	v_add_u32_e32 v2, 0x428, v36
	ds_write2_b32 v2, v8, v9 offset1:1
	v_add_u32_e32 v2, 0x840, v36
	s_waitcnt vmcnt(5)
	ds_write2_b32 v2, v10, v11 offset1:1
	v_add_u32_e32 v2, 0x848, v36
	ds_write2_b32 v2, v12, v13 offset1:1
	v_add_u32_e32 v2, 0xc60, v36
	s_waitcnt vmcnt(4)
	ds_write2_b32 v2, v14, v15 offset1:1
	v_add_u32_e32 v2, 0xc68, v36
	ds_write2_b32 v2, v16, v17 offset1:1
	v_add_u32_e32 v2, 0x1080, v36
	s_waitcnt vmcnt(3)
	ds_write2_b32 v2, v18, v19 offset1:1
	v_add_u32_e32 v2, 0x1088, v36
	ds_write2_b32 v2, v20, v21 offset1:1
	v_add_u32_e32 v2, 0x14a0, v36
	s_waitcnt vmcnt(2)
	ds_write2_b32 v2, v22, v23 offset1:1
	v_add_u32_e32 v2, 0x14a8, v36
	ds_write2_b32 v2, v24, v25 offset1:1
	v_add_u32_e32 v2, 0x18c0, v36
	s_waitcnt vmcnt(1)
	ds_write2_b32 v2, v26, v27 offset1:1
	v_add_u32_e32 v2, 0x18c8, v36
	ds_write2_b32 v2, v28, v29 offset1:1
	v_add_u32_e32 v2, 0x1ce0, v36
	s_waitcnt vmcnt(0)
	ds_write2_b32 v2, v30, v31 offset1:1
	v_add_u32_e32 v2, 0x1ce8, v36
	ds_write2_b32 v2, v32, v33 offset1:1
	s_waitcnt lgkmcnt(0)
	v_lshlrev_b32_e32 v2, 2, v35
	v_or3_b32 v26, s14, v0, v2
	v_mul_u32_u24_e32 v0, 0xb00, v35
	ds_read2_b32 v[6:7], v26 offset0:33 offset1:41
	ds_read2_b32 v[8:9], v26 offset1:8
	ds_read2_b32 v[10:11], v26 offset0:66 offset1:74
	ds_read2_b32 v[12:13], v26 offset0:99 offset1:107
	ds_read2_b32 v[14:15], v26 offset0:132 offset1:140
	ds_read2_b32 v[16:17], v26 offset0:165 offset1:173
	ds_read2_b32 v[18:19], v26 offset0:198 offset1:206
	ds_read2_b32 v[20:21], v26 offset0:231 offset1:239
	v_lshlrev_b32_e32 v0, 1, v0
	v_lshl_add_u64 v[22:23], s[0:1], 0, v[0:1]
	v_mov_b32_e32 v35, v1
	v_lshl_add_u64 v[22:23], v[22:23], 0, v[34:35]
	s_mov_b32 s0, 0x1c00000
	v_add_co_u32_e32 v24, vcc, s0, v22
	s_mov_b32 s0, 0x1c0b000
	s_nop 0
	v_addc_co_u32_e32 v25, vcc, 0, v23, vcc
	s_waitcnt lgkmcnt(6)
	v_cvt_pk_bf16_f32 v2, v8, v6
	s_waitcnt lgkmcnt(4)
	v_cvt_pk_bf16_f32 v3, v10, v12
	s_waitcnt lgkmcnt(2)
	v_cvt_pk_bf16_f32 v4, v14, v16
	s_waitcnt lgkmcnt(0)
	v_cvt_pk_bf16_f32 v5, v18, v20
	v_add_co_u32_e32 v6, vcc, s0, v22
	global_store_dwordx4 v[24:25], v[2:5], off sc0 sc1
	s_mov_b32 s0, 0x1c16000
	s_nop 0
	v_cvt_pk_bf16_f32 v2, v9, v7
	v_cvt_pk_bf16_f32 v3, v11, v13
	v_cvt_pk_bf16_f32 v4, v15, v17
	v_cvt_pk_bf16_f32 v5, v19, v21
	v_addc_co_u32_e32 v7, vcc, 0, v23, vcc
	global_store_dwordx4 v[6:7], v[2:5], off sc0 sc1
	ds_read2_b32 v[6:7], v26 offset0:49 offset1:57
	ds_read2_b32 v[8:9], v26 offset0:16 offset1:24
	ds_read2_b32 v[10:11], v26 offset0:82 offset1:90
	ds_read2_b32 v[12:13], v26 offset0:115 offset1:123
	ds_read2_b32 v[14:15], v26 offset0:148 offset1:156
	ds_read2_b32 v[16:17], v26 offset0:181 offset1:189
	ds_read2_b32 v[18:19], v26 offset0:214 offset1:222
	ds_read2_b32 v[20:21], v26 offset0:247 offset1:255
	v_add_co_u32_e32 v24, vcc, s0, v22
	s_waitcnt lgkmcnt(6)
	v_cvt_pk_bf16_f32 v2, v8, v6
	v_addc_co_u32_e32 v25, vcc, 0, v23, vcc
	s_waitcnt lgkmcnt(4)
	v_cvt_pk_bf16_f32 v3, v10, v12
	s_waitcnt lgkmcnt(2)
	v_cvt_pk_bf16_f32 v4, v14, v16
	s_waitcnt lgkmcnt(0)
	v_cvt_pk_bf16_f32 v5, v18, v20
	v_add_co_u32_e32 v6, vcc, 0x1c21000, v22
	global_store_dwordx4 v[24:25], v[2:5], off sc0 sc1
	s_nop 1
	v_cvt_pk_bf16_f32 v2, v9, v7
	v_cvt_pk_bf16_f32 v3, v11, v13
	v_cvt_pk_bf16_f32 v4, v15, v17
	v_cvt_pk_bf16_f32 v5, v19, v21
	v_addc_co_u32_e32 v7, vcc, 0, v23, vcc
	global_store_dwordx4 v[6:7], v[2:5], off sc0 sc1
	s_waitcnt lgkmcnt(0)

.LBB0_2009:
	s_waitcnt vmcnt(0)
	v_ffbh_u32_e32 v161, v157
	v_min_u32_e32 v161, 32, v161
	v_lshlrev_b64 v[156:157], v161, v[156:157]
	v_min_u32_e32 v156, 1, v156
	v_or_b32_e32 v156, v157, v156
	v_cvt_f32_u32_e32 v156, v156
	v_sub_u32_e32 v157, 32, v161
	s_mov_b32 s36, 0x358637bd
	v_mov_b64_e32 v[166:167], s[36:37]
	v_ldexp_f32 v157, v156, v157
	v_ffbh_u32_e32 v156, v155
	v_min_u32_e32 v156, 32, v156
	v_lshlrev_b64 v[154:155], v156, v[154:155]
	v_min_u32_e32 v154, 1, v154
	v_or_b32_e32 v154, v155, v154
	v_cvt_f32_u32_e32 v154, v154
	v_sub_u32_e32 v155, 32, v156
	s_mov_b32 s40, 0x32800000
	s_mov_b32 s29, -1
	v_ldexp_f32 v156, v154, v155
	v_pk_fma_f32 v[154:155], v[156:157], s[40:41], v[166:167] op_sel_hi:[1,0,0]
	s_movk_i32 s95, 0x100
	v_mul_f32_e32 v156, 0x4b800000, v155
	v_cmp_gt_f32_e64 s[36:37], s96, v155
	v_cmp_gt_f32_e32 vcc, s96, v154
	v_mbcnt_lo_u32_b32 v0, s29, 0
	v_cndmask_b32_e64 v155, v155, v156, s[36:37]
	v_rsq_f32_e32 v155, v155
	v_mbcnt_hi_u32_b32 v159, s29, v0
	s_lshl_b32 s29, s58, 8
	v_lshrrev_b32_e32 v160, 1, v159
	v_mul_f32_e32 v156, 0x45800000, v155
	v_cndmask_b32_e64 v156, v155, v156, s[36:37]
	v_mul_f32_e32 v155, 0x4b800000, v154
	v_cndmask_b32_e32 v154, v154, v155, vcc
	v_rsq_f32_e32 v154, v154
	v_and_b32_e32 v0, 15, v159
	s_add_i32 s29, s29, s34
	v_and_b32_e32 v160, 56, v160
	v_mul_f32_e32 v155, 0x45800000, v154
	v_cndmask_b32_e32 v154, v154, v155, vcc
	v_ffbh_u32_e32 v155, v153
	v_min_u32_e32 v155, 32, v155
	v_lshlrev_b64 v[152:153], v155, v[152:153]
	v_min_u32_e32 v152, 1, v152
	v_or_b32_e32 v152, v153, v152
	v_cvt_f32_u32_e32 v152, v152
	v_sub_u32_e32 v153, 32, v155
	v_or_b32_e32 v158, s29, v0
	v_add_u32_e32 v160, s85, v160
	v_ldexp_f32 v153, v152, v153
	v_ffbh_u32_e32 v152, v151
	v_min_u32_e32 v152, 32, v152
	v_lshlrev_b64 v[150:151], v152, v[150:151]
	v_min_u32_e32 v150, 1, v150
	v_or_b32_e32 v150, v151, v150
	v_cvt_f32_u32_e32 v150, v150
	v_sub_u32_e32 v151, 32, v152
	s_cmp_gt_i32 s50, 15
	v_ldexp_f32 v152, v150, v151
	v_pk_fma_f32 v[150:151], v[152:153], s[40:41], v[166:167] op_sel_hi:[1,0,0]
	s_nop 0
	v_mul_f32_e32 v152, 0x4b800000, v151
	v_cmp_gt_f32_e64 s[36:37], s96, v151
	v_cmp_gt_f32_e32 vcc, s96, v150
	s_nop 0
	v_cndmask_b32_e64 v151, v151, v152, s[36:37]
	v_rsq_f32_e32 v151, v151
	s_nop 0
	v_mul_f32_e32 v152, 0x45800000, v151
	v_cndmask_b32_e64 v152, v151, v152, s[36:37]
	v_mul_f32_e32 v151, 0x4b800000, v150
	v_cndmask_b32_e32 v150, v150, v151, vcc
	v_rsq_f32_e32 v150, v150
	s_nop 0
	v_mul_f32_e32 v151, 0x45800000, v150
	v_cndmask_b32_e32 v150, v150, v151, vcc
	v_ffbh_u32_e32 v151, v149
	v_min_u32_e32 v151, 32, v151
	v_lshlrev_b64 v[148:149], v151, v[148:149]
	v_min_u32_e32 v148, 1, v148
	v_or_b32_e32 v148, v149, v148
	v_cvt_f32_u32_e32 v148, v148
	v_sub_u32_e32 v149, 32, v151
	v_ldexp_f32 v149, v148, v149
	v_ffbh_u32_e32 v148, v147
	v_min_u32_e32 v148, 32, v148
	v_lshlrev_b64 v[146:147], v148, v[146:147]
	v_min_u32_e32 v146, 1, v146
	v_or_b32_e32 v146, v147, v146
	v_cvt_f32_u32_e32 v146, v146
	v_sub_u32_e32 v147, 32, v148
	v_ldexp_f32 v148, v146, v147
	v_pk_fma_f32 v[146:147], v[148:149], s[40:41], v[166:167] op_sel_hi:[1,0,0]
	s_nop 0
	v_mul_f32_e32 v148, 0x4b800000, v147
	v_cmp_gt_f32_e64 s[36:37], s96, v147
	v_cmp_gt_f32_e32 vcc, s96, v146
	s_nop 0
	v_cndmask_b32_e64 v147, v147, v148, s[36:37]
	v_rsq_f32_e32 v147, v147
	s_nop 0
	v_mul_f32_e32 v148, 0x45800000, v147
	v_cndmask_b32_e64 v148, v147, v148, s[36:37]
	v_mul_f32_e32 v147, 0x4b800000, v146
	v_cndmask_b32_e32 v146, v146, v147, vcc
	v_rsq_f32_e32 v146, v146
	s_nop 0
	v_mul_f32_e32 v147, 0x45800000, v146
	v_cndmask_b32_e32 v146, v146, v147, vcc
	v_ffbh_u32_e32 v147, v145
	v_min_u32_e32 v147, 32, v147
	v_lshlrev_b64 v[144:145], v147, v[144:145]
	v_min_u32_e32 v144, 1, v144
	v_or_b32_e32 v144, v145, v144
	v_cvt_f32_u32_e32 v144, v144
	v_sub_u32_e32 v145, 32, v147
	v_ldexp_f32 v145, v144, v145
	v_ffbh_u32_e32 v144, v143
	v_min_u32_e32 v144, 32, v144
	v_lshlrev_b64 v[142:143], v144, v[142:143]
	v_min_u32_e32 v142, 1, v142
	v_or_b32_e32 v142, v143, v142
	v_cvt_f32_u32_e32 v142, v142
	v_sub_u32_e32 v143, 32, v144
	v_ldexp_f32 v144, v142, v143
	v_pk_fma_f32 v[142:143], v[144:145], s[40:41], v[166:167] op_sel_hi:[1,0,0]
	s_nop 0
	v_mul_f32_e32 v144, 0x4b800000, v143
	v_cmp_gt_f32_e64 s[36:37], s96, v143
	v_cmp_gt_f32_e32 vcc, s96, v142
	s_nop 0
	v_cndmask_b32_e64 v143, v143, v144, s[36:37]
	v_rsq_f32_e32 v143, v143
	s_nop 0
	v_mul_f32_e32 v144, 0x45800000, v143
	v_cndmask_b32_e64 v144, v143, v144, s[36:37]
	v_mul_f32_e32 v143, 0x4b800000, v142
	v_cndmask_b32_e32 v142, v142, v143, vcc
	v_rsq_f32_e32 v142, v142
	s_mov_b64 s[36:37], -1
	v_mul_f32_e32 v143, 0x45800000, v142
	v_cndmask_b32_e32 v142, v142, v143, vcc
	s_cbranch_scc0 .LBB0_2021
	s_cmp_gt_u32 s50, 19
	s_cbranch_scc0 .LBB0_2018
	s_and_b64 vcc, exec, s[38:39]
	s_cbranch_vccz .LBB0_2015
	v_readlane_b32 s36, v253, 45
	v_cmp_gt_u32_e32 vcc, 16, v159
	v_readlane_b32 s37, v253, 46
	s_and_b64 s[40:41], s[36:37], vcc
	s_and_saveexec_b64 s[36:37], s[40:41]
	s_cbranch_execz .LBB0_2014
	v_ashrrev_i32_e32 v159, 31, v158
	v_lshlrev_b64 v[166:167], 5, v[158:159]
	v_mul_f32_e32 v172, 0x3d3504f3, v156
	v_lshl_add_u64 v[170:171], s[42:43], 0, v[166:167]
	v_pk_mul_f32 v[168:169], v[172:173], v[128:129] op_sel_hi:[0,1]
	v_pk_mul_f32 v[166:167], v[172:173], v[126:127] op_sel_hi:[0,1]
	global_store_dwordx4 v[170:171], v[166:169], off sc0 sc1
	v_mul_f32_e32 v174, 0x3d3504f3, v154
	s_mov_b64 s[40:41], 0x1000
	v_pk_mul_f32 v[168:169], v[172:173], v[124:125] op_sel_hi:[0,1]
	v_pk_mul_f32 v[166:167], v[172:173], v[122:123] op_sel_hi:[0,1]
	global_store_dwordx4 v[170:171], v[166:169], off offset:16 sc0 sc1
	s_nop 1
	v_or_b32_e32 v166, 16, v158
	v_ashrrev_i32_e32 v167, 31, v166
	v_lshlrev_b64 v[166:167], 5, v[166:167]
	v_lshl_add_u64 v[172:173], s[42:43], 0, v[166:167]
	v_pk_mul_f32 v[168:169], v[174:175], v[116:117] op_sel_hi:[0,1]
	v_pk_mul_f32 v[166:167], v[174:175], v[114:115] op_sel_hi:[0,1]
	global_store_dwordx4 v[172:173], v[166:169], off sc0 sc1
	s_nop 1
	v_pk_mul_f32 v[168:169], v[174:175], v[108:109] op_sel_hi:[0,1]
	v_pk_mul_f32 v[166:167], v[174:175], v[106:107] op_sel_hi:[0,1]
	global_store_dwordx4 v[172:173], v[166:169], off offset:16 sc0 sc1
	v_mul_f32_e32 v174, 0x3d3504f3, v152
	s_nop 0
	v_or_b32_e32 v166, 32, v158
	v_ashrrev_i32_e32 v167, 31, v166
	v_lshlrev_b64 v[166:167], 5, v[166:167]
	v_lshl_add_u64 v[172:173], s[42:43], 0, v[166:167]
	v_pk_mul_f32 v[168:169], v[174:175], v[100:101] op_sel_hi:[0,1]
	v_pk_mul_f32 v[166:167], v[174:175], v[98:99] op_sel_hi:[0,1]
	global_store_dwordx4 v[172:173], v[166:169], off sc0 sc1
	s_nop 1
	v_pk_mul_f32 v[168:169], v[174:175], v[92:93] op_sel_hi:[0,1]
	v_pk_mul_f32 v[166:167], v[174:175], v[90:91] op_sel_hi:[0,1]
	global_store_dwordx4 v[172:173], v[166:169], off offset:16 sc0 sc1
	v_mul_f32_e32 v174, 0x3d3504f3, v150
	s_nop 0
	v_or_b32_e32 v166, 48, v158
	v_ashrrev_i32_e32 v167, 31, v166
	v_lshlrev_b64 v[166:167], 5, v[166:167]
	v_lshl_add_u64 v[172:173], s[42:43], 0, v[166:167]
	v_pk_mul_f32 v[168:169], v[174:175], v[84:85] op_sel_hi:[0,1]
	v_pk_mul_f32 v[166:167], v[174:175], v[82:83] op_sel_hi:[0,1]
	global_store_dwordx4 v[172:173], v[166:169], off sc0 sc1
	s_nop 1
	v_pk_mul_f32 v[168:169], v[174:175], v[76:77] op_sel_hi:[0,1]
	v_pk_mul_f32 v[166:167], v[174:175], v[74:75] op_sel_hi:[0,1]
	global_store_dwordx4 v[172:173], v[166:169], off offset:16 sc0 sc1
	v_lshl_add_u64 v[172:173], v[170:171], 0, s[40:41]
	s_movk_i32 s40, 0x1000
	v_mul_f32_e32 v174, 0x3d3504f3, v148
	v_add_co_u32_e32 v176, vcc, s40, v170
	v_pk_mul_f32 v[168:169], v[174:175], v[64:65] op_sel_hi:[0,1]
	v_pk_mul_f32 v[166:167], v[174:175], v[62:63] op_sel_hi:[0,1]
	v_addc_co_u32_e32 v177, vcc, 0, v171, vcc
	global_store_dwordx4 v[176:177], v[166:169], off sc0 sc1
	s_mov_b64 s[40:41], 0x1200
	s_nop 0
	v_pk_mul_f32 v[168:169], v[174:175], v[60:61] op_sel_hi:[0,1]
	v_pk_mul_f32 v[166:167], v[174:175], v[58:59] op_sel_hi:[0,1]
	v_mul_f32_e32 v174, 0x3d3504f3, v146
	global_store_dwordx4 v[172:173], v[166:169], off offset:16 sc0 sc1
	v_lshl_add_u64 v[172:173], v[170:171], 0, s[40:41]
	s_mov_b64 s[40:41], 0x1400
	v_pk_mul_f32 v[168:169], v[174:175], v[56:57] op_sel_hi:[0,1]
	v_pk_mul_f32 v[166:167], v[174:175], v[54:55] op_sel_hi:[0,1]
	global_store_dwordx4 v[176:177], v[166:169], off offset:512 sc0 sc1
	s_nop 1
	v_pk_mul_f32 v[168:169], v[174:175], v[48:49] op_sel_hi:[0,1]
	v_pk_mul_f32 v[166:167], v[174:175], v[46:47] op_sel_hi:[0,1]
	v_mul_f32_e32 v174, 0x3d3504f3, v144
	global_store_dwordx4 v[172:173], v[166:169], off offset:16 sc0 sc1
	v_lshl_add_u64 v[172:173], v[170:171], 0, s[40:41]
	s_mov_b64 s[40:41], 0x1600
	v_pk_mul_f32 v[168:169], v[174:175], v[40:41] op_sel_hi:[0,1]
	v_pk_mul_f32 v[166:167], v[174:175], v[38:39] op_sel_hi:[0,1]
	global_store_dwordx4 v[176:177], v[166:169], off offset:1024 sc0 sc1
	v_lshl_add_u64 v[170:171], v[170:171], 0, s[40:41]
	s_nop 0
	v_pk_mul_f32 v[168:169], v[174:175], v[32:33] op_sel_hi:[0,1]
	v_pk_mul_f32 v[166:167], v[174:175], v[30:31] op_sel_hi:[0,1]
	global_store_dwordx4 v[172:173], v[166:169], off offset:16 sc0 sc1
	v_mul_f32_e32 v172, 0x3d3504f3, v142
	s_nop 0
	v_pk_mul_f32 v[168:169], v[172:173], v[24:25] op_sel_hi:[0,1]
	v_pk_mul_f32 v[166:167], v[172:173], v[22:23] op_sel_hi:[0,1]
	global_store_dwordx4 v[176:177], v[166:169], off offset:1536 sc0 sc1
	s_nop 1
	v_pk_mul_f32 v[168:169], v[172:173], v[16:17] op_sel_hi:[0,1]
	v_pk_mul_f32 v[166:167], v[172:173], v[14:15] op_sel_hi:[0,1]
	global_store_dwordx4 v[170:171], v[166:169], off offset:16 sc0 sc1

.LBB0_2015:
	s_andn2_b64 vcc, exec, s[36:37]
	s_cbranch_vccnz .LBB0_2017
	s_ashr_i32 s36, s29, 5
	s_ashr_i32 s37, s36, 31
	s_lshl_b64 s[40:41], s[36:37], 12
	v_pk_mul_f32 v[168:169], v[156:157], v[128:129] op_sel_hi:[0,1]
	v_pk_mul_f32 v[166:167], v[156:157], v[126:127] op_sel_hi:[0,1]
	v_pk_mul_f32 v[170:171], v[156:157], v[124:125] op_sel_hi:[0,1]
	v_pk_mul_f32 v[172:173], v[156:157], v[122:123] op_sel_hi:[0,1]
	s_add_u32 s40, s44, s40
	v_lshlrev_b32_e32 v145, 6, v160
	v_cvt_pk_bf16_f32 v166, v166, v167
	v_cvt_pk_bf16_f32 v167, v168, v169
	v_cvt_pk_bf16_f32 v168, v172, v173
	v_cvt_pk_bf16_f32 v169, v170, v171
	s_addc_u32 s41, s45, s41
	v_lshl_or_b32 v145, v0, 4, v145
	s_or_b32 s36, s36, 1
	global_store_dwordx4 v145, v[166:169], s[40:41] sc0 sc1
	v_pk_mul_f32 v[170:171], v[154:155], v[108:109] op_sel_hi:[0,1]
	v_pk_mul_f32 v[172:173], v[154:155], v[106:107] op_sel_hi:[0,1]
	v_pk_mul_f32 v[168:169], v[154:155], v[116:117] op_sel_hi:[0,1]
	v_pk_mul_f32 v[166:167], v[154:155], v[114:115] op_sel_hi:[0,1]
	s_ashr_i32 s37, s36, 31
	v_cvt_pk_bf16_f32 v166, v166, v167
	v_cvt_pk_bf16_f32 v167, v168, v169
	v_cvt_pk_bf16_f32 v168, v172, v173
	v_cvt_pk_bf16_f32 v169, v170, v171
	s_lshl_b64 s[36:37], s[36:37], 12
	global_store_dwordx4 v145, v[166:169], s[40:41] offset:256 sc0 sc1
	v_pk_mul_f32 v[170:171], v[152:153], v[92:93] op_sel_hi:[0,1]
	v_pk_mul_f32 v[172:173], v[152:153], v[90:91] op_sel_hi:[0,1]
	v_pk_mul_f32 v[168:169], v[152:153], v[100:101] op_sel_hi:[0,1]
	v_pk_mul_f32 v[166:167], v[152:153], v[98:99] op_sel_hi:[0,1]
	s_add_u32 s36, s44, s36
	v_cvt_pk_bf16_f32 v166, v166, v167
	v_cvt_pk_bf16_f32 v167, v168, v169
	v_cvt_pk_bf16_f32 v168, v172, v173
	v_cvt_pk_bf16_f32 v169, v170, v171
	s_addc_u32 s37, s45, s37
	global_store_dwordx4 v145, v[166:169], s[36:37] sc0 sc1
	v_or_b32_e32 v0, 48, v158
	v_pk_mul_f32 v[170:171], v[150:151], v[76:77] op_sel_hi:[0,1]
	v_pk_mul_f32 v[168:169], v[150:151], v[84:85] op_sel_hi:[0,1]
	v_pk_mul_f32 v[166:167], v[150:151], v[82:83] op_sel_hi:[0,1]
	v_cvt_pk_bf16_f32 v166, v166, v167
	v_cvt_pk_bf16_f32 v167, v168, v169
	v_cvt_pk_bf16_f32 v169, v170, v171
	v_ashrrev_i32_e32 v170, 5, v0
	v_lshlrev_b32_e32 v143, 5, v160
	v_ashrrev_i32_e32 v171, 31, v170
	v_lshlrev_b32_e32 v0, 3, v0
	s_movk_i32 s40, 0xf8
	s_add_i32 s36, s29, 0x80
	v_lshlrev_b64 v[170:171], 12, v[170:171]
	v_and_or_b32 v0, v0, s40, v143
	s_ashr_i32 s36, s36, 5
	v_pk_mul_f32 v[172:173], v[150:151], v[74:75] op_sel_hi:[0,1]
	v_lshl_add_u64 v[170:171], s[44:45], 0, v[170:171]
	v_lshlrev_b32_e32 v0, 1, v0
	s_ashr_i32 s37, s36, 31
	v_cvt_pk_bf16_f32 v168, v172, v173
	v_lshl_add_u64 v[170:171], v[170:171], 0, v[0:1]
	s_lshl_b64 s[36:37], s[36:37], 12
	global_store_dwordx4 v[170:171], v[166:169], off sc0 sc1
	v_pk_mul_f32 v[170:171], v[148:149], v[60:61] op_sel_hi:[0,1]
	v_pk_mul_f32 v[172:173], v[148:149], v[58:59] op_sel_hi:[0,1]
	v_pk_mul_f32 v[168:169], v[148:149], v[64:65] op_sel_hi:[0,1]
	v_pk_mul_f32 v[166:167], v[148:149], v[62:63] op_sel_hi:[0,1]
	s_add_u32 s36, s44, s36
	v_cvt_pk_bf16_f32 v166, v166, v167
	v_cvt_pk_bf16_f32 v167, v168, v169
	v_cvt_pk_bf16_f32 v168, v172, v173
	v_cvt_pk_bf16_f32 v169, v170, v171
	s_addc_u32 s37, s45, s37
	global_store_dwordx4 v145, v[166:169], s[36:37] sc0 sc1
	v_add_u32_e32 v0, 0x90, v158
	v_pk_mul_f32 v[170:171], v[146:147], v[48:49] op_sel_hi:[0,1]
	v_pk_mul_f32 v[168:169], v[146:147], v[56:57] op_sel_hi:[0,1]
	v_pk_mul_f32 v[166:167], v[146:147], v[54:55] op_sel_hi:[0,1]
	v_cvt_pk_bf16_f32 v166, v166, v167
	v_cvt_pk_bf16_f32 v167, v168, v169
	v_cvt_pk_bf16_f32 v169, v170, v171
	v_ashrrev_i32_e32 v170, 5, v0
	v_ashrrev_i32_e32 v171, 31, v170
	v_lshlrev_b32_e32 v0, 3, v0
	s_addk_i32 s29, 0xa0
	v_lshlrev_b64 v[170:171], 12, v[170:171]
	v_and_or_b32 v0, v0, s40, v143
	s_ashr_i32 s36, s29, 5
	v_pk_mul_f32 v[172:173], v[146:147], v[46:47] op_sel_hi:[0,1]
	v_lshl_add_u64 v[170:171], s[44:45], 0, v[170:171]
	v_lshlrev_b32_e32 v0, 1, v0
	s_ashr_i32 s37, s36, 31
	v_cvt_pk_bf16_f32 v168, v172, v173
	v_lshl_add_u64 v[170:171], v[170:171], 0, v[0:1]
	s_lshl_b64 s[36:37], s[36:37], 12
	global_store_dwordx4 v[170:171], v[166:169], off sc0 sc1
	v_pk_mul_f32 v[170:171], v[144:145], v[32:33] op_sel_hi:[0,1]
	v_pk_mul_f32 v[172:173], v[144:145], v[30:31] op_sel_hi:[0,1]
	v_pk_mul_f32 v[168:169], v[144:145], v[40:41] op_sel_hi:[0,1]
	v_pk_mul_f32 v[166:167], v[144:145], v[38:39] op_sel_hi:[0,1]
	s_add_u32 s36, s44, s36
	v_cvt_pk_bf16_f32 v166, v166, v167
	v_cvt_pk_bf16_f32 v167, v168, v169
	v_cvt_pk_bf16_f32 v168, v172, v173
	v_cvt_pk_bf16_f32 v169, v170, v171
	s_addc_u32 s37, s45, s37
	global_store_dwordx4 v145, v[166:169], s[36:37] sc0 sc1
	v_add_u32_e32 v0, 0xb0, v158
	v_pk_mul_f32 v[170:171], v[142:143], v[16:17] op_sel_hi:[0,1]
	v_pk_mul_f32 v[168:169], v[142:143], v[24:25] op_sel_hi:[0,1]
	v_pk_mul_f32 v[166:167], v[142:143], v[22:23] op_sel_hi:[0,1]
	v_cvt_pk_bf16_f32 v166, v166, v167
	v_cvt_pk_bf16_f32 v167, v168, v169
	v_cvt_pk_bf16_f32 v169, v170, v171
	v_ashrrev_i32_e32 v170, 5, v0
	v_ashrrev_i32_e32 v171, 31, v170
	v_lshlrev_b32_e32 v0, 3, v0
	v_lshlrev_b64 v[170:171], 12, v[170:171]
	v_and_or_b32 v0, v0, s40, v143
	v_pk_mul_f32 v[172:173], v[142:143], v[14:15] op_sel_hi:[0,1]
	v_lshl_add_u64 v[170:171], s[44:45], 0, v[170:171]
	v_lshlrev_b32_e32 v0, 1, v0
	v_cvt_pk_bf16_f32 v168, v172, v173
	v_lshl_add_u64 v[170:171], v[170:171], 0, v[0:1]
	global_store_dwordx4 v[170:171], v[166:169], off sc0 sc1

.LBB0_2018:
	s_andn2_b64 vcc, exec, s[36:37]
	s_cbranch_vccnz .LBB0_2020
	s_lshl_b32 s29, s50, 8
	s_add_u32 s36, s74, s29
	s_addc_u32 s37, s75, 0
	v_lshlrev_b32_e32 v0, 1, v160
	v_lshl_add_u64 v[166:167], s[36:37], 0, v[0:1]
	s_mov_b64 s[36:37], 0xd7ff000
	v_lshl_add_u64 v[170:171], v[166:167], 0, s[36:37]
	v_mul_f32_e32 v0, v156, v156
	v_pk_mul_f32 v[166:167], v[128:129], v[120:121]
	v_pk_mul_f32 v[168:169], v[126:127], v[118:119]
	v_pk_mul_f32 v[172:173], v[0:1], v[166:167] op_sel_hi:[0,1]
	v_pk_mul_f32 v[166:167], v[0:1], v[168:169] op_sel_hi:[0,1]
	v_pk_mul_f32 v[168:169], v[124:125], v[112:113]
	v_pk_mul_f32 v[174:175], v[122:123], v[110:111]
	v_ashrrev_i32_e32 v159, 31, v158
	v_pk_mul_f32 v[176:177], v[0:1], v[168:169] op_sel_hi:[0,1]
	v_pk_mul_f32 v[168:169], v[0:1], v[174:175] op_sel_hi:[0,1]
	v_cvt_pk_bf16_f32 v166, v166, v167
	v_cvt_pk_bf16_f32 v167, v172, v173
	v_lshlrev_b64 v[172:173], 10, v[158:159]
	v_cvt_pk_bf16_f32 v168, v168, v169
	v_cvt_pk_bf16_f32 v169, v176, v177
	v_lshl_add_u64 v[172:173], v[170:171], 0, v[172:173]
	global_store_dwordx4 v[172:173], v[166:169], off sc0 sc1
	v_mul_f32_e32 v0, v154, v154
	v_pk_mul_f32 v[176:177], v[106:107], v[94:95]
	v_pk_mul_f32 v[166:167], v[116:117], v[104:105]
	v_pk_mul_f32 v[168:169], v[114:115], v[102:103]
	v_pk_mul_f32 v[174:175], v[0:1], v[166:167] op_sel_hi:[0,1]
	v_pk_mul_f32 v[166:167], v[0:1], v[168:169] op_sel_hi:[0,1]
	v_cvt_pk_bf16_f32 v166, v166, v167
	v_cvt_pk_bf16_f32 v167, v174, v175
	v_or_b32_e32 v174, 16, v158
	v_pk_mul_f32 v[168:169], v[108:109], v[96:97]
	v_ashrrev_i32_e32 v175, 31, v174
	v_pk_mul_f32 v[178:179], v[0:1], v[168:169] op_sel_hi:[0,1]
	v_pk_mul_f32 v[168:169], v[0:1], v[176:177] op_sel_hi:[0,1]
	v_lshlrev_b64 v[174:175], 10, v[174:175]
	v_cvt_pk_bf16_f32 v168, v168, v169
	v_cvt_pk_bf16_f32 v169, v178, v179
	v_lshl_add_u64 v[174:175], v[170:171], 0, v[174:175]
	global_store_dwordx4 v[174:175], v[166:169], off sc0 sc1
	v_mul_f32_e32 v0, v152, v152
	v_pk_mul_f32 v[176:177], v[90:91], v[78:79]
	v_pk_mul_f32 v[166:167], v[100:101], v[88:89]
	v_pk_mul_f32 v[168:169], v[98:99], v[86:87]
	v_pk_mul_f32 v[174:175], v[0:1], v[166:167] op_sel_hi:[0,1]
	v_pk_mul_f32 v[166:167], v[0:1], v[168:169] op_sel_hi:[0,1]
	v_cvt_pk_bf16_f32 v166, v166, v167
	v_cvt_pk_bf16_f32 v167, v174, v175
	v_or_b32_e32 v174, 32, v158
	v_pk_mul_f32 v[168:169], v[92:93], v[80:81]
	v_ashrrev_i32_e32 v175, 31, v174
	v_pk_mul_f32 v[178:179], v[0:1], v[168:169] op_sel_hi:[0,1]
	v_pk_mul_f32 v[168:169], v[0:1], v[176:177] op_sel_hi:[0,1]
	v_lshlrev_b64 v[174:175], 10, v[174:175]
	v_cvt_pk_bf16_f32 v168, v168, v169
	v_cvt_pk_bf16_f32 v169, v178, v179
	v_lshl_add_u64 v[174:175], v[170:171], 0, v[174:175]
	global_store_dwordx4 v[174:175], v[166:169], off sc0 sc1
	v_mul_f32_e32 v0, v150, v150
	v_pk_mul_f32 v[176:177], v[74:75], v[66:67]
	v_pk_mul_f32 v[166:167], v[84:85], v[72:73]
	v_pk_mul_f32 v[168:169], v[82:83], v[70:71]
	v_pk_mul_f32 v[174:175], v[0:1], v[166:167] op_sel_hi:[0,1]
	v_pk_mul_f32 v[166:167], v[0:1], v[168:169] op_sel_hi:[0,1]
	v_cvt_pk_bf16_f32 v166, v166, v167
	v_cvt_pk_bf16_f32 v167, v174, v175
	v_or_b32_e32 v174, 48, v158
	v_pk_mul_f32 v[168:169], v[76:77], v[68:69]
	v_ashrrev_i32_e32 v175, 31, v174
	v_pk_mul_f32 v[178:179], v[0:1], v[168:169] op_sel_hi:[0,1]
	v_pk_mul_f32 v[168:169], v[0:1], v[176:177] op_sel_hi:[0,1]
	v_lshlrev_b64 v[174:175], 10, v[174:175]
	v_cvt_pk_bf16_f32 v168, v168, v169
	v_cvt_pk_bf16_f32 v169, v178, v179
	v_lshl_add_u64 v[170:171], v[170:171], 0, v[174:175]
	global_store_dwordx4 v[170:171], v[166:169], off sc0 sc1
	v_mul_f32_e32 v0, v148, v148
	v_pk_mul_f32 v[174:175], v[58:59], v[42:43]
	v_pk_mul_f32 v[166:167], v[64:65], v[52:53]
	v_pk_mul_f32 v[168:169], v[62:63], v[50:51]
	v_pk_mul_f32 v[170:171], v[0:1], v[166:167] op_sel_hi:[0,1]
	v_pk_mul_f32 v[166:167], v[0:1], v[168:169] op_sel_hi:[0,1]
	v_pk_mul_f32 v[168:169], v[60:61], v[44:45]
	s_mov_b32 s29, 0x20000
	v_pk_mul_f32 v[176:177], v[0:1], v[168:169] op_sel_hi:[0,1]
	v_pk_mul_f32 v[168:169], v[0:1], v[174:175] op_sel_hi:[0,1]
	v_cvt_pk_bf16_f32 v166, v166, v167
	v_cvt_pk_bf16_f32 v167, v170, v171
	v_add_co_u32_e32 v170, vcc, s29, v172
	v_cvt_pk_bf16_f32 v168, v168, v169
	v_cvt_pk_bf16_f32 v169, v176, v177
	v_addc_co_u32_e32 v171, vcc, 0, v173, vcc
	global_store_dwordx4 v[170:171], v[166:169], off sc0 sc1
	v_mul_f32_e32 v0, v146, v146
	v_pk_mul_f32 v[174:175], v[46:47], v[26:27]
	v_pk_mul_f32 v[166:167], v[56:57], v[36:37]
	v_pk_mul_f32 v[168:169], v[54:55], v[34:35]
	v_pk_mul_f32 v[170:171], v[0:1], v[166:167] op_sel_hi:[0,1]
	v_pk_mul_f32 v[166:167], v[0:1], v[168:169] op_sel_hi:[0,1]
	v_pk_mul_f32 v[168:169], v[48:49], v[28:29]
	s_mov_b32 s29, 0x24000
	v_pk_mul_f32 v[176:177], v[0:1], v[168:169] op_sel_hi:[0,1]
	v_pk_mul_f32 v[168:169], v[0:1], v[174:175] op_sel_hi:[0,1]
	v_cvt_pk_bf16_f32 v166, v166, v167
	v_cvt_pk_bf16_f32 v167, v170, v171
	v_add_co_u32_e32 v170, vcc, s29, v172
	v_cvt_pk_bf16_f32 v168, v168, v169
	v_cvt_pk_bf16_f32 v169, v176, v177
	v_addc_co_u32_e32 v171, vcc, 0, v173, vcc
	global_store_dwordx4 v[170:171], v[166:169], off sc0 sc1
	v_mul_f32_e32 v0, v144, v144
	v_pk_mul_f32 v[174:175], v[30:31], v[10:11]
	v_pk_mul_f32 v[166:167], v[40:41], v[20:21]
	v_pk_mul_f32 v[168:169], v[38:39], v[18:19]
	v_pk_mul_f32 v[170:171], v[0:1], v[166:167] op_sel_hi:[0,1]
	v_pk_mul_f32 v[166:167], v[0:1], v[168:169] op_sel_hi:[0,1]
	v_pk_mul_f32 v[168:169], v[32:33], v[12:13]
	s_mov_b32 s29, 0x28000
	v_pk_mul_f32 v[176:177], v[0:1], v[168:169] op_sel_hi:[0,1]
	v_pk_mul_f32 v[168:169], v[0:1], v[174:175] op_sel_hi:[0,1]
	v_cvt_pk_bf16_f32 v166, v166, v167
	v_cvt_pk_bf16_f32 v167, v170, v171
	v_add_co_u32_e32 v170, vcc, s29, v172
	v_cvt_pk_bf16_f32 v168, v168, v169
	v_cvt_pk_bf16_f32 v169, v176, v177
	v_addc_co_u32_e32 v171, vcc, 0, v173, vcc
	global_store_dwordx4 v[170:171], v[166:169], off sc0 sc1
	v_mul_f32_e32 v0, v142, v142
	v_pk_mul_f32 v[174:175], v[14:15], v[2:3]
	v_pk_mul_f32 v[166:167], v[24:25], v[8:9]
	v_pk_mul_f32 v[168:169], v[22:23], v[6:7]
	v_pk_mul_f32 v[170:171], v[0:1], v[166:167] op_sel_hi:[0,1]
	v_pk_mul_f32 v[166:167], v[0:1], v[168:169] op_sel_hi:[0,1]
	v_pk_mul_f32 v[168:169], v[16:17], v[4:5]
	v_cvt_pk_bf16_f32 v166, v166, v167
	v_pk_mul_f32 v[176:177], v[0:1], v[168:169] op_sel_hi:[0,1]
	v_pk_mul_f32 v[168:169], v[0:1], v[174:175] op_sel_hi:[0,1]
	v_cvt_pk_bf16_f32 v167, v170, v171
	v_add_co_u32_e32 v170, vcc, 0x2c000, v172
	v_cvt_pk_bf16_f32 v168, v168, v169
	v_cvt_pk_bf16_f32 v169, v176, v177
	v_addc_co_u32_e32 v171, vcc, 0, v173, vcc
	global_store_dwordx4 v[170:171], v[166:169], off sc0 sc1

.LBB0_2042:
	s_cmp_eq_u32 s29, 3
	s_cselect_b64 s[40:41], -1, 0
	s_or_b64 vcc, s[36:37], s[40:41]
	s_add_u32 s29, s74, s60
	s_addc_u32 s37, s75, s61
	s_lshl_b32 s36, s50, 9
	s_and_b32 s36, s36, 0x200
	v_mov_b32_e32 v0, 0x3e38aa3b
	s_add_u32 s36, s29, s36
	v_cndmask_b32_e32 v143, 1.0, v0, vcc
	s_addc_u32 s37, s37, 0
	v_lshlrev_b32_e32 v0, 1, v160
	v_lshl_add_u64 v[166:167], s[36:37], 0, v[0:1]
	v_ashrrev_i32_e32 v159, 31, v158
	v_mul_f32_e32 v0, v143, v156
	v_lshlrev_b64 v[160:161], 10, v[158:159]
	v_pk_mul_f32 v[128:129], v[0:1], v[128:129] op_sel_hi:[0,1]
	v_pk_mul_f32 v[126:127], v[0:1], v[126:127] op_sel_hi:[0,1]
	v_pk_mul_f32 v[156:157], v[0:1], v[124:125] op_sel_hi:[0,1]
	v_pk_mul_f32 v[124:125], v[0:1], v[122:123] op_sel_hi:[0,1]
	v_lshl_add_u64 v[160:161], v[166:167], 0, v[160:161]
	v_cvt_pk_bf16_f32 v122, v126, v127
	v_cvt_pk_bf16_f32 v123, v128, v129
	v_cvt_pk_bf16_f32 v124, v124, v125
	v_cvt_pk_bf16_f32 v125, v156, v157
	global_store_dwordx4 v[160:161], v[122:125], off sc0 sc1
	v_pk_mul_f32 v[120:121], v[0:1], v[120:121] op_sel_hi:[0,1]
	v_pk_mul_f32 v[118:119], v[0:1], v[118:119] op_sel_hi:[0,1]
	v_pk_mul_f32 v[122:123], v[0:1], v[112:113] op_sel_hi:[0,1]
	v_pk_mul_f32 v[112:113], v[0:1], v[110:111] op_sel_hi:[0,1]
	v_cvt_pk_bf16_f32 v110, v118, v119
	v_cvt_pk_bf16_f32 v111, v120, v121
	v_cvt_pk_bf16_f32 v112, v112, v113
	v_cvt_pk_bf16_f32 v113, v122, v123
	global_store_dwordx4 v[160:161], v[110:113], off offset:256 sc0 sc1
	v_mul_f32_e32 v0, v143, v154
	v_pk_mul_f32 v[114:115], v[0:1], v[114:115] op_sel_hi:[0,1]
	v_or_b32_e32 v110, 16, v158
	v_ashrrev_i32_e32 v111, 31, v110
	v_lshlrev_b64 v[110:111], 10, v[110:111]
	v_pk_mul_f32 v[112:113], v[0:1], v[116:117] op_sel_hi:[0,1]
	v_pk_mul_f32 v[116:117], v[0:1], v[108:109] op_sel_hi:[0,1]
	v_pk_mul_f32 v[108:109], v[0:1], v[106:107] op_sel_hi:[0,1]
	v_lshl_add_u64 v[110:111], v[166:167], 0, v[110:111]
	v_cvt_pk_bf16_f32 v106, v114, v115
	v_cvt_pk_bf16_f32 v107, v112, v113
	v_cvt_pk_bf16_f32 v108, v108, v109
	v_cvt_pk_bf16_f32 v109, v116, v117
	global_store_dwordx4 v[110:111], v[106:109], off sc0 sc1
	v_pk_mul_f32 v[104:105], v[0:1], v[104:105] op_sel_hi:[0,1]
	v_pk_mul_f32 v[102:103], v[0:1], v[102:103] op_sel_hi:[0,1]
	v_pk_mul_f32 v[106:107], v[0:1], v[96:97] op_sel_hi:[0,1]
	v_pk_mul_f32 v[96:97], v[0:1], v[94:95] op_sel_hi:[0,1]
	v_cvt_pk_bf16_f32 v94, v102, v103
	v_cvt_pk_bf16_f32 v95, v104, v105
	v_cvt_pk_bf16_f32 v96, v96, v97
	v_cvt_pk_bf16_f32 v97, v106, v107
	global_store_dwordx4 v[110:111], v[94:97], off offset:256 sc0 sc1
	v_mul_f32_e32 v0, v143, v152
	v_pk_mul_f32 v[98:99], v[0:1], v[98:99] op_sel_hi:[0,1]
	v_or_b32_e32 v94, 32, v158
	v_ashrrev_i32_e32 v95, 31, v94
	v_lshlrev_b64 v[94:95], 10, v[94:95]
	v_pk_mul_f32 v[96:97], v[0:1], v[100:101] op_sel_hi:[0,1]
	v_pk_mul_f32 v[100:101], v[0:1], v[92:93] op_sel_hi:[0,1]
	v_pk_mul_f32 v[92:93], v[0:1], v[90:91] op_sel_hi:[0,1]
	v_lshl_add_u64 v[94:95], v[166:167], 0, v[94:95]
	v_cvt_pk_bf16_f32 v90, v98, v99
	v_cvt_pk_bf16_f32 v91, v96, v97
	v_cvt_pk_bf16_f32 v92, v92, v93
	v_cvt_pk_bf16_f32 v93, v100, v101
	global_store_dwordx4 v[94:95], v[90:93], off sc0 sc1
	v_pk_mul_f32 v[88:89], v[0:1], v[88:89] op_sel_hi:[0,1]
	v_pk_mul_f32 v[86:87], v[0:1], v[86:87] op_sel_hi:[0,1]
	v_pk_mul_f32 v[90:91], v[0:1], v[80:81] op_sel_hi:[0,1]
	v_pk_mul_f32 v[80:81], v[0:1], v[78:79] op_sel_hi:[0,1]
	v_cvt_pk_bf16_f32 v78, v86, v87
	v_cvt_pk_bf16_f32 v79, v88, v89
	v_cvt_pk_bf16_f32 v80, v80, v81
	v_cvt_pk_bf16_f32 v81, v90, v91
	global_store_dwordx4 v[94:95], v[78:81], off offset:256 sc0 sc1
	v_mul_f32_e32 v0, v143, v150
	v_pk_mul_f32 v[82:83], v[0:1], v[82:83] op_sel_hi:[0,1]
	v_or_b32_e32 v78, 48, v158
	v_ashrrev_i32_e32 v79, 31, v78
	v_lshlrev_b64 v[78:79], 10, v[78:79]
	v_pk_mul_f32 v[80:81], v[0:1], v[84:85] op_sel_hi:[0,1]
	v_pk_mul_f32 v[84:85], v[0:1], v[76:77] op_sel_hi:[0,1]
	v_pk_mul_f32 v[76:77], v[0:1], v[74:75] op_sel_hi:[0,1]
	v_lshl_add_u64 v[78:79], v[166:167], 0, v[78:79]
	v_cvt_pk_bf16_f32 v74, v82, v83
	v_cvt_pk_bf16_f32 v75, v80, v81
	v_cvt_pk_bf16_f32 v76, v76, v77
	v_cvt_pk_bf16_f32 v77, v84, v85
	global_store_dwordx4 v[78:79], v[74:77], off sc0 sc1
	v_pk_mul_f32 v[72:73], v[0:1], v[72:73] op_sel_hi:[0,1]
	v_pk_mul_f32 v[70:71], v[0:1], v[70:71] op_sel_hi:[0,1]
	v_pk_mul_f32 v[74:75], v[0:1], v[68:69] op_sel_hi:[0,1]
	v_pk_mul_f32 v[68:69], v[0:1], v[66:67] op_sel_hi:[0,1]
	v_mul_f32_e32 v0, v143, v148
	v_cvt_pk_bf16_f32 v66, v70, v71
	v_cvt_pk_bf16_f32 v67, v72, v73
	v_cvt_pk_bf16_f32 v68, v68, v69
	v_cvt_pk_bf16_f32 v69, v74, v75
	v_pk_mul_f32 v[62:63], v[0:1], v[62:63] op_sel_hi:[0,1]
	s_mov_b32 s29, 0x20000
	global_store_dwordx4 v[78:79], v[66:69], off offset:256 sc0 sc1
	v_pk_mul_f32 v[64:65], v[0:1], v[64:65] op_sel_hi:[0,1]
	v_pk_mul_f32 v[52:53], v[0:1], v[52:53] op_sel_hi:[0,1]
	v_pk_mul_f32 v[68:69], v[0:1], v[60:61] op_sel_hi:[0,1]
	v_pk_mul_f32 v[60:61], v[0:1], v[58:59] op_sel_hi:[0,1]
	v_cvt_pk_bf16_f32 v58, v62, v63
	v_add_co_u32_e32 v62, vcc, s29, v160
	v_cvt_pk_bf16_f32 v59, v64, v65
	v_cvt_pk_bf16_f32 v60, v60, v61
	v_cvt_pk_bf16_f32 v61, v68, v69
	v_addc_co_u32_e32 v63, vcc, 0, v161, vcc
	global_store_dwordx4 v[62:63], v[58:61], off sc0 sc1
	v_pk_mul_f32 v[50:51], v[0:1], v[50:51] op_sel_hi:[0,1]
	v_lshl_add_u64 v[66:67], v[160:161], 0, s[24:25]
	v_pk_mul_f32 v[58:59], v[0:1], v[44:45] op_sel_hi:[0,1]
	v_pk_mul_f32 v[44:45], v[0:1], v[42:43] op_sel_hi:[0,1]
	v_cvt_pk_bf16_f32 v42, v50, v51
	v_cvt_pk_bf16_f32 v43, v52, v53
	v_cvt_pk_bf16_f32 v44, v44, v45
	v_cvt_pk_bf16_f32 v45, v58, v59
	v_mul_f32_e32 v0, v143, v146
	global_store_dwordx4 v[66:67], v[42:45], off offset:256 sc0 sc1
	v_pk_mul_f32 v[46:47], v[0:1], v[46:47] op_sel_hi:[0,1]
	s_mov_b32 s29, 0x24000
	v_pk_mul_f32 v[44:45], v[0:1], v[56:57] op_sel_hi:[0,1]
	v_pk_mul_f32 v[42:43], v[0:1], v[54:55] op_sel_hi:[0,1]
	v_pk_mul_f32 v[48:49], v[0:1], v[48:49] op_sel_hi:[0,1]
	v_cvt_pk_bf16_f32 v42, v42, v43
	v_cvt_pk_bf16_f32 v43, v44, v45
	v_cvt_pk_bf16_f32 v44, v46, v47
	v_add_co_u32_e32 v46, vcc, s29, v160
	v_cvt_pk_bf16_f32 v45, v48, v49
	s_nop 0
	v_addc_co_u32_e32 v47, vcc, 0, v161, vcc
	s_mov_b64 s[36:37], 0x24000
	global_store_dwordx4 v[46:47], v[42:45], off sc0 sc1
	v_pk_mul_f32 v[36:37], v[0:1], v[36:37] op_sel_hi:[0,1]
	v_pk_mul_f32 v[34:35], v[0:1], v[34:35] op_sel_hi:[0,1]
	v_pk_mul_f32 v[42:43], v[0:1], v[28:29] op_sel_hi:[0,1]
	v_pk_mul_f32 v[28:29], v[0:1], v[26:27] op_sel_hi:[0,1]
	v_lshl_add_u64 v[50:51], v[160:161], 0, s[36:37]
	v_cvt_pk_bf16_f32 v26, v34, v35
	v_cvt_pk_bf16_f32 v27, v36, v37
	v_cvt_pk_bf16_f32 v28, v28, v29
	v_cvt_pk_bf16_f32 v29, v42, v43
	v_mul_f32_e32 v0, v143, v144
	global_store_dwordx4 v[50:51], v[26:29], off offset:256 sc0 sc1
	v_pk_mul_f32 v[30:31], v[0:1], v[30:31] op_sel_hi:[0,1]
	s_mov_b32 s29, 0x28000
	v_pk_mul_f32 v[28:29], v[0:1], v[40:41] op_sel_hi:[0,1]
	v_pk_mul_f32 v[26:27], v[0:1], v[38:39] op_sel_hi:[0,1]
	v_pk_mul_f32 v[32:33], v[0:1], v[32:33] op_sel_hi:[0,1]
	v_cvt_pk_bf16_f32 v26, v26, v27
	v_cvt_pk_bf16_f32 v27, v28, v29
	v_cvt_pk_bf16_f32 v28, v30, v31
	v_add_co_u32_e32 v30, vcc, s29, v160
	v_cvt_pk_bf16_f32 v29, v32, v33
	s_nop 0
	v_addc_co_u32_e32 v31, vcc, 0, v161, vcc
	s_mov_b64 s[36:37], 0x28000
	global_store_dwordx4 v[30:31], v[26:29], off sc0 sc1
	v_pk_mul_f32 v[20:21], v[0:1], v[20:21] op_sel_hi:[0,1]
	v_pk_mul_f32 v[18:19], v[0:1], v[18:19] op_sel_hi:[0,1]
	v_pk_mul_f32 v[26:27], v[0:1], v[12:13] op_sel_hi:[0,1]
	v_pk_mul_f32 v[12:13], v[0:1], v[10:11] op_sel_hi:[0,1]
	v_lshl_add_u64 v[34:35], v[160:161], 0, s[36:37]
	v_cvt_pk_bf16_f32 v10, v18, v19
	v_cvt_pk_bf16_f32 v11, v20, v21
	v_cvt_pk_bf16_f32 v12, v12, v13
	v_cvt_pk_bf16_f32 v13, v26, v27
	v_mul_f32_e32 v0, v143, v142
	global_store_dwordx4 v[34:35], v[10:13], off offset:256 sc0 sc1
	v_pk_mul_f32 v[14:15], v[0:1], v[14:15] op_sel_hi:[0,1]
	s_mov_b32 s29, 0x2c000
	v_pk_mul_f32 v[12:13], v[0:1], v[24:25] op_sel_hi:[0,1]
	v_pk_mul_f32 v[10:11], v[0:1], v[22:23] op_sel_hi:[0,1]
	v_pk_mul_f32 v[16:17], v[0:1], v[16:17] op_sel_hi:[0,1]
	v_cvt_pk_bf16_f32 v10, v10, v11
	v_cvt_pk_bf16_f32 v11, v12, v13
	v_cvt_pk_bf16_f32 v12, v14, v15
	v_add_co_u32_e32 v14, vcc, s29, v160
	v_cvt_pk_bf16_f32 v13, v16, v17
	s_nop 0
	v_addc_co_u32_e32 v15, vcc, 0, v161, vcc
	s_mov_b64 s[36:37], 0x2c000
	global_store_dwordx4 v[14:15], v[10:13], off sc0 sc1
	v_pk_mul_f32 v[8:9], v[0:1], v[8:9] op_sel_hi:[0,1]
	v_pk_mul_f32 v[6:7], v[0:1], v[6:7] op_sel_hi:[0,1]
	v_pk_mul_f32 v[10:11], v[0:1], v[4:5] op_sel_hi:[0,1]
	v_pk_mul_f32 v[4:5], v[0:1], v[2:3] op_sel_hi:[0,1]
	v_lshl_add_u64 v[18:19], v[160:161], 0, s[36:37]
	v_cvt_pk_bf16_f32 v2, v6, v7
	v_cvt_pk_bf16_f32 v3, v8, v9
	v_cvt_pk_bf16_f32 v4, v4, v5
	v_cvt_pk_bf16_f32 v5, v10, v11
	global_store_dwordx4 v[18:19], v[2:5], off offset:256 sc0 sc1

.LBB0_2070:
	s_mov_b32 s17, -1
	s_ashr_i32 s51, s50, 31
	s_lshl_b64 s[50:51], s[50:51], 21
	v_mbcnt_lo_u32_b32 v0, s17, 0
	v_mbcnt_hi_u32_b32 v146, s17, v0
	s_add_u32 s17, s89, s50
	s_addc_u32 s29, s90, s51
	s_ashr_i32 s39, s38, 31
	s_lshl_b64 s[38:39], s[38:39], 9
	s_add_u32 s17, s17, s38
	s_addc_u32 s29, s29, s39
	s_add_u32 s38, s17, s92
	s_addc_u32 s39, s29, 0
	v_and_b32_e32 v0, 0x70, v146
	v_lshl_add_u64 v[144:145], s[38:39], 0, v[0:1]
	v_and_or_b32 v0, v146, 15, s67
	v_lshl_add_u32 v146, s16, 8, v0
	v_ashrrev_i32_e32 v147, 31, v146
	v_lshlrev_b64 v[148:149], 12, v[146:147]
	v_lshl_add_u64 v[148:149], v[144:145], 0, v[148:149]
	s_mov_b64 s[16:17], 0x80000
	v_cvt_pk_bf16_f32 v70, v70, v71
	v_cvt_pk_bf16_f32 v71, v72, v73
	v_cvt_pk_bf16_f32 v72, v66, v67
	v_lshl_add_u64 v[66:67], v[148:149], 0, s[16:17]
	s_mov_b32 s16, 0x80000
	v_cvt_pk_bf16_f32 v62, v62, v63
	v_cvt_pk_bf16_f32 v63, v64, v65
	v_cvt_pk_bf16_f32 v64, v58, v59
	v_add_co_u32_e32 v58, vcc, s16, v148
	v_cvt_pk_bf16_f32 v46, v46, v47
	v_cvt_pk_bf16_f32 v47, v48, v49
	v_cvt_pk_bf16_f32 v48, v42, v43
	v_cvt_pk_bf16_f32 v49, v44, v45
	s_mov_b64 s[16:17], 0x90000
	v_addc_co_u32_e32 v59, vcc, 0, v149, vcc
	global_store_dwordx4 v[66:67], v[46:49], off offset:256 sc0 sc1
	v_cvt_pk_bf16_f32 v30, v30, v31
	v_cvt_pk_bf16_f32 v31, v32, v33
	v_lshl_add_u64 v[46:47], v[148:149], 0, s[16:17]
	s_mov_b32 s16, 0x90000
	v_add_co_u32_e32 v48, vcc, s16, v148
	v_cvt_pk_bf16_f32 v32, v26, v27
	v_cvt_pk_bf16_f32 v33, v28, v29
	s_mov_b64 s[16:17], 0xa0000
	v_cvt_pk_bf16_f32 v110, v110, v111
	v_cvt_pk_bf16_f32 v111, v112, v113
	v_cvt_pk_bf16_f32 v112, v106, v107
	v_or_b32_e32 v106, 16, v146
	v_addc_co_u32_e32 v49, vcc, 0, v149, vcc
	global_store_dwordx4 v[46:47], v[30:33], off offset:256 sc0 sc1
	v_ashrrev_i32_e32 v107, 31, v106
	v_cvt_pk_bf16_f32 v94, v94, v95
	v_lshl_add_u64 v[30:31], v[148:149], 0, s[16:17]
	s_mov_b32 s16, 0xa0000
	v_cvt_pk_bf16_f32 v95, v96, v97
	v_cvt_pk_bf16_f32 v96, v90, v91
	v_or_b32_e32 v90, 32, v146
	v_add_co_u32_e32 v32, vcc, s16, v148
	v_cvt_pk_bf16_f32 v14, v14, v15
	v_cvt_pk_bf16_f32 v15, v16, v17
	v_cvt_pk_bf16_f32 v16, v10, v11
	v_cvt_pk_bf16_f32 v17, v12, v13
	s_mov_b64 s[16:17], 0xb0000
	v_cvt_pk_bf16_f32 v113, v108, v109
	v_lshlrev_b64 v[106:107], 12, v[106:107]
	v_ashrrev_i32_e32 v91, 31, v90
	v_cvt_pk_bf16_f32 v78, v78, v79
	v_cvt_pk_bf16_f32 v79, v80, v81
	v_cvt_pk_bf16_f32 v80, v74, v75
	v_or_b32_e32 v74, 48, v146
	v_addc_co_u32_e32 v33, vcc, 0, v149, vcc
	global_store_dwordx4 v[30:31], v[14:17], off offset:256 sc0 sc1
	global_store_dwordx4 v[148:149], v[110:113], off offset:256 sc0 sc1
	v_cvt_pk_bf16_f32 v97, v92, v93
	v_lshl_add_u64 v[14:15], v[148:149], 0, s[16:17]
	s_mov_b32 s16, 0xb0000
	v_lshl_add_u64 v[110:111], v[144:145], 0, v[106:107]
	v_lshlrev_b64 v[90:91], 12, v[90:91]
	v_ashrrev_i32_e32 v75, 31, v74
	v_add_co_u32_e32 v16, vcc, s16, v148
	global_store_dwordx4 v[110:111], v[94:97], off offset:256 sc0 sc1
	v_cvt_pk_bf16_f32 v81, v76, v77
	v_lshlrev_b64 v[74:75], 12, v[74:75]
	v_lshl_add_u64 v[94:95], v[144:145], 0, v[90:91]
	v_addc_co_u32_e32 v17, vcc, 0, v149, vcc
	v_cvt_pk_bf16_f32 v126, v126, v127
	v_cvt_pk_bf16_f32 v127, v128, v129
	v_cvt_pk_bf16_f32 v128, v122, v123
	v_cvt_pk_bf16_f32 v129, v124, v125
	v_cvt_pk_bf16_f32 v106, v118, v119
	v_cvt_pk_bf16_f32 v107, v120, v121
	v_cvt_pk_bf16_f32 v108, v114, v115
	v_cvt_pk_bf16_f32 v109, v116, v117
	v_cvt_pk_bf16_f32 v90, v102, v103
	v_cvt_pk_bf16_f32 v91, v104, v105
	v_cvt_pk_bf16_f32 v92, v98, v99
	v_cvt_pk_bf16_f32 v93, v100, v101
	global_store_dwordx4 v[94:95], v[78:81], off offset:256 sc0 sc1
	v_cvt_pk_bf16_f32 v76, v82, v83
	v_cvt_pk_bf16_f32 v77, v84, v85
	v_lshl_add_u64 v[78:79], v[144:145], 0, v[74:75]
	v_cvt_pk_bf16_f32 v74, v86, v87
	v_cvt_pk_bf16_f32 v75, v88, v89
	v_cvt_pk_bf16_f32 v73, v68, v69
	v_cvt_pk_bf16_f32 v65, v60, v61
	v_cvt_pk_bf16_f32 v42, v54, v55
	v_cvt_pk_bf16_f32 v43, v56, v57
	v_cvt_pk_bf16_f32 v44, v50, v51
	v_cvt_pk_bf16_f32 v45, v52, v53
	v_cvt_pk_bf16_f32 v26, v38, v39
	v_cvt_pk_bf16_f32 v27, v40, v41
	v_cvt_pk_bf16_f32 v28, v34, v35
	v_cvt_pk_bf16_f32 v29, v36, v37
	v_cvt_pk_bf16_f32 v10, v22, v23
	v_cvt_pk_bf16_f32 v11, v24, v25
	v_cvt_pk_bf16_f32 v12, v18, v19
	v_cvt_pk_bf16_f32 v13, v20, v21
	v_cvt_pk_bf16_f32 v6, v6, v7
	v_cvt_pk_bf16_f32 v7, v8, v9
	v_cvt_pk_bf16_f32 v8, v2, v3
	v_cvt_pk_bf16_f32 v9, v4, v5
	s_and_b64 vcc, exec, s[36:37]
	s_mov_b64 s[16:17], -1
	s_movk_i32 s95, 0x100
	s_movk_i32 s94, 0x2000
	global_store_dwordx4 v[148:149], v[126:129], off sc0 sc1
	global_store_dwordx4 v[110:111], v[106:109], off sc0 sc1
	global_store_dwordx4 v[94:95], v[90:93], off sc0 sc1
	global_store_dwordx4 v[78:79], v[74:77], off sc0 sc1
	global_store_dwordx4 v[78:79], v[70:73], off offset:256 sc0 sc1
	global_store_dwordx4 v[58:59], v[62:65], off sc0 sc1
	global_store_dwordx4 v[48:49], v[42:45], off sc0 sc1
	global_store_dwordx4 v[32:33], v[26:29], off sc0 sc1
	global_store_dwordx4 v[16:17], v[10:13], off sc0 sc1
	global_store_dwordx4 v[14:15], v[6:9], off offset:256 sc0 sc1
	s_cbranch_vccnz .LBB0_2055
	s_andn2_b64 vcc, exec, s[0:1]
	s_cbranch_vccnz .LBB0_2054
	s_barrier
	s_branch .LBB0_2054
